# speedup vs baseline: 1.0803x; 1.0741x over previous
_Z16closed_form_mainPKfS0_PKiPf:
	s_load_dwordx8 s[16:23], s[0:1], 0x0
	s_lshr_b32 s6, s2, 3
	v_readfirstlane_b32 s0, v0
	s_mul_hi_u32 s7, s6, 0x24924925
	s_lshr_b32 s4, s0, 6
	s_and_b32 s0, s2, 7
	s_mul_i32 s1, s7, 7
	s_bfe_u32 s5, s2, 0x10003
	s_sub_i32 s1, s6, s1
	s_mul_i32 s36, s0, 7
	s_xor_b32 s3, s4, s5
	s_add_i32 s36, s36, s1
	s_waitcnt lgkmcnt(0)
	s_mov_b64 s[28:29], s[22:23]
	v_and_b32_e32 v19, 63, v0
	s_cmp_lt_u32 s36, 52
	s_mov_b64 s[0:1], -1
	s_cbranch_scc0 .LBB0_32
	s_mul_hi_u32 s0, s6, 0x20820821
	s_lshr_b32 s38, s0, 3
	s_mul_hi_u32 s0, s7, 0x1c71c71d
	s_mul_i32 s0, s0, 9
	s_sub_i32 s0, s7, s0
	v_add_u32_e32 v2, -3, v19
	v_mad_u64_u32 v[0:1], s[0:1], s0, 57, v[2:3]
	s_mov_b64 s[24:25], s[18:19]
	v_mov_b32_e32 v1, 0x200
	v_med3_i32 v1, v0, 0, v1
	s_mul_i32 s34, s36, 10
	s_and_b32 s17, s17, 0xffff
	s_and_b32 s25, s25, 0xffff
	v_cmp_gt_u32_e64 s[0:1], 57, v2
	s_mov_b32 s19, 0x20000
	s_mov_b32 s18, 0xe0e038
	s_mov_b32 s26, 0x606018
	s_mul_i32 s35, s38, 0x70701c
	s_mul_i32 s33, s38, 0x30300c
	v_lshlrev_b32_e32 v28, 2, v1
	v_mul_u32_u24_e32 v27, 12, v1
	v_lshlrev_b32_e32 v23, 4, v19
	s_cmp_lg_u32 s4, s5
	v_sub_u32_e64 v29, s34, 2 clamp
	s_cbranch_scc0 .LBB0_15
	s_mov_b32 s27, s19
	s_and_b32 s21, s21, 0xffff
	s_mov_b32 s22, 0x202008
	s_mov_b32 s23, s19
	s_mul_i32 s38, s38, 0x101004
	s_add_i32 s39, s35, 0x505014
	s_movk_i32 s37, 0x80
	v_add_u32_e32 v18, -1, v0
	s_movk_i32 s4, 0x201
	s_movk_i32 s5, 0x1ff
	v_cmp_gt_u32_e64 s[40:41], s4, v0
	v_cmp_gt_u32_e64 s[42:43], s5, v18
	v_mov_b32_e32 v18, 0x42c80000
	v_mov_b32_e32 v22, 0x3de38e39
	v_mov_b32_e32 v26, 0x3a3d6628
	v_mov_b32_e32 v1, 0
	s_add_i32 s4, s34, -3
	s_max_i32 s4, s4, 0
	s_mul_i32 s4, s4, 0x804
	s_add_i32 s4, s4, s38
	buffer_load_dword v29, v28, s[20:23], s4 offen nt
	s_add_i32 s4, s34, -2
	s_max_i32 s4, s4, 0
	s_mul_i32 s4, s4, 0x804
	s_add_i32 s4, s4, s38
	buffer_load_dword v2, v28, s[20:23], s4 offen nt
	s_add_i32 s5, s34, -2
	s_max_i32 s5, s5, 0
	s_mul_i32 s6, s5, 0x804
	s_add_i32 s6, s6, s39
	s_add_i32 s7, s6, 0x101004
	s_mul_i32 s9, s5, 0x180c
	s_add_i32 s9, s9, s33
	s_add_i32 s4, s34, -1
	s_max_i32 s4, s4, 0
	s_mul_i32 s4, s4, 0x804
	s_add_i32 s4, s4, s38
	buffer_load_dword v3, v28, s[20:23], s4 offen nt
	buffer_load_dwordx3 v[8:10], v27, s[24:27], s9 offen nt
	buffer_load_dword v4, v28, s[16:19], s6 offen nt
	buffer_load_dword v5, v28, s[16:19], s7 offen nt
	s_add_i32 s5, s34, -1
	s_max_i32 s5, s5, 0
	s_mul_i32 s6, s5, 0x804
	s_add_i32 s6, s6, s39
	s_add_i32 s7, s6, 0x101004
	s_mul_i32 s9, s5, 0x180c
	s_add_i32 s9, s9, s33
	s_add_i32 s4, s34, 0
	s_min_i32 s4, s4, 0x200
	s_mul_i32 s4, s4, 0x804
	s_add_i32 s4, s4, s38
	buffer_load_dword v16, v28, s[20:23], s4 offen nt
	buffer_load_dwordx3 v[12:14], v27, s[24:27], s9 offen nt
	buffer_load_dword v6, v28, s[16:19], s6 offen nt
	buffer_load_dword v7, v28, s[16:19], s7 offen nt
	s_waitcnt vmcnt(8)
	s_add_i32 s4, s34, -3
	s_cmpk_lt_u32 s4, 0x201
	s_cselect_b64 s[12:13], s[40:41], 0
	v_cmp_eq_u32_e64 s[14:15], s37, v29
	s_and_b64 s[14:15], s[14:15], s[12:13]
	v_cndmask_b32_e64 v17, 0, 1, s[14:15]
	s_add_i32 s4, s34, -2
	s_cmpk_lt_u32 s4, 0x201
	s_cselect_b64 s[12:13], s[40:41], 0
	v_cmp_eq_u32_e64 s[14:15], s37, v2
	s_and_b64 s[14:15], s[14:15], s[12:13]
	v_cndmask_b32_e64 v20, 0, 1, s[14:15]
	s_nop 0
	v_or_b32_dpp v21, v17, v17 wave_shr:1 row_mask:0xf bank_mask:0xf bound_ctrl:1
	v_or_b32_dpp v24, v20, v20 wave_shr:1 row_mask:0xf bank_mask:0xf bound_ctrl:1
	s_nop 1
	v_or_b32_dpp v21, v17, v21 wave_shl:1 row_mask:0xf bank_mask:0xf bound_ctrl:1
	v_or_b32_dpp v24, v20, v24 wave_shl:1 row_mask:0xf bank_mask:0xf bound_ctrl:1
	s_nop 1
	v_or_b32_dpp v25, v21, v21 wave_shr:1 row_mask:0xf bank_mask:0xf bound_ctrl:1
	v_or_b32_dpp v30, v24, v24 wave_shr:1 row_mask:0xf bank_mask:0xf bound_ctrl:1
	s_nop 1
	v_or_b32_dpp v25, v21, v25 wave_shl:1 row_mask:0xf bank_mask:0xf bound_ctrl:1
	v_or_b32_dpp v30, v24, v30 wave_shl:1 row_mask:0xf bank_mask:0xf bound_ctrl:1
	v_mov_b32_e32 v17, 0
	v_mov_b32_e32 v24, 0
	s_add_i32 s5, s34, 0
	s_min_i32 s5, s5, 0x200
	s_mul_i32 s6, s5, 0x804
	s_add_i32 s6, s6, s39
	s_add_i32 s7, s6, 0x101004
	s_mul_i32 s9, s5, 0x180c
	s_add_i32 s9, s9, s33
	s_add_i32 s4, s34, 1
	s_min_i32 s4, s4, 0x200
	s_mul_i32 s4, s4, 0x804
	s_add_i32 s4, s4, s38
	buffer_load_dword v31, v28, s[20:23], s4 offen nt
	buffer_load_dwordx3 v[32:34], v27, s[24:27], s9 offen nt
	buffer_load_dword v20, v28, s[16:19], s6 offen nt
	buffer_load_dword v21, v28, s[16:19], s7 offen nt
	s_waitcnt vmcnt(8)
	s_add_i32 s4, s34, -1
	s_cmpk_lt_u32 s4, 0x201
	s_cselect_b64 s[12:13], s[40:41], 0
	v_cmp_eq_u32_e64 s[14:15], s37, v3
	s_and_b64 s[14:15], s[14:15], s[12:13]
	v_cndmask_b32_e64 v36, 0, 1, s[14:15]
	v_mul_f32_e64 v38, v8, v8
	v_mul_f32_e64 v39, v8, v9
	v_mul_f32_e64 v40, v8, v10
	v_mul_f32_e64 v41, v9, v9
	v_mul_f32_e64 v42, v9, v10
	v_mul_f32_e64 v43, v10, v10
	v_or_b32_dpp v37, v36, v36 wave_shr:1 row_mask:0xf bank_mask:0xf bound_ctrl:1
	s_nop 1
	v_or_b32_dpp v37, v36, v37 wave_shl:1 row_mask:0xf bank_mask:0xf bound_ctrl:1
	s_nop 1
	v_or_b32_dpp v44, v37, v37 wave_shr:1 row_mask:0xf bank_mask:0xf bound_ctrl:1
	s_nop 1
	v_or_b32_dpp v44, v37, v44 wave_shl:1 row_mask:0xf bank_mask:0xf bound_ctrl:1
	v_or3_b32 v45, v44, v30, v25
	v_or3_b32 v45, v45, v17, v24
	s_add_i32 s4, s34, -4
	s_cmpk_lt_u32 s4, 0x1ff
	s_cselect_b64 s[12:13], s[42:43], 0
	v_cmp_ne_u32_e64 s[30:31], 0, v45
	s_and_b64 s[30:31], s[30:31], s[12:13]
	v_cndmask_b32_e64 v45, 0, 1.0, s[30:31]
	v_add_f32_dpp v36, v8, v8 wave_shr:1 row_mask:0xf bank_mask:0xf bound_ctrl:1
	v_add_f32_dpp v37, v9, v9 wave_shr:1 row_mask:0xf bank_mask:0xf bound_ctrl:1
	v_add_f32_dpp v46, v10, v10 wave_shr:1 row_mask:0xf bank_mask:0xf bound_ctrl:1
	v_add_f32_dpp v47, v38, v38 wave_shr:1 row_mask:0xf bank_mask:0xf bound_ctrl:1
	v_add_f32_dpp v48, v39, v39 wave_shr:1 row_mask:0xf bank_mask:0xf bound_ctrl:1
	v_add_f32_dpp v49, v40, v40 wave_shr:1 row_mask:0xf bank_mask:0xf bound_ctrl:1
	v_add_f32_dpp v50, v41, v41 wave_shr:1 row_mask:0xf bank_mask:0xf bound_ctrl:1
	v_add_f32_dpp v51, v42, v42 wave_shr:1 row_mask:0xf bank_mask:0xf bound_ctrl:1
	v_add_f32_dpp v52, v43, v43 wave_shr:1 row_mask:0xf bank_mask:0xf bound_ctrl:1
	v_add_f32_dpp v53, v45, v45 wave_shr:1 row_mask:0xf bank_mask:0xf bound_ctrl:1
	v_add_f32_dpp v36, v8, v36 wave_shl:1 row_mask:0xf bank_mask:0xf bound_ctrl:1
	v_add_f32_dpp v37, v9, v37 wave_shl:1 row_mask:0xf bank_mask:0xf bound_ctrl:1
	v_add_f32_dpp v46, v10, v46 wave_shl:1 row_mask:0xf bank_mask:0xf bound_ctrl:1
	v_add_f32_dpp v47, v38, v47 wave_shl:1 row_mask:0xf bank_mask:0xf bound_ctrl:1
	v_add_f32_dpp v48, v39, v48 wave_shl:1 row_mask:0xf bank_mask:0xf bound_ctrl:1
	v_add_f32_dpp v49, v40, v49 wave_shl:1 row_mask:0xf bank_mask:0xf bound_ctrl:1
	v_add_f32_dpp v50, v41, v50 wave_shl:1 row_mask:0xf bank_mask:0xf bound_ctrl:1
	v_add_f32_dpp v51, v42, v51 wave_shl:1 row_mask:0xf bank_mask:0xf bound_ctrl:1
	v_add_f32_dpp v52, v43, v52 wave_shl:1 row_mask:0xf bank_mask:0xf bound_ctrl:1
	v_add_f32_dpp v53, v45, v53 wave_shl:1 row_mask:0xf bank_mask:0xf bound_ctrl:1
	s_barrier
	v_pk_mul_f32 v[38:39], v[4:5], v[8:9] op_sel_hi:[1,0]
	v_pk_mul_f32 v[40:41], v[4:5], v[8:9] op_sel:[0,1]
	v_pk_mul_f32 v[42:43], v[4:5], v[10:11] op_sel_hi:[1,0]
	v_add_f32_dpp v54, v4, v4 wave_shr:1 row_mask:0xf bank_mask:0xf bound_ctrl:1
	v_add_f32_dpp v55, v5, v5 wave_shr:1 row_mask:0xf bank_mask:0xf bound_ctrl:1
	v_add_f32_dpp v56, v38, v38 wave_shr:1 row_mask:0xf bank_mask:0xf bound_ctrl:1
	v_add_f32_dpp v57, v39, v39 wave_shr:1 row_mask:0xf bank_mask:0xf bound_ctrl:1
	v_add_f32_dpp v58, v40, v40 wave_shr:1 row_mask:0xf bank_mask:0xf bound_ctrl:1
	v_add_f32_dpp v59, v41, v41 wave_shr:1 row_mask:0xf bank_mask:0xf bound_ctrl:1
	v_add_f32_dpp v60, v42, v42 wave_shr:1 row_mask:0xf bank_mask:0xf bound_ctrl:1
	v_add_f32_dpp v61, v43, v43 wave_shr:1 row_mask:0xf bank_mask:0xf bound_ctrl:1
	v_add_f32_dpp v54, v4, v54 wave_shl:1 row_mask:0xf bank_mask:0xf bound_ctrl:1
	v_add_f32_dpp v55, v5, v55 wave_shl:1 row_mask:0xf bank_mask:0xf bound_ctrl:1
	v_add_f32_dpp v56, v38, v56 wave_shl:1 row_mask:0xf bank_mask:0xf bound_ctrl:1
	v_add_f32_dpp v57, v39, v57 wave_shl:1 row_mask:0xf bank_mask:0xf bound_ctrl:1
	v_add_f32_dpp v58, v40, v58 wave_shl:1 row_mask:0xf bank_mask:0xf bound_ctrl:1
	v_add_f32_dpp v59, v41, v59 wave_shl:1 row_mask:0xf bank_mask:0xf bound_ctrl:1
	v_add_f32_dpp v60, v42, v60 wave_shl:1 row_mask:0xf bank_mask:0xf bound_ctrl:1
	v_add_f32_dpp v61, v43, v61 wave_shl:1 row_mask:0xf bank_mask:0xf bound_ctrl:1
	s_add_i32 s5, s34, 1
	s_min_i32 s5, s5, 0x200
	s_mul_i32 s6, s5, 0x804
	s_add_i32 s6, s6, s39
	s_add_i32 s7, s6, 0x101004
	s_mul_i32 s9, s5, 0x180c
	s_add_i32 s9, s9, s33
	s_add_i32 s4, s34, 2
	s_min_i32 s4, s4, 0x200
	s_mul_i32 s4, s4, 0x804
	s_add_i32 s4, s4, s38
	buffer_load_dword v24, v28, s[20:23], s4 offen nt
	buffer_load_dwordx3 v[40:42], v27, s[24:27], s9 offen nt
	buffer_load_dword v38, v28, s[16:19], s6 offen nt
	buffer_load_dword v39, v28, s[16:19], s7 offen nt
	s_waitcnt vmcnt(8)
	s_add_i32 s4, s34, 0
	s_cmpk_lt_u32 s4, 0x201
	s_cselect_b64 s[12:13], s[40:41], 0
	v_cmp_eq_u32_e64 s[14:15], s37, v16
	s_and_b64 s[14:15], s[14:15], s[12:13]
	v_cndmask_b32_e64 v45, 0, 1, s[14:15]
	v_mul_f32_e64 v62, v12, v12
	v_mul_f32_e64 v63, v12, v13
	v_mul_f32_e64 v64, v12, v14
	v_mul_f32_e64 v65, v13, v13
	v_mul_f32_e64 v66, v13, v14
	v_mul_f32_e64 v67, v14, v14
	v_or_b32_dpp v68, v45, v45 wave_shr:1 row_mask:0xf bank_mask:0xf bound_ctrl:1
	s_nop 1
	v_or_b32_dpp v68, v45, v68 wave_shl:1 row_mask:0xf bank_mask:0xf bound_ctrl:1
	s_nop 1
	v_or_b32_dpp v69, v68, v68 wave_shr:1 row_mask:0xf bank_mask:0xf bound_ctrl:1
	s_nop 1
	v_or_b32_dpp v69, v68, v69 wave_shl:1 row_mask:0xf bank_mask:0xf bound_ctrl:1
	v_or3_b32 v45, v69, v44, v30
	v_or3_b32 v45, v45, v25, v17
	s_add_i32 s4, s34, -3
	s_cmpk_lt_u32 s4, 0x1ff
	s_cselect_b64 s[12:13], s[42:43], 0
	v_cmp_ne_u32_e64 s[30:31], 0, v45
	s_and_b64 s[30:31], s[30:31], s[12:13]
	v_cndmask_b32_e64 v45, 0, 1.0, s[30:31]
	v_add_f32_dpp v70, v12, v12 wave_shr:1 row_mask:0xf bank_mask:0xf bound_ctrl:1
	v_add_f32_dpp v71, v13, v13 wave_shr:1 row_mask:0xf bank_mask:0xf bound_ctrl:1
	v_add_f32_dpp v72, v14, v14 wave_shr:1 row_mask:0xf bank_mask:0xf bound_ctrl:1
	v_add_f32_dpp v73, v62, v62 wave_shr:1 row_mask:0xf bank_mask:0xf bound_ctrl:1
	v_add_f32_dpp v74, v63, v63 wave_shr:1 row_mask:0xf bank_mask:0xf bound_ctrl:1
	v_add_f32_dpp v75, v64, v64 wave_shr:1 row_mask:0xf bank_mask:0xf bound_ctrl:1
	v_add_f32_dpp v76, v65, v65 wave_shr:1 row_mask:0xf bank_mask:0xf bound_ctrl:1
	v_add_f32_dpp v77, v66, v66 wave_shr:1 row_mask:0xf bank_mask:0xf bound_ctrl:1
	v_add_f32_dpp v78, v67, v67 wave_shr:1 row_mask:0xf bank_mask:0xf bound_ctrl:1
	v_add_f32_dpp v79, v45, v45 wave_shr:1 row_mask:0xf bank_mask:0xf bound_ctrl:1
	v_add_f32_dpp v70, v12, v70 wave_shl:1 row_mask:0xf bank_mask:0xf bound_ctrl:1
	v_add_f32_dpp v71, v13, v71 wave_shl:1 row_mask:0xf bank_mask:0xf bound_ctrl:1
	v_add_f32_dpp v72, v14, v72 wave_shl:1 row_mask:0xf bank_mask:0xf bound_ctrl:1
	v_add_f32_dpp v73, v62, v73 wave_shl:1 row_mask:0xf bank_mask:0xf bound_ctrl:1
	v_add_f32_dpp v74, v63, v74 wave_shl:1 row_mask:0xf bank_mask:0xf bound_ctrl:1
	v_add_f32_dpp v75, v64, v75 wave_shl:1 row_mask:0xf bank_mask:0xf bound_ctrl:1
	v_add_f32_dpp v76, v65, v76 wave_shl:1 row_mask:0xf bank_mask:0xf bound_ctrl:1
	v_add_f32_dpp v77, v66, v77 wave_shl:1 row_mask:0xf bank_mask:0xf bound_ctrl:1
	v_add_f32_dpp v78, v67, v78 wave_shl:1 row_mask:0xf bank_mask:0xf bound_ctrl:1
	v_add_f32_dpp v79, v45, v79 wave_shl:1 row_mask:0xf bank_mask:0xf bound_ctrl:1
	s_barrier
	v_pk_mul_f32 v[62:63], v[6:7], v[12:13] op_sel_hi:[1,0]
	v_pk_mul_f32 v[64:65], v[6:7], v[12:13] op_sel:[0,1]
	v_pk_mul_f32 v[66:67], v[6:7], v[14:15] op_sel_hi:[1,0]
	v_add_f32_dpp v80, v6, v6 wave_shr:1 row_mask:0xf bank_mask:0xf bound_ctrl:1
	v_add_f32_dpp v81, v7, v7 wave_shr:1 row_mask:0xf bank_mask:0xf bound_ctrl:1
	v_add_f32_dpp v82, v62, v62 wave_shr:1 row_mask:0xf bank_mask:0xf bound_ctrl:1
	v_add_f32_dpp v83, v63, v63 wave_shr:1 row_mask:0xf bank_mask:0xf bound_ctrl:1
	v_add_f32_dpp v84, v64, v64 wave_shr:1 row_mask:0xf bank_mask:0xf bound_ctrl:1
	v_add_f32_dpp v85, v65, v65 wave_shr:1 row_mask:0xf bank_mask:0xf bound_ctrl:1
	v_add_f32_dpp v86, v66, v66 wave_shr:1 row_mask:0xf bank_mask:0xf bound_ctrl:1
	v_add_f32_dpp v87, v67, v67 wave_shr:1 row_mask:0xf bank_mask:0xf bound_ctrl:1
	v_add_f32_dpp v80, v6, v80 wave_shl:1 row_mask:0xf bank_mask:0xf bound_ctrl:1
	v_add_f32_dpp v81, v7, v81 wave_shl:1 row_mask:0xf bank_mask:0xf bound_ctrl:1
	v_add_f32_dpp v82, v62, v82 wave_shl:1 row_mask:0xf bank_mask:0xf bound_ctrl:1
	v_add_f32_dpp v83, v63, v83 wave_shl:1 row_mask:0xf bank_mask:0xf bound_ctrl:1
	v_add_f32_dpp v84, v64, v84 wave_shl:1 row_mask:0xf bank_mask:0xf bound_ctrl:1
	v_add_f32_dpp v85, v65, v85 wave_shl:1 row_mask:0xf bank_mask:0xf bound_ctrl:1
	v_add_f32_dpp v86, v66, v86 wave_shl:1 row_mask:0xf bank_mask:0xf bound_ctrl:1
	v_add_f32_dpp v87, v67, v87 wave_shl:1 row_mask:0xf bank_mask:0xf bound_ctrl:1
	s_add_i32 s5, s34, 2
	s_min_i32 s5, s5, 0x200
	s_mul_i32 s6, s5, 0x804
	s_add_i32 s6, s6, s39
	s_add_i32 s7, s6, 0x101004
	s_mul_i32 s9, s5, 0x180c
	s_add_i32 s9, s9, s33
	s_add_i32 s4, s34, 3
	s_min_i32 s4, s4, 0x200
	s_mul_i32 s4, s4, 0x804
	s_add_i32 s4, s4, s38
	buffer_load_dword v17, v28, s[20:23], s4 offen nt
	buffer_load_dwordx3 v[64:66], v27, s[24:27], s9 offen nt
	buffer_load_dword v62, v28, s[16:19], s6 offen nt
	buffer_load_dword v63, v28, s[16:19], s7 offen nt
	s_waitcnt vmcnt(8)
	s_add_i32 s4, s34, 1
	s_cmpk_lt_u32 s4, 0x201
	s_cselect_b64 s[12:13], s[40:41], 0
	v_cmp_eq_u32_e64 s[14:15], s37, v31
	s_and_b64 s[14:15], s[14:15], s[12:13]
	v_cndmask_b32_e64 v29, 0, 1, s[14:15]
	v_mul_f32_e64 v88, v32, v32
	v_mul_f32_e64 v89, v32, v33
	v_mul_f32_e64 v90, v32, v34
	v_mul_f32_e64 v91, v33, v33
	v_mul_f32_e64 v92, v33, v34
	v_mul_f32_e64 v93, v34, v34
	v_or_b32_dpp v45, v29, v29 wave_shr:1 row_mask:0xf bank_mask:0xf bound_ctrl:1
	s_nop 1
	v_or_b32_dpp v45, v29, v45 wave_shl:1 row_mask:0xf bank_mask:0xf bound_ctrl:1
	s_nop 1
	v_or_b32_dpp v68, v45, v45 wave_shr:1 row_mask:0xf bank_mask:0xf bound_ctrl:1
	s_nop 1
	v_or_b32_dpp v68, v45, v68 wave_shl:1 row_mask:0xf bank_mask:0xf bound_ctrl:1
	v_or3_b32 v29, v68, v69, v44
	v_or3_b32 v29, v29, v30, v25
	s_add_i32 s4, s34, -2
	s_cmpk_lt_u32 s4, 0x1ff
	s_cselect_b64 s[12:13], s[42:43], 0
	v_cmp_ne_u32_e64 s[30:31], 0, v29
	s_and_b64 s[30:31], s[30:31], s[12:13]
	v_cndmask_b32_e64 v29, 0, 1.0, s[30:31]
	v_add_f32_dpp v94, v32, v32 wave_shr:1 row_mask:0xf bank_mask:0xf bound_ctrl:1
	v_add_f32_dpp v95, v33, v33 wave_shr:1 row_mask:0xf bank_mask:0xf bound_ctrl:1
	v_add_f32_dpp v96, v34, v34 wave_shr:1 row_mask:0xf bank_mask:0xf bound_ctrl:1
	v_add_f32_dpp v97, v88, v88 wave_shr:1 row_mask:0xf bank_mask:0xf bound_ctrl:1
	v_add_f32_dpp v98, v89, v89 wave_shr:1 row_mask:0xf bank_mask:0xf bound_ctrl:1
	v_add_f32_dpp v99, v90, v90 wave_shr:1 row_mask:0xf bank_mask:0xf bound_ctrl:1
	v_add_f32_dpp v100, v91, v91 wave_shr:1 row_mask:0xf bank_mask:0xf bound_ctrl:1
	v_add_f32_dpp v101, v92, v92 wave_shr:1 row_mask:0xf bank_mask:0xf bound_ctrl:1
	v_add_f32_dpp v102, v93, v93 wave_shr:1 row_mask:0xf bank_mask:0xf bound_ctrl:1
	v_add_f32_dpp v103, v29, v29 wave_shr:1 row_mask:0xf bank_mask:0xf bound_ctrl:1
	v_add_f32_dpp v94, v32, v94 wave_shl:1 row_mask:0xf bank_mask:0xf bound_ctrl:1
	v_add_f32_dpp v95, v33, v95 wave_shl:1 row_mask:0xf bank_mask:0xf bound_ctrl:1
	v_add_f32_dpp v96, v34, v96 wave_shl:1 row_mask:0xf bank_mask:0xf bound_ctrl:1
	v_add_f32_dpp v97, v88, v97 wave_shl:1 row_mask:0xf bank_mask:0xf bound_ctrl:1
	v_add_f32_dpp v98, v89, v98 wave_shl:1 row_mask:0xf bank_mask:0xf bound_ctrl:1
	v_add_f32_dpp v99, v90, v99 wave_shl:1 row_mask:0xf bank_mask:0xf bound_ctrl:1
	v_add_f32_dpp v100, v91, v100 wave_shl:1 row_mask:0xf bank_mask:0xf bound_ctrl:1
	v_add_f32_dpp v101, v92, v101 wave_shl:1 row_mask:0xf bank_mask:0xf bound_ctrl:1
	v_add_f32_dpp v102, v93, v102 wave_shl:1 row_mask:0xf bank_mask:0xf bound_ctrl:1
	v_add_f32_dpp v103, v29, v103 wave_shl:1 row_mask:0xf bank_mask:0xf bound_ctrl:1
	v_pk_add_f32 v[88:89], v[70:71], v[94:95]
	v_pk_add_f32 v[90:91], v[36:37], v[88:89]
	v_pk_add_f32 v[36:37], v[72:73], v[96:97]
	v_pk_add_f32 v[70:71], v[46:47], v[36:37]
	v_pk_add_f32 v[46:47], v[74:75], v[98:99]
	v_pk_add_f32 v[72:73], v[48:49], v[46:47]
	v_pk_add_f32 v[48:49], v[76:77], v[100:101]
	v_pk_add_f32 v[74:75], v[50:51], v[48:49]
	v_pk_add_f32 v[50:51], v[78:79], v[102:103]
	v_pk_add_f32 v[76:77], v[52:53], v[50:51]
	v_mul_f32_e64 v104, v90, v22
	v_mul_f32_e64 v105, v91, v22
	v_mul_f32_e64 v106, v70, v22
	v_fma_f32 v29, v71, v22, v26
	v_mul_f32_e64 v45, v72, v22
	v_mul_f32_e64 v52, v73, v22
	v_fma_f32 v53, v74, v22, v26
	v_mul_f32_e64 v78, v75, v22
	v_fma_f32 v79, v76, v22, v26
	v_fma_f32 v29, -v104, v104, v29
	v_fma_f32 v45, -v104, v105, v45
	v_fma_f32 v52, -v104, v106, v52
	v_fma_f32 v53, -v105, v105, v53
	v_fma_f32 v78, -v105, v106, v78
	v_fma_f32 v79, -v106, v106, v79
	v_mul_f32_e64 v92, v78, v78
	v_mul_f32_e64 v93, v45, v79
	v_mul_f32_e64 v116, v52, v53
	v_mul_f32_e64 v117, v52, v52
	v_mul_f32_e64 v118, v29, v78
	v_mul_f32_e64 v119, v45, v45
	v_fma_f32 v92, v53, v79, -v92
	v_fma_f32 v93, v52, v78, -v93
	v_fma_f32 v116, v45, v78, -v116
	v_fma_f32 v117, v29, v79, -v117
	v_fma_f32 v118, v45, v52, -v118
	v_fma_f32 v119, v29, v53, -v119
	v_mul_f32_e64 v120, v29, v92
	v_fma_f32 v120, v45, v93, v120
	v_fma_f32 v120, v52, v116, v120
	v_rcp_f32_e32 v120, v120
	v_cmp_ne_u32_e64 vcc, s37, v2
	v_mul_f32_e64 v120, v120, v22
	v_cndmask_b32_e64 v120, 0, v120, s[30:31]
	v_cndmask_b32_e64 v29, 0, v18, vcc
	v_cndmask_b32_e64 v113, 0, v22, s[30:31]
	v_mul_f32_e64 v107, v92, v120
	v_mul_f32_e64 v108, v93, v120
	v_mul_f32_e64 v109, v116, v120
	v_mul_f32_e64 v110, v117, v120
	v_mul_f32_e64 v111, v118, v120
	v_mul_f32_e64 v112, v119, v120
	v_add_f32_e64 v114, v77, v29
	v_mov_b32_e32 v115, v2
	ds_write_b128 v23, v[104:107]
	ds_write_b128 v23, v[108:111] offset:1024
	ds_write_b128 v23, v[112:115] offset:2048
	s_waitcnt lgkmcnt(0)
	s_barrier
	v_pk_mul_f32 v[52:53], v[20:21], v[32:33] op_sel_hi:[1,0]
	v_pk_mul_f32 v[70:71], v[20:21], v[32:33] op_sel:[0,1]
	v_pk_mul_f32 v[72:73], v[20:21], v[34:35] op_sel_hi:[1,0]
	v_add_f32_dpp v74, v20, v20 wave_shr:1 row_mask:0xf bank_mask:0xf bound_ctrl:1
	v_add_f32_dpp v75, v21, v21 wave_shr:1 row_mask:0xf bank_mask:0xf bound_ctrl:1
	v_add_f32_dpp v76, v52, v52 wave_shr:1 row_mask:0xf bank_mask:0xf bound_ctrl:1
	v_add_f32_dpp v77, v53, v53 wave_shr:1 row_mask:0xf bank_mask:0xf bound_ctrl:1
	v_add_f32_dpp v78, v70, v70 wave_shr:1 row_mask:0xf bank_mask:0xf bound_ctrl:1
	v_add_f32_dpp v79, v71, v71 wave_shr:1 row_mask:0xf bank_mask:0xf bound_ctrl:1
	v_add_f32_dpp v90, v72, v72 wave_shr:1 row_mask:0xf bank_mask:0xf bound_ctrl:1
	v_add_f32_dpp v91, v73, v73 wave_shr:1 row_mask:0xf bank_mask:0xf bound_ctrl:1
	v_add_f32_dpp v74, v20, v74 wave_shl:1 row_mask:0xf bank_mask:0xf bound_ctrl:1
	v_add_f32_dpp v75, v21, v75 wave_shl:1 row_mask:0xf bank_mask:0xf bound_ctrl:1
	v_add_f32_dpp v76, v52, v76 wave_shl:1 row_mask:0xf bank_mask:0xf bound_ctrl:1
	v_add_f32_dpp v77, v53, v77 wave_shl:1 row_mask:0xf bank_mask:0xf bound_ctrl:1
	v_add_f32_dpp v78, v70, v78 wave_shl:1 row_mask:0xf bank_mask:0xf bound_ctrl:1
	v_add_f32_dpp v79, v71, v79 wave_shl:1 row_mask:0xf bank_mask:0xf bound_ctrl:1
	v_add_f32_dpp v90, v72, v90 wave_shl:1 row_mask:0xf bank_mask:0xf bound_ctrl:1
	v_add_f32_dpp v91, v73, v91 wave_shl:1 row_mask:0xf bank_mask:0xf bound_ctrl:1
	v_pk_add_f32 v[52:53], v[80:81], v[74:75]
	v_pk_add_f32 v[70:71], v[54:55], v[52:53]
	v_pk_add_f32 v[54:55], v[82:83], v[76:77]
	v_pk_add_f32 v[72:73], v[56:57], v[54:55]
	v_pk_add_f32 v[56:57], v[84:85], v[78:79]
	v_pk_add_f32 v[80:81], v[58:59], v[56:57]
	v_pk_add_f32 v[58:59], v[86:87], v[90:91]
	v_pk_add_f32 v[82:83], v[60:61], v[58:59]
	v_pk_fma_f32 v[72:73], v[104:105], v[70:71], v[72:73] op_sel_hi:[0,1,1] neg_lo:[1,0,0] neg_hi:[1,0,0]
	v_pk_fma_f32 v[80:81], v[104:105], v[70:71], v[80:81] op_sel:[1,0,0] neg_lo:[1,0,0] neg_hi:[1,0,0]
	v_pk_fma_f32 v[82:83], v[106:107], v[70:71], v[82:83] op_sel_hi:[0,1,1] neg_lo:[1,0,0] neg_hi:[1,0,0]
	v_pk_mul_f32 v[60:61], v[106:107], v[72:73] op_sel:[1,0]
	v_pk_mul_f32 v[84:85], v[108:109], v[72:73] op_sel_hi:[0,1]
	v_pk_mul_f32 v[86:87], v[108:109], v[72:73] op_sel:[1,0]
	v_pk_fma_f32 v[60:61], v[108:109], v[80:81], v[60:61] op_sel_hi:[0,1,1]
	v_pk_fma_f32 v[84:85], v[110:111], v[80:81], v[84:85] op_sel_hi:[0,1,1]
	v_pk_fma_f32 v[86:87], v[110:111], v[80:81], v[86:87] op_sel:[1,0,0]
	v_pk_fma_f32 v[60:61], v[108:109], v[82:83], v[60:61] op_sel:[1,0,0]
	v_pk_fma_f32 v[84:85], v[110:111], v[82:83], v[84:85] op_sel:[1,0,0]
	v_pk_fma_f32 v[86:87], v[112:113], v[82:83], v[86:87] op_sel_hi:[0,1,1]
	v_pk_mul_f32 v[92:93], v[104:105], v[60:61] op_sel_hi:[0,1]
	v_pk_fma_f32 v[92:93], v[104:105], v[84:85], v[92:93] op_sel:[1,0,0]
	v_pk_fma_f32 v[92:93], v[106:107], v[86:87], v[92:93] op_sel_hi:[0,1,1]
	v_pk_fma_f32 v[92:93], v[112:113], v[70:71], v[92:93] op_sel:[1,0,0] neg_lo:[0,0,1] neg_hi:[0,0,1]
	v_add_f32_dpp v70, v60, v60 wave_shr:1 row_mask:0xf bank_mask:0xf bound_ctrl:1
	v_add_f32_dpp v71, v61, v61 wave_shr:1 row_mask:0xf bank_mask:0xf bound_ctrl:1
	v_add_f32_dpp v72, v84, v84 wave_shr:1 row_mask:0xf bank_mask:0xf bound_ctrl:1
	v_add_f32_dpp v73, v85, v85 wave_shr:1 row_mask:0xf bank_mask:0xf bound_ctrl:1
	v_add_f32_dpp v80, v86, v86 wave_shr:1 row_mask:0xf bank_mask:0xf bound_ctrl:1
	v_add_f32_dpp v81, v87, v87 wave_shr:1 row_mask:0xf bank_mask:0xf bound_ctrl:1
	v_add_f32_dpp v82, v92, v92 wave_shr:1 row_mask:0xf bank_mask:0xf bound_ctrl:1
	v_add_f32_dpp v83, v93, v93 wave_shr:1 row_mask:0xf bank_mask:0xf bound_ctrl:1
	v_add_f32_dpp v70, v60, v70 wave_shl:1 row_mask:0xf bank_mask:0xf bound_ctrl:1
	v_add_f32_dpp v71, v61, v71 wave_shl:1 row_mask:0xf bank_mask:0xf bound_ctrl:1
	v_add_f32_dpp v72, v84, v72 wave_shl:1 row_mask:0xf bank_mask:0xf bound_ctrl:1
	v_add_f32_dpp v73, v85, v73 wave_shl:1 row_mask:0xf bank_mask:0xf bound_ctrl:1
	v_add_f32_dpp v80, v86, v80 wave_shl:1 row_mask:0xf bank_mask:0xf bound_ctrl:1
	v_add_f32_dpp v81, v87, v81 wave_shl:1 row_mask:0xf bank_mask:0xf bound_ctrl:1
	v_add_f32_dpp v82, v92, v82 wave_shl:1 row_mask:0xf bank_mask:0xf bound_ctrl:1
	v_add_f32_dpp v83, v93, v83 wave_shl:1 row_mask:0xf bank_mask:0xf bound_ctrl:1
	s_add_i32 s5, s34, 3
	s_min_i32 s5, s5, 0x200
	s_mul_i32 s6, s5, 0x804
	s_add_i32 s6, s6, s39
	s_add_i32 s7, s6, 0x101004
	s_mul_i32 s9, s5, 0x180c
	s_add_i32 s9, s9, s33
	s_add_i32 s4, s34, 4
	s_min_i32 s4, s4, 0x200
	s_mul_i32 s4, s4, 0x804
	s_add_i32 s4, s4, s38
	buffer_load_dword v2, v28, s[20:23], s4 offen nt
	buffer_load_dwordx3 v[8:10], v27, s[24:27], s9 offen nt
	buffer_load_dword v4, v28, s[16:19], s6 offen nt
	buffer_load_dword v5, v28, s[16:19], s7 offen nt
	s_waitcnt vmcnt(8)
	s_add_i32 s4, s34, 2
	s_cmpk_lt_u32 s4, 0x201
	s_cselect_b64 s[12:13], s[40:41], 0
	v_cmp_eq_u32_e64 s[14:15], s37, v24
	s_and_b64 s[14:15], s[14:15], s[12:13]
	v_cndmask_b32_e64 v25, 0, 1, s[14:15]
	v_mul_f32_e64 v60, v40, v40
	v_mul_f32_e64 v61, v40, v41
	v_mul_f32_e64 v84, v40, v42
	v_mul_f32_e64 v85, v41, v41
	v_mul_f32_e64 v86, v41, v42
	v_mul_f32_e64 v87, v42, v42
	v_or_b32_dpp v29, v25, v25 wave_shr:1 row_mask:0xf bank_mask:0xf bound_ctrl:1
	s_nop 1
	v_or_b32_dpp v29, v25, v29 wave_shl:1 row_mask:0xf bank_mask:0xf bound_ctrl:1
	s_nop 1
	v_or_b32_dpp v45, v29, v29 wave_shr:1 row_mask:0xf bank_mask:0xf bound_ctrl:1
	s_nop 1
	v_or_b32_dpp v45, v29, v45 wave_shl:1 row_mask:0xf bank_mask:0xf bound_ctrl:1
	v_or3_b32 v25, v45, v68, v69
	v_or3_b32 v25, v25, v44, v30
	s_add_i32 s4, s34, -1
	s_cmpk_lt_u32 s4, 0x1ff
	s_cselect_b64 s[12:13], s[42:43], 0
	v_cmp_ne_u32_e64 s[30:31], 0, v25
	s_and_b64 s[30:31], s[30:31], s[12:13]
	v_cndmask_b32_e64 v25, 0, 1.0, s[30:31]
	v_add_f32_dpp v92, v40, v40 wave_shr:1 row_mask:0xf bank_mask:0xf bound_ctrl:1
	v_add_f32_dpp v93, v41, v41 wave_shr:1 row_mask:0xf bank_mask:0xf bound_ctrl:1
	v_add_f32_dpp v104, v42, v42 wave_shr:1 row_mask:0xf bank_mask:0xf bound_ctrl:1
	v_add_f32_dpp v105, v60, v60 wave_shr:1 row_mask:0xf bank_mask:0xf bound_ctrl:1
	v_add_f32_dpp v106, v61, v61 wave_shr:1 row_mask:0xf bank_mask:0xf bound_ctrl:1
	v_add_f32_dpp v107, v84, v84 wave_shr:1 row_mask:0xf bank_mask:0xf bound_ctrl:1
	v_add_f32_dpp v108, v85, v85 wave_shr:1 row_mask:0xf bank_mask:0xf bound_ctrl:1
	v_add_f32_dpp v109, v86, v86 wave_shr:1 row_mask:0xf bank_mask:0xf bound_ctrl:1
	v_add_f32_dpp v110, v87, v87 wave_shr:1 row_mask:0xf bank_mask:0xf bound_ctrl:1
	v_add_f32_dpp v111, v25, v25 wave_shr:1 row_mask:0xf bank_mask:0xf bound_ctrl:1
	v_add_f32_dpp v92, v40, v92 wave_shl:1 row_mask:0xf bank_mask:0xf bound_ctrl:1
	v_add_f32_dpp v93, v41, v93 wave_shl:1 row_mask:0xf bank_mask:0xf bound_ctrl:1
	v_add_f32_dpp v104, v42, v104 wave_shl:1 row_mask:0xf bank_mask:0xf bound_ctrl:1
	v_add_f32_dpp v105, v60, v105 wave_shl:1 row_mask:0xf bank_mask:0xf bound_ctrl:1
	v_add_f32_dpp v106, v61, v106 wave_shl:1 row_mask:0xf bank_mask:0xf bound_ctrl:1
	v_add_f32_dpp v107, v84, v107 wave_shl:1 row_mask:0xf bank_mask:0xf bound_ctrl:1
	v_add_f32_dpp v108, v85, v108 wave_shl:1 row_mask:0xf bank_mask:0xf bound_ctrl:1
	v_add_f32_dpp v109, v86, v109 wave_shl:1 row_mask:0xf bank_mask:0xf bound_ctrl:1
	v_add_f32_dpp v110, v87, v110 wave_shl:1 row_mask:0xf bank_mask:0xf bound_ctrl:1
	v_add_f32_dpp v111, v25, v111 wave_shl:1 row_mask:0xf bank_mask:0xf bound_ctrl:1
	v_pk_add_f32 v[60:61], v[88:89], v[92:93]
	v_pk_add_f32 v[84:85], v[36:37], v[104:105]
	v_pk_add_f32 v[36:37], v[46:47], v[106:107]
	v_pk_add_f32 v[46:47], v[48:49], v[108:109]
	v_pk_add_f32 v[48:49], v[50:51], v[110:111]
	v_mul_f32_e64 v112, v60, v22
	v_mul_f32_e64 v113, v61, v22
	v_mul_f32_e64 v114, v84, v22
	v_fma_f32 v25, v85, v22, v26
	v_mul_f32_e64 v29, v36, v22
	v_mul_f32_e64 v50, v37, v22
	v_fma_f32 v51, v46, v22, v26
	v_mul_f32_e64 v86, v47, v22
	v_fma_f32 v87, v48, v22, v26
	v_fma_f32 v25, -v112, v112, v25
	v_fma_f32 v29, -v112, v113, v29
	v_fma_f32 v50, -v112, v114, v50
	v_fma_f32 v51, -v113, v113, v51
	v_fma_f32 v86, -v113, v114, v86
	v_fma_f32 v87, -v114, v114, v87
	v_mul_f32_e64 v88, v86, v86
	v_mul_f32_e64 v89, v29, v87
	v_mul_f32_e64 v124, v50, v51
	v_mul_f32_e64 v125, v50, v50
	v_mul_f32_e64 v126, v25, v86
	v_mul_f32_e64 v127, v29, v29
	v_fma_f32 v88, v51, v87, -v88
	v_fma_f32 v89, v50, v86, -v89
	v_fma_f32 v124, v29, v86, -v124
	v_fma_f32 v125, v25, v87, -v125
	v_fma_f32 v126, v29, v50, -v126
	v_fma_f32 v127, v25, v51, -v127
	v_mul_f32_e64 v128, v25, v88
	v_fma_f32 v128, v29, v89, v128
	v_fma_f32 v128, v50, v124, v128
	v_rcp_f32_e32 v128, v128
	v_cmp_ne_u32_e64 vcc, s37, v3
	v_mul_f32_e64 v128, v128, v22
	v_cndmask_b32_e64 v128, 0, v128, s[30:31]
	v_cndmask_b32_e64 v25, 0, v18, vcc
	v_cndmask_b32_e64 v121, 0, v22, s[30:31]
	v_mul_f32_e64 v115, v88, v128
	v_mul_f32_e64 v116, v89, v128
	v_mul_f32_e64 v117, v124, v128
	v_mul_f32_e64 v118, v125, v128
	v_mul_f32_e64 v119, v126, v128
	v_mul_f32_e64 v120, v127, v128
	v_add_f32_e64 v122, v49, v25
	v_mov_b32_e32 v123, v3
	ds_write_b128 v23, v[112:115] offset:3072
	ds_write_b128 v23, v[116:119] offset:4096
	ds_write_b128 v23, v[120:123] offset:5120
	s_waitcnt lgkmcnt(0)
	s_barrier
	v_pk_mul_f32 v[36:37], v[38:39], v[40:41] op_sel_hi:[1,0]
	v_pk_mul_f32 v[46:47], v[38:39], v[40:41] op_sel:[0,1]
	v_pk_mul_f32 v[48:49], v[38:39], v[42:43] op_sel_hi:[1,0]
	v_add_f32_dpp v50, v38, v38 wave_shr:1 row_mask:0xf bank_mask:0xf bound_ctrl:1
	v_add_f32_dpp v51, v39, v39 wave_shr:1 row_mask:0xf bank_mask:0xf bound_ctrl:1
	v_add_f32_dpp v60, v36, v36 wave_shr:1 row_mask:0xf bank_mask:0xf bound_ctrl:1
	v_add_f32_dpp v61, v37, v37 wave_shr:1 row_mask:0xf bank_mask:0xf bound_ctrl:1
	v_add_f32_dpp v84, v46, v46 wave_shr:1 row_mask:0xf bank_mask:0xf bound_ctrl:1
	v_add_f32_dpp v85, v47, v47 wave_shr:1 row_mask:0xf bank_mask:0xf bound_ctrl:1
	v_add_f32_dpp v86, v48, v48 wave_shr:1 row_mask:0xf bank_mask:0xf bound_ctrl:1
	v_add_f32_dpp v87, v49, v49 wave_shr:1 row_mask:0xf bank_mask:0xf bound_ctrl:1
	v_add_f32_dpp v50, v38, v50 wave_shl:1 row_mask:0xf bank_mask:0xf bound_ctrl:1
	v_add_f32_dpp v51, v39, v51 wave_shl:1 row_mask:0xf bank_mask:0xf bound_ctrl:1
	v_add_f32_dpp v60, v36, v60 wave_shl:1 row_mask:0xf bank_mask:0xf bound_ctrl:1
	v_add_f32_dpp v61, v37, v61 wave_shl:1 row_mask:0xf bank_mask:0xf bound_ctrl:1
	v_add_f32_dpp v84, v46, v84 wave_shl:1 row_mask:0xf bank_mask:0xf bound_ctrl:1
	v_add_f32_dpp v85, v47, v85 wave_shl:1 row_mask:0xf bank_mask:0xf bound_ctrl:1
	v_add_f32_dpp v86, v48, v86 wave_shl:1 row_mask:0xf bank_mask:0xf bound_ctrl:1
	v_add_f32_dpp v87, v49, v87 wave_shl:1 row_mask:0xf bank_mask:0xf bound_ctrl:1
	v_pk_add_f32 v[36:37], v[52:53], v[50:51]
	v_pk_add_f32 v[46:47], v[54:55], v[60:61]
	v_pk_add_f32 v[48:49], v[56:57], v[84:85]
	v_pk_add_f32 v[52:53], v[58:59], v[86:87]
	v_pk_fma_f32 v[46:47], v[112:113], v[36:37], v[46:47] op_sel_hi:[0,1,1] neg_lo:[1,0,0] neg_hi:[1,0,0]
	v_pk_fma_f32 v[48:49], v[112:113], v[36:37], v[48:49] op_sel:[1,0,0] neg_lo:[1,0,0] neg_hi:[1,0,0]
	v_pk_fma_f32 v[52:53], v[114:115], v[36:37], v[52:53] op_sel_hi:[0,1,1] neg_lo:[1,0,0] neg_hi:[1,0,0]
	v_pk_mul_f32 v[54:55], v[114:115], v[46:47] op_sel:[1,0]
	v_pk_mul_f32 v[56:57], v[116:117], v[46:47] op_sel_hi:[0,1]
	v_pk_mul_f32 v[58:59], v[116:117], v[46:47] op_sel:[1,0]
	v_pk_fma_f32 v[54:55], v[116:117], v[48:49], v[54:55] op_sel_hi:[0,1,1]
	v_pk_fma_f32 v[56:57], v[118:119], v[48:49], v[56:57] op_sel_hi:[0,1,1]
	v_pk_fma_f32 v[58:59], v[118:119], v[48:49], v[58:59] op_sel:[1,0,0]
	v_pk_fma_f32 v[54:55], v[116:117], v[52:53], v[54:55] op_sel:[1,0,0]
	v_pk_fma_f32 v[56:57], v[118:119], v[52:53], v[56:57] op_sel:[1,0,0]
	v_pk_fma_f32 v[58:59], v[120:121], v[52:53], v[58:59] op_sel_hi:[0,1,1]
	v_pk_mul_f32 v[88:89], v[112:113], v[54:55] op_sel_hi:[0,1]
	v_pk_fma_f32 v[88:89], v[112:113], v[56:57], v[88:89] op_sel:[1,0,0]
	v_pk_fma_f32 v[88:89], v[114:115], v[58:59], v[88:89] op_sel_hi:[0,1,1]
	v_pk_fma_f32 v[88:89], v[120:121], v[36:37], v[88:89] op_sel:[1,0,0] neg_lo:[0,0,1] neg_hi:[0,0,1]
	v_add_f32_dpp v36, v54, v54 wave_shr:1 row_mask:0xf bank_mask:0xf bound_ctrl:1
	v_add_f32_dpp v37, v55, v55 wave_shr:1 row_mask:0xf bank_mask:0xf bound_ctrl:1
	v_add_f32_dpp v46, v56, v56 wave_shr:1 row_mask:0xf bank_mask:0xf bound_ctrl:1
	v_add_f32_dpp v47, v57, v57 wave_shr:1 row_mask:0xf bank_mask:0xf bound_ctrl:1
	v_add_f32_dpp v48, v58, v58 wave_shr:1 row_mask:0xf bank_mask:0xf bound_ctrl:1
	v_add_f32_dpp v49, v59, v59 wave_shr:1 row_mask:0xf bank_mask:0xf bound_ctrl:1
	v_add_f32_dpp v52, v88, v88 wave_shr:1 row_mask:0xf bank_mask:0xf bound_ctrl:1
	v_add_f32_dpp v53, v89, v89 wave_shr:1 row_mask:0xf bank_mask:0xf bound_ctrl:1
	v_add_f32_dpp v36, v54, v36 wave_shl:1 row_mask:0xf bank_mask:0xf bound_ctrl:1
	v_add_f32_dpp v37, v55, v37 wave_shl:1 row_mask:0xf bank_mask:0xf bound_ctrl:1
	v_add_f32_dpp v46, v56, v46 wave_shl:1 row_mask:0xf bank_mask:0xf bound_ctrl:1
	v_add_f32_dpp v47, v57, v47 wave_shl:1 row_mask:0xf bank_mask:0xf bound_ctrl:1
	v_add_f32_dpp v48, v58, v48 wave_shl:1 row_mask:0xf bank_mask:0xf bound_ctrl:1
	v_add_f32_dpp v49, v59, v49 wave_shl:1 row_mask:0xf bank_mask:0xf bound_ctrl:1
	v_add_f32_dpp v52, v88, v52 wave_shl:1 row_mask:0xf bank_mask:0xf bound_ctrl:1
	v_add_f32_dpp v53, v89, v53 wave_shl:1 row_mask:0xf bank_mask:0xf bound_ctrl:1
	s_add_i32 s5, s34, 4
	s_min_i32 s5, s5, 0x200
	s_mul_i32 s6, s5, 0x804
	s_add_i32 s6, s6, s39
	s_add_i32 s7, s6, 0x101004
	s_mul_i32 s9, s5, 0x180c
	s_add_i32 s9, s9, s33
	s_add_i32 s4, s34, 5
	s_min_i32 s4, s4, 0x200
	s_mul_i32 s4, s4, 0x804
	s_add_i32 s4, s4, s38
	buffer_load_dword v3, v28, s[20:23], s4 offen nt
	buffer_load_dwordx3 v[12:14], v27, s[24:27], s9 offen nt
	buffer_load_dword v6, v28, s[16:19], s6 offen nt
	buffer_load_dword v7, v28, s[16:19], s7 offen nt
	s_waitcnt vmcnt(8)
	s_add_i32 s4, s34, 3
	s_cmpk_lt_u32 s4, 0x201
	s_cselect_b64 s[12:13], s[40:41], 0
	v_cmp_eq_u32_e64 s[14:15], s37, v17
	s_and_b64 s[14:15], s[14:15], s[12:13]
	v_cndmask_b32_e64 v25, 0, 1, s[14:15]
	v_mul_f32_e64 v54, v64, v64
	v_mul_f32_e64 v55, v64, v65
	v_mul_f32_e64 v56, v64, v66
	v_mul_f32_e64 v57, v65, v65
	v_mul_f32_e64 v58, v65, v66
	v_mul_f32_e64 v59, v66, v66
	v_or_b32_dpp v29, v25, v25 wave_shr:1 row_mask:0xf bank_mask:0xf bound_ctrl:1
	s_nop 1
	v_or_b32_dpp v29, v25, v29 wave_shl:1 row_mask:0xf bank_mask:0xf bound_ctrl:1
	s_nop 1
	v_or_b32_dpp v30, v29, v29 wave_shr:1 row_mask:0xf bank_mask:0xf bound_ctrl:1
	s_nop 1
	v_or_b32_dpp v30, v29, v30 wave_shl:1 row_mask:0xf bank_mask:0xf bound_ctrl:1
	v_or3_b32 v25, v30, v45, v68
	v_or3_b32 v25, v25, v69, v44
	s_add_i32 s4, s34, 0
	s_cmpk_lt_u32 s4, 0x1ff
	s_cselect_b64 s[12:13], s[42:43], 0
	v_cmp_ne_u32_e64 s[30:31], 0, v25
	s_and_b64 s[30:31], s[30:31], s[12:13]
	v_cndmask_b32_e64 v25, 0, 1.0, s[30:31]
	v_add_f32_dpp v88, v64, v64 wave_shr:1 row_mask:0xf bank_mask:0xf bound_ctrl:1
	v_add_f32_dpp v89, v65, v65 wave_shr:1 row_mask:0xf bank_mask:0xf bound_ctrl:1
	v_add_f32_dpp v112, v66, v66 wave_shr:1 row_mask:0xf bank_mask:0xf bound_ctrl:1
	v_add_f32_dpp v113, v54, v54 wave_shr:1 row_mask:0xf bank_mask:0xf bound_ctrl:1
	v_add_f32_dpp v114, v55, v55 wave_shr:1 row_mask:0xf bank_mask:0xf bound_ctrl:1
	v_add_f32_dpp v115, v56, v56 wave_shr:1 row_mask:0xf bank_mask:0xf bound_ctrl:1
	v_add_f32_dpp v116, v57, v57 wave_shr:1 row_mask:0xf bank_mask:0xf bound_ctrl:1
	v_add_f32_dpp v117, v58, v58 wave_shr:1 row_mask:0xf bank_mask:0xf bound_ctrl:1
	v_add_f32_dpp v118, v59, v59 wave_shr:1 row_mask:0xf bank_mask:0xf bound_ctrl:1
	v_add_f32_dpp v119, v25, v25 wave_shr:1 row_mask:0xf bank_mask:0xf bound_ctrl:1
	v_add_f32_dpp v88, v64, v88 wave_shl:1 row_mask:0xf bank_mask:0xf bound_ctrl:1
	v_add_f32_dpp v89, v65, v89 wave_shl:1 row_mask:0xf bank_mask:0xf bound_ctrl:1
	v_add_f32_dpp v112, v66, v112 wave_shl:1 row_mask:0xf bank_mask:0xf bound_ctrl:1
	v_add_f32_dpp v113, v54, v113 wave_shl:1 row_mask:0xf bank_mask:0xf bound_ctrl:1
	v_add_f32_dpp v114, v55, v114 wave_shl:1 row_mask:0xf bank_mask:0xf bound_ctrl:1
	v_add_f32_dpp v115, v56, v115 wave_shl:1 row_mask:0xf bank_mask:0xf bound_ctrl:1
	v_add_f32_dpp v116, v57, v116 wave_shl:1 row_mask:0xf bank_mask:0xf bound_ctrl:1
	v_add_f32_dpp v117, v58, v117 wave_shl:1 row_mask:0xf bank_mask:0xf bound_ctrl:1
	v_add_f32_dpp v118, v59, v118 wave_shl:1 row_mask:0xf bank_mask:0xf bound_ctrl:1
	v_add_f32_dpp v119, v25, v119 wave_shl:1 row_mask:0xf bank_mask:0xf bound_ctrl:1
	v_pk_add_f32 v[54:55], v[92:93], v[88:89]
	v_pk_add_f32 v[56:57], v[94:95], v[54:55]
	v_pk_add_f32 v[58:59], v[104:105], v[112:113]
	v_pk_add_f32 v[92:93], v[96:97], v[58:59]
	v_pk_add_f32 v[94:95], v[106:107], v[114:115]
	v_pk_add_f32 v[96:97], v[98:99], v[94:95]
	v_pk_add_f32 v[98:99], v[108:109], v[116:117]
	v_pk_add_f32 v[104:105], v[100:101], v[98:99]
	v_pk_add_f32 v[100:101], v[110:111], v[118:119]
	v_pk_add_f32 v[106:107], v[102:103], v[100:101]
	v_mul_f32_e64 v108, v56, v22
	v_mul_f32_e64 v109, v57, v22
	v_mul_f32_e64 v110, v92, v22
	v_fma_f32 v25, v93, v22, v26
	v_mul_f32_e64 v29, v96, v22
	v_mul_f32_e64 v102, v97, v22
	v_fma_f32 v103, v104, v22, v26
	v_mul_f32_e64 v128, v105, v22
	v_fma_f32 v129, v106, v22, v26
	v_fma_f32 v25, -v108, v108, v25
	v_fma_f32 v29, -v108, v109, v29
	v_fma_f32 v102, -v108, v110, v102
	v_fma_f32 v103, -v109, v109, v103
	v_fma_f32 v128, -v109, v110, v128
	v_fma_f32 v129, -v110, v110, v129
	v_mul_f32_e64 v130, v128, v128
	v_mul_f32_e64 v131, v29, v129
	v_mul_f32_e64 v132, v102, v103
	v_mul_f32_e64 v133, v102, v102
	v_mul_f32_e64 v134, v25, v128
	v_mul_f32_e64 v135, v29, v29
	v_fma_f32 v130, v103, v129, -v130
	v_fma_f32 v131, v102, v128, -v131
	v_fma_f32 v132, v29, v128, -v132
	v_fma_f32 v133, v25, v129, -v133
	v_fma_f32 v134, v29, v102, -v134
	v_fma_f32 v135, v25, v103, -v135
	v_mul_f32_e64 v136, v25, v130
	v_fma_f32 v136, v29, v131, v136
	v_fma_f32 v136, v102, v132, v136
	v_rcp_f32_e32 v136, v136
	v_cmp_ne_u32_e64 vcc, s37, v16
	v_mul_f32_e64 v136, v136, v22
	v_cndmask_b32_e64 v136, 0, v136, s[30:31]
	v_cndmask_b32_e64 v25, 0, v18, vcc
	v_cndmask_b32_e64 v125, 0, v22, s[30:31]
	v_mul_f32_e64 v111, v130, v136
	v_mul_f32_e64 v120, v131, v136
	v_mul_f32_e64 v121, v132, v136
	v_mul_f32_e64 v122, v133, v136
	v_mul_f32_e64 v123, v134, v136
	v_mul_f32_e64 v124, v135, v136
	v_add_f32_e64 v126, v107, v25
	v_mov_b32_e32 v127, v16
	ds_write_b128 v23, v[108:111]
	ds_write_b128 v23, v[120:123] offset:1024
	ds_write_b128 v23, v[124:127] offset:2048
	s_waitcnt lgkmcnt(0)
	s_barrier
	v_pk_mul_f32 v[56:57], v[62:63], v[64:65] op_sel_hi:[1,0]
	v_pk_mul_f32 v[92:93], v[62:63], v[64:65] op_sel:[0,1]
	v_pk_mul_f32 v[96:97], v[62:63], v[66:67] op_sel_hi:[1,0]
	v_add_f32_dpp v102, v62, v62 wave_shr:1 row_mask:0xf bank_mask:0xf bound_ctrl:1
	v_add_f32_dpp v103, v63, v63 wave_shr:1 row_mask:0xf bank_mask:0xf bound_ctrl:1
	v_add_f32_dpp v104, v56, v56 wave_shr:1 row_mask:0xf bank_mask:0xf bound_ctrl:1
	v_add_f32_dpp v105, v57, v57 wave_shr:1 row_mask:0xf bank_mask:0xf bound_ctrl:1
	v_add_f32_dpp v106, v92, v92 wave_shr:1 row_mask:0xf bank_mask:0xf bound_ctrl:1
	v_add_f32_dpp v107, v93, v93 wave_shr:1 row_mask:0xf bank_mask:0xf bound_ctrl:1
	v_add_f32_dpp v128, v96, v96 wave_shr:1 row_mask:0xf bank_mask:0xf bound_ctrl:1
	v_add_f32_dpp v129, v97, v97 wave_shr:1 row_mask:0xf bank_mask:0xf bound_ctrl:1
	v_add_f32_dpp v102, v62, v102 wave_shl:1 row_mask:0xf bank_mask:0xf bound_ctrl:1
	v_add_f32_dpp v103, v63, v103 wave_shl:1 row_mask:0xf bank_mask:0xf bound_ctrl:1
	v_add_f32_dpp v104, v56, v104 wave_shl:1 row_mask:0xf bank_mask:0xf bound_ctrl:1
	v_add_f32_dpp v105, v57, v105 wave_shl:1 row_mask:0xf bank_mask:0xf bound_ctrl:1
	v_add_f32_dpp v106, v92, v106 wave_shl:1 row_mask:0xf bank_mask:0xf bound_ctrl:1
	v_add_f32_dpp v107, v93, v107 wave_shl:1 row_mask:0xf bank_mask:0xf bound_ctrl:1
	v_add_f32_dpp v128, v96, v128 wave_shl:1 row_mask:0xf bank_mask:0xf bound_ctrl:1
	v_add_f32_dpp v129, v97, v129 wave_shl:1 row_mask:0xf bank_mask:0xf bound_ctrl:1
	v_pk_add_f32 v[56:57], v[50:51], v[102:103]
	v_pk_add_f32 v[92:93], v[74:75], v[56:57]
	v_pk_add_f32 v[50:51], v[60:61], v[104:105]
	v_pk_add_f32 v[74:75], v[76:77], v[50:51]
	v_pk_add_f32 v[60:61], v[84:85], v[106:107]
	v_pk_add_f32 v[76:77], v[78:79], v[60:61]
	v_pk_add_f32 v[78:79], v[86:87], v[128:129]
	v_pk_add_f32 v[84:85], v[90:91], v[78:79]
	v_pk_fma_f32 v[74:75], v[108:109], v[92:93], v[74:75] op_sel_hi:[0,1,1] neg_lo:[1,0,0] neg_hi:[1,0,0]
	v_pk_fma_f32 v[76:77], v[108:109], v[92:93], v[76:77] op_sel:[1,0,0] neg_lo:[1,0,0] neg_hi:[1,0,0]
	v_pk_fma_f32 v[84:85], v[110:111], v[92:93], v[84:85] op_sel_hi:[0,1,1] neg_lo:[1,0,0] neg_hi:[1,0,0]
	v_pk_mul_f32 v[86:87], v[110:111], v[74:75] op_sel:[1,0]
	v_pk_mul_f32 v[90:91], v[120:121], v[74:75] op_sel_hi:[0,1]
	v_pk_mul_f32 v[96:97], v[120:121], v[74:75] op_sel:[1,0]
	v_pk_fma_f32 v[86:87], v[120:121], v[76:77], v[86:87] op_sel_hi:[0,1,1]
	v_pk_fma_f32 v[90:91], v[122:123], v[76:77], v[90:91] op_sel_hi:[0,1,1]
	v_pk_fma_f32 v[96:97], v[122:123], v[76:77], v[96:97] op_sel:[1,0,0]
	v_pk_fma_f32 v[86:87], v[120:121], v[84:85], v[86:87] op_sel:[1,0,0]
	v_pk_fma_f32 v[90:91], v[122:123], v[84:85], v[90:91] op_sel:[1,0,0]
	v_pk_fma_f32 v[96:97], v[124:125], v[84:85], v[96:97] op_sel_hi:[0,1,1]
	v_pk_mul_f32 v[130:131], v[108:109], v[86:87] op_sel_hi:[0,1]
	v_pk_fma_f32 v[130:131], v[108:109], v[90:91], v[130:131] op_sel:[1,0,0]
	v_pk_fma_f32 v[130:131], v[110:111], v[96:97], v[130:131] op_sel_hi:[0,1,1]
	v_pk_fma_f32 v[130:131], v[124:125], v[92:93], v[130:131] op_sel:[1,0,0] neg_lo:[0,0,1] neg_hi:[0,0,1]
	v_cmp_eq_u32_e64 s[10:11], 6, v127
	v_cmp_eq_u32_e64 s[14:15], 7, v127
	v_add_f32_dpp v74, v86, v86 wave_shr:1 row_mask:0xf bank_mask:0xf bound_ctrl:1
	v_add_f32_dpp v75, v87, v87 wave_shr:1 row_mask:0xf bank_mask:0xf bound_ctrl:1
	v_add_f32_dpp v76, v90, v90 wave_shr:1 row_mask:0xf bank_mask:0xf bound_ctrl:1
	v_add_f32_dpp v77, v91, v91 wave_shr:1 row_mask:0xf bank_mask:0xf bound_ctrl:1
	v_add_f32_dpp v84, v96, v96 wave_shr:1 row_mask:0xf bank_mask:0xf bound_ctrl:1
	v_add_f32_dpp v85, v97, v97 wave_shr:1 row_mask:0xf bank_mask:0xf bound_ctrl:1
	v_add_f32_dpp v92, v130, v130 wave_shr:1 row_mask:0xf bank_mask:0xf bound_ctrl:1
	v_add_f32_dpp v93, v131, v131 wave_shr:1 row_mask:0xf bank_mask:0xf bound_ctrl:1
	v_add_f32_dpp v74, v86, v74 wave_shl:1 row_mask:0xf bank_mask:0xf bound_ctrl:1
	v_add_f32_dpp v75, v87, v75 wave_shl:1 row_mask:0xf bank_mask:0xf bound_ctrl:1
	v_add_f32_dpp v76, v90, v76 wave_shl:1 row_mask:0xf bank_mask:0xf bound_ctrl:1
	v_add_f32_dpp v77, v91, v77 wave_shl:1 row_mask:0xf bank_mask:0xf bound_ctrl:1
	v_add_f32_dpp v84, v96, v84 wave_shl:1 row_mask:0xf bank_mask:0xf bound_ctrl:1
	v_add_f32_dpp v85, v97, v85 wave_shl:1 row_mask:0xf bank_mask:0xf bound_ctrl:1
	v_add_f32_dpp v92, v130, v92 wave_shl:1 row_mask:0xf bank_mask:0xf bound_ctrl:1
	v_add_f32_dpp v93, v131, v93 wave_shl:1 row_mask:0xf bank_mask:0xf bound_ctrl:1
	v_pk_add_f32 v[86:87], v[36:37], v[74:75]
	v_pk_add_f32 v[90:91], v[70:71], v[86:87]
	v_pk_add_f32 v[36:37], v[46:47], v[76:77]
	v_pk_add_f32 v[70:71], v[72:73], v[36:37]
	v_pk_add_f32 v[46:47], v[48:49], v[84:85]
	v_pk_add_f32 v[72:73], v[80:81], v[46:47]
	v_pk_add_f32 v[48:49], v[52:53], v[92:93]
	v_pk_add_f32 v[80:81], v[82:83], v[48:49]
	v_pk_fma_f32 v[80:81], v[32:33], v[90:91], v[80:81] op_sel_hi:[0,1,1]
	v_pk_fma_f32 v[80:81], v[32:33], v[70:71], v[80:81] op_sel:[1,0,0]
	v_pk_fma_f32 v[80:81], v[34:35], v[72:73], v[80:81] op_sel_hi:[0,1,1]
	v_cndmask_b32_e64 v52, 0, v18, s[10:11]
	v_cndmask_b32_e64 v53, 0, v18, s[14:15]
	v_pk_fma_f32 v[80:81], v[20:21], v[126:127], v[80:81] op_sel_hi:[1,0,1] neg_lo:[0,0,1] neg_hi:[0,0,1]
	s_add_i32 s4, s34, 0
	s_cmpk_lt_i32 s4, 0x201
	s_cselect_b64 s[12:13], s[0:1], 0
	v_pk_add_f32 v[80:81], v[80:81], v[52:53] neg_lo:[0,1] neg_hi:[0,1]
	v_pk_mul_f32 v[82:83], v[80:81], v[80:81]
	v_add_f32_e32 v82, v82, v83
	v_cndmask_b32_e64 v83, 0, v82, s[12:13]
	v_add_f32_e32 v1, v1, v83
	s_add_i32 s5, s34, 5
	s_min_i32 s5, s5, 0x200
	s_mul_i32 s6, s5, 0x804
	s_add_i32 s6, s6, s39
	s_add_i32 s7, s6, 0x101004
	s_mul_i32 s9, s5, 0x180c
	s_add_i32 s9, s9, s33
	s_add_i32 s4, s34, 6
	s_min_i32 s4, s4, 0x200
	s_mul_i32 s4, s4, 0x804
	s_add_i32 s4, s4, s38
	buffer_load_dword v16, v28, s[20:23], s4 offen nt
	buffer_load_dwordx3 v[32:34], v27, s[24:27], s9 offen nt
	buffer_load_dword v20, v28, s[16:19], s6 offen nt
	buffer_load_dword v21, v28, s[16:19], s7 offen nt
	s_waitcnt vmcnt(8)
	s_add_i32 s4, s34, 4
	s_cmpk_lt_u32 s4, 0x201
	s_cselect_b64 s[12:13], s[40:41], 0
	v_cmp_eq_u32_e64 s[14:15], s37, v2
	s_and_b64 s[14:15], s[14:15], s[12:13]
	v_cndmask_b32_e64 v25, 0, 1, s[14:15]
	v_mul_f32_e64 v52, v8, v8
	v_mul_f32_e64 v53, v8, v9
	v_mul_f32_e64 v70, v8, v10
	v_mul_f32_e64 v71, v9, v9
	v_mul_f32_e64 v72, v9, v10
	v_mul_f32_e64 v73, v10, v10
	v_or_b32_dpp v29, v25, v25 wave_shr:1 row_mask:0xf bank_mask:0xf bound_ctrl:1
	s_nop 1
	v_or_b32_dpp v29, v25, v29 wave_shl:1 row_mask:0xf bank_mask:0xf bound_ctrl:1
	s_nop 1
	v_or_b32_dpp v44, v29, v29 wave_shr:1 row_mask:0xf bank_mask:0xf bound_ctrl:1
	s_nop 1
	v_or_b32_dpp v44, v29, v44 wave_shl:1 row_mask:0xf bank_mask:0xf bound_ctrl:1
	v_or3_b32 v25, v44, v30, v45
	v_or3_b32 v25, v25, v68, v69
	s_add_i32 s4, s34, 1
	s_cmpk_lt_u32 s4, 0x1ff
	s_cselect_b64 s[12:13], s[42:43], 0
	v_cmp_ne_u32_e64 s[30:31], 0, v25
	s_and_b64 s[30:31], s[30:31], s[12:13]
	v_cndmask_b32_e64 v25, 0, 1.0, s[30:31]
	v_add_f32_dpp v80, v8, v8 wave_shr:1 row_mask:0xf bank_mask:0xf bound_ctrl:1
	v_add_f32_dpp v81, v9, v9 wave_shr:1 row_mask:0xf bank_mask:0xf bound_ctrl:1
	v_add_f32_dpp v82, v10, v10 wave_shr:1 row_mask:0xf bank_mask:0xf bound_ctrl:1
	v_add_f32_dpp v83, v52, v52 wave_shr:1 row_mask:0xf bank_mask:0xf bound_ctrl:1
	v_add_f32_dpp v90, v53, v53 wave_shr:1 row_mask:0xf bank_mask:0xf bound_ctrl:1
	v_add_f32_dpp v91, v70, v70 wave_shr:1 row_mask:0xf bank_mask:0xf bound_ctrl:1
	v_add_f32_dpp v96, v71, v71 wave_shr:1 row_mask:0xf bank_mask:0xf bound_ctrl:1
	v_add_f32_dpp v97, v72, v72 wave_shr:1 row_mask:0xf bank_mask:0xf bound_ctrl:1
	v_add_f32_dpp v108, v73, v73 wave_shr:1 row_mask:0xf bank_mask:0xf bound_ctrl:1
	v_add_f32_dpp v109, v25, v25 wave_shr:1 row_mask:0xf bank_mask:0xf bound_ctrl:1
	v_add_f32_dpp v80, v8, v80 wave_shl:1 row_mask:0xf bank_mask:0xf bound_ctrl:1
	v_add_f32_dpp v81, v9, v81 wave_shl:1 row_mask:0xf bank_mask:0xf bound_ctrl:1
	v_add_f32_dpp v82, v10, v82 wave_shl:1 row_mask:0xf bank_mask:0xf bound_ctrl:1
	v_add_f32_dpp v83, v52, v83 wave_shl:1 row_mask:0xf bank_mask:0xf bound_ctrl:1
	v_add_f32_dpp v90, v53, v90 wave_shl:1 row_mask:0xf bank_mask:0xf bound_ctrl:1
	v_add_f32_dpp v91, v70, v91 wave_shl:1 row_mask:0xf bank_mask:0xf bound_ctrl:1
	v_add_f32_dpp v96, v71, v96 wave_shl:1 row_mask:0xf bank_mask:0xf bound_ctrl:1
	v_add_f32_dpp v97, v72, v97 wave_shl:1 row_mask:0xf bank_mask:0xf bound_ctrl:1
	v_add_f32_dpp v108, v73, v108 wave_shl:1 row_mask:0xf bank_mask:0xf bound_ctrl:1
	v_add_f32_dpp v109, v25, v109 wave_shl:1 row_mask:0xf bank_mask:0xf bound_ctrl:1
	v_pk_add_f32 v[52:53], v[54:55], v[80:81]
	v_pk_add_f32 v[54:55], v[58:59], v[82:83]
	v_pk_add_f32 v[58:59], v[94:95], v[90:91]
	v_pk_add_f32 v[70:71], v[98:99], v[96:97]
	v_pk_add_f32 v[72:73], v[100:101], v[108:109]
	v_mul_f32_e64 v120, v52, v22
	v_mul_f32_e64 v121, v53, v22
	v_mul_f32_e64 v122, v54, v22
	v_fma_f32 v25, v55, v22, v26
	v_mul_f32_e64 v29, v58, v22
	v_mul_f32_e64 v94, v59, v22
	v_fma_f32 v95, v70, v22, v26
	v_mul_f32_e64 v98, v71, v22
	v_fma_f32 v99, v72, v22, v26
	v_fma_f32 v25, -v120, v120, v25
	v_fma_f32 v29, -v120, v121, v29
	v_fma_f32 v94, -v120, v122, v94
	v_fma_f32 v95, -v121, v121, v95
	v_fma_f32 v98, -v121, v122, v98
	v_fma_f32 v99, -v122, v122, v99
	v_mul_f32_e64 v100, v98, v98
	v_mul_f32_e64 v101, v29, v99
	v_mul_f32_e64 v110, v94, v95
	v_mul_f32_e64 v111, v94, v94
	v_mul_f32_e64 v130, v25, v98
	v_mul_f32_e64 v131, v29, v29
	v_fma_f32 v100, v95, v99, -v100
	v_fma_f32 v101, v94, v98, -v101
	v_fma_f32 v110, v29, v98, -v110
	v_fma_f32 v111, v25, v99, -v111
	v_fma_f32 v130, v29, v94, -v130
	v_fma_f32 v131, v25, v95, -v131
	v_mul_f32_e64 v136, v25, v100
	v_fma_f32 v136, v29, v101, v136
	v_fma_f32 v136, v94, v110, v136
	v_rcp_f32_e32 v136, v136
	v_cmp_ne_u32_e64 vcc, s37, v31
	v_mul_f32_e64 v136, v136, v22
	v_cndmask_b32_e64 v136, 0, v136, s[30:31]
	v_cndmask_b32_e64 v25, 0, v18, vcc
	v_cndmask_b32_e64 v133, 0, v22, s[30:31]
	v_mul_f32_e64 v123, v100, v136
	v_mul_f32_e64 v124, v101, v136
	v_mul_f32_e64 v125, v110, v136
	v_mul_f32_e64 v126, v111, v136
	v_mul_f32_e64 v127, v130, v136
	v_mul_f32_e64 v132, v131, v136
	v_add_f32_e64 v134, v73, v25
	v_mov_b32_e32 v135, v31
	ds_write_b128 v23, v[120:123] offset:3072
	ds_write_b128 v23, v[124:127] offset:4096
	ds_write_b128 v23, v[132:135] offset:5120
	s_waitcnt lgkmcnt(0)
	s_barrier
	v_pk_mul_f32 v[52:53], v[4:5], v[8:9] op_sel_hi:[1,0]
	v_pk_mul_f32 v[54:55], v[4:5], v[8:9] op_sel:[0,1]
	v_pk_mul_f32 v[58:59], v[4:5], v[10:11] op_sel_hi:[1,0]
	v_add_f32_dpp v70, v4, v4 wave_shr:1 row_mask:0xf bank_mask:0xf bound_ctrl:1
	v_add_f32_dpp v71, v5, v5 wave_shr:1 row_mask:0xf bank_mask:0xf bound_ctrl:1
	v_add_f32_dpp v72, v52, v52 wave_shr:1 row_mask:0xf bank_mask:0xf bound_ctrl:1
	v_add_f32_dpp v73, v53, v53 wave_shr:1 row_mask:0xf bank_mask:0xf bound_ctrl:1
	v_add_f32_dpp v94, v54, v54 wave_shr:1 row_mask:0xf bank_mask:0xf bound_ctrl:1
	v_add_f32_dpp v95, v55, v55 wave_shr:1 row_mask:0xf bank_mask:0xf bound_ctrl:1
	v_add_f32_dpp v98, v58, v58 wave_shr:1 row_mask:0xf bank_mask:0xf bound_ctrl:1
	v_add_f32_dpp v99, v59, v59 wave_shr:1 row_mask:0xf bank_mask:0xf bound_ctrl:1
	v_add_f32_dpp v70, v4, v70 wave_shl:1 row_mask:0xf bank_mask:0xf bound_ctrl:1
	v_add_f32_dpp v71, v5, v71 wave_shl:1 row_mask:0xf bank_mask:0xf bound_ctrl:1
	v_add_f32_dpp v72, v52, v72 wave_shl:1 row_mask:0xf bank_mask:0xf bound_ctrl:1
	v_add_f32_dpp v73, v53, v73 wave_shl:1 row_mask:0xf bank_mask:0xf bound_ctrl:1
	v_add_f32_dpp v94, v54, v94 wave_shl:1 row_mask:0xf bank_mask:0xf bound_ctrl:1
	v_add_f32_dpp v95, v55, v95 wave_shl:1 row_mask:0xf bank_mask:0xf bound_ctrl:1
	v_add_f32_dpp v98, v58, v98 wave_shl:1 row_mask:0xf bank_mask:0xf bound_ctrl:1
	v_add_f32_dpp v99, v59, v99 wave_shl:1 row_mask:0xf bank_mask:0xf bound_ctrl:1
	v_pk_add_f32 v[52:53], v[56:57], v[70:71]
	v_pk_add_f32 v[54:55], v[50:51], v[72:73]
	v_pk_add_f32 v[50:51], v[60:61], v[94:95]
	v_pk_add_f32 v[56:57], v[78:79], v[98:99]
	v_pk_fma_f32 v[54:55], v[120:121], v[52:53], v[54:55] op_sel_hi:[0,1,1] neg_lo:[1,0,0] neg_hi:[1,0,0]
	v_pk_fma_f32 v[50:51], v[120:121], v[52:53], v[50:51] op_sel:[1,0,0] neg_lo:[1,0,0] neg_hi:[1,0,0]
	v_pk_fma_f32 v[56:57], v[122:123], v[52:53], v[56:57] op_sel_hi:[0,1,1] neg_lo:[1,0,0] neg_hi:[1,0,0]
	v_pk_mul_f32 v[58:59], v[122:123], v[54:55] op_sel:[1,0]
	v_pk_mul_f32 v[60:61], v[124:125], v[54:55] op_sel_hi:[0,1]
	v_pk_mul_f32 v[78:79], v[124:125], v[54:55] op_sel:[1,0]
	v_pk_fma_f32 v[58:59], v[124:125], v[50:51], v[58:59] op_sel_hi:[0,1,1]
	v_pk_fma_f32 v[60:61], v[126:127], v[50:51], v[60:61] op_sel_hi:[0,1,1]
	v_pk_fma_f32 v[78:79], v[126:127], v[50:51], v[78:79] op_sel:[1,0,0]
	v_pk_fma_f32 v[58:59], v[124:125], v[56:57], v[58:59] op_sel:[1,0,0]
	v_pk_fma_f32 v[60:61], v[126:127], v[56:57], v[60:61] op_sel:[1,0,0]
	v_pk_fma_f32 v[78:79], v[132:133], v[56:57], v[78:79] op_sel_hi:[0,1,1]
	v_pk_mul_f32 v[100:101], v[120:121], v[58:59] op_sel_hi:[0,1]
	v_pk_fma_f32 v[100:101], v[120:121], v[60:61], v[100:101] op_sel:[1,0,0]
	v_pk_fma_f32 v[100:101], v[122:123], v[78:79], v[100:101] op_sel_hi:[0,1,1]
	v_pk_fma_f32 v[100:101], v[132:133], v[52:53], v[100:101] op_sel:[1,0,0] neg_lo:[0,0,1] neg_hi:[0,0,1]
	v_cmp_eq_u32_e64 s[10:11], 6, v135
	v_cmp_eq_u32_e64 s[14:15], 7, v135
	v_add_f32_dpp v50, v58, v58 wave_shr:1 row_mask:0xf bank_mask:0xf bound_ctrl:1
	v_add_f32_dpp v51, v59, v59 wave_shr:1 row_mask:0xf bank_mask:0xf bound_ctrl:1
	v_add_f32_dpp v52, v60, v60 wave_shr:1 row_mask:0xf bank_mask:0xf bound_ctrl:1
	v_add_f32_dpp v53, v61, v61 wave_shr:1 row_mask:0xf bank_mask:0xf bound_ctrl:1
	v_add_f32_dpp v54, v78, v78 wave_shr:1 row_mask:0xf bank_mask:0xf bound_ctrl:1
	v_add_f32_dpp v55, v79, v79 wave_shr:1 row_mask:0xf bank_mask:0xf bound_ctrl:1
	v_add_f32_dpp v56, v100, v100 wave_shr:1 row_mask:0xf bank_mask:0xf bound_ctrl:1
	v_add_f32_dpp v57, v101, v101 wave_shr:1 row_mask:0xf bank_mask:0xf bound_ctrl:1
	v_add_f32_dpp v50, v58, v50 wave_shl:1 row_mask:0xf bank_mask:0xf bound_ctrl:1
	v_add_f32_dpp v51, v59, v51 wave_shl:1 row_mask:0xf bank_mask:0xf bound_ctrl:1
	v_add_f32_dpp v52, v60, v52 wave_shl:1 row_mask:0xf bank_mask:0xf bound_ctrl:1
	v_add_f32_dpp v53, v61, v53 wave_shl:1 row_mask:0xf bank_mask:0xf bound_ctrl:1
	v_add_f32_dpp v54, v78, v54 wave_shl:1 row_mask:0xf bank_mask:0xf bound_ctrl:1
	v_add_f32_dpp v55, v79, v55 wave_shl:1 row_mask:0xf bank_mask:0xf bound_ctrl:1
	v_add_f32_dpp v56, v100, v56 wave_shl:1 row_mask:0xf bank_mask:0xf bound_ctrl:1
	v_add_f32_dpp v57, v101, v57 wave_shl:1 row_mask:0xf bank_mask:0xf bound_ctrl:1
	v_pk_add_f32 v[58:59], v[86:87], v[50:51]
	v_pk_add_f32 v[60:61], v[36:37], v[52:53]
	v_pk_add_f32 v[36:37], v[46:47], v[54:55]
	v_pk_add_f32 v[46:47], v[48:49], v[56:57]
	v_pk_fma_f32 v[46:47], v[40:41], v[58:59], v[46:47] op_sel_hi:[0,1,1]
	v_pk_fma_f32 v[46:47], v[40:41], v[60:61], v[46:47] op_sel:[1,0,0]
	v_pk_fma_f32 v[46:47], v[42:43], v[36:37], v[46:47] op_sel_hi:[0,1,1]
	v_cndmask_b32_e64 v48, 0, v18, s[10:11]
	v_cndmask_b32_e64 v49, 0, v18, s[14:15]
	v_pk_fma_f32 v[46:47], v[38:39], v[134:135], v[46:47] op_sel_hi:[1,0,1] neg_lo:[0,0,1] neg_hi:[0,0,1]
	s_add_i32 s4, s34, 1
	s_cmpk_lt_i32 s4, 0x201
	s_cselect_b64 s[12:13], s[0:1], 0
	v_pk_add_f32 v[46:47], v[46:47], v[48:49] neg_lo:[0,1] neg_hi:[0,1]
	v_pk_mul_f32 v[78:79], v[46:47], v[46:47]
	v_add_f32_e32 v78, v78, v79
	v_cndmask_b32_e64 v79, 0, v78, s[12:13]
	v_add_f32_e32 v1, v1, v79
	s_add_i32 s5, s34, 6
	s_min_i32 s5, s5, 0x200
	s_mul_i32 s6, s5, 0x804
	s_add_i32 s6, s6, s39
	s_add_i32 s7, s6, 0x101004
	s_mul_i32 s9, s5, 0x180c
	s_add_i32 s9, s9, s33
	s_add_i32 s4, s34, 7
	s_min_i32 s4, s4, 0x200
	s_mul_i32 s4, s4, 0x804
	s_add_i32 s4, s4, s38
	buffer_load_dword v25, v28, s[20:23], s4 offen nt
	buffer_load_dwordx3 v[40:42], v27, s[24:27], s9 offen nt
	buffer_load_dword v36, v28, s[16:19], s6 offen nt
	buffer_load_dword v37, v28, s[16:19], s7 offen nt
	s_waitcnt vmcnt(8)
	s_add_i32 s4, s34, 5
	s_cmpk_lt_u32 s4, 0x201
	s_cselect_b64 s[12:13], s[40:41], 0
	v_cmp_eq_u32_e64 s[14:15], s37, v3
	s_and_b64 s[14:15], s[14:15], s[12:13]
	v_cndmask_b32_e64 v29, 0, 1, s[14:15]
	v_mul_f32_e64 v38, v12, v12
	v_mul_f32_e64 v39, v12, v13
	v_mul_f32_e64 v46, v12, v14
	v_mul_f32_e64 v47, v13, v13
	v_mul_f32_e64 v48, v13, v14
	v_mul_f32_e64 v49, v14, v14
	v_or_b32_dpp v31, v29, v29 wave_shr:1 row_mask:0xf bank_mask:0xf bound_ctrl:1
	s_nop 1
	v_or_b32_dpp v31, v29, v31 wave_shl:1 row_mask:0xf bank_mask:0xf bound_ctrl:1
	s_nop 1
	v_or_b32_dpp v69, v31, v31 wave_shr:1 row_mask:0xf bank_mask:0xf bound_ctrl:1
	s_nop 1
	v_or_b32_dpp v69, v31, v69 wave_shl:1 row_mask:0xf bank_mask:0xf bound_ctrl:1
	v_or3_b32 v29, v69, v44, v30
	v_or3_b32 v29, v29, v45, v68
	s_add_i32 s4, s34, 2
	s_cmpk_lt_u32 s4, 0x1ff
	s_cselect_b64 s[12:13], s[42:43], 0
	v_cmp_ne_u32_e64 s[30:31], 0, v29
	s_and_b64 s[30:31], s[30:31], s[12:13]
	v_cndmask_b32_e64 v29, 0, 1.0, s[30:31]
	v_add_f32_dpp v58, v12, v12 wave_shr:1 row_mask:0xf bank_mask:0xf bound_ctrl:1
	v_add_f32_dpp v59, v13, v13 wave_shr:1 row_mask:0xf bank_mask:0xf bound_ctrl:1
	v_add_f32_dpp v60, v14, v14 wave_shr:1 row_mask:0xf bank_mask:0xf bound_ctrl:1
	v_add_f32_dpp v61, v38, v38 wave_shr:1 row_mask:0xf bank_mask:0xf bound_ctrl:1
	v_add_f32_dpp v78, v39, v39 wave_shr:1 row_mask:0xf bank_mask:0xf bound_ctrl:1
	v_add_f32_dpp v79, v46, v46 wave_shr:1 row_mask:0xf bank_mask:0xf bound_ctrl:1
	v_add_f32_dpp v86, v47, v47 wave_shr:1 row_mask:0xf bank_mask:0xf bound_ctrl:1
	v_add_f32_dpp v87, v48, v48 wave_shr:1 row_mask:0xf bank_mask:0xf bound_ctrl:1
	v_add_f32_dpp v100, v49, v49 wave_shr:1 row_mask:0xf bank_mask:0xf bound_ctrl:1
	v_add_f32_dpp v101, v29, v29 wave_shr:1 row_mask:0xf bank_mask:0xf bound_ctrl:1
	v_add_f32_dpp v58, v12, v58 wave_shl:1 row_mask:0xf bank_mask:0xf bound_ctrl:1
	v_add_f32_dpp v59, v13, v59 wave_shl:1 row_mask:0xf bank_mask:0xf bound_ctrl:1
	v_add_f32_dpp v60, v14, v60 wave_shl:1 row_mask:0xf bank_mask:0xf bound_ctrl:1
	v_add_f32_dpp v61, v38, v61 wave_shl:1 row_mask:0xf bank_mask:0xf bound_ctrl:1
	v_add_f32_dpp v78, v39, v78 wave_shl:1 row_mask:0xf bank_mask:0xf bound_ctrl:1
	v_add_f32_dpp v79, v46, v79 wave_shl:1 row_mask:0xf bank_mask:0xf bound_ctrl:1
	v_add_f32_dpp v86, v47, v86 wave_shl:1 row_mask:0xf bank_mask:0xf bound_ctrl:1
	v_add_f32_dpp v87, v48, v87 wave_shl:1 row_mask:0xf bank_mask:0xf bound_ctrl:1
	v_add_f32_dpp v100, v49, v100 wave_shl:1 row_mask:0xf bank_mask:0xf bound_ctrl:1
	v_add_f32_dpp v101, v29, v101 wave_shl:1 row_mask:0xf bank_mask:0xf bound_ctrl:1
	v_pk_add_f32 v[38:39], v[80:81], v[58:59]
	v_pk_add_f32 v[46:47], v[88:89], v[38:39]
	v_pk_add_f32 v[48:49], v[82:83], v[60:61]
	v_pk_add_f32 v[80:81], v[112:113], v[48:49]
	v_pk_add_f32 v[82:83], v[90:91], v[78:79]
	v_pk_add_f32 v[88:89], v[114:115], v[82:83]
	v_pk_add_f32 v[90:91], v[96:97], v[86:87]
	v_pk_add_f32 v[110:111], v[116:117], v[90:91]
	v_pk_add_f32 v[96:97], v[108:109], v[100:101]
	v_pk_add_f32 v[112:113], v[118:119], v[96:97]
	v_mul_f32_e64 v116, v46, v22
	v_mul_f32_e64 v117, v47, v22
	v_mul_f32_e64 v118, v80, v22
	v_fma_f32 v29, v81, v22, v26
	v_mul_f32_e64 v31, v88, v22
	v_mul_f32_e64 v108, v89, v22
	v_fma_f32 v109, v110, v22, v26
	v_mul_f32_e64 v114, v111, v22
	v_fma_f32 v115, v112, v22, v26
	v_fma_f32 v29, -v116, v116, v29
	v_fma_f32 v31, -v116, v117, v31
	v_fma_f32 v108, -v116, v118, v108
	v_fma_f32 v109, -v117, v117, v109
	v_fma_f32 v114, -v117, v118, v114
	v_fma_f32 v115, -v118, v118, v115
	v_mul_f32_e64 v130, v114, v114
	v_mul_f32_e64 v131, v31, v115
	v_mul_f32_e64 v132, v108, v109
	v_mul_f32_e64 v133, v108, v108
	v_mul_f32_e64 v134, v29, v114
	v_mul_f32_e64 v135, v31, v31
	v_fma_f32 v130, v109, v115, -v130
	v_fma_f32 v131, v108, v114, -v131
	v_fma_f32 v132, v31, v114, -v132
	v_fma_f32 v133, v29, v115, -v133
	v_fma_f32 v134, v31, v108, -v134
	v_fma_f32 v135, v29, v109, -v135
	v_mul_f32_e64 v136, v29, v130
	v_fma_f32 v136, v31, v131, v136
	v_fma_f32 v136, v108, v132, v136
	v_rcp_f32_e32 v136, v136
	v_cmp_ne_u32_e64 vcc, s37, v24
	v_mul_f32_e64 v136, v136, v22
	v_cndmask_b32_e64 v136, 0, v136, s[30:31]
	v_cndmask_b32_e64 v29, 0, v18, vcc
	v_cndmask_b32_e64 v125, 0, v22, s[30:31]
	v_mul_f32_e64 v119, v130, v136
	v_mul_f32_e64 v120, v131, v136
	v_mul_f32_e64 v121, v132, v136
	v_mul_f32_e64 v122, v133, v136
	v_mul_f32_e64 v123, v134, v136
	v_mul_f32_e64 v124, v135, v136
	v_add_f32_e64 v126, v113, v29
	v_mov_b32_e32 v127, v24
	ds_write_b128 v23, v[116:119]
	ds_write_b128 v23, v[120:123] offset:1024
	ds_write_b128 v23, v[124:127] offset:2048
	s_waitcnt lgkmcnt(0)
	s_barrier
	v_pk_mul_f32 v[46:47], v[6:7], v[12:13] op_sel_hi:[1,0]
	v_pk_mul_f32 v[80:81], v[6:7], v[12:13] op_sel:[0,1]
	v_pk_mul_f32 v[88:89], v[6:7], v[14:15] op_sel_hi:[1,0]
	v_add_f32_dpp v108, v6, v6 wave_shr:1 row_mask:0xf bank_mask:0xf bound_ctrl:1
	v_add_f32_dpp v109, v7, v7 wave_shr:1 row_mask:0xf bank_mask:0xf bound_ctrl:1
	v_add_f32_dpp v110, v46, v46 wave_shr:1 row_mask:0xf bank_mask:0xf bound_ctrl:1
	v_add_f32_dpp v111, v47, v47 wave_shr:1 row_mask:0xf bank_mask:0xf bound_ctrl:1
	v_add_f32_dpp v112, v80, v80 wave_shr:1 row_mask:0xf bank_mask:0xf bound_ctrl:1
	v_add_f32_dpp v113, v81, v81 wave_shr:1 row_mask:0xf bank_mask:0xf bound_ctrl:1
	v_add_f32_dpp v114, v88, v88 wave_shr:1 row_mask:0xf bank_mask:0xf bound_ctrl:1
	v_add_f32_dpp v115, v89, v89 wave_shr:1 row_mask:0xf bank_mask:0xf bound_ctrl:1
	v_add_f32_dpp v108, v6, v108 wave_shl:1 row_mask:0xf bank_mask:0xf bound_ctrl:1
	v_add_f32_dpp v109, v7, v109 wave_shl:1 row_mask:0xf bank_mask:0xf bound_ctrl:1
	v_add_f32_dpp v110, v46, v110 wave_shl:1 row_mask:0xf bank_mask:0xf bound_ctrl:1
	v_add_f32_dpp v111, v47, v111 wave_shl:1 row_mask:0xf bank_mask:0xf bound_ctrl:1
	v_add_f32_dpp v112, v80, v112 wave_shl:1 row_mask:0xf bank_mask:0xf bound_ctrl:1
	v_add_f32_dpp v113, v81, v113 wave_shl:1 row_mask:0xf bank_mask:0xf bound_ctrl:1
	v_add_f32_dpp v114, v88, v114 wave_shl:1 row_mask:0xf bank_mask:0xf bound_ctrl:1
	v_add_f32_dpp v115, v89, v115 wave_shl:1 row_mask:0xf bank_mask:0xf bound_ctrl:1
	v_pk_add_f32 v[46:47], v[70:71], v[108:109]
	v_pk_add_f32 v[80:81], v[102:103], v[46:47]
	v_pk_add_f32 v[70:71], v[72:73], v[110:111]
	v_pk_add_f32 v[88:89], v[104:105], v[70:71]
	v_pk_add_f32 v[72:73], v[94:95], v[112:113]
	v_pk_add_f32 v[102:103], v[106:107], v[72:73]
	v_pk_add_f32 v[94:95], v[98:99], v[114:115]
	v_pk_add_f32 v[104:105], v[128:129], v[94:95]
	v_pk_fma_f32 v[88:89], v[116:117], v[80:81], v[88:89] op_sel_hi:[0,1,1] neg_lo:[1,0,0] neg_hi:[1,0,0]
	v_pk_fma_f32 v[102:103], v[116:117], v[80:81], v[102:103] op_sel:[1,0,0] neg_lo:[1,0,0] neg_hi:[1,0,0]
	v_pk_fma_f32 v[104:105], v[118:119], v[80:81], v[104:105] op_sel_hi:[0,1,1] neg_lo:[1,0,0] neg_hi:[1,0,0]
	v_pk_mul_f32 v[98:99], v[118:119], v[88:89] op_sel:[1,0]
	v_pk_mul_f32 v[106:107], v[120:121], v[88:89] op_sel_hi:[0,1]
	v_pk_mul_f32 v[128:129], v[120:121], v[88:89] op_sel:[1,0]
	v_pk_fma_f32 v[98:99], v[120:121], v[102:103], v[98:99] op_sel_hi:[0,1,1]
	v_pk_fma_f32 v[106:107], v[122:123], v[102:103], v[106:107] op_sel_hi:[0,1,1]
	v_pk_fma_f32 v[128:129], v[122:123], v[102:103], v[128:129] op_sel:[1,0,0]
	v_pk_fma_f32 v[98:99], v[120:121], v[104:105], v[98:99] op_sel:[1,0,0]
	v_pk_fma_f32 v[106:107], v[122:123], v[104:105], v[106:107] op_sel:[1,0,0]
	v_pk_fma_f32 v[128:129], v[124:125], v[104:105], v[128:129] op_sel_hi:[0,1,1]
	v_pk_mul_f32 v[130:131], v[116:117], v[98:99] op_sel_hi:[0,1]
	v_pk_fma_f32 v[130:131], v[116:117], v[106:107], v[130:131] op_sel:[1,0,0]
	v_pk_fma_f32 v[130:131], v[118:119], v[128:129], v[130:131] op_sel_hi:[0,1,1]
	v_pk_fma_f32 v[130:131], v[124:125], v[80:81], v[130:131] op_sel:[1,0,0] neg_lo:[0,0,1] neg_hi:[0,0,1]
	v_cmp_eq_u32_e64 s[10:11], 6, v127
	v_cmp_eq_u32_e64 s[14:15], 7, v127
	v_add_f32_dpp v80, v98, v98 wave_shr:1 row_mask:0xf bank_mask:0xf bound_ctrl:1
	v_add_f32_dpp v81, v99, v99 wave_shr:1 row_mask:0xf bank_mask:0xf bound_ctrl:1
	v_add_f32_dpp v88, v106, v106 wave_shr:1 row_mask:0xf bank_mask:0xf bound_ctrl:1
	v_add_f32_dpp v89, v107, v107 wave_shr:1 row_mask:0xf bank_mask:0xf bound_ctrl:1
	v_add_f32_dpp v102, v128, v128 wave_shr:1 row_mask:0xf bank_mask:0xf bound_ctrl:1
	v_add_f32_dpp v103, v129, v129 wave_shr:1 row_mask:0xf bank_mask:0xf bound_ctrl:1
	v_add_f32_dpp v104, v130, v130 wave_shr:1 row_mask:0xf bank_mask:0xf bound_ctrl:1
	v_add_f32_dpp v105, v131, v131 wave_shr:1 row_mask:0xf bank_mask:0xf bound_ctrl:1
	v_add_f32_dpp v80, v98, v80 wave_shl:1 row_mask:0xf bank_mask:0xf bound_ctrl:1
	v_add_f32_dpp v81, v99, v81 wave_shl:1 row_mask:0xf bank_mask:0xf bound_ctrl:1
	v_add_f32_dpp v88, v106, v88 wave_shl:1 row_mask:0xf bank_mask:0xf bound_ctrl:1
	v_add_f32_dpp v89, v107, v89 wave_shl:1 row_mask:0xf bank_mask:0xf bound_ctrl:1
	v_add_f32_dpp v102, v128, v102 wave_shl:1 row_mask:0xf bank_mask:0xf bound_ctrl:1
	v_add_f32_dpp v103, v129, v103 wave_shl:1 row_mask:0xf bank_mask:0xf bound_ctrl:1
	v_add_f32_dpp v104, v130, v104 wave_shl:1 row_mask:0xf bank_mask:0xf bound_ctrl:1
	v_add_f32_dpp v105, v131, v105 wave_shl:1 row_mask:0xf bank_mask:0xf bound_ctrl:1
	v_pk_add_f32 v[98:99], v[50:51], v[80:81]
	v_pk_add_f32 v[106:107], v[74:75], v[98:99]
	v_pk_add_f32 v[50:51], v[52:53], v[88:89]
	v_pk_add_f32 v[74:75], v[76:77], v[50:51]
	v_pk_add_f32 v[52:53], v[54:55], v[102:103]
	v_pk_add_f32 v[76:77], v[84:85], v[52:53]
	v_pk_add_f32 v[54:55], v[56:57], v[104:105]
	v_pk_add_f32 v[84:85], v[92:93], v[54:55]
	v_pk_fma_f32 v[84:85], v[64:65], v[106:107], v[84:85] op_sel_hi:[0,1,1]
	v_pk_fma_f32 v[84:85], v[64:65], v[74:75], v[84:85] op_sel:[1,0,0]
	v_pk_fma_f32 v[84:85], v[66:67], v[76:77], v[84:85] op_sel_hi:[0,1,1]
	v_cndmask_b32_e64 v56, 0, v18, s[10:11]
	v_cndmask_b32_e64 v57, 0, v18, s[14:15]
	v_pk_fma_f32 v[84:85], v[62:63], v[126:127], v[84:85] op_sel_hi:[1,0,1] neg_lo:[0,0,1] neg_hi:[0,0,1]
	s_add_i32 s4, s34, 2
	s_cmpk_lt_i32 s4, 0x201
	s_cselect_b64 s[12:13], s[0:1], 0
	v_pk_add_f32 v[84:85], v[84:85], v[56:57] neg_lo:[0,1] neg_hi:[0,1]
	v_pk_mul_f32 v[92:93], v[84:85], v[84:85]
	v_add_f32_e32 v92, v92, v93
	v_cndmask_b32_e64 v93, 0, v92, s[12:13]
	v_add_f32_e32 v1, v1, v93
	s_add_i32 s5, s34, 7
	s_min_i32 s5, s5, 0x200
	s_mul_i32 s6, s5, 0x804
	s_add_i32 s6, s6, s39
	s_add_i32 s7, s6, 0x101004
	s_mul_i32 s9, s5, 0x180c
	s_add_i32 s9, s9, s33
	s_add_i32 s4, s34, 8
	s_min_i32 s4, s4, 0x200
	s_mul_i32 s4, s4, 0x804
	s_add_i32 s4, s4, s38
	buffer_load_dword v24, v28, s[20:23], s4 offen nt
	buffer_load_dwordx3 v[64:66], v27, s[24:27], s9 offen nt
	buffer_load_dword v56, v28, s[16:19], s6 offen nt
	buffer_load_dword v57, v28, s[16:19], s7 offen nt
	s_waitcnt vmcnt(8)
	s_add_i32 s4, s34, 6
	s_cmpk_lt_u32 s4, 0x201
	s_cselect_b64 s[12:13], s[40:41], 0
	v_cmp_eq_u32_e64 s[14:15], s37, v16
	s_and_b64 s[14:15], s[14:15], s[12:13]
	v_cndmask_b32_e64 v29, 0, 1, s[14:15]
	v_mul_f32_e64 v62, v32, v32
	v_mul_f32_e64 v63, v32, v33
	v_mul_f32_e64 v74, v32, v34
	v_mul_f32_e64 v75, v33, v33
	v_mul_f32_e64 v76, v33, v34
	v_mul_f32_e64 v77, v34, v34
	v_or_b32_dpp v31, v29, v29 wave_shr:1 row_mask:0xf bank_mask:0xf bound_ctrl:1
	s_nop 1
	v_or_b32_dpp v31, v29, v31 wave_shl:1 row_mask:0xf bank_mask:0xf bound_ctrl:1
	s_nop 1
	v_or_b32_dpp v68, v31, v31 wave_shr:1 row_mask:0xf bank_mask:0xf bound_ctrl:1
	s_nop 1
	v_or_b32_dpp v68, v31, v68 wave_shl:1 row_mask:0xf bank_mask:0xf bound_ctrl:1
	v_or3_b32 v29, v68, v69, v44
	v_or3_b32 v29, v29, v30, v45
	s_add_i32 s4, s34, 3
	s_cmpk_lt_u32 s4, 0x1ff
	s_cselect_b64 s[12:13], s[42:43], 0
	v_cmp_ne_u32_e64 s[30:31], 0, v29
	s_and_b64 s[30:31], s[30:31], s[12:13]
	v_cndmask_b32_e64 v29, 0, 1.0, s[30:31]
	v_add_f32_dpp v84, v32, v32 wave_shr:1 row_mask:0xf bank_mask:0xf bound_ctrl:1
	v_add_f32_dpp v85, v33, v33 wave_shr:1 row_mask:0xf bank_mask:0xf bound_ctrl:1
	v_add_f32_dpp v92, v34, v34 wave_shr:1 row_mask:0xf bank_mask:0xf bound_ctrl:1
	v_add_f32_dpp v93, v62, v62 wave_shr:1 row_mask:0xf bank_mask:0xf bound_ctrl:1
	v_add_f32_dpp v106, v63, v63 wave_shr:1 row_mask:0xf bank_mask:0xf bound_ctrl:1
	v_add_f32_dpp v107, v74, v74 wave_shr:1 row_mask:0xf bank_mask:0xf bound_ctrl:1
	v_add_f32_dpp v116, v75, v75 wave_shr:1 row_mask:0xf bank_mask:0xf bound_ctrl:1
	v_add_f32_dpp v117, v76, v76 wave_shr:1 row_mask:0xf bank_mask:0xf bound_ctrl:1
	v_add_f32_dpp v118, v77, v77 wave_shr:1 row_mask:0xf bank_mask:0xf bound_ctrl:1
	v_add_f32_dpp v119, v29, v29 wave_shr:1 row_mask:0xf bank_mask:0xf bound_ctrl:1
	v_add_f32_dpp v84, v32, v84 wave_shl:1 row_mask:0xf bank_mask:0xf bound_ctrl:1
	v_add_f32_dpp v85, v33, v85 wave_shl:1 row_mask:0xf bank_mask:0xf bound_ctrl:1
	v_add_f32_dpp v92, v34, v92 wave_shl:1 row_mask:0xf bank_mask:0xf bound_ctrl:1
	v_add_f32_dpp v93, v62, v93 wave_shl:1 row_mask:0xf bank_mask:0xf bound_ctrl:1
	v_add_f32_dpp v106, v63, v106 wave_shl:1 row_mask:0xf bank_mask:0xf bound_ctrl:1
	v_add_f32_dpp v107, v74, v107 wave_shl:1 row_mask:0xf bank_mask:0xf bound_ctrl:1
	v_add_f32_dpp v116, v75, v116 wave_shl:1 row_mask:0xf bank_mask:0xf bound_ctrl:1
	v_add_f32_dpp v117, v76, v117 wave_shl:1 row_mask:0xf bank_mask:0xf bound_ctrl:1
	v_add_f32_dpp v118, v77, v118 wave_shl:1 row_mask:0xf bank_mask:0xf bound_ctrl:1
	v_add_f32_dpp v119, v29, v119 wave_shl:1 row_mask:0xf bank_mask:0xf bound_ctrl:1
	v_pk_add_f32 v[62:63], v[38:39], v[84:85]
	v_pk_add_f32 v[38:39], v[48:49], v[92:93]
	v_pk_add_f32 v[48:49], v[82:83], v[106:107]
	v_pk_add_f32 v[74:75], v[90:91], v[116:117]
	v_pk_add_f32 v[76:77], v[96:97], v[118:119]
	v_mul_f32_e64 v120, v62, v22
	v_mul_f32_e64 v121, v63, v22
	v_mul_f32_e64 v122, v38, v22
	v_fma_f32 v29, v39, v22, v26
	v_mul_f32_e64 v31, v48, v22
	v_mul_f32_e64 v82, v49, v22
	v_fma_f32 v83, v74, v22, v26
	v_mul_f32_e64 v90, v75, v22
	v_fma_f32 v91, v76, v22, v26
	v_fma_f32 v29, -v120, v120, v29
	v_fma_f32 v31, -v120, v121, v31
	v_fma_f32 v82, -v120, v122, v82
	v_fma_f32 v83, -v121, v121, v83
	v_fma_f32 v90, -v121, v122, v90
	v_fma_f32 v91, -v122, v122, v91
	v_mul_f32_e64 v96, v90, v90
	v_mul_f32_e64 v97, v31, v91
	v_mul_f32_e64 v132, v82, v83
	v_mul_f32_e64 v133, v82, v82
	v_mul_f32_e64 v134, v29, v90
	v_mul_f32_e64 v135, v31, v31
	v_fma_f32 v96, v83, v91, -v96
	v_fma_f32 v97, v82, v90, -v97
	v_fma_f32 v132, v31, v90, -v132
	v_fma_f32 v133, v29, v91, -v133
	v_fma_f32 v134, v31, v82, -v134
	v_fma_f32 v135, v29, v83, -v135
	v_mul_f32_e64 v136, v29, v96
	v_fma_f32 v136, v31, v97, v136
	v_fma_f32 v136, v82, v132, v136
	v_rcp_f32_e32 v136, v136
	v_cmp_ne_u32_e64 vcc, s37, v17
	v_mul_f32_e64 v136, v136, v22
	v_cndmask_b32_e64 v136, 0, v136, s[30:31]
	v_cndmask_b32_e64 v29, 0, v18, vcc
	v_cndmask_b32_e64 v129, 0, v22, s[30:31]
	v_mul_f32_e64 v123, v96, v136
	v_mul_f32_e64 v124, v97, v136
	v_mul_f32_e64 v125, v132, v136
	v_mul_f32_e64 v126, v133, v136
	v_mul_f32_e64 v127, v134, v136
	v_mul_f32_e64 v128, v135, v136
	v_add_f32_e64 v130, v77, v29
	v_mov_b32_e32 v131, v17
	ds_write_b128 v23, v[120:123] offset:3072
	ds_write_b128 v23, v[124:127] offset:4096
	ds_write_b128 v23, v[128:131] offset:5120
	s_waitcnt lgkmcnt(0)
	s_barrier
	v_pk_mul_f32 v[38:39], v[20:21], v[32:33] op_sel_hi:[1,0]
	v_pk_mul_f32 v[48:49], v[20:21], v[32:33] op_sel:[0,1]
	v_pk_mul_f32 v[62:63], v[20:21], v[34:35] op_sel_hi:[1,0]
	v_add_f32_dpp v74, v20, v20 wave_shr:1 row_mask:0xf bank_mask:0xf bound_ctrl:1
	v_add_f32_dpp v75, v21, v21 wave_shr:1 row_mask:0xf bank_mask:0xf bound_ctrl:1
	v_add_f32_dpp v76, v38, v38 wave_shr:1 row_mask:0xf bank_mask:0xf bound_ctrl:1
	v_add_f32_dpp v77, v39, v39 wave_shr:1 row_mask:0xf bank_mask:0xf bound_ctrl:1
	v_add_f32_dpp v82, v48, v48 wave_shr:1 row_mask:0xf bank_mask:0xf bound_ctrl:1
	v_add_f32_dpp v83, v49, v49 wave_shr:1 row_mask:0xf bank_mask:0xf bound_ctrl:1
	v_add_f32_dpp v90, v62, v62 wave_shr:1 row_mask:0xf bank_mask:0xf bound_ctrl:1
	v_add_f32_dpp v91, v63, v63 wave_shr:1 row_mask:0xf bank_mask:0xf bound_ctrl:1
	v_add_f32_dpp v74, v20, v74 wave_shl:1 row_mask:0xf bank_mask:0xf bound_ctrl:1
	v_add_f32_dpp v75, v21, v75 wave_shl:1 row_mask:0xf bank_mask:0xf bound_ctrl:1
	v_add_f32_dpp v76, v38, v76 wave_shl:1 row_mask:0xf bank_mask:0xf bound_ctrl:1
	v_add_f32_dpp v77, v39, v77 wave_shl:1 row_mask:0xf bank_mask:0xf bound_ctrl:1
	v_add_f32_dpp v82, v48, v82 wave_shl:1 row_mask:0xf bank_mask:0xf bound_ctrl:1
	v_add_f32_dpp v83, v49, v83 wave_shl:1 row_mask:0xf bank_mask:0xf bound_ctrl:1
	v_add_f32_dpp v90, v62, v90 wave_shl:1 row_mask:0xf bank_mask:0xf bound_ctrl:1
	v_add_f32_dpp v91, v63, v91 wave_shl:1 row_mask:0xf bank_mask:0xf bound_ctrl:1
	v_pk_add_f32 v[38:39], v[46:47], v[74:75]
	v_pk_add_f32 v[46:47], v[70:71], v[76:77]
	v_pk_add_f32 v[48:49], v[72:73], v[82:83]
	v_pk_add_f32 v[62:63], v[94:95], v[90:91]
	v_pk_fma_f32 v[46:47], v[120:121], v[38:39], v[46:47] op_sel_hi:[0,1,1] neg_lo:[1,0,0] neg_hi:[1,0,0]
	v_pk_fma_f32 v[48:49], v[120:121], v[38:39], v[48:49] op_sel:[1,0,0] neg_lo:[1,0,0] neg_hi:[1,0,0]
	v_pk_fma_f32 v[62:63], v[122:123], v[38:39], v[62:63] op_sel_hi:[0,1,1] neg_lo:[1,0,0] neg_hi:[1,0,0]
	v_pk_mul_f32 v[70:71], v[122:123], v[46:47] op_sel:[1,0]
	v_pk_mul_f32 v[72:73], v[124:125], v[46:47] op_sel_hi:[0,1]
	v_pk_mul_f32 v[94:95], v[124:125], v[46:47] op_sel:[1,0]
	v_pk_fma_f32 v[70:71], v[124:125], v[48:49], v[70:71] op_sel_hi:[0,1,1]
	v_pk_fma_f32 v[72:73], v[126:127], v[48:49], v[72:73] op_sel_hi:[0,1,1]
	v_pk_fma_f32 v[94:95], v[126:127], v[48:49], v[94:95] op_sel:[1,0,0]
	v_pk_fma_f32 v[70:71], v[124:125], v[62:63], v[70:71] op_sel:[1,0,0]
	v_pk_fma_f32 v[72:73], v[126:127], v[62:63], v[72:73] op_sel:[1,0,0]
	v_pk_fma_f32 v[94:95], v[128:129], v[62:63], v[94:95] op_sel_hi:[0,1,1]
	v_pk_mul_f32 v[96:97], v[120:121], v[70:71] op_sel_hi:[0,1]
	v_pk_fma_f32 v[96:97], v[120:121], v[72:73], v[96:97] op_sel:[1,0,0]
	v_pk_fma_f32 v[96:97], v[122:123], v[94:95], v[96:97] op_sel_hi:[0,1,1]
	v_pk_fma_f32 v[96:97], v[128:129], v[38:39], v[96:97] op_sel:[1,0,0] neg_lo:[0,0,1] neg_hi:[0,0,1]
	v_cmp_eq_u32_e64 s[10:11], 6, v131
	v_cmp_eq_u32_e64 s[14:15], 7, v131
	v_add_f32_dpp v38, v70, v70 wave_shr:1 row_mask:0xf bank_mask:0xf bound_ctrl:1
	v_add_f32_dpp v39, v71, v71 wave_shr:1 row_mask:0xf bank_mask:0xf bound_ctrl:1
	v_add_f32_dpp v46, v72, v72 wave_shr:1 row_mask:0xf bank_mask:0xf bound_ctrl:1
	v_add_f32_dpp v47, v73, v73 wave_shr:1 row_mask:0xf bank_mask:0xf bound_ctrl:1
	v_add_f32_dpp v48, v94, v94 wave_shr:1 row_mask:0xf bank_mask:0xf bound_ctrl:1
	v_add_f32_dpp v49, v95, v95 wave_shr:1 row_mask:0xf bank_mask:0xf bound_ctrl:1
	v_add_f32_dpp v62, v96, v96 wave_shr:1 row_mask:0xf bank_mask:0xf bound_ctrl:1
	v_add_f32_dpp v63, v97, v97 wave_shr:1 row_mask:0xf bank_mask:0xf bound_ctrl:1
	v_add_f32_dpp v38, v70, v38 wave_shl:1 row_mask:0xf bank_mask:0xf bound_ctrl:1
	v_add_f32_dpp v39, v71, v39 wave_shl:1 row_mask:0xf bank_mask:0xf bound_ctrl:1
	v_add_f32_dpp v46, v72, v46 wave_shl:1 row_mask:0xf bank_mask:0xf bound_ctrl:1
	v_add_f32_dpp v47, v73, v47 wave_shl:1 row_mask:0xf bank_mask:0xf bound_ctrl:1
	v_add_f32_dpp v48, v94, v48 wave_shl:1 row_mask:0xf bank_mask:0xf bound_ctrl:1
	v_add_f32_dpp v49, v95, v49 wave_shl:1 row_mask:0xf bank_mask:0xf bound_ctrl:1
	v_add_f32_dpp v62, v96, v62 wave_shl:1 row_mask:0xf bank_mask:0xf bound_ctrl:1
	v_add_f32_dpp v63, v97, v63 wave_shl:1 row_mask:0xf bank_mask:0xf bound_ctrl:1
	v_pk_add_f32 v[70:71], v[98:99], v[38:39]
	v_pk_add_f32 v[72:73], v[50:51], v[46:47]
	v_pk_add_f32 v[50:51], v[52:53], v[48:49]
	v_pk_add_f32 v[52:53], v[54:55], v[62:63]
	v_pk_fma_f32 v[52:53], v[8:9], v[70:71], v[52:53] op_sel_hi:[0,1,1]
	v_pk_fma_f32 v[52:53], v[8:9], v[72:73], v[52:53] op_sel:[1,0,0]
	v_pk_fma_f32 v[52:53], v[10:11], v[50:51], v[52:53] op_sel_hi:[0,1,1]
	v_cndmask_b32_e64 v54, 0, v18, s[10:11]
	v_cndmask_b32_e64 v55, 0, v18, s[14:15]
	v_pk_fma_f32 v[52:53], v[4:5], v[130:131], v[52:53] op_sel_hi:[1,0,1] neg_lo:[0,0,1] neg_hi:[0,0,1]
	s_add_i32 s4, s34, 3
	s_cmpk_lt_i32 s4, 0x201
	s_cselect_b64 s[12:13], s[0:1], 0
	v_pk_add_f32 v[52:53], v[52:53], v[54:55] neg_lo:[0,1] neg_hi:[0,1]
	v_pk_mul_f32 v[94:95], v[52:53], v[52:53]
	v_add_f32_e32 v94, v94, v95
	v_cndmask_b32_e64 v95, 0, v94, s[12:13]
	v_add_f32_e32 v1, v1, v95
	s_add_i32 s5, s34, 8
	s_min_i32 s5, s5, 0x200
	s_mul_i32 s6, s5, 0x804
	s_add_i32 s6, s6, s39
	s_add_i32 s7, s6, 0x101004
	s_mul_i32 s9, s5, 0x180c
	s_add_i32 s9, s9, s33
	s_add_i32 s4, s34, 9
	s_min_i32 s4, s4, 0x200
	s_mul_i32 s4, s4, 0x804
	s_add_i32 s4, s4, s38
	buffer_load_dword v17, v28, s[20:23], s4 offen nt
	buffer_load_dwordx3 v[8:10], v27, s[24:27], s9 offen nt
	buffer_load_dword v4, v28, s[16:19], s6 offen nt
	buffer_load_dword v5, v28, s[16:19], s7 offen nt
	s_waitcnt vmcnt(8)
	s_add_i32 s4, s34, 7
	s_cmpk_lt_u32 s4, 0x201
	s_cselect_b64 s[12:13], s[40:41], 0
	v_cmp_eq_u32_e64 s[14:15], s37, v25
	s_and_b64 s[14:15], s[14:15], s[12:13]
	v_cndmask_b32_e64 v29, 0, 1, s[14:15]
	v_mul_f32_e64 v50, v40, v40
	v_mul_f32_e64 v51, v40, v41
	v_mul_f32_e64 v52, v40, v42
	v_mul_f32_e64 v53, v41, v41
	v_mul_f32_e64 v54, v41, v42
	v_mul_f32_e64 v55, v42, v42
	v_or_b32_dpp v31, v29, v29 wave_shr:1 row_mask:0xf bank_mask:0xf bound_ctrl:1
	s_nop 1
	v_or_b32_dpp v31, v29, v31 wave_shl:1 row_mask:0xf bank_mask:0xf bound_ctrl:1
	s_nop 1
	v_or_b32_dpp v45, v31, v31 wave_shr:1 row_mask:0xf bank_mask:0xf bound_ctrl:1
	s_nop 1
	v_or_b32_dpp v45, v31, v45 wave_shl:1 row_mask:0xf bank_mask:0xf bound_ctrl:1
	v_or3_b32 v29, v45, v68, v69
	v_or3_b32 v29, v29, v44, v30
	s_add_i32 s4, s34, 4
	s_cmpk_lt_u32 s4, 0x1ff
	s_cselect_b64 s[12:13], s[42:43], 0
	v_cmp_ne_u32_e64 s[30:31], 0, v29
	s_and_b64 s[30:31], s[30:31], s[12:13]
	v_cndmask_b32_e64 v29, 0, 1.0, s[30:31]
	v_add_f32_dpp v70, v40, v40 wave_shr:1 row_mask:0xf bank_mask:0xf bound_ctrl:1
	v_add_f32_dpp v71, v41, v41 wave_shr:1 row_mask:0xf bank_mask:0xf bound_ctrl:1
	v_add_f32_dpp v72, v42, v42 wave_shr:1 row_mask:0xf bank_mask:0xf bound_ctrl:1
	v_add_f32_dpp v73, v50, v50 wave_shr:1 row_mask:0xf bank_mask:0xf bound_ctrl:1
	v_add_f32_dpp v94, v51, v51 wave_shr:1 row_mask:0xf bank_mask:0xf bound_ctrl:1
	v_add_f32_dpp v95, v52, v52 wave_shr:1 row_mask:0xf bank_mask:0xf bound_ctrl:1
	v_add_f32_dpp v96, v53, v53 wave_shr:1 row_mask:0xf bank_mask:0xf bound_ctrl:1
	v_add_f32_dpp v97, v54, v54 wave_shr:1 row_mask:0xf bank_mask:0xf bound_ctrl:1
	v_add_f32_dpp v98, v55, v55 wave_shr:1 row_mask:0xf bank_mask:0xf bound_ctrl:1
	v_add_f32_dpp v99, v29, v29 wave_shr:1 row_mask:0xf bank_mask:0xf bound_ctrl:1
	v_add_f32_dpp v70, v40, v70 wave_shl:1 row_mask:0xf bank_mask:0xf bound_ctrl:1
	v_add_f32_dpp v71, v41, v71 wave_shl:1 row_mask:0xf bank_mask:0xf bound_ctrl:1
	v_add_f32_dpp v72, v42, v72 wave_shl:1 row_mask:0xf bank_mask:0xf bound_ctrl:1
	v_add_f32_dpp v73, v50, v73 wave_shl:1 row_mask:0xf bank_mask:0xf bound_ctrl:1
	v_add_f32_dpp v94, v51, v94 wave_shl:1 row_mask:0xf bank_mask:0xf bound_ctrl:1
	v_add_f32_dpp v95, v52, v95 wave_shl:1 row_mask:0xf bank_mask:0xf bound_ctrl:1
	v_add_f32_dpp v96, v53, v96 wave_shl:1 row_mask:0xf bank_mask:0xf bound_ctrl:1
	v_add_f32_dpp v97, v54, v97 wave_shl:1 row_mask:0xf bank_mask:0xf bound_ctrl:1
	v_add_f32_dpp v98, v55, v98 wave_shl:1 row_mask:0xf bank_mask:0xf bound_ctrl:1
	v_add_f32_dpp v99, v29, v99 wave_shl:1 row_mask:0xf bank_mask:0xf bound_ctrl:1
	v_pk_add_f32 v[50:51], v[84:85], v[70:71]
	v_pk_add_f32 v[52:53], v[58:59], v[50:51]
	v_pk_add_f32 v[54:55], v[92:93], v[72:73]
	v_pk_add_f32 v[58:59], v[60:61], v[54:55]
	v_pk_add_f32 v[60:61], v[106:107], v[94:95]
	v_pk_add_f32 v[84:85], v[78:79], v[60:61]
	v_pk_add_f32 v[78:79], v[116:117], v[96:97]
	v_pk_add_f32 v[92:93], v[86:87], v[78:79]
	v_pk_add_f32 v[86:87], v[118:119], v[98:99]
	v_pk_add_f32 v[106:107], v[100:101], v[86:87]
	v_mul_f32_e64 v116, v52, v22
	v_mul_f32_e64 v117, v53, v22
	v_mul_f32_e64 v118, v58, v22
	v_fma_f32 v29, v59, v22, v26
	v_mul_f32_e64 v31, v84, v22
	v_mul_f32_e64 v100, v85, v22
	v_fma_f32 v101, v92, v22, v26
	v_mul_f32_e64 v128, v93, v22
	v_fma_f32 v129, v106, v22, v26
	v_fma_f32 v29, -v116, v116, v29
	v_fma_f32 v31, -v116, v117, v31
	v_fma_f32 v100, -v116, v118, v100
	v_fma_f32 v101, -v117, v117, v101
	v_fma_f32 v128, -v117, v118, v128
	v_fma_f32 v129, -v118, v118, v129
	v_mul_f32_e64 v130, v128, v128
	v_mul_f32_e64 v131, v31, v129
	v_mul_f32_e64 v132, v100, v101
	v_mul_f32_e64 v133, v100, v100
	v_mul_f32_e64 v134, v29, v128
	v_mul_f32_e64 v135, v31, v31
	v_fma_f32 v130, v101, v129, -v130
	v_fma_f32 v131, v100, v128, -v131
	v_fma_f32 v132, v31, v128, -v132
	v_fma_f32 v133, v29, v129, -v133
	v_fma_f32 v134, v31, v100, -v134
	v_fma_f32 v135, v29, v101, -v135
	v_mul_f32_e64 v136, v29, v130
	v_fma_f32 v136, v31, v131, v136
	v_fma_f32 v136, v100, v132, v136
	v_rcp_f32_e32 v136, v136
	v_cmp_ne_u32_e64 vcc, s37, v2
	v_mul_f32_e64 v136, v136, v22
	v_cndmask_b32_e64 v136, 0, v136, s[30:31]
	v_cndmask_b32_e64 v29, 0, v18, vcc
	v_cndmask_b32_e64 v125, 0, v22, s[30:31]
	v_mul_f32_e64 v119, v130, v136
	v_mul_f32_e64 v120, v131, v136
	v_mul_f32_e64 v121, v132, v136
	v_mul_f32_e64 v122, v133, v136
	v_mul_f32_e64 v123, v134, v136
	v_mul_f32_e64 v124, v135, v136
	v_add_f32_e64 v126, v107, v29
	v_mov_b32_e32 v127, v2
	ds_write_b128 v23, v[116:119]
	ds_write_b128 v23, v[120:123] offset:1024
	ds_write_b128 v23, v[124:127] offset:2048
	s_waitcnt lgkmcnt(0)
	s_barrier
	v_pk_mul_f32 v[30:31], v[36:37], v[40:41] op_sel_hi:[1,0]
	v_pk_mul_f32 v[52:53], v[36:37], v[40:41] op_sel:[0,1]
	v_pk_mul_f32 v[58:59], v[36:37], v[42:43] op_sel_hi:[1,0]
	v_add_f32_dpp v84, v36, v36 wave_shr:1 row_mask:0xf bank_mask:0xf bound_ctrl:1
	v_add_f32_dpp v85, v37, v37 wave_shr:1 row_mask:0xf bank_mask:0xf bound_ctrl:1
	v_add_f32_dpp v92, v30, v30 wave_shr:1 row_mask:0xf bank_mask:0xf bound_ctrl:1
	v_add_f32_dpp v93, v31, v31 wave_shr:1 row_mask:0xf bank_mask:0xf bound_ctrl:1
	v_add_f32_dpp v100, v52, v52 wave_shr:1 row_mask:0xf bank_mask:0xf bound_ctrl:1
	v_add_f32_dpp v101, v53, v53 wave_shr:1 row_mask:0xf bank_mask:0xf bound_ctrl:1
	v_add_f32_dpp v106, v58, v58 wave_shr:1 row_mask:0xf bank_mask:0xf bound_ctrl:1
	v_add_f32_dpp v107, v59, v59 wave_shr:1 row_mask:0xf bank_mask:0xf bound_ctrl:1
	v_add_f32_dpp v84, v36, v84 wave_shl:1 row_mask:0xf bank_mask:0xf bound_ctrl:1
	v_add_f32_dpp v85, v37, v85 wave_shl:1 row_mask:0xf bank_mask:0xf bound_ctrl:1
	v_add_f32_dpp v92, v30, v92 wave_shl:1 row_mask:0xf bank_mask:0xf bound_ctrl:1
	v_add_f32_dpp v93, v31, v93 wave_shl:1 row_mask:0xf bank_mask:0xf bound_ctrl:1
	v_add_f32_dpp v100, v52, v100 wave_shl:1 row_mask:0xf bank_mask:0xf bound_ctrl:1
	v_add_f32_dpp v101, v53, v101 wave_shl:1 row_mask:0xf bank_mask:0xf bound_ctrl:1
	v_add_f32_dpp v106, v58, v106 wave_shl:1 row_mask:0xf bank_mask:0xf bound_ctrl:1
	v_add_f32_dpp v107, v59, v107 wave_shl:1 row_mask:0xf bank_mask:0xf bound_ctrl:1
	v_pk_add_f32 v[30:31], v[74:75], v[84:85]
	v_pk_add_f32 v[52:53], v[108:109], v[30:31]
	v_pk_add_f32 v[58:59], v[76:77], v[92:93]
	v_pk_add_f32 v[74:75], v[110:111], v[58:59]
	v_pk_add_f32 v[76:77], v[82:83], v[100:101]
	v_pk_add_f32 v[108:109], v[112:113], v[76:77]
	v_pk_add_f32 v[82:83], v[90:91], v[106:107]
	v_pk_add_f32 v[110:111], v[114:115], v[82:83]
	v_pk_fma_f32 v[74:75], v[116:117], v[52:53], v[74:75] op_sel_hi:[0,1,1] neg_lo:[1,0,0] neg_hi:[1,0,0]
	v_pk_fma_f32 v[108:109], v[116:117], v[52:53], v[108:109] op_sel:[1,0,0] neg_lo:[1,0,0] neg_hi:[1,0,0]
	v_pk_fma_f32 v[110:111], v[118:119], v[52:53], v[110:111] op_sel_hi:[0,1,1] neg_lo:[1,0,0] neg_hi:[1,0,0]
	v_pk_mul_f32 v[90:91], v[118:119], v[74:75] op_sel:[1,0]
	v_pk_mul_f32 v[112:113], v[120:121], v[74:75] op_sel_hi:[0,1]
	v_pk_mul_f32 v[114:115], v[120:121], v[74:75] op_sel:[1,0]
	v_pk_fma_f32 v[90:91], v[120:121], v[108:109], v[90:91] op_sel_hi:[0,1,1]
	v_pk_fma_f32 v[112:113], v[122:123], v[108:109], v[112:113] op_sel_hi:[0,1,1]
	v_pk_fma_f32 v[114:115], v[122:123], v[108:109], v[114:115] op_sel:[1,0,0]
	v_pk_fma_f32 v[90:91], v[120:121], v[110:111], v[90:91] op_sel:[1,0,0]
	v_pk_fma_f32 v[112:113], v[122:123], v[110:111], v[112:113] op_sel:[1,0,0]
	v_pk_fma_f32 v[114:115], v[124:125], v[110:111], v[114:115] op_sel_hi:[0,1,1]
	v_pk_mul_f32 v[128:129], v[116:117], v[90:91] op_sel_hi:[0,1]
	v_pk_fma_f32 v[128:129], v[116:117], v[112:113], v[128:129] op_sel:[1,0,0]
	v_pk_fma_f32 v[128:129], v[118:119], v[114:115], v[128:129] op_sel_hi:[0,1,1]
	v_pk_fma_f32 v[128:129], v[124:125], v[52:53], v[128:129] op_sel:[1,0,0] neg_lo:[0,0,1] neg_hi:[0,0,1]
	v_cmp_eq_u32_e64 s[10:11], 6, v127
	v_cmp_eq_u32_e64 s[14:15], 7, v127
	v_add_f32_dpp v52, v90, v90 wave_shr:1 row_mask:0xf bank_mask:0xf bound_ctrl:1
	v_add_f32_dpp v53, v91, v91 wave_shr:1 row_mask:0xf bank_mask:0xf bound_ctrl:1
	v_add_f32_dpp v74, v112, v112 wave_shr:1 row_mask:0xf bank_mask:0xf bound_ctrl:1
	v_add_f32_dpp v75, v113, v113 wave_shr:1 row_mask:0xf bank_mask:0xf bound_ctrl:1
	v_add_f32_dpp v108, v114, v114 wave_shr:1 row_mask:0xf bank_mask:0xf bound_ctrl:1
	v_add_f32_dpp v109, v115, v115 wave_shr:1 row_mask:0xf bank_mask:0xf bound_ctrl:1
	v_add_f32_dpp v110, v128, v128 wave_shr:1 row_mask:0xf bank_mask:0xf bound_ctrl:1
	v_add_f32_dpp v111, v129, v129 wave_shr:1 row_mask:0xf bank_mask:0xf bound_ctrl:1
	v_add_f32_dpp v52, v90, v52 wave_shl:1 row_mask:0xf bank_mask:0xf bound_ctrl:1
	v_add_f32_dpp v53, v91, v53 wave_shl:1 row_mask:0xf bank_mask:0xf bound_ctrl:1
	v_add_f32_dpp v74, v112, v74 wave_shl:1 row_mask:0xf bank_mask:0xf bound_ctrl:1
	v_add_f32_dpp v75, v113, v75 wave_shl:1 row_mask:0xf bank_mask:0xf bound_ctrl:1
	v_add_f32_dpp v108, v114, v108 wave_shl:1 row_mask:0xf bank_mask:0xf bound_ctrl:1
	v_add_f32_dpp v109, v115, v109 wave_shl:1 row_mask:0xf bank_mask:0xf bound_ctrl:1
	v_add_f32_dpp v110, v128, v110 wave_shl:1 row_mask:0xf bank_mask:0xf bound_ctrl:1
	v_add_f32_dpp v111, v129, v111 wave_shl:1 row_mask:0xf bank_mask:0xf bound_ctrl:1
	v_pk_add_f32 v[90:91], v[38:39], v[52:53]
	v_pk_add_f32 v[112:113], v[80:81], v[90:91]
	v_pk_add_f32 v[38:39], v[46:47], v[74:75]
	v_pk_add_f32 v[80:81], v[88:89], v[38:39]
	v_pk_add_f32 v[46:47], v[48:49], v[108:109]
	v_pk_add_f32 v[88:89], v[102:103], v[46:47]
	v_pk_add_f32 v[48:49], v[62:63], v[110:111]
	v_pk_add_f32 v[102:103], v[104:105], v[48:49]
	v_pk_fma_f32 v[102:103], v[12:13], v[112:113], v[102:103] op_sel_hi:[0,1,1]
	v_pk_fma_f32 v[102:103], v[12:13], v[80:81], v[102:103] op_sel:[1,0,0]
	v_pk_fma_f32 v[102:103], v[14:15], v[88:89], v[102:103] op_sel_hi:[0,1,1]
	v_cndmask_b32_e64 v62, 0, v18, s[10:11]
	v_cndmask_b32_e64 v63, 0, v18, s[14:15]
	v_pk_fma_f32 v[102:103], v[6:7], v[126:127], v[102:103] op_sel_hi:[1,0,1] neg_lo:[0,0,1] neg_hi:[0,0,1]
	s_add_i32 s4, s34, 4
	s_cmpk_lt_i32 s4, 0x201
	s_cselect_b64 s[12:13], s[0:1], 0
	v_pk_add_f32 v[102:103], v[102:103], v[62:63] neg_lo:[0,1] neg_hi:[0,1]
	v_pk_mul_f32 v[104:105], v[102:103], v[102:103]
	v_add_f32_e32 v104, v104, v105
	v_cndmask_b32_e64 v105, 0, v104, s[12:13]
	v_add_f32_e32 v1, v1, v105
	s_add_i32 s5, s34, 9
	s_min_i32 s5, s5, 0x200
	s_mul_i32 s6, s5, 0x804
	s_add_i32 s6, s6, s39
	s_add_i32 s7, s6, 0x101004
	s_mul_i32 s9, s5, 0x180c
	s_add_i32 s9, s9, s33
	s_add_i32 s4, s34, 10
	s_min_i32 s4, s4, 0x200
	s_mul_i32 s4, s4, 0x804
	s_add_i32 s4, s4, s38
	buffer_load_dword v2, v28, s[20:23], s4 offen nt
	buffer_load_dwordx3 v[12:14], v27, s[24:27], s9 offen nt
	buffer_load_dword v6, v28, s[16:19], s6 offen nt
	buffer_load_dword v7, v28, s[16:19], s7 offen nt
	s_waitcnt vmcnt(8)
	s_add_i32 s4, s34, 8
	s_cmpk_lt_u32 s4, 0x201
	s_cselect_b64 s[12:13], s[40:41], 0
	v_cmp_eq_u32_e64 s[14:15], s37, v24
	s_and_b64 s[14:15], s[14:15], s[12:13]
	v_cndmask_b32_e64 v29, 0, 1, s[14:15]
	v_mul_f32_e64 v62, v64, v64
	v_mul_f32_e64 v63, v64, v65
	v_mul_f32_e64 v80, v64, v66
	v_mul_f32_e64 v81, v65, v65
	v_mul_f32_e64 v88, v65, v66
	v_mul_f32_e64 v89, v66, v66
	v_or_b32_dpp v102, v29, v29 wave_shr:1 row_mask:0xf bank_mask:0xf bound_ctrl:1
	s_nop 1
	v_or_b32_dpp v102, v29, v102 wave_shl:1 row_mask:0xf bank_mask:0xf bound_ctrl:1
	s_nop 1
	v_or_b32_dpp v103, v102, v102 wave_shr:1 row_mask:0xf bank_mask:0xf bound_ctrl:1
	s_nop 1
	v_or_b32_dpp v103, v102, v103 wave_shl:1 row_mask:0xf bank_mask:0xf bound_ctrl:1
	v_or3_b32 v29, v103, v45, v68
	v_or3_b32 v29, v29, v69, v44
	s_add_i32 s4, s34, 5
	s_cmpk_lt_u32 s4, 0x1ff
	s_cselect_b64 s[12:13], s[42:43], 0
	v_cmp_ne_u32_e64 s[30:31], 0, v29
	s_and_b64 s[30:31], s[30:31], s[12:13]
	v_cndmask_b32_e64 v29, 0, 1.0, s[30:31]
	v_add_f32_dpp v104, v64, v64 wave_shr:1 row_mask:0xf bank_mask:0xf bound_ctrl:1
	v_add_f32_dpp v105, v65, v65 wave_shr:1 row_mask:0xf bank_mask:0xf bound_ctrl:1
	v_add_f32_dpp v112, v66, v66 wave_shr:1 row_mask:0xf bank_mask:0xf bound_ctrl:1
	v_add_f32_dpp v113, v62, v62 wave_shr:1 row_mask:0xf bank_mask:0xf bound_ctrl:1
	v_add_f32_dpp v114, v63, v63 wave_shr:1 row_mask:0xf bank_mask:0xf bound_ctrl:1
	v_add_f32_dpp v115, v80, v80 wave_shr:1 row_mask:0xf bank_mask:0xf bound_ctrl:1
	v_add_f32_dpp v116, v81, v81 wave_shr:1 row_mask:0xf bank_mask:0xf bound_ctrl:1
	v_add_f32_dpp v117, v88, v88 wave_shr:1 row_mask:0xf bank_mask:0xf bound_ctrl:1
	v_add_f32_dpp v118, v89, v89 wave_shr:1 row_mask:0xf bank_mask:0xf bound_ctrl:1
	v_add_f32_dpp v119, v29, v29 wave_shr:1 row_mask:0xf bank_mask:0xf bound_ctrl:1
	v_add_f32_dpp v104, v64, v104 wave_shl:1 row_mask:0xf bank_mask:0xf bound_ctrl:1
	v_add_f32_dpp v105, v65, v105 wave_shl:1 row_mask:0xf bank_mask:0xf bound_ctrl:1
	v_add_f32_dpp v112, v66, v112 wave_shl:1 row_mask:0xf bank_mask:0xf bound_ctrl:1
	v_add_f32_dpp v113, v62, v113 wave_shl:1 row_mask:0xf bank_mask:0xf bound_ctrl:1
	v_add_f32_dpp v114, v63, v114 wave_shl:1 row_mask:0xf bank_mask:0xf bound_ctrl:1
	v_add_f32_dpp v115, v80, v115 wave_shl:1 row_mask:0xf bank_mask:0xf bound_ctrl:1
	v_add_f32_dpp v116, v81, v116 wave_shl:1 row_mask:0xf bank_mask:0xf bound_ctrl:1
	v_add_f32_dpp v117, v88, v117 wave_shl:1 row_mask:0xf bank_mask:0xf bound_ctrl:1
	v_add_f32_dpp v118, v89, v118 wave_shl:1 row_mask:0xf bank_mask:0xf bound_ctrl:1
	v_add_f32_dpp v119, v29, v119 wave_shl:1 row_mask:0xf bank_mask:0xf bound_ctrl:1
	v_pk_add_f32 v[62:63], v[50:51], v[104:105]
	v_pk_add_f32 v[50:51], v[54:55], v[112:113]
	v_pk_add_f32 v[54:55], v[60:61], v[114:115]
	v_pk_add_f32 v[60:61], v[78:79], v[116:117]
	v_pk_add_f32 v[78:79], v[86:87], v[118:119]
	v_mul_f32_e64 v120, v62, v22
	v_mul_f32_e64 v121, v63, v22
	v_mul_f32_e64 v122, v50, v22
	v_fma_f32 v29, v51, v22, v26
	v_mul_f32_e64 v102, v54, v22
	v_mul_f32_e64 v80, v55, v22
	v_fma_f32 v81, v60, v22, v26
	v_mul_f32_e64 v86, v61, v22
	v_fma_f32 v87, v78, v22, v26
	v_fma_f32 v29, -v120, v120, v29
	v_fma_f32 v102, -v120, v121, v102
	v_fma_f32 v80, -v120, v122, v80
	v_fma_f32 v81, -v121, v121, v81
	v_fma_f32 v86, -v121, v122, v86
	v_fma_f32 v87, -v122, v122, v87
	v_mul_f32_e64 v88, v86, v86
	v_mul_f32_e64 v89, v102, v87
	v_mul_f32_e64 v132, v80, v81
	v_mul_f32_e64 v133, v80, v80
	v_mul_f32_e64 v134, v29, v86
	v_mul_f32_e64 v135, v102, v102
	v_fma_f32 v88, v81, v87, -v88
	v_fma_f32 v89, v80, v86, -v89
	v_fma_f32 v132, v102, v86, -v132
	v_fma_f32 v133, v29, v87, -v133
	v_fma_f32 v134, v102, v80, -v134
	v_fma_f32 v135, v29, v81, -v135
	v_mul_f32_e64 v136, v29, v88
	v_fma_f32 v136, v102, v89, v136
	v_fma_f32 v136, v80, v132, v136
	v_rcp_f32_e32 v136, v136
	v_cmp_ne_u32_e64 vcc, s37, v3
	v_mul_f32_e64 v136, v136, v22
	v_cndmask_b32_e64 v136, 0, v136, s[30:31]
	v_cndmask_b32_e64 v29, 0, v18, vcc
	v_cndmask_b32_e64 v129, 0, v22, s[30:31]
	v_mul_f32_e64 v123, v88, v136
	v_mul_f32_e64 v124, v89, v136
	v_mul_f32_e64 v125, v132, v136
	v_mul_f32_e64 v126, v133, v136
	v_mul_f32_e64 v127, v134, v136
	v_mul_f32_e64 v128, v135, v136
	v_add_f32_e64 v130, v79, v29
	v_mov_b32_e32 v131, v3
	ds_write_b128 v23, v[120:123] offset:3072
	ds_write_b128 v23, v[124:127] offset:4096
	ds_write_b128 v23, v[128:131] offset:5120
	s_waitcnt lgkmcnt(0)
	s_barrier
	v_pk_mul_f32 v[50:51], v[56:57], v[64:65] op_sel_hi:[1,0]
	v_pk_mul_f32 v[54:55], v[56:57], v[64:65] op_sel:[0,1]
	v_pk_mul_f32 v[60:61], v[56:57], v[66:67] op_sel_hi:[1,0]
	v_add_f32_dpp v62, v56, v56 wave_shr:1 row_mask:0xf bank_mask:0xf bound_ctrl:1
	v_add_f32_dpp v63, v57, v57 wave_shr:1 row_mask:0xf bank_mask:0xf bound_ctrl:1
	v_add_f32_dpp v78, v50, v50 wave_shr:1 row_mask:0xf bank_mask:0xf bound_ctrl:1
	v_add_f32_dpp v79, v51, v51 wave_shr:1 row_mask:0xf bank_mask:0xf bound_ctrl:1
	v_add_f32_dpp v80, v54, v54 wave_shr:1 row_mask:0xf bank_mask:0xf bound_ctrl:1
	v_add_f32_dpp v81, v55, v55 wave_shr:1 row_mask:0xf bank_mask:0xf bound_ctrl:1
	v_add_f32_dpp v86, v60, v60 wave_shr:1 row_mask:0xf bank_mask:0xf bound_ctrl:1
	v_add_f32_dpp v87, v61, v61 wave_shr:1 row_mask:0xf bank_mask:0xf bound_ctrl:1
	v_add_f32_dpp v62, v56, v62 wave_shl:1 row_mask:0xf bank_mask:0xf bound_ctrl:1
	v_add_f32_dpp v63, v57, v63 wave_shl:1 row_mask:0xf bank_mask:0xf bound_ctrl:1
	v_add_f32_dpp v78, v50, v78 wave_shl:1 row_mask:0xf bank_mask:0xf bound_ctrl:1
	v_add_f32_dpp v79, v51, v79 wave_shl:1 row_mask:0xf bank_mask:0xf bound_ctrl:1
	v_add_f32_dpp v80, v54, v80 wave_shl:1 row_mask:0xf bank_mask:0xf bound_ctrl:1
	v_add_f32_dpp v81, v55, v81 wave_shl:1 row_mask:0xf bank_mask:0xf bound_ctrl:1
	v_add_f32_dpp v86, v60, v86 wave_shl:1 row_mask:0xf bank_mask:0xf bound_ctrl:1
	v_add_f32_dpp v87, v61, v87 wave_shl:1 row_mask:0xf bank_mask:0xf bound_ctrl:1
	v_pk_add_f32 v[50:51], v[30:31], v[62:63]
	v_pk_add_f32 v[30:31], v[58:59], v[78:79]
	v_pk_add_f32 v[54:55], v[76:77], v[80:81]
	v_pk_add_f32 v[58:59], v[82:83], v[86:87]
	v_pk_fma_f32 v[30:31], v[120:121], v[50:51], v[30:31] op_sel_hi:[0,1,1] neg_lo:[1,0,0] neg_hi:[1,0,0]
	v_pk_fma_f32 v[54:55], v[120:121], v[50:51], v[54:55] op_sel:[1,0,0] neg_lo:[1,0,0] neg_hi:[1,0,0]
	v_pk_fma_f32 v[58:59], v[122:123], v[50:51], v[58:59] op_sel_hi:[0,1,1] neg_lo:[1,0,0] neg_hi:[1,0,0]
	v_pk_mul_f32 v[60:61], v[122:123], v[30:31] op_sel:[1,0]
	v_pk_mul_f32 v[76:77], v[124:125], v[30:31] op_sel_hi:[0,1]
	v_pk_mul_f32 v[82:83], v[124:125], v[30:31] op_sel:[1,0]
	v_pk_fma_f32 v[60:61], v[124:125], v[54:55], v[60:61] op_sel_hi:[0,1,1]
	v_pk_fma_f32 v[76:77], v[126:127], v[54:55], v[76:77] op_sel_hi:[0,1,1]
	v_pk_fma_f32 v[82:83], v[126:127], v[54:55], v[82:83] op_sel:[1,0,0]
	v_pk_fma_f32 v[60:61], v[124:125], v[58:59], v[60:61] op_sel:[1,0,0]
	v_pk_fma_f32 v[76:77], v[126:127], v[58:59], v[76:77] op_sel:[1,0,0]
	v_pk_fma_f32 v[82:83], v[128:129], v[58:59], v[82:83] op_sel_hi:[0,1,1]
	v_pk_mul_f32 v[88:89], v[120:121], v[60:61] op_sel_hi:[0,1]
	v_pk_fma_f32 v[88:89], v[120:121], v[76:77], v[88:89] op_sel:[1,0,0]
	v_pk_fma_f32 v[88:89], v[122:123], v[82:83], v[88:89] op_sel_hi:[0,1,1]
	v_pk_fma_f32 v[88:89], v[128:129], v[50:51], v[88:89] op_sel:[1,0,0] neg_lo:[0,0,1] neg_hi:[0,0,1]
	v_cmp_eq_u32_e64 s[10:11], 6, v131
	v_cmp_eq_u32_e64 s[14:15], 7, v131
	v_add_f32_dpp v30, v60, v60 wave_shr:1 row_mask:0xf bank_mask:0xf bound_ctrl:1
	v_add_f32_dpp v31, v61, v61 wave_shr:1 row_mask:0xf bank_mask:0xf bound_ctrl:1
	v_add_f32_dpp v50, v76, v76 wave_shr:1 row_mask:0xf bank_mask:0xf bound_ctrl:1
	v_add_f32_dpp v51, v77, v77 wave_shr:1 row_mask:0xf bank_mask:0xf bound_ctrl:1
	v_add_f32_dpp v54, v82, v82 wave_shr:1 row_mask:0xf bank_mask:0xf bound_ctrl:1
	v_add_f32_dpp v55, v83, v83 wave_shr:1 row_mask:0xf bank_mask:0xf bound_ctrl:1
	v_add_f32_dpp v58, v88, v88 wave_shr:1 row_mask:0xf bank_mask:0xf bound_ctrl:1
	v_add_f32_dpp v59, v89, v89 wave_shr:1 row_mask:0xf bank_mask:0xf bound_ctrl:1
	v_add_f32_dpp v30, v60, v30 wave_shl:1 row_mask:0xf bank_mask:0xf bound_ctrl:1
	v_add_f32_dpp v31, v61, v31 wave_shl:1 row_mask:0xf bank_mask:0xf bound_ctrl:1
	v_add_f32_dpp v50, v76, v50 wave_shl:1 row_mask:0xf bank_mask:0xf bound_ctrl:1
	v_add_f32_dpp v51, v77, v51 wave_shl:1 row_mask:0xf bank_mask:0xf bound_ctrl:1
	v_add_f32_dpp v54, v82, v54 wave_shl:1 row_mask:0xf bank_mask:0xf bound_ctrl:1
	v_add_f32_dpp v55, v83, v55 wave_shl:1 row_mask:0xf bank_mask:0xf bound_ctrl:1
	v_add_f32_dpp v58, v88, v58 wave_shl:1 row_mask:0xf bank_mask:0xf bound_ctrl:1
	v_add_f32_dpp v59, v89, v59 wave_shl:1 row_mask:0xf bank_mask:0xf bound_ctrl:1
	v_pk_add_f32 v[60:61], v[90:91], v[30:31]
	v_pk_add_f32 v[76:77], v[38:39], v[50:51]
	v_pk_add_f32 v[38:39], v[46:47], v[54:55]
	v_pk_add_f32 v[46:47], v[48:49], v[58:59]
	v_pk_fma_f32 v[46:47], v[32:33], v[60:61], v[46:47] op_sel_hi:[0,1,1]
	v_pk_fma_f32 v[46:47], v[32:33], v[76:77], v[46:47] op_sel:[1,0,0]
	v_pk_fma_f32 v[46:47], v[34:35], v[38:39], v[46:47] op_sel_hi:[0,1,1]
	v_cndmask_b32_e64 v48, 0, v18, s[10:11]
	v_cndmask_b32_e64 v49, 0, v18, s[14:15]
	v_pk_fma_f32 v[46:47], v[20:21], v[130:131], v[46:47] op_sel_hi:[1,0,1] neg_lo:[0,0,1] neg_hi:[0,0,1]
	s_add_i32 s4, s34, 5
	s_cmpk_lt_i32 s4, 0x201
	s_cselect_b64 s[12:13], s[0:1], 0
	v_pk_add_f32 v[46:47], v[46:47], v[48:49] neg_lo:[0,1] neg_hi:[0,1]
	v_pk_mul_f32 v[82:83], v[46:47], v[46:47]
	v_add_f32_e32 v82, v82, v83
	v_cndmask_b32_e64 v83, 0, v82, s[12:13]
	v_add_f32_e32 v1, v1, v83
	s_add_i32 s5, s34, 10
	s_min_i32 s5, s5, 0x200
	s_mul_i32 s6, s5, 0x804
	s_add_i32 s6, s6, s39
	s_add_i32 s7, s6, 0x101004
	s_mul_i32 s9, s5, 0x180c
	s_add_i32 s9, s9, s33
	s_add_i32 s4, s34, 11
	s_min_i32 s4, s4, 0x200
	s_mul_i32 s4, s4, 0x804
	s_add_i32 s4, s4, s38
	buffer_load_dword v3, v28, s[20:23], s4 offen nt
	buffer_load_dwordx3 v[32:34], v27, s[24:27], s9 offen nt
	buffer_load_dword v20, v28, s[16:19], s6 offen nt
	buffer_load_dword v21, v28, s[16:19], s7 offen nt
	s_waitcnt vmcnt(8)
	s_add_i32 s4, s34, 9
	s_cmpk_lt_u32 s4, 0x201
	s_cselect_b64 s[12:13], s[40:41], 0
	v_cmp_eq_u32_e64 s[14:15], s37, v17
	s_and_b64 s[14:15], s[14:15], s[12:13]
	v_cndmask_b32_e64 v29, 0, 1, s[14:15]
	v_mul_f32_e64 v38, v8, v8
	v_mul_f32_e64 v39, v8, v9
	v_mul_f32_e64 v46, v8, v10
	v_mul_f32_e64 v47, v9, v9
	v_mul_f32_e64 v48, v9, v10
	v_mul_f32_e64 v49, v10, v10
	v_or_b32_dpp v44, v29, v29 wave_shr:1 row_mask:0xf bank_mask:0xf bound_ctrl:1
	s_nop 1
	v_or_b32_dpp v44, v29, v44 wave_shl:1 row_mask:0xf bank_mask:0xf bound_ctrl:1
	s_nop 1
	v_or_b32_dpp v102, v44, v44 wave_shr:1 row_mask:0xf bank_mask:0xf bound_ctrl:1
	s_nop 1
	v_or_b32_dpp v102, v44, v102 wave_shl:1 row_mask:0xf bank_mask:0xf bound_ctrl:1
	v_or3_b32 v29, v102, v103, v45
	v_or3_b32 v29, v29, v68, v69
	s_add_i32 s4, s34, 6
	s_cmpk_lt_u32 s4, 0x1ff
	s_cselect_b64 s[12:13], s[42:43], 0
	v_cmp_ne_u32_e64 s[30:31], 0, v29
	s_and_b64 s[30:31], s[30:31], s[12:13]
	v_cndmask_b32_e64 v29, 0, 1.0, s[30:31]
	v_add_f32_dpp v60, v8, v8 wave_shr:1 row_mask:0xf bank_mask:0xf bound_ctrl:1
	v_add_f32_dpp v61, v9, v9 wave_shr:1 row_mask:0xf bank_mask:0xf bound_ctrl:1
	v_add_f32_dpp v76, v10, v10 wave_shr:1 row_mask:0xf bank_mask:0xf bound_ctrl:1
	v_add_f32_dpp v77, v38, v38 wave_shr:1 row_mask:0xf bank_mask:0xf bound_ctrl:1
	v_add_f32_dpp v82, v39, v39 wave_shr:1 row_mask:0xf bank_mask:0xf bound_ctrl:1
	v_add_f32_dpp v83, v46, v46 wave_shr:1 row_mask:0xf bank_mask:0xf bound_ctrl:1
	v_add_f32_dpp v88, v47, v47 wave_shr:1 row_mask:0xf bank_mask:0xf bound_ctrl:1
	v_add_f32_dpp v89, v48, v48 wave_shr:1 row_mask:0xf bank_mask:0xf bound_ctrl:1
	v_add_f32_dpp v90, v49, v49 wave_shr:1 row_mask:0xf bank_mask:0xf bound_ctrl:1
	v_add_f32_dpp v91, v29, v29 wave_shr:1 row_mask:0xf bank_mask:0xf bound_ctrl:1
	v_add_f32_dpp v60, v8, v60 wave_shl:1 row_mask:0xf bank_mask:0xf bound_ctrl:1
	v_add_f32_dpp v61, v9, v61 wave_shl:1 row_mask:0xf bank_mask:0xf bound_ctrl:1
	v_add_f32_dpp v76, v10, v76 wave_shl:1 row_mask:0xf bank_mask:0xf bound_ctrl:1
	v_add_f32_dpp v77, v38, v77 wave_shl:1 row_mask:0xf bank_mask:0xf bound_ctrl:1
	v_add_f32_dpp v82, v39, v82 wave_shl:1 row_mask:0xf bank_mask:0xf bound_ctrl:1
	v_add_f32_dpp v83, v46, v83 wave_shl:1 row_mask:0xf bank_mask:0xf bound_ctrl:1
	v_add_f32_dpp v88, v47, v88 wave_shl:1 row_mask:0xf bank_mask:0xf bound_ctrl:1
	v_add_f32_dpp v89, v48, v89 wave_shl:1 row_mask:0xf bank_mask:0xf bound_ctrl:1
	v_add_f32_dpp v90, v49, v90 wave_shl:1 row_mask:0xf bank_mask:0xf bound_ctrl:1
	v_add_f32_dpp v91, v29, v91 wave_shl:1 row_mask:0xf bank_mask:0xf bound_ctrl:1
	v_pk_add_f32 v[38:39], v[104:105], v[60:61]
	v_pk_add_f32 v[46:47], v[70:71], v[38:39]
	v_pk_add_f32 v[48:49], v[112:113], v[76:77]
	v_pk_add_f32 v[70:71], v[72:73], v[48:49]
	v_pk_add_f32 v[72:73], v[114:115], v[82:83]
	v_pk_add_f32 v[104:105], v[94:95], v[72:73]
	v_pk_add_f32 v[94:95], v[116:117], v[88:89]
	v_pk_add_f32 v[112:113], v[96:97], v[94:95]
	v_pk_add_f32 v[96:97], v[118:119], v[90:91]
	v_pk_add_f32 v[114:115], v[98:99], v[96:97]
	v_mul_f32_e64 v116, v46, v22
	v_mul_f32_e64 v117, v47, v22
	v_mul_f32_e64 v118, v70, v22
	v_fma_f32 v29, v71, v22, v26
	v_mul_f32_e64 v44, v104, v22
	v_mul_f32_e64 v98, v105, v22
	v_fma_f32 v99, v112, v22, v26
	v_mul_f32_e64 v128, v113, v22
	v_fma_f32 v129, v114, v22, v26
	v_fma_f32 v29, -v116, v116, v29
	v_fma_f32 v44, -v116, v117, v44
	v_fma_f32 v98, -v116, v118, v98
	v_fma_f32 v99, -v117, v117, v99
	v_fma_f32 v128, -v117, v118, v128
	v_fma_f32 v129, -v118, v118, v129
	v_mul_f32_e64 v130, v128, v128
	v_mul_f32_e64 v131, v44, v129
	v_mul_f32_e64 v132, v98, v99
	v_mul_f32_e64 v133, v98, v98
	v_mul_f32_e64 v134, v29, v128
	v_mul_f32_e64 v135, v44, v44
	v_fma_f32 v130, v99, v129, -v130
	v_fma_f32 v131, v98, v128, -v131
	v_fma_f32 v132, v44, v128, -v132
	v_fma_f32 v133, v29, v129, -v133
	v_fma_f32 v134, v44, v98, -v134
	v_fma_f32 v135, v29, v99, -v135
	v_mul_f32_e64 v136, v29, v130
	v_fma_f32 v136, v44, v131, v136
	v_fma_f32 v136, v98, v132, v136
	v_rcp_f32_e32 v136, v136
	v_cmp_ne_u32_e64 vcc, s37, v16
	v_mul_f32_e64 v136, v136, v22
	v_cndmask_b32_e64 v136, 0, v136, s[30:31]
	v_cndmask_b32_e64 v29, 0, v18, vcc
	v_cndmask_b32_e64 v125, 0, v22, s[30:31]
	v_mul_f32_e64 v119, v130, v136
	v_mul_f32_e64 v120, v131, v136
	v_mul_f32_e64 v121, v132, v136
	v_mul_f32_e64 v122, v133, v136
	v_mul_f32_e64 v123, v134, v136
	v_mul_f32_e64 v124, v135, v136
	v_add_f32_e64 v126, v115, v29
	v_mov_b32_e32 v127, v16
	ds_write_b128 v23, v[116:119]
	ds_write_b128 v23, v[120:123] offset:1024
	ds_write_b128 v23, v[124:127] offset:2048
	s_waitcnt lgkmcnt(0)
	s_barrier
	v_pk_mul_f32 v[46:47], v[4:5], v[8:9] op_sel_hi:[1,0]
	v_pk_mul_f32 v[70:71], v[4:5], v[8:9] op_sel:[0,1]
	v_pk_mul_f32 v[98:99], v[4:5], v[10:11] op_sel_hi:[1,0]
	v_add_f32_dpp v104, v4, v4 wave_shr:1 row_mask:0xf bank_mask:0xf bound_ctrl:1
	v_add_f32_dpp v105, v5, v5 wave_shr:1 row_mask:0xf bank_mask:0xf bound_ctrl:1
	v_add_f32_dpp v112, v46, v46 wave_shr:1 row_mask:0xf bank_mask:0xf bound_ctrl:1
	v_add_f32_dpp v113, v47, v47 wave_shr:1 row_mask:0xf bank_mask:0xf bound_ctrl:1
	v_add_f32_dpp v114, v70, v70 wave_shr:1 row_mask:0xf bank_mask:0xf bound_ctrl:1
	v_add_f32_dpp v115, v71, v71 wave_shr:1 row_mask:0xf bank_mask:0xf bound_ctrl:1
	v_add_f32_dpp v128, v98, v98 wave_shr:1 row_mask:0xf bank_mask:0xf bound_ctrl:1
	v_add_f32_dpp v129, v99, v99 wave_shr:1 row_mask:0xf bank_mask:0xf bound_ctrl:1
	v_add_f32_dpp v104, v4, v104 wave_shl:1 row_mask:0xf bank_mask:0xf bound_ctrl:1
	v_add_f32_dpp v105, v5, v105 wave_shl:1 row_mask:0xf bank_mask:0xf bound_ctrl:1
	v_add_f32_dpp v112, v46, v112 wave_shl:1 row_mask:0xf bank_mask:0xf bound_ctrl:1
	v_add_f32_dpp v113, v47, v113 wave_shl:1 row_mask:0xf bank_mask:0xf bound_ctrl:1
	v_add_f32_dpp v114, v70, v114 wave_shl:1 row_mask:0xf bank_mask:0xf bound_ctrl:1
	v_add_f32_dpp v115, v71, v115 wave_shl:1 row_mask:0xf bank_mask:0xf bound_ctrl:1
	v_add_f32_dpp v128, v98, v128 wave_shl:1 row_mask:0xf bank_mask:0xf bound_ctrl:1
	v_add_f32_dpp v129, v99, v129 wave_shl:1 row_mask:0xf bank_mask:0xf bound_ctrl:1
	v_pk_add_f32 v[46:47], v[62:63], v[104:105]
	v_pk_add_f32 v[70:71], v[84:85], v[46:47]
	v_pk_add_f32 v[62:63], v[78:79], v[112:113]
	v_pk_add_f32 v[84:85], v[92:93], v[62:63]
	v_pk_add_f32 v[78:79], v[80:81], v[114:115]
	v_pk_add_f32 v[92:93], v[100:101], v[78:79]
	v_pk_add_f32 v[80:81], v[86:87], v[128:129]
	v_pk_add_f32 v[98:99], v[106:107], v[80:81]
	v_pk_fma_f32 v[84:85], v[116:117], v[70:71], v[84:85] op_sel_hi:[0,1,1] neg_lo:[1,0,0] neg_hi:[1,0,0]
	v_pk_fma_f32 v[92:93], v[116:117], v[70:71], v[92:93] op_sel:[1,0,0] neg_lo:[1,0,0] neg_hi:[1,0,0]
	v_pk_fma_f32 v[98:99], v[118:119], v[70:71], v[98:99] op_sel_hi:[0,1,1] neg_lo:[1,0,0] neg_hi:[1,0,0]
	v_pk_mul_f32 v[86:87], v[118:119], v[84:85] op_sel:[1,0]
	v_pk_mul_f32 v[100:101], v[120:121], v[84:85] op_sel_hi:[0,1]
	v_pk_mul_f32 v[106:107], v[120:121], v[84:85] op_sel:[1,0]
	v_pk_fma_f32 v[86:87], v[120:121], v[92:93], v[86:87] op_sel_hi:[0,1,1]
	v_pk_fma_f32 v[100:101], v[122:123], v[92:93], v[100:101] op_sel_hi:[0,1,1]
	v_pk_fma_f32 v[106:107], v[122:123], v[92:93], v[106:107] op_sel:[1,0,0]
	v_pk_fma_f32 v[86:87], v[120:121], v[98:99], v[86:87] op_sel:[1,0,0]
	v_pk_fma_f32 v[100:101], v[122:123], v[98:99], v[100:101] op_sel:[1,0,0]
	v_pk_fma_f32 v[106:107], v[124:125], v[98:99], v[106:107] op_sel_hi:[0,1,1]
	v_pk_mul_f32 v[130:131], v[116:117], v[86:87] op_sel_hi:[0,1]
	v_pk_fma_f32 v[130:131], v[116:117], v[100:101], v[130:131] op_sel:[1,0,0]
	v_pk_fma_f32 v[130:131], v[118:119], v[106:107], v[130:131] op_sel_hi:[0,1,1]
	v_pk_fma_f32 v[130:131], v[124:125], v[70:71], v[130:131] op_sel:[1,0,0] neg_lo:[0,0,1] neg_hi:[0,0,1]
	v_cmp_eq_u32_e64 s[10:11], 6, v127
	v_cmp_eq_u32_e64 s[14:15], 7, v127
	v_add_f32_dpp v70, v86, v86 wave_shr:1 row_mask:0xf bank_mask:0xf bound_ctrl:1
	v_add_f32_dpp v71, v87, v87 wave_shr:1 row_mask:0xf bank_mask:0xf bound_ctrl:1
	v_add_f32_dpp v84, v100, v100 wave_shr:1 row_mask:0xf bank_mask:0xf bound_ctrl:1
	v_add_f32_dpp v85, v101, v101 wave_shr:1 row_mask:0xf bank_mask:0xf bound_ctrl:1
	v_add_f32_dpp v92, v106, v106 wave_shr:1 row_mask:0xf bank_mask:0xf bound_ctrl:1
	v_add_f32_dpp v93, v107, v107 wave_shr:1 row_mask:0xf bank_mask:0xf bound_ctrl:1
	v_add_f32_dpp v98, v130, v130 wave_shr:1 row_mask:0xf bank_mask:0xf bound_ctrl:1
	v_add_f32_dpp v99, v131, v131 wave_shr:1 row_mask:0xf bank_mask:0xf bound_ctrl:1
	v_add_f32_dpp v70, v86, v70 wave_shl:1 row_mask:0xf bank_mask:0xf bound_ctrl:1
	v_add_f32_dpp v71, v87, v71 wave_shl:1 row_mask:0xf bank_mask:0xf bound_ctrl:1
	v_add_f32_dpp v84, v100, v84 wave_shl:1 row_mask:0xf bank_mask:0xf bound_ctrl:1
	v_add_f32_dpp v85, v101, v85 wave_shl:1 row_mask:0xf bank_mask:0xf bound_ctrl:1
	v_add_f32_dpp v92, v106, v92 wave_shl:1 row_mask:0xf bank_mask:0xf bound_ctrl:1
	v_add_f32_dpp v93, v107, v93 wave_shl:1 row_mask:0xf bank_mask:0xf bound_ctrl:1
	v_add_f32_dpp v98, v130, v98 wave_shl:1 row_mask:0xf bank_mask:0xf bound_ctrl:1
	v_add_f32_dpp v99, v131, v99 wave_shl:1 row_mask:0xf bank_mask:0xf bound_ctrl:1
	v_pk_add_f32 v[86:87], v[30:31], v[70:71]
	v_pk_add_f32 v[100:101], v[52:53], v[86:87]
	v_pk_add_f32 v[30:31], v[50:51], v[84:85]
	v_pk_add_f32 v[52:53], v[74:75], v[30:31]
	v_pk_add_f32 v[50:51], v[54:55], v[92:93]
	v_pk_add_f32 v[74:75], v[108:109], v[50:51]
	v_pk_add_f32 v[54:55], v[58:59], v[98:99]
	v_pk_add_f32 v[106:107], v[110:111], v[54:55]
	v_pk_fma_f32 v[106:107], v[40:41], v[100:101], v[106:107] op_sel_hi:[0,1,1]
	v_pk_fma_f32 v[106:107], v[40:41], v[52:53], v[106:107] op_sel:[1,0,0]
	v_pk_fma_f32 v[106:107], v[42:43], v[74:75], v[106:107] op_sel_hi:[0,1,1]
	v_cndmask_b32_e64 v58, 0, v18, s[10:11]
	v_cndmask_b32_e64 v59, 0, v18, s[14:15]
	v_pk_fma_f32 v[106:107], v[36:37], v[126:127], v[106:107] op_sel_hi:[1,0,1] neg_lo:[0,0,1] neg_hi:[0,0,1]
	s_add_i32 s4, s34, 6
	s_cmpk_lt_i32 s4, 0x201
	s_cselect_b64 s[12:13], s[0:1], 0
	v_pk_add_f32 v[106:107], v[106:107], v[58:59] neg_lo:[0,1] neg_hi:[0,1]
	v_pk_mul_f32 v[108:109], v[106:107], v[106:107]
	v_add_f32_e32 v108, v108, v109
	v_cndmask_b32_e64 v109, 0, v108, s[12:13]
	v_add_f32_e32 v1, v1, v109
	s_add_i32 s5, s34, 11
	s_min_i32 s5, s5, 0x200
	s_mul_i32 s6, s5, 0x804
	s_add_i32 s6, s6, s39
	s_add_i32 s7, s6, 0x101004
	s_mul_i32 s9, s5, 0x180c
	s_add_i32 s9, s9, s33
	s_add_i32 s4, s34, 12
	s_min_i32 s4, s4, 0x200
	s_mul_i32 s4, s4, 0x804
	s_add_i32 s4, s4, s38
	buffer_load_dword v16, v28, s[20:23], s4 offen nt
	buffer_load_dwordx3 v[40:42], v27, s[24:27], s9 offen nt
	buffer_load_dword v36, v28, s[16:19], s6 offen nt
	buffer_load_dword v37, v28, s[16:19], s7 offen nt
	s_waitcnt vmcnt(8)
	s_add_i32 s4, s34, 10
	s_cmpk_lt_u32 s4, 0x201
	s_cselect_b64 s[12:13], s[40:41], 0
	v_cmp_eq_u32_e64 s[14:15], s37, v2
	s_and_b64 s[14:15], s[14:15], s[12:13]
	v_cndmask_b32_e64 v29, 0, 1, s[14:15]
	v_mul_f32_e64 v52, v12, v12
	v_mul_f32_e64 v53, v12, v13
	v_mul_f32_e64 v58, v12, v14
	v_mul_f32_e64 v59, v13, v13
	v_mul_f32_e64 v74, v13, v14
	v_mul_f32_e64 v75, v14, v14
	v_or_b32_dpp v44, v29, v29 wave_shr:1 row_mask:0xf bank_mask:0xf bound_ctrl:1
	s_nop 1
	v_or_b32_dpp v44, v29, v44 wave_shl:1 row_mask:0xf bank_mask:0xf bound_ctrl:1
	s_nop 1
	v_or_b32_dpp v69, v44, v44 wave_shr:1 row_mask:0xf bank_mask:0xf bound_ctrl:1
	s_nop 1
	v_or_b32_dpp v69, v44, v69 wave_shl:1 row_mask:0xf bank_mask:0xf bound_ctrl:1
	v_or3_b32 v29, v69, v102, v103
	v_or3_b32 v29, v29, v45, v68
	s_add_i32 s4, s34, 7
	s_cmpk_lt_u32 s4, 0x1ff
	s_cselect_b64 s[12:13], s[42:43], 0
	v_cmp_ne_u32_e64 s[30:31], 0, v29
	s_and_b64 s[30:31], s[30:31], s[12:13]
	v_cndmask_b32_e64 v29, 0, 1.0, s[30:31]
	v_add_f32_dpp v100, v12, v12 wave_shr:1 row_mask:0xf bank_mask:0xf bound_ctrl:1
	v_add_f32_dpp v101, v13, v13 wave_shr:1 row_mask:0xf bank_mask:0xf bound_ctrl:1
	v_add_f32_dpp v106, v14, v14 wave_shr:1 row_mask:0xf bank_mask:0xf bound_ctrl:1
	v_add_f32_dpp v107, v52, v52 wave_shr:1 row_mask:0xf bank_mask:0xf bound_ctrl:1
	v_add_f32_dpp v108, v53, v53 wave_shr:1 row_mask:0xf bank_mask:0xf bound_ctrl:1
	v_add_f32_dpp v109, v58, v58 wave_shr:1 row_mask:0xf bank_mask:0xf bound_ctrl:1
	v_add_f32_dpp v110, v59, v59 wave_shr:1 row_mask:0xf bank_mask:0xf bound_ctrl:1
	v_add_f32_dpp v111, v74, v74 wave_shr:1 row_mask:0xf bank_mask:0xf bound_ctrl:1
	v_add_f32_dpp v116, v75, v75 wave_shr:1 row_mask:0xf bank_mask:0xf bound_ctrl:1
	v_add_f32_dpp v117, v29, v29 wave_shr:1 row_mask:0xf bank_mask:0xf bound_ctrl:1
	v_add_f32_dpp v100, v12, v100 wave_shl:1 row_mask:0xf bank_mask:0xf bound_ctrl:1
	v_add_f32_dpp v101, v13, v101 wave_shl:1 row_mask:0xf bank_mask:0xf bound_ctrl:1
	v_add_f32_dpp v106, v14, v106 wave_shl:1 row_mask:0xf bank_mask:0xf bound_ctrl:1
	v_add_f32_dpp v107, v52, v107 wave_shl:1 row_mask:0xf bank_mask:0xf bound_ctrl:1
	v_add_f32_dpp v108, v53, v108 wave_shl:1 row_mask:0xf bank_mask:0xf bound_ctrl:1
	v_add_f32_dpp v109, v58, v109 wave_shl:1 row_mask:0xf bank_mask:0xf bound_ctrl:1
	v_add_f32_dpp v110, v59, v110 wave_shl:1 row_mask:0xf bank_mask:0xf bound_ctrl:1
	v_add_f32_dpp v111, v74, v111 wave_shl:1 row_mask:0xf bank_mask:0xf bound_ctrl:1
	v_add_f32_dpp v116, v75, v116 wave_shl:1 row_mask:0xf bank_mask:0xf bound_ctrl:1
	v_add_f32_dpp v117, v29, v117 wave_shl:1 row_mask:0xf bank_mask:0xf bound_ctrl:1
	v_pk_add_f32 v[52:53], v[38:39], v[100:101]
	v_pk_add_f32 v[38:39], v[48:49], v[106:107]
	v_pk_add_f32 v[48:49], v[72:73], v[108:109]
	v_pk_add_f32 v[58:59], v[94:95], v[110:111]
	v_pk_add_f32 v[72:73], v[96:97], v[116:117]
	v_mul_f32_e64 v120, v52, v22
	v_mul_f32_e64 v121, v53, v22
	v_mul_f32_e64 v122, v38, v22
	v_fma_f32 v29, v39, v22, v26
	v_mul_f32_e64 v44, v48, v22
	v_mul_f32_e64 v74, v49, v22
	v_fma_f32 v75, v58, v22, v26
	v_mul_f32_e64 v94, v59, v22
	v_fma_f32 v95, v72, v22, v26
	v_fma_f32 v29, -v120, v120, v29
	v_fma_f32 v44, -v120, v121, v44
	v_fma_f32 v74, -v120, v122, v74
	v_fma_f32 v75, -v121, v121, v75
	v_fma_f32 v94, -v121, v122, v94
	v_fma_f32 v95, -v122, v122, v95
	v_mul_f32_e64 v96, v94, v94
	v_mul_f32_e64 v97, v44, v95
	v_mul_f32_e64 v118, v74, v75
	v_mul_f32_e64 v119, v74, v74
	v_mul_f32_e64 v130, v29, v94
	v_mul_f32_e64 v131, v44, v44
	v_fma_f32 v96, v75, v95, -v96
	v_fma_f32 v97, v74, v94, -v97
	v_fma_f32 v118, v44, v94, -v118
	v_fma_f32 v119, v29, v95, -v119
	v_fma_f32 v130, v44, v74, -v130
	v_fma_f32 v131, v29, v75, -v131
	v_mul_f32_e64 v136, v29, v96
	v_fma_f32 v136, v44, v97, v136
	v_fma_f32 v136, v74, v118, v136
	v_rcp_f32_e32 v136, v136
	v_cmp_ne_u32_e64 vcc, s37, v25
	v_mul_f32_e64 v136, v136, v22
	v_cndmask_b32_e64 v136, 0, v136, s[30:31]
	v_cndmask_b32_e64 v29, 0, v18, vcc
	v_cndmask_b32_e64 v133, 0, v22, s[30:31]
	v_mul_f32_e64 v123, v96, v136
	v_mul_f32_e64 v124, v97, v136
	v_mul_f32_e64 v125, v118, v136
	v_mul_f32_e64 v126, v119, v136
	v_mul_f32_e64 v127, v130, v136
	v_mul_f32_e64 v132, v131, v136
	v_add_f32_e64 v134, v73, v29
	v_mov_b32_e32 v135, v25
	ds_write_b128 v23, v[120:123] offset:3072
	ds_write_b128 v23, v[124:127] offset:4096
	ds_write_b128 v23, v[132:135] offset:5120
	s_waitcnt lgkmcnt(0)
	s_barrier
	v_pk_mul_f32 v[38:39], v[6:7], v[12:13] op_sel_hi:[1,0]
	v_pk_mul_f32 v[48:49], v[6:7], v[12:13] op_sel:[0,1]
	v_pk_mul_f32 v[52:53], v[6:7], v[14:15] op_sel_hi:[1,0]
	v_add_f32_dpp v58, v6, v6 wave_shr:1 row_mask:0xf bank_mask:0xf bound_ctrl:1
	v_add_f32_dpp v59, v7, v7 wave_shr:1 row_mask:0xf bank_mask:0xf bound_ctrl:1
	v_add_f32_dpp v72, v38, v38 wave_shr:1 row_mask:0xf bank_mask:0xf bound_ctrl:1
	v_add_f32_dpp v73, v39, v39 wave_shr:1 row_mask:0xf bank_mask:0xf bound_ctrl:1
	v_add_f32_dpp v74, v48, v48 wave_shr:1 row_mask:0xf bank_mask:0xf bound_ctrl:1
	v_add_f32_dpp v75, v49, v49 wave_shr:1 row_mask:0xf bank_mask:0xf bound_ctrl:1
	v_add_f32_dpp v94, v52, v52 wave_shr:1 row_mask:0xf bank_mask:0xf bound_ctrl:1
	v_add_f32_dpp v95, v53, v53 wave_shr:1 row_mask:0xf bank_mask:0xf bound_ctrl:1
	v_add_f32_dpp v58, v6, v58 wave_shl:1 row_mask:0xf bank_mask:0xf bound_ctrl:1
	v_add_f32_dpp v59, v7, v59 wave_shl:1 row_mask:0xf bank_mask:0xf bound_ctrl:1
	v_add_f32_dpp v72, v38, v72 wave_shl:1 row_mask:0xf bank_mask:0xf bound_ctrl:1
	v_add_f32_dpp v73, v39, v73 wave_shl:1 row_mask:0xf bank_mask:0xf bound_ctrl:1
	v_add_f32_dpp v74, v48, v74 wave_shl:1 row_mask:0xf bank_mask:0xf bound_ctrl:1
	v_add_f32_dpp v75, v49, v75 wave_shl:1 row_mask:0xf bank_mask:0xf bound_ctrl:1
	v_add_f32_dpp v94, v52, v94 wave_shl:1 row_mask:0xf bank_mask:0xf bound_ctrl:1
	v_add_f32_dpp v95, v53, v95 wave_shl:1 row_mask:0xf bank_mask:0xf bound_ctrl:1
	v_pk_add_f32 v[38:39], v[46:47], v[58:59]
	v_pk_add_f32 v[46:47], v[62:63], v[72:73]
	v_pk_add_f32 v[48:49], v[78:79], v[74:75]
	v_pk_add_f32 v[52:53], v[80:81], v[94:95]
	v_pk_fma_f32 v[46:47], v[120:121], v[38:39], v[46:47] op_sel_hi:[0,1,1] neg_lo:[1,0,0] neg_hi:[1,0,0]
	v_pk_fma_f32 v[48:49], v[120:121], v[38:39], v[48:49] op_sel:[1,0,0] neg_lo:[1,0,0] neg_hi:[1,0,0]
	v_pk_fma_f32 v[52:53], v[122:123], v[38:39], v[52:53] op_sel_hi:[0,1,1] neg_lo:[1,0,0] neg_hi:[1,0,0]
	v_pk_mul_f32 v[62:63], v[122:123], v[46:47] op_sel:[1,0]
	v_pk_mul_f32 v[78:79], v[124:125], v[46:47] op_sel_hi:[0,1]
	v_pk_mul_f32 v[80:81], v[124:125], v[46:47] op_sel:[1,0]
	v_pk_fma_f32 v[62:63], v[124:125], v[48:49], v[62:63] op_sel_hi:[0,1,1]
	v_pk_fma_f32 v[78:79], v[126:127], v[48:49], v[78:79] op_sel_hi:[0,1,1]
	v_pk_fma_f32 v[80:81], v[126:127], v[48:49], v[80:81] op_sel:[1,0,0]
	v_pk_fma_f32 v[62:63], v[124:125], v[52:53], v[62:63] op_sel:[1,0,0]
	v_pk_fma_f32 v[78:79], v[126:127], v[52:53], v[78:79] op_sel:[1,0,0]
	v_pk_fma_f32 v[80:81], v[132:133], v[52:53], v[80:81] op_sel_hi:[0,1,1]
	v_pk_mul_f32 v[96:97], v[120:121], v[62:63] op_sel_hi:[0,1]
	v_pk_fma_f32 v[96:97], v[120:121], v[78:79], v[96:97] op_sel:[1,0,0]
	v_pk_fma_f32 v[96:97], v[122:123], v[80:81], v[96:97] op_sel_hi:[0,1,1]
	v_pk_fma_f32 v[96:97], v[132:133], v[38:39], v[96:97] op_sel:[1,0,0] neg_lo:[0,0,1] neg_hi:[0,0,1]
	v_cmp_eq_u32_e64 s[10:11], 6, v135
	v_cmp_eq_u32_e64 s[14:15], 7, v135
	v_add_f32_dpp v38, v62, v62 wave_shr:1 row_mask:0xf bank_mask:0xf bound_ctrl:1
	v_add_f32_dpp v39, v63, v63 wave_shr:1 row_mask:0xf bank_mask:0xf bound_ctrl:1
	v_add_f32_dpp v46, v78, v78 wave_shr:1 row_mask:0xf bank_mask:0xf bound_ctrl:1
	v_add_f32_dpp v47, v79, v79 wave_shr:1 row_mask:0xf bank_mask:0xf bound_ctrl:1
	v_add_f32_dpp v48, v80, v80 wave_shr:1 row_mask:0xf bank_mask:0xf bound_ctrl:1
	v_add_f32_dpp v49, v81, v81 wave_shr:1 row_mask:0xf bank_mask:0xf bound_ctrl:1
	v_add_f32_dpp v52, v96, v96 wave_shr:1 row_mask:0xf bank_mask:0xf bound_ctrl:1
	v_add_f32_dpp v53, v97, v97 wave_shr:1 row_mask:0xf bank_mask:0xf bound_ctrl:1
	v_add_f32_dpp v38, v62, v38 wave_shl:1 row_mask:0xf bank_mask:0xf bound_ctrl:1
	v_add_f32_dpp v39, v63, v39 wave_shl:1 row_mask:0xf bank_mask:0xf bound_ctrl:1
	v_add_f32_dpp v46, v78, v46 wave_shl:1 row_mask:0xf bank_mask:0xf bound_ctrl:1
	v_add_f32_dpp v47, v79, v47 wave_shl:1 row_mask:0xf bank_mask:0xf bound_ctrl:1
	v_add_f32_dpp v48, v80, v48 wave_shl:1 row_mask:0xf bank_mask:0xf bound_ctrl:1
	v_add_f32_dpp v49, v81, v49 wave_shl:1 row_mask:0xf bank_mask:0xf bound_ctrl:1
	v_add_f32_dpp v52, v96, v52 wave_shl:1 row_mask:0xf bank_mask:0xf bound_ctrl:1
	v_add_f32_dpp v53, v97, v53 wave_shl:1 row_mask:0xf bank_mask:0xf bound_ctrl:1
	v_pk_add_f32 v[62:63], v[86:87], v[38:39]
	v_pk_add_f32 v[78:79], v[30:31], v[46:47]
	v_pk_add_f32 v[30:31], v[50:51], v[48:49]
	v_pk_add_f32 v[50:51], v[54:55], v[52:53]
	v_pk_fma_f32 v[50:51], v[64:65], v[62:63], v[50:51] op_sel_hi:[0,1,1]
	v_pk_fma_f32 v[50:51], v[64:65], v[78:79], v[50:51] op_sel:[1,0,0]
	v_pk_fma_f32 v[50:51], v[66:67], v[30:31], v[50:51] op_sel_hi:[0,1,1]
	v_cndmask_b32_e64 v54, 0, v18, s[10:11]
	v_cndmask_b32_e64 v55, 0, v18, s[14:15]
	v_pk_fma_f32 v[50:51], v[56:57], v[134:135], v[50:51] op_sel_hi:[1,0,1] neg_lo:[0,0,1] neg_hi:[0,0,1]
	s_add_i32 s4, s34, 7
	s_cmpk_lt_i32 s4, 0x201
	s_cselect_b64 s[12:13], s[0:1], 0
	v_pk_add_f32 v[50:51], v[50:51], v[54:55] neg_lo:[0,1] neg_hi:[0,1]
	v_pk_mul_f32 v[80:81], v[50:51], v[50:51]
	v_add_f32_e32 v80, v80, v81
	v_cndmask_b32_e64 v81, 0, v80, s[12:13]
	v_add_f32_e32 v1, v1, v81
	s_waitcnt vmcnt(4)
	s_add_i32 s4, s34, 11
	s_cmpk_lt_u32 s4, 0x201
	s_cselect_b64 s[12:13], s[40:41], 0
	v_cmp_eq_u32_e64 s[14:15], s37, v3
	s_and_b64 s[14:15], s[14:15], s[12:13]
	v_cndmask_b32_e64 v25, 0, 1, s[14:15]
	v_mul_f32_e64 v30, v32, v32
	v_mul_f32_e64 v31, v32, v33
	v_mul_f32_e64 v50, v32, v34
	v_mul_f32_e64 v51, v33, v33
	v_mul_f32_e64 v54, v33, v34
	v_mul_f32_e64 v55, v34, v34
	v_or_b32_dpp v29, v25, v25 wave_shr:1 row_mask:0xf bank_mask:0xf bound_ctrl:1
	s_nop 1
	v_or_b32_dpp v29, v25, v29 wave_shl:1 row_mask:0xf bank_mask:0xf bound_ctrl:1
	s_nop 1
	v_or_b32_dpp v44, v29, v29 wave_shr:1 row_mask:0xf bank_mask:0xf bound_ctrl:1
	s_nop 1
	v_or_b32_dpp v44, v29, v44 wave_shl:1 row_mask:0xf bank_mask:0xf bound_ctrl:1
	v_or3_b32 v25, v44, v69, v102
	v_or3_b32 v25, v25, v103, v45
	s_add_i32 s4, s34, 8
	s_cmpk_lt_u32 s4, 0x1ff
	s_cselect_b64 s[12:13], s[42:43], 0
	v_cmp_ne_u32_e64 s[30:31], 0, v25
	s_and_b64 s[30:31], s[30:31], s[12:13]
	v_cndmask_b32_e64 v25, 0, 1.0, s[30:31]
	v_add_f32_dpp v56, v32, v32 wave_shr:1 row_mask:0xf bank_mask:0xf bound_ctrl:1
	v_add_f32_dpp v57, v33, v33 wave_shr:1 row_mask:0xf bank_mask:0xf bound_ctrl:1
	v_add_f32_dpp v62, v34, v34 wave_shr:1 row_mask:0xf bank_mask:0xf bound_ctrl:1
	v_add_f32_dpp v63, v30, v30 wave_shr:1 row_mask:0xf bank_mask:0xf bound_ctrl:1
	v_add_f32_dpp v64, v31, v31 wave_shr:1 row_mask:0xf bank_mask:0xf bound_ctrl:1
	v_add_f32_dpp v65, v50, v50 wave_shr:1 row_mask:0xf bank_mask:0xf bound_ctrl:1
	v_add_f32_dpp v66, v51, v51 wave_shr:1 row_mask:0xf bank_mask:0xf bound_ctrl:1
	v_add_f32_dpp v67, v54, v54 wave_shr:1 row_mask:0xf bank_mask:0xf bound_ctrl:1
	v_add_f32_dpp v78, v55, v55 wave_shr:1 row_mask:0xf bank_mask:0xf bound_ctrl:1
	v_add_f32_dpp v79, v25, v25 wave_shr:1 row_mask:0xf bank_mask:0xf bound_ctrl:1
	v_add_f32_dpp v56, v32, v56 wave_shl:1 row_mask:0xf bank_mask:0xf bound_ctrl:1
	v_add_f32_dpp v57, v33, v57 wave_shl:1 row_mask:0xf bank_mask:0xf bound_ctrl:1
	v_add_f32_dpp v62, v34, v62 wave_shl:1 row_mask:0xf bank_mask:0xf bound_ctrl:1
	v_add_f32_dpp v63, v30, v63 wave_shl:1 row_mask:0xf bank_mask:0xf bound_ctrl:1
	v_add_f32_dpp v64, v31, v64 wave_shl:1 row_mask:0xf bank_mask:0xf bound_ctrl:1
	v_add_f32_dpp v65, v50, v65 wave_shl:1 row_mask:0xf bank_mask:0xf bound_ctrl:1
	v_add_f32_dpp v66, v51, v66 wave_shl:1 row_mask:0xf bank_mask:0xf bound_ctrl:1
	v_add_f32_dpp v67, v54, v67 wave_shl:1 row_mask:0xf bank_mask:0xf bound_ctrl:1
	v_add_f32_dpp v78, v55, v78 wave_shl:1 row_mask:0xf bank_mask:0xf bound_ctrl:1
	v_add_f32_dpp v79, v25, v79 wave_shl:1 row_mask:0xf bank_mask:0xf bound_ctrl:1
	v_pk_add_f32 v[30:31], v[100:101], v[56:57]
	v_pk_add_f32 v[50:51], v[60:61], v[30:31]
	v_pk_add_f32 v[54:55], v[106:107], v[62:63]
	v_pk_add_f32 v[60:61], v[76:77], v[54:55]
	v_pk_add_f32 v[76:77], v[108:109], v[64:65]
	v_pk_add_f32 v[80:81], v[82:83], v[76:77]
	v_pk_add_f32 v[82:83], v[110:111], v[66:67]
	v_pk_add_f32 v[86:87], v[88:89], v[82:83]
	v_pk_add_f32 v[88:89], v[116:117], v[78:79]
	v_pk_add_f32 v[96:97], v[90:91], v[88:89]
	v_mul_f32_e64 v108, v50, v22
	v_mul_f32_e64 v109, v51, v22
	v_mul_f32_e64 v110, v60, v22
	v_fma_f32 v25, v61, v22, v26
	v_mul_f32_e64 v29, v80, v22
	v_mul_f32_e64 v68, v81, v22
	v_fma_f32 v90, v86, v22, v26
	v_mul_f32_e64 v91, v87, v22
	v_fma_f32 v100, v96, v22, v26
	v_fma_f32 v25, -v108, v108, v25
	v_fma_f32 v29, -v108, v109, v29
	v_fma_f32 v68, -v108, v110, v68
	v_fma_f32 v90, -v109, v109, v90
	v_fma_f32 v91, -v109, v110, v91
	v_fma_f32 v100, -v110, v110, v100
	v_mul_f32_e64 v101, v91, v91
	v_mul_f32_e64 v106, v29, v100
	v_mul_f32_e64 v107, v68, v90
	v_mul_f32_e64 v124, v68, v68
	v_mul_f32_e64 v125, v25, v91
	v_mul_f32_e64 v126, v29, v29
	v_fma_f32 v101, v90, v100, -v101
	v_fma_f32 v106, v68, v91, -v106
	v_fma_f32 v107, v29, v91, -v107
	v_fma_f32 v124, v25, v100, -v124
	v_fma_f32 v125, v29, v68, -v125
	v_fma_f32 v126, v25, v90, -v126
	v_mul_f32_e64 v127, v25, v101
	v_fma_f32 v127, v29, v106, v127
	v_fma_f32 v127, v68, v107, v127
	v_rcp_f32_e32 v127, v127
	v_cmp_ne_u32_e64 vcc, s37, v24
	v_mul_f32_e64 v127, v127, v22
	v_cndmask_b32_e64 v127, 0, v127, s[30:31]
	v_cndmask_b32_e64 v25, 0, v18, vcc
	v_cndmask_b32_e64 v121, 0, v22, s[30:31]
	v_mul_f32_e64 v111, v101, v127
	v_mul_f32_e64 v116, v106, v127
	v_mul_f32_e64 v117, v107, v127
	v_mul_f32_e64 v118, v124, v127
	v_mul_f32_e64 v119, v125, v127
	v_mul_f32_e64 v120, v126, v127
	v_add_f32_e64 v122, v97, v25
	v_mov_b32_e32 v123, v24
	ds_write_b128 v23, v[108:111]
	ds_write_b128 v23, v[116:119] offset:1024
	ds_write_b128 v23, v[120:123] offset:2048
	s_waitcnt lgkmcnt(0)
	s_barrier
	v_pk_mul_f32 v[24:25], v[20:21], v[32:33] op_sel_hi:[1,0]
	v_pk_mul_f32 v[50:51], v[20:21], v[32:33] op_sel:[0,1]
	v_pk_mul_f32 v[60:61], v[20:21], v[34:35] op_sel_hi:[1,0]
	v_add_f32_dpp v80, v20, v20 wave_shr:1 row_mask:0xf bank_mask:0xf bound_ctrl:1
	v_add_f32_dpp v81, v21, v21 wave_shr:1 row_mask:0xf bank_mask:0xf bound_ctrl:1
	v_add_f32_dpp v86, v24, v24 wave_shr:1 row_mask:0xf bank_mask:0xf bound_ctrl:1
	v_add_f32_dpp v87, v25, v25 wave_shr:1 row_mask:0xf bank_mask:0xf bound_ctrl:1
	v_add_f32_dpp v90, v50, v50 wave_shr:1 row_mask:0xf bank_mask:0xf bound_ctrl:1
	v_add_f32_dpp v91, v51, v51 wave_shr:1 row_mask:0xf bank_mask:0xf bound_ctrl:1
	v_add_f32_dpp v96, v60, v60 wave_shr:1 row_mask:0xf bank_mask:0xf bound_ctrl:1
	v_add_f32_dpp v97, v61, v61 wave_shr:1 row_mask:0xf bank_mask:0xf bound_ctrl:1
	v_add_f32_dpp v80, v20, v80 wave_shl:1 row_mask:0xf bank_mask:0xf bound_ctrl:1
	v_add_f32_dpp v81, v21, v81 wave_shl:1 row_mask:0xf bank_mask:0xf bound_ctrl:1
	v_add_f32_dpp v86, v24, v86 wave_shl:1 row_mask:0xf bank_mask:0xf bound_ctrl:1
	v_add_f32_dpp v87, v25, v87 wave_shl:1 row_mask:0xf bank_mask:0xf bound_ctrl:1
	v_add_f32_dpp v90, v50, v90 wave_shl:1 row_mask:0xf bank_mask:0xf bound_ctrl:1
	v_add_f32_dpp v91, v51, v91 wave_shl:1 row_mask:0xf bank_mask:0xf bound_ctrl:1
	v_add_f32_dpp v96, v60, v96 wave_shl:1 row_mask:0xf bank_mask:0xf bound_ctrl:1
	v_add_f32_dpp v97, v61, v97 wave_shl:1 row_mask:0xf bank_mask:0xf bound_ctrl:1
	v_pk_add_f32 v[24:25], v[58:59], v[80:81]
	v_pk_add_f32 v[50:51], v[104:105], v[24:25]
	v_pk_add_f32 v[58:59], v[72:73], v[86:87]
	v_pk_add_f32 v[60:61], v[112:113], v[58:59]
	v_pk_add_f32 v[72:73], v[74:75], v[90:91]
	v_pk_add_f32 v[100:101], v[114:115], v[72:73]
	v_pk_add_f32 v[74:75], v[94:95], v[96:97]
	v_pk_add_f32 v[104:105], v[128:129], v[74:75]
	v_pk_fma_f32 v[60:61], v[108:109], v[50:51], v[60:61] op_sel_hi:[0,1,1] neg_lo:[1,0,0] neg_hi:[1,0,0]
	v_pk_fma_f32 v[100:101], v[108:109], v[50:51], v[100:101] op_sel:[1,0,0] neg_lo:[1,0,0] neg_hi:[1,0,0]
	v_pk_fma_f32 v[104:105], v[110:111], v[50:51], v[104:105] op_sel_hi:[0,1,1] neg_lo:[1,0,0] neg_hi:[1,0,0]
	v_pk_mul_f32 v[94:95], v[110:111], v[60:61] op_sel:[1,0]
	v_pk_mul_f32 v[106:107], v[116:117], v[60:61] op_sel_hi:[0,1]
	v_pk_mul_f32 v[112:113], v[116:117], v[60:61] op_sel:[1,0]
	v_pk_fma_f32 v[94:95], v[116:117], v[100:101], v[94:95] op_sel_hi:[0,1,1]
	v_pk_fma_f32 v[106:107], v[118:119], v[100:101], v[106:107] op_sel_hi:[0,1,1]
	v_pk_fma_f32 v[112:113], v[118:119], v[100:101], v[112:113] op_sel:[1,0,0]
	v_pk_fma_f32 v[94:95], v[116:117], v[104:105], v[94:95] op_sel:[1,0,0]
	v_pk_fma_f32 v[106:107], v[118:119], v[104:105], v[106:107] op_sel:[1,0,0]
	v_pk_fma_f32 v[112:113], v[120:121], v[104:105], v[112:113] op_sel_hi:[0,1,1]
	v_pk_mul_f32 v[114:115], v[108:109], v[94:95] op_sel_hi:[0,1]
	v_pk_fma_f32 v[114:115], v[108:109], v[106:107], v[114:115] op_sel:[1,0,0]
	v_pk_fma_f32 v[114:115], v[110:111], v[112:113], v[114:115] op_sel_hi:[0,1,1]
	v_pk_fma_f32 v[114:115], v[120:121], v[50:51], v[114:115] op_sel:[1,0,0] neg_lo:[0,0,1] neg_hi:[0,0,1]
	v_cmp_eq_u32_e64 s[10:11], 6, v123
	v_cmp_eq_u32_e64 s[14:15], 7, v123
	v_add_f32_dpp v50, v94, v94 wave_shr:1 row_mask:0xf bank_mask:0xf bound_ctrl:1
	v_add_f32_dpp v51, v95, v95 wave_shr:1 row_mask:0xf bank_mask:0xf bound_ctrl:1
	v_add_f32_dpp v60, v106, v106 wave_shr:1 row_mask:0xf bank_mask:0xf bound_ctrl:1
	v_add_f32_dpp v61, v107, v107 wave_shr:1 row_mask:0xf bank_mask:0xf bound_ctrl:1
	v_add_f32_dpp v100, v112, v112 wave_shr:1 row_mask:0xf bank_mask:0xf bound_ctrl:1
	v_add_f32_dpp v101, v113, v113 wave_shr:1 row_mask:0xf bank_mask:0xf bound_ctrl:1
	v_add_f32_dpp v104, v114, v114 wave_shr:1 row_mask:0xf bank_mask:0xf bound_ctrl:1
	v_add_f32_dpp v105, v115, v115 wave_shr:1 row_mask:0xf bank_mask:0xf bound_ctrl:1
	v_add_f32_dpp v50, v94, v50 wave_shl:1 row_mask:0xf bank_mask:0xf bound_ctrl:1
	v_add_f32_dpp v51, v95, v51 wave_shl:1 row_mask:0xf bank_mask:0xf bound_ctrl:1
	v_add_f32_dpp v60, v106, v60 wave_shl:1 row_mask:0xf bank_mask:0xf bound_ctrl:1
	v_add_f32_dpp v61, v107, v61 wave_shl:1 row_mask:0xf bank_mask:0xf bound_ctrl:1
	v_add_f32_dpp v100, v112, v100 wave_shl:1 row_mask:0xf bank_mask:0xf bound_ctrl:1
	v_add_f32_dpp v101, v113, v101 wave_shl:1 row_mask:0xf bank_mask:0xf bound_ctrl:1
	v_add_f32_dpp v104, v114, v104 wave_shl:1 row_mask:0xf bank_mask:0xf bound_ctrl:1
	v_add_f32_dpp v105, v115, v105 wave_shl:1 row_mask:0xf bank_mask:0xf bound_ctrl:1
	v_pk_add_f32 v[94:95], v[38:39], v[50:51]
	v_pk_add_f32 v[106:107], v[70:71], v[94:95]
	v_pk_add_f32 v[38:39], v[46:47], v[60:61]
	v_pk_add_f32 v[70:71], v[84:85], v[38:39]
	v_pk_add_f32 v[46:47], v[48:49], v[100:101]
	v_pk_add_f32 v[84:85], v[92:93], v[46:47]
	v_pk_add_f32 v[48:49], v[52:53], v[104:105]
	v_pk_add_f32 v[92:93], v[98:99], v[48:49]
	v_pk_fma_f32 v[92:93], v[8:9], v[106:107], v[92:93] op_sel_hi:[0,1,1]
	v_pk_fma_f32 v[92:93], v[8:9], v[70:71], v[92:93] op_sel:[1,0,0]
	v_pk_fma_f32 v[92:93], v[10:11], v[84:85], v[92:93] op_sel_hi:[0,1,1]
	v_cndmask_b32_e64 v52, 0, v18, s[10:11]
	v_cndmask_b32_e64 v53, 0, v18, s[14:15]
	v_pk_fma_f32 v[92:93], v[4:5], v[122:123], v[92:93] op_sel_hi:[1,0,1] neg_lo:[0,0,1] neg_hi:[0,0,1]
	s_add_i32 s4, s34, 8
	s_cmpk_lt_i32 s4, 0x201
	s_cselect_b64 s[12:13], s[0:1], 0
	v_pk_add_f32 v[92:93], v[92:93], v[52:53] neg_lo:[0,1] neg_hi:[0,1]
	v_pk_mul_f32 v[98:99], v[92:93], v[92:93]
	v_add_f32_e32 v98, v98, v99
	v_cndmask_b32_e64 v99, 0, v98, s[12:13]
	v_add_f32_e32 v1, v1, v99
	s_waitcnt vmcnt(0)
	s_add_i32 s4, s34, 12
	s_cmpk_lt_u32 s4, 0x201
	s_cselect_b64 s[12:13], s[40:41], 0
	v_cmp_eq_u32_e64 s[14:15], s37, v16
	s_and_b64 s[14:15], s[14:15], s[12:13]
	v_cndmask_b32_e64 v29, 0, 1, s[14:15]
	v_mul_f32_e64 v4, v40, v40
	v_mul_f32_e64 v5, v40, v41
	v_mul_f32_e64 v8, v40, v42
	v_mul_f32_e64 v9, v41, v41
	v_mul_f32_e64 v10, v41, v42
	v_mul_f32_e64 v11, v42, v42
	v_or_b32_dpp v45, v29, v29 wave_shr:1 row_mask:0xf bank_mask:0xf bound_ctrl:1
	s_nop 1
	v_or_b32_dpp v45, v29, v45 wave_shl:1 row_mask:0xf bank_mask:0xf bound_ctrl:1
	s_nop 1
	v_or_b32_dpp v68, v45, v45 wave_shr:1 row_mask:0xf bank_mask:0xf bound_ctrl:1
	s_nop 1
	v_or_b32_dpp v68, v45, v68 wave_shl:1 row_mask:0xf bank_mask:0xf bound_ctrl:1
	v_or3_b32 v29, v68, v44, v69
	v_or3_b32 v29, v29, v102, v103
	s_add_i32 s4, s34, 9
	s_cmpk_lt_u32 s4, 0x1ff
	s_cselect_b64 s[12:13], s[42:43], 0
	v_cmp_ne_u32_e64 s[30:31], 0, v29
	s_and_b64 s[30:31], s[30:31], s[12:13]
	v_cndmask_b32_e64 v29, 0, 1.0, s[30:31]
	v_add_f32_dpp v52, v40, v40 wave_shr:1 row_mask:0xf bank_mask:0xf bound_ctrl:1
	v_add_f32_dpp v53, v41, v41 wave_shr:1 row_mask:0xf bank_mask:0xf bound_ctrl:1
	v_add_f32_dpp v70, v42, v42 wave_shr:1 row_mask:0xf bank_mask:0xf bound_ctrl:1
	v_add_f32_dpp v71, v4, v4 wave_shr:1 row_mask:0xf bank_mask:0xf bound_ctrl:1
	v_add_f32_dpp v84, v5, v5 wave_shr:1 row_mask:0xf bank_mask:0xf bound_ctrl:1
	v_add_f32_dpp v85, v8, v8 wave_shr:1 row_mask:0xf bank_mask:0xf bound_ctrl:1
	v_add_f32_dpp v92, v9, v9 wave_shr:1 row_mask:0xf bank_mask:0xf bound_ctrl:1
	v_add_f32_dpp v93, v10, v10 wave_shr:1 row_mask:0xf bank_mask:0xf bound_ctrl:1
	v_add_f32_dpp v98, v11, v11 wave_shr:1 row_mask:0xf bank_mask:0xf bound_ctrl:1
	v_add_f32_dpp v99, v29, v29 wave_shr:1 row_mask:0xf bank_mask:0xf bound_ctrl:1
	v_add_f32_dpp v52, v40, v52 wave_shl:1 row_mask:0xf bank_mask:0xf bound_ctrl:1
	v_add_f32_dpp v53, v41, v53 wave_shl:1 row_mask:0xf bank_mask:0xf bound_ctrl:1
	v_add_f32_dpp v70, v42, v70 wave_shl:1 row_mask:0xf bank_mask:0xf bound_ctrl:1
	v_add_f32_dpp v71, v4, v71 wave_shl:1 row_mask:0xf bank_mask:0xf bound_ctrl:1
	v_add_f32_dpp v84, v5, v84 wave_shl:1 row_mask:0xf bank_mask:0xf bound_ctrl:1
	v_add_f32_dpp v85, v8, v85 wave_shl:1 row_mask:0xf bank_mask:0xf bound_ctrl:1
	v_add_f32_dpp v92, v9, v92 wave_shl:1 row_mask:0xf bank_mask:0xf bound_ctrl:1
	v_add_f32_dpp v93, v10, v93 wave_shl:1 row_mask:0xf bank_mask:0xf bound_ctrl:1
	v_add_f32_dpp v98, v11, v98 wave_shl:1 row_mask:0xf bank_mask:0xf bound_ctrl:1
	v_add_f32_dpp v99, v29, v99 wave_shl:1 row_mask:0xf bank_mask:0xf bound_ctrl:1
	v_pk_add_f32 v[4:5], v[30:31], v[52:53]
	v_pk_add_f32 v[8:9], v[54:55], v[70:71]
	v_pk_add_f32 v[10:11], v[76:77], v[84:85]
	v_pk_add_f32 v[30:31], v[82:83], v[92:93]
	v_pk_add_f32 v[54:55], v[88:89], v[98:99]
	v_mul_f32_e64 v108, v4, v22
	v_mul_f32_e64 v109, v5, v22
	v_mul_f32_e64 v110, v8, v22
	v_fma_f32 v29, v9, v22, v26
	v_mul_f32_e64 v45, v10, v22
	v_mul_f32_e64 v76, v11, v22
	v_fma_f32 v77, v30, v22, v26
	v_mul_f32_e64 v82, v31, v22
	v_fma_f32 v83, v54, v22, v26
	v_fma_f32 v29, -v108, v108, v29
	v_fma_f32 v45, -v108, v109, v45
	v_fma_f32 v76, -v108, v110, v76
	v_fma_f32 v77, -v109, v109, v77
	v_fma_f32 v82, -v109, v110, v82
	v_fma_f32 v83, -v110, v110, v83
	v_mul_f32_e64 v88, v82, v82
	v_mul_f32_e64 v89, v45, v83
	v_mul_f32_e64 v106, v76, v77
	v_mul_f32_e64 v107, v76, v76
	v_mul_f32_e64 v120, v29, v82
	v_mul_f32_e64 v121, v45, v45
	v_fma_f32 v88, v77, v83, -v88
	v_fma_f32 v89, v76, v82, -v89
	v_fma_f32 v106, v45, v82, -v106
	v_fma_f32 v107, v29, v83, -v107
	v_fma_f32 v120, v45, v76, -v120
	v_fma_f32 v121, v29, v77, -v121
	v_mul_f32_e64 v122, v29, v88
	v_fma_f32 v122, v45, v89, v122
	v_fma_f32 v122, v76, v106, v122
	v_rcp_f32_e32 v122, v122
	v_cmp_ne_u32_e64 vcc, s37, v17
	v_mul_f32_e64 v122, v122, v22
	v_cndmask_b32_e64 v122, 0, v122, s[30:31]
	v_cndmask_b32_e64 v29, 0, v18, vcc
	v_cndmask_b32_e64 v117, 0, v22, s[30:31]
	v_mul_f32_e64 v111, v88, v122
	v_mul_f32_e64 v112, v89, v122
	v_mul_f32_e64 v113, v106, v122
	v_mul_f32_e64 v114, v107, v122
	v_mul_f32_e64 v115, v120, v122
	v_mul_f32_e64 v116, v121, v122
	v_add_f32_e64 v118, v55, v29
	v_mov_b32_e32 v119, v17
	ds_write_b128 v23, v[108:111] offset:3072
	ds_write_b128 v23, v[112:115] offset:4096
	ds_write_b128 v23, v[116:119] offset:5120
	s_waitcnt lgkmcnt(0)
	s_barrier
	v_pk_mul_f32 v[4:5], v[36:37], v[40:41] op_sel_hi:[1,0]
	v_pk_mul_f32 v[8:9], v[36:37], v[40:41] op_sel:[0,1]
	v_pk_mul_f32 v[10:11], v[36:37], v[42:43] op_sel_hi:[1,0]
	v_add_f32_dpp v30, v36, v36 wave_shr:1 row_mask:0xf bank_mask:0xf bound_ctrl:1
	v_add_f32_dpp v31, v37, v37 wave_shr:1 row_mask:0xf bank_mask:0xf bound_ctrl:1
	v_add_f32_dpp v54, v4, v4 wave_shr:1 row_mask:0xf bank_mask:0xf bound_ctrl:1
	v_add_f32_dpp v55, v5, v5 wave_shr:1 row_mask:0xf bank_mask:0xf bound_ctrl:1
	v_add_f32_dpp v76, v8, v8 wave_shr:1 row_mask:0xf bank_mask:0xf bound_ctrl:1
	v_add_f32_dpp v77, v9, v9 wave_shr:1 row_mask:0xf bank_mask:0xf bound_ctrl:1
	v_add_f32_dpp v82, v10, v10 wave_shr:1 row_mask:0xf bank_mask:0xf bound_ctrl:1
	v_add_f32_dpp v83, v11, v11 wave_shr:1 row_mask:0xf bank_mask:0xf bound_ctrl:1
	v_add_f32_dpp v30, v36, v30 wave_shl:1 row_mask:0xf bank_mask:0xf bound_ctrl:1
	v_add_f32_dpp v31, v37, v31 wave_shl:1 row_mask:0xf bank_mask:0xf bound_ctrl:1
	v_add_f32_dpp v54, v4, v54 wave_shl:1 row_mask:0xf bank_mask:0xf bound_ctrl:1
	v_add_f32_dpp v55, v5, v55 wave_shl:1 row_mask:0xf bank_mask:0xf bound_ctrl:1
	v_add_f32_dpp v76, v8, v76 wave_shl:1 row_mask:0xf bank_mask:0xf bound_ctrl:1
	v_add_f32_dpp v77, v9, v77 wave_shl:1 row_mask:0xf bank_mask:0xf bound_ctrl:1
	v_add_f32_dpp v82, v10, v82 wave_shl:1 row_mask:0xf bank_mask:0xf bound_ctrl:1
	v_add_f32_dpp v83, v11, v83 wave_shl:1 row_mask:0xf bank_mask:0xf bound_ctrl:1
	v_pk_add_f32 v[4:5], v[24:25], v[30:31]
	v_pk_add_f32 v[8:9], v[58:59], v[54:55]
	v_pk_add_f32 v[10:11], v[72:73], v[76:77]
	v_pk_add_f32 v[24:25], v[74:75], v[82:83]
	v_pk_fma_f32 v[8:9], v[108:109], v[4:5], v[8:9] op_sel_hi:[0,1,1] neg_lo:[1,0,0] neg_hi:[1,0,0]
	v_pk_fma_f32 v[10:11], v[108:109], v[4:5], v[10:11] op_sel:[1,0,0] neg_lo:[1,0,0] neg_hi:[1,0,0]
	v_pk_fma_f32 v[24:25], v[110:111], v[4:5], v[24:25] op_sel_hi:[0,1,1] neg_lo:[1,0,0] neg_hi:[1,0,0]
	v_pk_mul_f32 v[58:59], v[110:111], v[8:9] op_sel:[1,0]
	v_pk_mul_f32 v[72:73], v[112:113], v[8:9] op_sel_hi:[0,1]
	v_pk_mul_f32 v[74:75], v[112:113], v[8:9] op_sel:[1,0]
	v_pk_fma_f32 v[58:59], v[112:113], v[10:11], v[58:59] op_sel_hi:[0,1,1]
	v_pk_fma_f32 v[72:73], v[114:115], v[10:11], v[72:73] op_sel_hi:[0,1,1]
	v_pk_fma_f32 v[74:75], v[114:115], v[10:11], v[74:75] op_sel:[1,0,0]
	v_pk_fma_f32 v[58:59], v[112:113], v[24:25], v[58:59] op_sel:[1,0,0]
	v_pk_fma_f32 v[72:73], v[114:115], v[24:25], v[72:73] op_sel:[1,0,0]
	v_pk_fma_f32 v[74:75], v[116:117], v[24:25], v[74:75] op_sel_hi:[0,1,1]
	v_pk_mul_f32 v[88:89], v[108:109], v[58:59] op_sel_hi:[0,1]
	v_pk_fma_f32 v[88:89], v[108:109], v[72:73], v[88:89] op_sel:[1,0,0]
	v_pk_fma_f32 v[88:89], v[110:111], v[74:75], v[88:89] op_sel_hi:[0,1,1]
	v_pk_fma_f32 v[88:89], v[116:117], v[4:5], v[88:89] op_sel:[1,0,0] neg_lo:[0,0,1] neg_hi:[0,0,1]
	v_cmp_eq_u32_e64 s[10:11], 6, v119
	v_cmp_eq_u32_e64 s[14:15], 7, v119
	v_add_f32_dpp v4, v58, v58 wave_shr:1 row_mask:0xf bank_mask:0xf bound_ctrl:1
	v_add_f32_dpp v5, v59, v59 wave_shr:1 row_mask:0xf bank_mask:0xf bound_ctrl:1
	v_add_f32_dpp v8, v72, v72 wave_shr:1 row_mask:0xf bank_mask:0xf bound_ctrl:1
	v_add_f32_dpp v9, v73, v73 wave_shr:1 row_mask:0xf bank_mask:0xf bound_ctrl:1
	v_add_f32_dpp v10, v74, v74 wave_shr:1 row_mask:0xf bank_mask:0xf bound_ctrl:1
	v_add_f32_dpp v11, v75, v75 wave_shr:1 row_mask:0xf bank_mask:0xf bound_ctrl:1
	v_add_f32_dpp v24, v88, v88 wave_shr:1 row_mask:0xf bank_mask:0xf bound_ctrl:1
	v_add_f32_dpp v25, v89, v89 wave_shr:1 row_mask:0xf bank_mask:0xf bound_ctrl:1
	v_add_f32_dpp v4, v58, v4 wave_shl:1 row_mask:0xf bank_mask:0xf bound_ctrl:1
	v_add_f32_dpp v5, v59, v5 wave_shl:1 row_mask:0xf bank_mask:0xf bound_ctrl:1
	v_add_f32_dpp v8, v72, v8 wave_shl:1 row_mask:0xf bank_mask:0xf bound_ctrl:1
	v_add_f32_dpp v9, v73, v9 wave_shl:1 row_mask:0xf bank_mask:0xf bound_ctrl:1
	v_add_f32_dpp v10, v74, v10 wave_shl:1 row_mask:0xf bank_mask:0xf bound_ctrl:1
	v_add_f32_dpp v11, v75, v11 wave_shl:1 row_mask:0xf bank_mask:0xf bound_ctrl:1
	v_add_f32_dpp v24, v88, v24 wave_shl:1 row_mask:0xf bank_mask:0xf bound_ctrl:1
	v_add_f32_dpp v25, v89, v25 wave_shl:1 row_mask:0xf bank_mask:0xf bound_ctrl:1
	v_pk_add_f32 v[58:59], v[94:95], v[4:5]
	v_pk_add_f32 v[72:73], v[38:39], v[8:9]
	v_pk_add_f32 v[38:39], v[46:47], v[10:11]
	v_pk_add_f32 v[46:47], v[48:49], v[24:25]
	v_pk_fma_f32 v[46:47], v[12:13], v[58:59], v[46:47] op_sel_hi:[0,1,1]
	v_pk_fma_f32 v[46:47], v[12:13], v[72:73], v[46:47] op_sel:[1,0,0]
	v_pk_fma_f32 v[46:47], v[14:15], v[38:39], v[46:47] op_sel_hi:[0,1,1]
	v_cndmask_b32_e64 v48, 0, v18, s[10:11]
	v_cndmask_b32_e64 v49, 0, v18, s[14:15]
	v_pk_fma_f32 v[46:47], v[6:7], v[118:119], v[46:47] op_sel_hi:[1,0,1] neg_lo:[0,0,1] neg_hi:[0,0,1]
	s_add_i32 s4, s34, 9
	s_cmpk_lt_i32 s4, 0x201
	s_cselect_b64 s[12:13], s[0:1], 0
	v_pk_add_f32 v[46:47], v[46:47], v[48:49] neg_lo:[0,1] neg_hi:[0,1]
	v_pk_mul_f32 v[74:75], v[46:47], v[46:47]
	v_add_f32_e32 v74, v74, v75
	v_cndmask_b32_e64 v75, 0, v74, s[12:13]
	v_add_f32_e32 v1, v1, v75
	v_mov_b32_e32 v0, v1
	s_branch .LBB0_29
.LBB0_15:
.LBB0_16:
	s_mov_b32 s27, s19
	v_mov_b32_e32 v1, 0x42c80000
	v_mov_b32_e32 v0, 0
	s_add_i32 s4, s34, -2
	s_max_i32 s4, s4, 0
	s_mul_i32 s5, s4, 0x804
	s_add_i32 s5, s5, s35
	s_add_i32 s6, s5, 0x101004
	s_add_i32 s7, s5, 0x202008
	s_add_i32 s8, s5, 0x30300c
	s_add_i32 s11, s5, 0x404010
	s_mul_i32 s9, s4, 0x180c
	s_add_i32 s9, s9, s33
	buffer_load_dword v2, v28, s[16:19], s5 offen nt
	buffer_load_dword v3, v28, s[16:19], s6 offen nt
	buffer_load_dword v4, v28, s[16:19], s7 offen nt
	buffer_load_dword v5, v28, s[16:19], s8 offen nt
	buffer_load_dword v6, v28, s[16:19], s11 offen nt
	buffer_load_dwordx3 v[8:10], v27, s[24:27], s9 offen nt
	s_add_i32 s4, s34, -1
	s_max_i32 s4, s4, 0
	s_mul_i32 s5, s4, 0x804
	s_add_i32 s5, s5, s35
	s_add_i32 s6, s5, 0x101004
	s_add_i32 s7, s5, 0x202008
	s_add_i32 s8, s5, 0x30300c
	s_add_i32 s11, s5, 0x404010
	s_mul_i32 s9, s4, 0x180c
	s_add_i32 s9, s9, s33
	buffer_load_dword v12, v28, s[16:19], s5 offen nt
	buffer_load_dword v13, v28, s[16:19], s6 offen nt
	buffer_load_dword v14, v28, s[16:19], s7 offen nt
	buffer_load_dword v15, v28, s[16:19], s8 offen nt
	buffer_load_dword v16, v28, s[16:19], s11 offen nt
	buffer_load_dwordx3 v[32:34], v27, s[24:27], s9 offen nt
	s_add_i32 s4, s34, 0
	s_min_i32 s4, s4, 0x200
	s_mul_i32 s5, s4, 0x804
	s_add_i32 s5, s5, s35
	s_add_i32 s6, s5, 0x101004
	s_add_i32 s7, s5, 0x202008
	s_add_i32 s8, s5, 0x30300c
	s_add_i32 s11, s5, 0x404010
	s_mul_i32 s9, s4, 0x180c
	s_add_i32 s9, s9, s33
	buffer_load_dword v20, v28, s[16:19], s5 offen nt
	buffer_load_dword v21, v28, s[16:19], s6 offen nt
	buffer_load_dword v24, v28, s[16:19], s7 offen nt
	buffer_load_dword v25, v28, s[16:19], s8 offen nt
	buffer_load_dword v30, v28, s[16:19], s11 offen nt
	buffer_load_dwordx3 v[36:38], v27, s[24:27], s9 offen nt
	s_waitcnt vmcnt(12)
	v_pk_mul_f32 v[40:41], v[2:3], v[8:9] op_sel_hi:[1,0]
	v_pk_mul_f32 v[42:43], v[4:5], v[8:9] op_sel_hi:[1,0]
	v_mul_f32_e64 v44, v6, v8
	v_pk_mul_f32 v[46:47], v[2:3], v[8:9] op_sel:[0,1]
	v_pk_mul_f32 v[48:49], v[4:5], v[8:9] op_sel:[0,1]
	v_mul_f32_e64 v50, v6, v9
	v_pk_mul_f32 v[52:53], v[2:3], v[10:11] op_sel_hi:[1,0]
	v_pk_mul_f32 v[54:55], v[4:5], v[10:11] op_sel_hi:[1,0]
	v_mul_f32_e64 v56, v6, v10
	v_add_f32_dpp v58, v2, v2 wave_shr:1 row_mask:0xf bank_mask:0xf bound_ctrl:1
	v_add_f32_dpp v59, v3, v3 wave_shr:1 row_mask:0xf bank_mask:0xf bound_ctrl:1
	v_add_f32_dpp v60, v4, v4 wave_shr:1 row_mask:0xf bank_mask:0xf bound_ctrl:1
	v_add_f32_dpp v61, v5, v5 wave_shr:1 row_mask:0xf bank_mask:0xf bound_ctrl:1
	v_add_f32_dpp v62, v6, v6 wave_shr:1 row_mask:0xf bank_mask:0xf bound_ctrl:1
	v_add_f32_dpp v64, v40, v40 wave_shr:1 row_mask:0xf bank_mask:0xf bound_ctrl:1
	v_add_f32_dpp v65, v41, v41 wave_shr:1 row_mask:0xf bank_mask:0xf bound_ctrl:1
	v_add_f32_dpp v66, v42, v42 wave_shr:1 row_mask:0xf bank_mask:0xf bound_ctrl:1
	v_add_f32_dpp v67, v43, v43 wave_shr:1 row_mask:0xf bank_mask:0xf bound_ctrl:1
	v_add_f32_dpp v68, v44, v44 wave_shr:1 row_mask:0xf bank_mask:0xf bound_ctrl:1
	v_add_f32_dpp v70, v46, v46 wave_shr:1 row_mask:0xf bank_mask:0xf bound_ctrl:1
	v_add_f32_dpp v71, v47, v47 wave_shr:1 row_mask:0xf bank_mask:0xf bound_ctrl:1
	v_add_f32_dpp v72, v48, v48 wave_shr:1 row_mask:0xf bank_mask:0xf bound_ctrl:1
	v_add_f32_dpp v73, v49, v49 wave_shr:1 row_mask:0xf bank_mask:0xf bound_ctrl:1
	v_add_f32_dpp v74, v50, v50 wave_shr:1 row_mask:0xf bank_mask:0xf bound_ctrl:1
	v_add_f32_dpp v76, v52, v52 wave_shr:1 row_mask:0xf bank_mask:0xf bound_ctrl:1
	v_add_f32_dpp v77, v53, v53 wave_shr:1 row_mask:0xf bank_mask:0xf bound_ctrl:1
	v_add_f32_dpp v78, v54, v54 wave_shr:1 row_mask:0xf bank_mask:0xf bound_ctrl:1
	v_add_f32_dpp v79, v55, v55 wave_shr:1 row_mask:0xf bank_mask:0xf bound_ctrl:1
	v_add_f32_dpp v80, v56, v56 wave_shr:1 row_mask:0xf bank_mask:0xf bound_ctrl:1
	v_add_f32_dpp v58, v2, v58 wave_shl:1 row_mask:0xf bank_mask:0xf bound_ctrl:1
	v_add_f32_dpp v59, v3, v59 wave_shl:1 row_mask:0xf bank_mask:0xf bound_ctrl:1
	v_add_f32_dpp v60, v4, v60 wave_shl:1 row_mask:0xf bank_mask:0xf bound_ctrl:1
	v_add_f32_dpp v61, v5, v61 wave_shl:1 row_mask:0xf bank_mask:0xf bound_ctrl:1
	v_add_f32_dpp v62, v6, v62 wave_shl:1 row_mask:0xf bank_mask:0xf bound_ctrl:1
	v_add_f32_dpp v64, v40, v64 wave_shl:1 row_mask:0xf bank_mask:0xf bound_ctrl:1
	v_add_f32_dpp v65, v41, v65 wave_shl:1 row_mask:0xf bank_mask:0xf bound_ctrl:1
	v_add_f32_dpp v66, v42, v66 wave_shl:1 row_mask:0xf bank_mask:0xf bound_ctrl:1
	v_add_f32_dpp v67, v43, v67 wave_shl:1 row_mask:0xf bank_mask:0xf bound_ctrl:1
	v_add_f32_dpp v68, v44, v68 wave_shl:1 row_mask:0xf bank_mask:0xf bound_ctrl:1
	v_add_f32_dpp v70, v46, v70 wave_shl:1 row_mask:0xf bank_mask:0xf bound_ctrl:1
	v_add_f32_dpp v71, v47, v71 wave_shl:1 row_mask:0xf bank_mask:0xf bound_ctrl:1
	v_add_f32_dpp v72, v48, v72 wave_shl:1 row_mask:0xf bank_mask:0xf bound_ctrl:1
	v_add_f32_dpp v73, v49, v73 wave_shl:1 row_mask:0xf bank_mask:0xf bound_ctrl:1
	v_add_f32_dpp v74, v50, v74 wave_shl:1 row_mask:0xf bank_mask:0xf bound_ctrl:1
	v_add_f32_dpp v76, v52, v76 wave_shl:1 row_mask:0xf bank_mask:0xf bound_ctrl:1
	v_add_f32_dpp v77, v53, v77 wave_shl:1 row_mask:0xf bank_mask:0xf bound_ctrl:1
	v_add_f32_dpp v78, v54, v78 wave_shl:1 row_mask:0xf bank_mask:0xf bound_ctrl:1
	v_add_f32_dpp v79, v55, v79 wave_shl:1 row_mask:0xf bank_mask:0xf bound_ctrl:1
	v_add_f32_dpp v80, v56, v80 wave_shl:1 row_mask:0xf bank_mask:0xf bound_ctrl:1
	s_barrier
	s_add_i32 s4, s34, 1
	s_min_i32 s4, s4, 0x200
	s_mul_i32 s5, s4, 0x804
	s_add_i32 s5, s5, s35
	s_add_i32 s6, s5, 0x101004
	s_add_i32 s7, s5, 0x202008
	s_add_i32 s8, s5, 0x30300c
	s_add_i32 s11, s5, 0x404010
	s_mul_i32 s9, s4, 0x180c
	s_add_i32 s9, s9, s33
	buffer_load_dword v40, v28, s[16:19], s5 offen nt
	buffer_load_dword v41, v28, s[16:19], s6 offen nt
	buffer_load_dword v42, v28, s[16:19], s7 offen nt
	buffer_load_dword v43, v28, s[16:19], s8 offen nt
	buffer_load_dword v44, v28, s[16:19], s11 offen nt
	buffer_load_dwordx3 v[48:50], v27, s[24:27], s9 offen nt
	s_waitcnt vmcnt(12)
	v_pk_mul_f32 v[46:47], v[12:13], v[32:33] op_sel_hi:[1,0]
	v_pk_mul_f32 v[52:53], v[14:15], v[32:33] op_sel_hi:[1,0]
	v_mul_f32_e64 v54, v16, v32
	v_pk_mul_f32 v[56:57], v[12:13], v[32:33] op_sel:[0,1]
	v_pk_mul_f32 v[82:83], v[14:15], v[32:33] op_sel:[0,1]
	v_mul_f32_e64 v84, v16, v33
	v_pk_mul_f32 v[86:87], v[12:13], v[34:35] op_sel_hi:[1,0]
	v_pk_mul_f32 v[88:89], v[14:15], v[34:35] op_sel_hi:[1,0]
	v_mul_f32_e64 v90, v16, v34
	v_add_f32_dpp v92, v12, v12 wave_shr:1 row_mask:0xf bank_mask:0xf bound_ctrl:1
	v_add_f32_dpp v93, v13, v13 wave_shr:1 row_mask:0xf bank_mask:0xf bound_ctrl:1
	v_add_f32_dpp v94, v14, v14 wave_shr:1 row_mask:0xf bank_mask:0xf bound_ctrl:1
	v_add_f32_dpp v95, v15, v15 wave_shr:1 row_mask:0xf bank_mask:0xf bound_ctrl:1
	v_add_f32_dpp v96, v16, v16 wave_shr:1 row_mask:0xf bank_mask:0xf bound_ctrl:1
	v_add_f32_dpp v98, v46, v46 wave_shr:1 row_mask:0xf bank_mask:0xf bound_ctrl:1
	v_add_f32_dpp v99, v47, v47 wave_shr:1 row_mask:0xf bank_mask:0xf bound_ctrl:1
	v_add_f32_dpp v100, v52, v52 wave_shr:1 row_mask:0xf bank_mask:0xf bound_ctrl:1
	v_add_f32_dpp v101, v53, v53 wave_shr:1 row_mask:0xf bank_mask:0xf bound_ctrl:1
	v_add_f32_dpp v102, v54, v54 wave_shr:1 row_mask:0xf bank_mask:0xf bound_ctrl:1
	v_add_f32_dpp v104, v56, v56 wave_shr:1 row_mask:0xf bank_mask:0xf bound_ctrl:1
	v_add_f32_dpp v105, v57, v57 wave_shr:1 row_mask:0xf bank_mask:0xf bound_ctrl:1
	v_add_f32_dpp v106, v82, v82 wave_shr:1 row_mask:0xf bank_mask:0xf bound_ctrl:1
	v_add_f32_dpp v107, v83, v83 wave_shr:1 row_mask:0xf bank_mask:0xf bound_ctrl:1
	v_add_f32_dpp v108, v84, v84 wave_shr:1 row_mask:0xf bank_mask:0xf bound_ctrl:1
	v_add_f32_dpp v110, v86, v86 wave_shr:1 row_mask:0xf bank_mask:0xf bound_ctrl:1
	v_add_f32_dpp v111, v87, v87 wave_shr:1 row_mask:0xf bank_mask:0xf bound_ctrl:1
	v_add_f32_dpp v112, v88, v88 wave_shr:1 row_mask:0xf bank_mask:0xf bound_ctrl:1
	v_add_f32_dpp v113, v89, v89 wave_shr:1 row_mask:0xf bank_mask:0xf bound_ctrl:1
	v_add_f32_dpp v114, v90, v90 wave_shr:1 row_mask:0xf bank_mask:0xf bound_ctrl:1
	v_add_f32_dpp v92, v12, v92 wave_shl:1 row_mask:0xf bank_mask:0xf bound_ctrl:1
	v_add_f32_dpp v93, v13, v93 wave_shl:1 row_mask:0xf bank_mask:0xf bound_ctrl:1
	v_add_f32_dpp v94, v14, v94 wave_shl:1 row_mask:0xf bank_mask:0xf bound_ctrl:1
	v_add_f32_dpp v95, v15, v95 wave_shl:1 row_mask:0xf bank_mask:0xf bound_ctrl:1
	v_add_f32_dpp v96, v16, v96 wave_shl:1 row_mask:0xf bank_mask:0xf bound_ctrl:1
	v_add_f32_dpp v98, v46, v98 wave_shl:1 row_mask:0xf bank_mask:0xf bound_ctrl:1
	v_add_f32_dpp v99, v47, v99 wave_shl:1 row_mask:0xf bank_mask:0xf bound_ctrl:1
	v_add_f32_dpp v100, v52, v100 wave_shl:1 row_mask:0xf bank_mask:0xf bound_ctrl:1
	v_add_f32_dpp v101, v53, v101 wave_shl:1 row_mask:0xf bank_mask:0xf bound_ctrl:1
	v_add_f32_dpp v102, v54, v102 wave_shl:1 row_mask:0xf bank_mask:0xf bound_ctrl:1
	v_add_f32_dpp v104, v56, v104 wave_shl:1 row_mask:0xf bank_mask:0xf bound_ctrl:1
	v_add_f32_dpp v105, v57, v105 wave_shl:1 row_mask:0xf bank_mask:0xf bound_ctrl:1
	v_add_f32_dpp v106, v82, v106 wave_shl:1 row_mask:0xf bank_mask:0xf bound_ctrl:1
	v_add_f32_dpp v107, v83, v107 wave_shl:1 row_mask:0xf bank_mask:0xf bound_ctrl:1
	v_add_f32_dpp v108, v84, v108 wave_shl:1 row_mask:0xf bank_mask:0xf bound_ctrl:1
	v_add_f32_dpp v110, v86, v110 wave_shl:1 row_mask:0xf bank_mask:0xf bound_ctrl:1
	v_add_f32_dpp v111, v87, v111 wave_shl:1 row_mask:0xf bank_mask:0xf bound_ctrl:1
	v_add_f32_dpp v112, v88, v112 wave_shl:1 row_mask:0xf bank_mask:0xf bound_ctrl:1
	v_add_f32_dpp v113, v89, v113 wave_shl:1 row_mask:0xf bank_mask:0xf bound_ctrl:1
	v_add_f32_dpp v114, v90, v114 wave_shl:1 row_mask:0xf bank_mask:0xf bound_ctrl:1
	s_barrier
	s_add_i32 s4, s34, 2
	s_min_i32 s4, s4, 0x200
	s_mul_i32 s5, s4, 0x804
	s_add_i32 s5, s5, s35
	s_add_i32 s6, s5, 0x101004
	s_add_i32 s7, s5, 0x202008
	s_add_i32 s8, s5, 0x30300c
	s_add_i32 s11, s5, 0x404010
	s_mul_i32 s9, s4, 0x180c
	s_add_i32 s9, s9, s33
	buffer_load_dword v46, v28, s[16:19], s5 offen nt
	buffer_load_dword v47, v28, s[16:19], s6 offen nt
	buffer_load_dword v52, v28, s[16:19], s7 offen nt
	buffer_load_dword v53, v28, s[16:19], s8 offen nt
	buffer_load_dword v54, v28, s[16:19], s11 offen nt
	buffer_load_dwordx3 v[84:86], v27, s[24:27], s9 offen nt
	s_waitcnt vmcnt(12)
	v_pk_mul_f32 v[56:57], v[20:21], v[36:37] op_sel_hi:[1,0]
	v_pk_mul_f32 v[82:83], v[24:25], v[36:37] op_sel_hi:[1,0]
	v_mul_f32_e64 v88, v30, v36
	v_pk_mul_f32 v[90:91], v[20:21], v[36:37] op_sel:[0,1]
	v_pk_mul_f32 v[116:117], v[24:25], v[36:37] op_sel:[0,1]
	v_mul_f32_e64 v118, v30, v37
	v_pk_mul_f32 v[120:121], v[20:21], v[38:39] op_sel_hi:[1,0]
	v_pk_mul_f32 v[122:123], v[24:25], v[38:39] op_sel_hi:[1,0]
	v_mul_f32_e64 v124, v30, v38
	v_add_f32_dpp v126, v20, v20 wave_shr:1 row_mask:0xf bank_mask:0xf bound_ctrl:1
	v_add_f32_dpp v127, v21, v21 wave_shr:1 row_mask:0xf bank_mask:0xf bound_ctrl:1
	v_add_f32_dpp v128, v24, v24 wave_shr:1 row_mask:0xf bank_mask:0xf bound_ctrl:1
	v_add_f32_dpp v129, v25, v25 wave_shr:1 row_mask:0xf bank_mask:0xf bound_ctrl:1
	v_add_f32_dpp v130, v30, v30 wave_shr:1 row_mask:0xf bank_mask:0xf bound_ctrl:1
	v_add_f32_dpp v132, v56, v56 wave_shr:1 row_mask:0xf bank_mask:0xf bound_ctrl:1
	v_add_f32_dpp v133, v57, v57 wave_shr:1 row_mask:0xf bank_mask:0xf bound_ctrl:1
	v_add_f32_dpp v134, v82, v82 wave_shr:1 row_mask:0xf bank_mask:0xf bound_ctrl:1
	v_add_f32_dpp v135, v83, v83 wave_shr:1 row_mask:0xf bank_mask:0xf bound_ctrl:1
	v_add_f32_dpp v136, v88, v88 wave_shr:1 row_mask:0xf bank_mask:0xf bound_ctrl:1
	v_add_f32_dpp v138, v90, v90 wave_shr:1 row_mask:0xf bank_mask:0xf bound_ctrl:1
	v_add_f32_dpp v139, v91, v91 wave_shr:1 row_mask:0xf bank_mask:0xf bound_ctrl:1
	v_add_f32_dpp v140, v116, v116 wave_shr:1 row_mask:0xf bank_mask:0xf bound_ctrl:1
	v_add_f32_dpp v141, v117, v117 wave_shr:1 row_mask:0xf bank_mask:0xf bound_ctrl:1
	v_add_f32_dpp v142, v118, v118 wave_shr:1 row_mask:0xf bank_mask:0xf bound_ctrl:1
	v_add_f32_dpp v144, v120, v120 wave_shr:1 row_mask:0xf bank_mask:0xf bound_ctrl:1
	v_add_f32_dpp v145, v121, v121 wave_shr:1 row_mask:0xf bank_mask:0xf bound_ctrl:1
	v_add_f32_dpp v146, v122, v122 wave_shr:1 row_mask:0xf bank_mask:0xf bound_ctrl:1
	v_add_f32_dpp v147, v123, v123 wave_shr:1 row_mask:0xf bank_mask:0xf bound_ctrl:1
	v_add_f32_dpp v148, v124, v124 wave_shr:1 row_mask:0xf bank_mask:0xf bound_ctrl:1
	v_add_f32_dpp v126, v20, v126 wave_shl:1 row_mask:0xf bank_mask:0xf bound_ctrl:1
	v_add_f32_dpp v127, v21, v127 wave_shl:1 row_mask:0xf bank_mask:0xf bound_ctrl:1
	v_add_f32_dpp v128, v24, v128 wave_shl:1 row_mask:0xf bank_mask:0xf bound_ctrl:1
	v_add_f32_dpp v129, v25, v129 wave_shl:1 row_mask:0xf bank_mask:0xf bound_ctrl:1
	v_add_f32_dpp v130, v30, v130 wave_shl:1 row_mask:0xf bank_mask:0xf bound_ctrl:1
	v_add_f32_dpp v132, v56, v132 wave_shl:1 row_mask:0xf bank_mask:0xf bound_ctrl:1
	v_add_f32_dpp v133, v57, v133 wave_shl:1 row_mask:0xf bank_mask:0xf bound_ctrl:1
	v_add_f32_dpp v134, v82, v134 wave_shl:1 row_mask:0xf bank_mask:0xf bound_ctrl:1
	v_add_f32_dpp v135, v83, v135 wave_shl:1 row_mask:0xf bank_mask:0xf bound_ctrl:1
	v_add_f32_dpp v136, v88, v136 wave_shl:1 row_mask:0xf bank_mask:0xf bound_ctrl:1
	v_add_f32_dpp v138, v90, v138 wave_shl:1 row_mask:0xf bank_mask:0xf bound_ctrl:1
	v_add_f32_dpp v139, v91, v139 wave_shl:1 row_mask:0xf bank_mask:0xf bound_ctrl:1
	v_add_f32_dpp v140, v116, v140 wave_shl:1 row_mask:0xf bank_mask:0xf bound_ctrl:1
	v_add_f32_dpp v141, v117, v141 wave_shl:1 row_mask:0xf bank_mask:0xf bound_ctrl:1
	v_add_f32_dpp v142, v118, v142 wave_shl:1 row_mask:0xf bank_mask:0xf bound_ctrl:1
	v_add_f32_dpp v144, v120, v144 wave_shl:1 row_mask:0xf bank_mask:0xf bound_ctrl:1
	v_add_f32_dpp v145, v121, v145 wave_shl:1 row_mask:0xf bank_mask:0xf bound_ctrl:1
	v_add_f32_dpp v146, v122, v146 wave_shl:1 row_mask:0xf bank_mask:0xf bound_ctrl:1
	v_add_f32_dpp v147, v123, v147 wave_shl:1 row_mask:0xf bank_mask:0xf bound_ctrl:1
	v_add_f32_dpp v148, v124, v148 wave_shl:1 row_mask:0xf bank_mask:0xf bound_ctrl:1
	s_barrier
	ds_read_b128 v[88:91], v23 offset:0
	ds_read_b128 v[116:119], v23 offset:1024
	ds_read_b128 v[120:123], v23 offset:2048
	v_pk_add_f32 v[56:57], v[92:93], v[126:127]
	v_pk_add_f32 v[82:83], v[58:59], v[56:57]
	v_pk_add_f32 v[58:59], v[94:95], v[128:129]
	v_pk_add_f32 v[92:93], v[60:61], v[58:59]
	v_add_f32_e64 v60, v96, v130
	v_add_f32_e64 v94, v62, v60
	v_pk_add_f32 v[62:63], v[98:99], v[132:133]
	v_pk_add_f32 v[96:97], v[64:65], v[62:63]
	v_pk_add_f32 v[64:65], v[100:101], v[134:135]
	v_pk_add_f32 v[98:99], v[66:67], v[64:65]
	v_add_f32_e64 v66, v102, v136
	v_add_f32_e64 v100, v68, v66
	v_pk_add_f32 v[68:69], v[104:105], v[138:139]
	v_pk_add_f32 v[102:103], v[70:71], v[68:69]
	v_pk_add_f32 v[70:71], v[106:107], v[140:141]
	v_pk_add_f32 v[104:105], v[72:73], v[70:71]
	v_add_f32_e64 v72, v108, v142
	v_add_f32_e64 v106, v74, v72
	v_pk_add_f32 v[74:75], v[110:111], v[144:145]
	v_pk_add_f32 v[108:109], v[76:77], v[74:75]
	v_pk_add_f32 v[76:77], v[112:113], v[146:147]
	v_pk_add_f32 v[110:111], v[78:79], v[76:77]
	v_add_f32_e64 v78, v114, v148
	v_add_f32_e64 v112, v80, v78
	s_waitcnt lgkmcnt(2)
	v_pk_fma_f32 v[96:97], v[88:89], v[82:83], v[96:97] op_sel_hi:[0,1,1] neg_lo:[1,0,0] neg_hi:[1,0,0]
	v_pk_fma_f32 v[98:99], v[88:89], v[92:93], v[98:99] op_sel_hi:[0,1,1] neg_lo:[1,0,0] neg_hi:[1,0,0]
	v_fma_f32 v100, -v88, v94, v100
	v_pk_fma_f32 v[102:103], v[88:89], v[82:83], v[102:103] op_sel:[1,0,0] neg_lo:[1,0,0] neg_hi:[1,0,0]
	v_pk_fma_f32 v[104:105], v[88:89], v[92:93], v[104:105] op_sel:[1,0,0] neg_lo:[1,0,0] neg_hi:[1,0,0]
	v_fma_f32 v106, -v89, v94, v106
	v_pk_fma_f32 v[108:109], v[90:91], v[82:83], v[108:109] op_sel_hi:[0,1,1] neg_lo:[1,0,0] neg_hi:[1,0,0]
	v_pk_fma_f32 v[110:111], v[90:91], v[92:93], v[110:111] op_sel_hi:[0,1,1] neg_lo:[1,0,0] neg_hi:[1,0,0]
	v_fma_f32 v112, -v90, v94, v112
	v_pk_mul_f32 v[80:81], v[90:91], v[96:97] op_sel:[1,0]
	v_pk_mul_f32 v[150:151], v[90:91], v[98:99] op_sel:[1,0]
	v_mul_f32_e64 v156, v91, v100
	s_waitcnt lgkmcnt(1)
	v_pk_mul_f32 v[114:115], v[116:117], v[96:97] op_sel_hi:[0,1]
	v_pk_mul_f32 v[152:153], v[116:117], v[98:99] op_sel_hi:[0,1]
	v_mul_f32_e64 v158, v116, v100
	v_pk_mul_f32 v[124:125], v[116:117], v[96:97] op_sel:[1,0]
	v_pk_mul_f32 v[154:155], v[116:117], v[98:99] op_sel:[1,0]
	v_mul_f32_e64 v160, v117, v100
	v_pk_fma_f32 v[80:81], v[116:117], v[102:103], v[80:81] op_sel_hi:[0,1,1]
	v_pk_fma_f32 v[150:151], v[116:117], v[104:105], v[150:151] op_sel_hi:[0,1,1]
	v_fma_f32 v156, v116, v106, v156
	v_pk_fma_f32 v[114:115], v[118:119], v[102:103], v[114:115] op_sel_hi:[0,1,1]
	v_pk_fma_f32 v[152:153], v[118:119], v[104:105], v[152:153] op_sel_hi:[0,1,1]
	v_fma_f32 v158, v118, v106, v158
	v_pk_fma_f32 v[124:125], v[118:119], v[102:103], v[124:125] op_sel:[1,0,0]
	v_pk_fma_f32 v[154:155], v[118:119], v[104:105], v[154:155] op_sel:[1,0,0]
	v_fma_f32 v160, v119, v106, v160
	v_pk_fma_f32 v[80:81], v[116:117], v[108:109], v[80:81] op_sel:[1,0,0]
	v_pk_fma_f32 v[150:151], v[116:117], v[110:111], v[150:151] op_sel:[1,0,0]
	v_fma_f32 v156, v117, v112, v156
	v_pk_fma_f32 v[114:115], v[118:119], v[108:109], v[114:115] op_sel:[1,0,0]
	v_pk_fma_f32 v[152:153], v[118:119], v[110:111], v[152:153] op_sel:[1,0,0]
	v_fma_f32 v158, v119, v112, v158
	s_waitcnt lgkmcnt(0)
	v_pk_fma_f32 v[124:125], v[120:121], v[108:109], v[124:125] op_sel_hi:[0,1,1]
	v_pk_fma_f32 v[154:155], v[120:121], v[110:111], v[154:155] op_sel_hi:[0,1,1]
	v_fma_f32 v160, v120, v112, v160
	v_pk_mul_f32 v[162:163], v[88:89], v[80:81] op_sel_hi:[0,1]
	v_pk_mul_f32 v[164:165], v[88:89], v[150:151] op_sel_hi:[0,1]
	v_mul_f32_e64 v166, v88, v156
	v_pk_fma_f32 v[162:163], v[88:89], v[114:115], v[162:163] op_sel:[1,0,0]
	v_pk_fma_f32 v[164:165], v[88:89], v[152:153], v[164:165] op_sel:[1,0,0]
	v_fma_f32 v166, v89, v158, v166
	v_pk_fma_f32 v[162:163], v[90:91], v[124:125], v[162:163] op_sel_hi:[0,1,1]
	v_pk_fma_f32 v[164:165], v[90:91], v[154:155], v[164:165] op_sel_hi:[0,1,1]
	v_fma_f32 v166, v90, v160, v166
	v_pk_fma_f32 v[162:163], v[120:121], v[82:83], v[162:163] op_sel:[1,0,0] neg_lo:[0,0,1] neg_hi:[0,0,1]
	v_pk_fma_f32 v[164:165], v[120:121], v[92:93], v[164:165] op_sel:[1,0,0] neg_lo:[0,0,1] neg_hi:[0,0,1]
	v_fma_f32 v166, v121, v94, -v166
	v_add_f32_dpp v82, v80, v80 wave_shr:1 row_mask:0xf bank_mask:0xf bound_ctrl:1
	v_add_f32_dpp v83, v81, v81 wave_shr:1 row_mask:0xf bank_mask:0xf bound_ctrl:1
	v_add_f32_dpp v92, v150, v150 wave_shr:1 row_mask:0xf bank_mask:0xf bound_ctrl:1
	v_add_f32_dpp v93, v151, v151 wave_shr:1 row_mask:0xf bank_mask:0xf bound_ctrl:1
	v_add_f32_dpp v94, v156, v156 wave_shr:1 row_mask:0xf bank_mask:0xf bound_ctrl:1
	v_add_f32_dpp v96, v114, v114 wave_shr:1 row_mask:0xf bank_mask:0xf bound_ctrl:1
	v_add_f32_dpp v97, v115, v115 wave_shr:1 row_mask:0xf bank_mask:0xf bound_ctrl:1
	v_add_f32_dpp v98, v152, v152 wave_shr:1 row_mask:0xf bank_mask:0xf bound_ctrl:1
	v_add_f32_dpp v99, v153, v153 wave_shr:1 row_mask:0xf bank_mask:0xf bound_ctrl:1
	v_add_f32_dpp v100, v158, v158 wave_shr:1 row_mask:0xf bank_mask:0xf bound_ctrl:1
	v_add_f32_dpp v102, v124, v124 wave_shr:1 row_mask:0xf bank_mask:0xf bound_ctrl:1
	v_add_f32_dpp v103, v125, v125 wave_shr:1 row_mask:0xf bank_mask:0xf bound_ctrl:1
	v_add_f32_dpp v104, v154, v154 wave_shr:1 row_mask:0xf bank_mask:0xf bound_ctrl:1
	v_add_f32_dpp v105, v155, v155 wave_shr:1 row_mask:0xf bank_mask:0xf bound_ctrl:1
	v_add_f32_dpp v106, v160, v160 wave_shr:1 row_mask:0xf bank_mask:0xf bound_ctrl:1
	v_add_f32_dpp v108, v162, v162 wave_shr:1 row_mask:0xf bank_mask:0xf bound_ctrl:1
	v_add_f32_dpp v109, v163, v163 wave_shr:1 row_mask:0xf bank_mask:0xf bound_ctrl:1
	v_add_f32_dpp v110, v164, v164 wave_shr:1 row_mask:0xf bank_mask:0xf bound_ctrl:1
	v_add_f32_dpp v111, v165, v165 wave_shr:1 row_mask:0xf bank_mask:0xf bound_ctrl:1
	v_add_f32_dpp v112, v166, v166 wave_shr:1 row_mask:0xf bank_mask:0xf bound_ctrl:1
	v_add_f32_dpp v82, v80, v82 wave_shl:1 row_mask:0xf bank_mask:0xf bound_ctrl:1
	v_add_f32_dpp v83, v81, v83 wave_shl:1 row_mask:0xf bank_mask:0xf bound_ctrl:1
	v_add_f32_dpp v92, v150, v92 wave_shl:1 row_mask:0xf bank_mask:0xf bound_ctrl:1
	v_add_f32_dpp v93, v151, v93 wave_shl:1 row_mask:0xf bank_mask:0xf bound_ctrl:1
	v_add_f32_dpp v94, v156, v94 wave_shl:1 row_mask:0xf bank_mask:0xf bound_ctrl:1
	v_add_f32_dpp v96, v114, v96 wave_shl:1 row_mask:0xf bank_mask:0xf bound_ctrl:1
	v_add_f32_dpp v97, v115, v97 wave_shl:1 row_mask:0xf bank_mask:0xf bound_ctrl:1
	v_add_f32_dpp v98, v152, v98 wave_shl:1 row_mask:0xf bank_mask:0xf bound_ctrl:1
	v_add_f32_dpp v99, v153, v99 wave_shl:1 row_mask:0xf bank_mask:0xf bound_ctrl:1
	v_add_f32_dpp v100, v158, v100 wave_shl:1 row_mask:0xf bank_mask:0xf bound_ctrl:1
	v_add_f32_dpp v102, v124, v102 wave_shl:1 row_mask:0xf bank_mask:0xf bound_ctrl:1
	v_add_f32_dpp v103, v125, v103 wave_shl:1 row_mask:0xf bank_mask:0xf bound_ctrl:1
	v_add_f32_dpp v104, v154, v104 wave_shl:1 row_mask:0xf bank_mask:0xf bound_ctrl:1
	v_add_f32_dpp v105, v155, v105 wave_shl:1 row_mask:0xf bank_mask:0xf bound_ctrl:1
	v_add_f32_dpp v106, v160, v106 wave_shl:1 row_mask:0xf bank_mask:0xf bound_ctrl:1
	v_add_f32_dpp v108, v162, v108 wave_shl:1 row_mask:0xf bank_mask:0xf bound_ctrl:1
	v_add_f32_dpp v109, v163, v109 wave_shl:1 row_mask:0xf bank_mask:0xf bound_ctrl:1
	v_add_f32_dpp v110, v164, v110 wave_shl:1 row_mask:0xf bank_mask:0xf bound_ctrl:1
	v_add_f32_dpp v111, v165, v111 wave_shl:1 row_mask:0xf bank_mask:0xf bound_ctrl:1
	v_add_f32_dpp v112, v166, v112 wave_shl:1 row_mask:0xf bank_mask:0xf bound_ctrl:1
	s_add_i32 s4, s34, 3
	s_min_i32 s4, s4, 0x200
	s_mul_i32 s5, s4, 0x804
	s_add_i32 s5, s5, s35
	s_add_i32 s6, s5, 0x101004
	s_add_i32 s7, s5, 0x202008
	s_add_i32 s8, s5, 0x30300c
	s_add_i32 s11, s5, 0x404010
	s_mul_i32 s9, s4, 0x180c
	s_add_i32 s9, s9, s33
	buffer_load_dword v2, v28, s[16:19], s5 offen nt
	buffer_load_dword v3, v28, s[16:19], s6 offen nt
	buffer_load_dword v4, v28, s[16:19], s7 offen nt
	buffer_load_dword v5, v28, s[16:19], s8 offen nt
	buffer_load_dword v6, v28, s[16:19], s11 offen nt
	buffer_load_dwordx3 v[8:10], v27, s[24:27], s9 offen nt
	s_waitcnt vmcnt(12)
	v_pk_mul_f32 v[80:81], v[40:41], v[48:49] op_sel_hi:[1,0]
	v_pk_mul_f32 v[88:89], v[42:43], v[48:49] op_sel_hi:[1,0]
	v_mul_f32_e64 v90, v44, v48
	v_pk_mul_f32 v[114:115], v[40:41], v[48:49] op_sel:[0,1]
	v_pk_mul_f32 v[116:117], v[42:43], v[48:49] op_sel:[0,1]
	v_mul_f32_e64 v118, v44, v49
	v_pk_mul_f32 v[120:121], v[40:41], v[50:51] op_sel_hi:[1,0]
	v_pk_mul_f32 v[122:123], v[42:43], v[50:51] op_sel_hi:[1,0]
	v_mul_f32_e64 v124, v44, v50
	v_add_f32_dpp v150, v40, v40 wave_shr:1 row_mask:0xf bank_mask:0xf bound_ctrl:1
	v_add_f32_dpp v151, v41, v41 wave_shr:1 row_mask:0xf bank_mask:0xf bound_ctrl:1
	v_add_f32_dpp v152, v42, v42 wave_shr:1 row_mask:0xf bank_mask:0xf bound_ctrl:1
	v_add_f32_dpp v153, v43, v43 wave_shr:1 row_mask:0xf bank_mask:0xf bound_ctrl:1
	v_add_f32_dpp v154, v44, v44 wave_shr:1 row_mask:0xf bank_mask:0xf bound_ctrl:1
	v_add_f32_dpp v156, v80, v80 wave_shr:1 row_mask:0xf bank_mask:0xf bound_ctrl:1
	v_add_f32_dpp v157, v81, v81 wave_shr:1 row_mask:0xf bank_mask:0xf bound_ctrl:1
	v_add_f32_dpp v158, v88, v88 wave_shr:1 row_mask:0xf bank_mask:0xf bound_ctrl:1
	v_add_f32_dpp v159, v89, v89 wave_shr:1 row_mask:0xf bank_mask:0xf bound_ctrl:1
	v_add_f32_dpp v160, v90, v90 wave_shr:1 row_mask:0xf bank_mask:0xf bound_ctrl:1
	v_add_f32_dpp v162, v114, v114 wave_shr:1 row_mask:0xf bank_mask:0xf bound_ctrl:1
	v_add_f32_dpp v163, v115, v115 wave_shr:1 row_mask:0xf bank_mask:0xf bound_ctrl:1
	v_add_f32_dpp v164, v116, v116 wave_shr:1 row_mask:0xf bank_mask:0xf bound_ctrl:1
	v_add_f32_dpp v165, v117, v117 wave_shr:1 row_mask:0xf bank_mask:0xf bound_ctrl:1
	v_add_f32_dpp v166, v118, v118 wave_shr:1 row_mask:0xf bank_mask:0xf bound_ctrl:1
	v_add_f32_dpp v168, v120, v120 wave_shr:1 row_mask:0xf bank_mask:0xf bound_ctrl:1
	v_add_f32_dpp v169, v121, v121 wave_shr:1 row_mask:0xf bank_mask:0xf bound_ctrl:1
	v_add_f32_dpp v170, v122, v122 wave_shr:1 row_mask:0xf bank_mask:0xf bound_ctrl:1
	v_add_f32_dpp v171, v123, v123 wave_shr:1 row_mask:0xf bank_mask:0xf bound_ctrl:1
	v_add_f32_dpp v172, v124, v124 wave_shr:1 row_mask:0xf bank_mask:0xf bound_ctrl:1
	v_add_f32_dpp v150, v40, v150 wave_shl:1 row_mask:0xf bank_mask:0xf bound_ctrl:1
	v_add_f32_dpp v151, v41, v151 wave_shl:1 row_mask:0xf bank_mask:0xf bound_ctrl:1
	v_add_f32_dpp v152, v42, v152 wave_shl:1 row_mask:0xf bank_mask:0xf bound_ctrl:1
	v_add_f32_dpp v153, v43, v153 wave_shl:1 row_mask:0xf bank_mask:0xf bound_ctrl:1
	v_add_f32_dpp v154, v44, v154 wave_shl:1 row_mask:0xf bank_mask:0xf bound_ctrl:1
	v_add_f32_dpp v156, v80, v156 wave_shl:1 row_mask:0xf bank_mask:0xf bound_ctrl:1
	v_add_f32_dpp v157, v81, v157 wave_shl:1 row_mask:0xf bank_mask:0xf bound_ctrl:1
	v_add_f32_dpp v158, v88, v158 wave_shl:1 row_mask:0xf bank_mask:0xf bound_ctrl:1
	v_add_f32_dpp v159, v89, v159 wave_shl:1 row_mask:0xf bank_mask:0xf bound_ctrl:1
	v_add_f32_dpp v160, v90, v160 wave_shl:1 row_mask:0xf bank_mask:0xf bound_ctrl:1
	v_add_f32_dpp v162, v114, v162 wave_shl:1 row_mask:0xf bank_mask:0xf bound_ctrl:1
	v_add_f32_dpp v163, v115, v163 wave_shl:1 row_mask:0xf bank_mask:0xf bound_ctrl:1
	v_add_f32_dpp v164, v116, v164 wave_shl:1 row_mask:0xf bank_mask:0xf bound_ctrl:1
	v_add_f32_dpp v165, v117, v165 wave_shl:1 row_mask:0xf bank_mask:0xf bound_ctrl:1
	v_add_f32_dpp v166, v118, v166 wave_shl:1 row_mask:0xf bank_mask:0xf bound_ctrl:1
	v_add_f32_dpp v168, v120, v168 wave_shl:1 row_mask:0xf bank_mask:0xf bound_ctrl:1
	v_add_f32_dpp v169, v121, v169 wave_shl:1 row_mask:0xf bank_mask:0xf bound_ctrl:1
	v_add_f32_dpp v170, v122, v170 wave_shl:1 row_mask:0xf bank_mask:0xf bound_ctrl:1
	v_add_f32_dpp v171, v123, v171 wave_shl:1 row_mask:0xf bank_mask:0xf bound_ctrl:1
	v_add_f32_dpp v172, v124, v172 wave_shl:1 row_mask:0xf bank_mask:0xf bound_ctrl:1
	s_barrier
	ds_read_b128 v[88:91], v23 offset:3072
	ds_read_b128 v[116:119], v23 offset:4096
	ds_read_b128 v[120:123], v23 offset:5120
	v_pk_add_f32 v[80:81], v[56:57], v[150:151]
	v_pk_add_f32 v[56:57], v[58:59], v[152:153]
	v_add_f32_e64 v58, v60, v154
	v_pk_add_f32 v[60:61], v[62:63], v[156:157]
	v_pk_add_f32 v[62:63], v[64:65], v[158:159]
	v_add_f32_e64 v64, v66, v160
	v_pk_add_f32 v[66:67], v[68:69], v[162:163]
	v_pk_add_f32 v[68:69], v[70:71], v[164:165]
	v_add_f32_e64 v70, v72, v166
	v_pk_add_f32 v[72:73], v[74:75], v[168:169]
	v_pk_add_f32 v[74:75], v[76:77], v[170:171]
	v_add_f32_e64 v76, v78, v172
	s_waitcnt lgkmcnt(2)
	v_pk_fma_f32 v[60:61], v[88:89], v[80:81], v[60:61] op_sel_hi:[0,1,1] neg_lo:[1,0,0] neg_hi:[1,0,0]
	v_pk_fma_f32 v[62:63], v[88:89], v[56:57], v[62:63] op_sel_hi:[0,1,1] neg_lo:[1,0,0] neg_hi:[1,0,0]
	v_fma_f32 v64, -v88, v58, v64
	v_pk_fma_f32 v[66:67], v[88:89], v[80:81], v[66:67] op_sel:[1,0,0] neg_lo:[1,0,0] neg_hi:[1,0,0]
	v_pk_fma_f32 v[68:69], v[88:89], v[56:57], v[68:69] op_sel:[1,0,0] neg_lo:[1,0,0] neg_hi:[1,0,0]
	v_fma_f32 v70, -v89, v58, v70
	v_pk_fma_f32 v[72:73], v[90:91], v[80:81], v[72:73] op_sel_hi:[0,1,1] neg_lo:[1,0,0] neg_hi:[1,0,0]
	v_pk_fma_f32 v[74:75], v[90:91], v[56:57], v[74:75] op_sel_hi:[0,1,1] neg_lo:[1,0,0] neg_hi:[1,0,0]
	v_fma_f32 v76, -v90, v58, v76
	v_pk_mul_f32 v[78:79], v[90:91], v[60:61] op_sel:[1,0]
	v_pk_mul_f32 v[174:175], v[90:91], v[62:63] op_sel:[1,0]
	v_mul_f32_e64 v180, v91, v64
	s_waitcnt lgkmcnt(1)
	v_pk_mul_f32 v[114:115], v[116:117], v[60:61] op_sel_hi:[0,1]
	v_pk_mul_f32 v[176:177], v[116:117], v[62:63] op_sel_hi:[0,1]
	v_mul_f32_e64 v182, v116, v64
	v_pk_mul_f32 v[124:125], v[116:117], v[60:61] op_sel:[1,0]
	v_pk_mul_f32 v[178:179], v[116:117], v[62:63] op_sel:[1,0]
	v_mul_f32_e64 v184, v117, v64
	v_pk_fma_f32 v[78:79], v[116:117], v[66:67], v[78:79] op_sel_hi:[0,1,1]
	v_pk_fma_f32 v[174:175], v[116:117], v[68:69], v[174:175] op_sel_hi:[0,1,1]
	v_fma_f32 v180, v116, v70, v180
	v_pk_fma_f32 v[114:115], v[118:119], v[66:67], v[114:115] op_sel_hi:[0,1,1]
	v_pk_fma_f32 v[176:177], v[118:119], v[68:69], v[176:177] op_sel_hi:[0,1,1]
	v_fma_f32 v182, v118, v70, v182
	v_pk_fma_f32 v[124:125], v[118:119], v[66:67], v[124:125] op_sel:[1,0,0]
	v_pk_fma_f32 v[178:179], v[118:119], v[68:69], v[178:179] op_sel:[1,0,0]
	v_fma_f32 v184, v119, v70, v184
	v_pk_fma_f32 v[78:79], v[116:117], v[72:73], v[78:79] op_sel:[1,0,0]
	v_pk_fma_f32 v[174:175], v[116:117], v[74:75], v[174:175] op_sel:[1,0,0]
	v_fma_f32 v180, v117, v76, v180
	v_pk_fma_f32 v[114:115], v[118:119], v[72:73], v[114:115] op_sel:[1,0,0]
	v_pk_fma_f32 v[176:177], v[118:119], v[74:75], v[176:177] op_sel:[1,0,0]
	v_fma_f32 v182, v119, v76, v182
	s_waitcnt lgkmcnt(0)
	v_pk_fma_f32 v[124:125], v[120:121], v[72:73], v[124:125] op_sel_hi:[0,1,1]
	v_pk_fma_f32 v[178:179], v[120:121], v[74:75], v[178:179] op_sel_hi:[0,1,1]
	v_fma_f32 v184, v120, v76, v184
	v_pk_mul_f32 v[186:187], v[88:89], v[78:79] op_sel_hi:[0,1]
	v_pk_mul_f32 v[188:189], v[88:89], v[174:175] op_sel_hi:[0,1]
	v_mul_f32_e64 v190, v88, v180
	v_pk_fma_f32 v[186:187], v[88:89], v[114:115], v[186:187] op_sel:[1,0,0]
	v_pk_fma_f32 v[188:189], v[88:89], v[176:177], v[188:189] op_sel:[1,0,0]
	v_fma_f32 v190, v89, v182, v190
	v_pk_fma_f32 v[186:187], v[90:91], v[124:125], v[186:187] op_sel_hi:[0,1,1]
	v_pk_fma_f32 v[188:189], v[90:91], v[178:179], v[188:189] op_sel_hi:[0,1,1]
	v_fma_f32 v190, v90, v184, v190
	v_pk_fma_f32 v[186:187], v[120:121], v[80:81], v[186:187] op_sel:[1,0,0] neg_lo:[0,0,1] neg_hi:[0,0,1]
	v_pk_fma_f32 v[188:189], v[120:121], v[56:57], v[188:189] op_sel:[1,0,0] neg_lo:[0,0,1] neg_hi:[0,0,1]
	v_fma_f32 v190, v121, v58, -v190
	v_add_f32_dpp v56, v78, v78 wave_shr:1 row_mask:0xf bank_mask:0xf bound_ctrl:1
	v_add_f32_dpp v57, v79, v79 wave_shr:1 row_mask:0xf bank_mask:0xf bound_ctrl:1
	v_add_f32_dpp v58, v174, v174 wave_shr:1 row_mask:0xf bank_mask:0xf bound_ctrl:1
	v_add_f32_dpp v59, v175, v175 wave_shr:1 row_mask:0xf bank_mask:0xf bound_ctrl:1
	v_add_f32_dpp v60, v180, v180 wave_shr:1 row_mask:0xf bank_mask:0xf bound_ctrl:1
	v_add_f32_dpp v62, v114, v114 wave_shr:1 row_mask:0xf bank_mask:0xf bound_ctrl:1
	v_add_f32_dpp v63, v115, v115 wave_shr:1 row_mask:0xf bank_mask:0xf bound_ctrl:1
	v_add_f32_dpp v64, v176, v176 wave_shr:1 row_mask:0xf bank_mask:0xf bound_ctrl:1
	v_add_f32_dpp v65, v177, v177 wave_shr:1 row_mask:0xf bank_mask:0xf bound_ctrl:1
	v_add_f32_dpp v66, v182, v182 wave_shr:1 row_mask:0xf bank_mask:0xf bound_ctrl:1
	v_add_f32_dpp v68, v124, v124 wave_shr:1 row_mask:0xf bank_mask:0xf bound_ctrl:1
	v_add_f32_dpp v69, v125, v125 wave_shr:1 row_mask:0xf bank_mask:0xf bound_ctrl:1
	v_add_f32_dpp v70, v178, v178 wave_shr:1 row_mask:0xf bank_mask:0xf bound_ctrl:1
	v_add_f32_dpp v71, v179, v179 wave_shr:1 row_mask:0xf bank_mask:0xf bound_ctrl:1
	v_add_f32_dpp v72, v184, v184 wave_shr:1 row_mask:0xf bank_mask:0xf bound_ctrl:1
	v_add_f32_dpp v74, v186, v186 wave_shr:1 row_mask:0xf bank_mask:0xf bound_ctrl:1
	v_add_f32_dpp v75, v187, v187 wave_shr:1 row_mask:0xf bank_mask:0xf bound_ctrl:1
	v_add_f32_dpp v76, v188, v188 wave_shr:1 row_mask:0xf bank_mask:0xf bound_ctrl:1
	v_add_f32_dpp v77, v189, v189 wave_shr:1 row_mask:0xf bank_mask:0xf bound_ctrl:1
	v_add_f32_dpp v80, v190, v190 wave_shr:1 row_mask:0xf bank_mask:0xf bound_ctrl:1
	v_add_f32_dpp v56, v78, v56 wave_shl:1 row_mask:0xf bank_mask:0xf bound_ctrl:1
	v_add_f32_dpp v57, v79, v57 wave_shl:1 row_mask:0xf bank_mask:0xf bound_ctrl:1
	v_add_f32_dpp v58, v174, v58 wave_shl:1 row_mask:0xf bank_mask:0xf bound_ctrl:1
	v_add_f32_dpp v59, v175, v59 wave_shl:1 row_mask:0xf bank_mask:0xf bound_ctrl:1
	v_add_f32_dpp v60, v180, v60 wave_shl:1 row_mask:0xf bank_mask:0xf bound_ctrl:1
	v_add_f32_dpp v62, v114, v62 wave_shl:1 row_mask:0xf bank_mask:0xf bound_ctrl:1
	v_add_f32_dpp v63, v115, v63 wave_shl:1 row_mask:0xf bank_mask:0xf bound_ctrl:1
	v_add_f32_dpp v64, v176, v64 wave_shl:1 row_mask:0xf bank_mask:0xf bound_ctrl:1
	v_add_f32_dpp v65, v177, v65 wave_shl:1 row_mask:0xf bank_mask:0xf bound_ctrl:1
	v_add_f32_dpp v66, v182, v66 wave_shl:1 row_mask:0xf bank_mask:0xf bound_ctrl:1
	v_add_f32_dpp v68, v124, v68 wave_shl:1 row_mask:0xf bank_mask:0xf bound_ctrl:1
	v_add_f32_dpp v69, v125, v69 wave_shl:1 row_mask:0xf bank_mask:0xf bound_ctrl:1
	v_add_f32_dpp v70, v178, v70 wave_shl:1 row_mask:0xf bank_mask:0xf bound_ctrl:1
	v_add_f32_dpp v71, v179, v71 wave_shl:1 row_mask:0xf bank_mask:0xf bound_ctrl:1
	v_add_f32_dpp v72, v184, v72 wave_shl:1 row_mask:0xf bank_mask:0xf bound_ctrl:1
	v_add_f32_dpp v74, v186, v74 wave_shl:1 row_mask:0xf bank_mask:0xf bound_ctrl:1
	v_add_f32_dpp v75, v187, v75 wave_shl:1 row_mask:0xf bank_mask:0xf bound_ctrl:1
	v_add_f32_dpp v76, v188, v76 wave_shl:1 row_mask:0xf bank_mask:0xf bound_ctrl:1
	v_add_f32_dpp v77, v189, v77 wave_shl:1 row_mask:0xf bank_mask:0xf bound_ctrl:1
	v_add_f32_dpp v80, v190, v80 wave_shl:1 row_mask:0xf bank_mask:0xf bound_ctrl:1
	s_add_i32 s4, s34, 4
	s_min_i32 s4, s4, 0x200
	s_mul_i32 s5, s4, 0x804
	s_add_i32 s5, s5, s35
	s_add_i32 s6, s5, 0x101004
	s_add_i32 s7, s5, 0x202008
	s_add_i32 s8, s5, 0x30300c
	s_add_i32 s11, s5, 0x404010
	s_mul_i32 s9, s4, 0x180c
	s_add_i32 s9, s9, s33
	buffer_load_dword v12, v28, s[16:19], s5 offen nt
	buffer_load_dword v13, v28, s[16:19], s6 offen nt
	buffer_load_dword v14, v28, s[16:19], s7 offen nt
	buffer_load_dword v15, v28, s[16:19], s8 offen nt
	buffer_load_dword v16, v28, s[16:19], s11 offen nt
	buffer_load_dwordx3 v[32:34], v27, s[24:27], s9 offen nt
	s_waitcnt vmcnt(12)
	v_pk_mul_f32 v[78:79], v[46:47], v[84:85] op_sel_hi:[1,0]
	v_pk_mul_f32 v[88:89], v[52:53], v[84:85] op_sel_hi:[1,0]
	v_mul_f32_e64 v90, v54, v84
	v_pk_mul_f32 v[114:115], v[46:47], v[84:85] op_sel:[0,1]
	v_pk_mul_f32 v[116:117], v[52:53], v[84:85] op_sel:[0,1]
	v_mul_f32_e64 v118, v54, v85
	v_pk_mul_f32 v[120:121], v[46:47], v[86:87] op_sel_hi:[1,0]
	v_pk_mul_f32 v[122:123], v[52:53], v[86:87] op_sel_hi:[1,0]
	v_mul_f32_e64 v124, v54, v86
	v_add_f32_dpp v174, v46, v46 wave_shr:1 row_mask:0xf bank_mask:0xf bound_ctrl:1
	v_add_f32_dpp v175, v47, v47 wave_shr:1 row_mask:0xf bank_mask:0xf bound_ctrl:1
	v_add_f32_dpp v176, v52, v52 wave_shr:1 row_mask:0xf bank_mask:0xf bound_ctrl:1
	v_add_f32_dpp v177, v53, v53 wave_shr:1 row_mask:0xf bank_mask:0xf bound_ctrl:1
	v_add_f32_dpp v178, v54, v54 wave_shr:1 row_mask:0xf bank_mask:0xf bound_ctrl:1
	v_add_f32_dpp v180, v78, v78 wave_shr:1 row_mask:0xf bank_mask:0xf bound_ctrl:1
	v_add_f32_dpp v181, v79, v79 wave_shr:1 row_mask:0xf bank_mask:0xf bound_ctrl:1
	v_add_f32_dpp v182, v88, v88 wave_shr:1 row_mask:0xf bank_mask:0xf bound_ctrl:1
	v_add_f32_dpp v183, v89, v89 wave_shr:1 row_mask:0xf bank_mask:0xf bound_ctrl:1
	v_add_f32_dpp v184, v90, v90 wave_shr:1 row_mask:0xf bank_mask:0xf bound_ctrl:1
	v_add_f32_dpp v186, v114, v114 wave_shr:1 row_mask:0xf bank_mask:0xf bound_ctrl:1
	v_add_f32_dpp v187, v115, v115 wave_shr:1 row_mask:0xf bank_mask:0xf bound_ctrl:1
	v_add_f32_dpp v188, v116, v116 wave_shr:1 row_mask:0xf bank_mask:0xf bound_ctrl:1
	v_add_f32_dpp v189, v117, v117 wave_shr:1 row_mask:0xf bank_mask:0xf bound_ctrl:1
	v_add_f32_dpp v190, v118, v118 wave_shr:1 row_mask:0xf bank_mask:0xf bound_ctrl:1
	v_add_f32_dpp v192, v120, v120 wave_shr:1 row_mask:0xf bank_mask:0xf bound_ctrl:1
	v_add_f32_dpp v193, v121, v121 wave_shr:1 row_mask:0xf bank_mask:0xf bound_ctrl:1
	v_add_f32_dpp v194, v122, v122 wave_shr:1 row_mask:0xf bank_mask:0xf bound_ctrl:1
	v_add_f32_dpp v195, v123, v123 wave_shr:1 row_mask:0xf bank_mask:0xf bound_ctrl:1
	v_add_f32_dpp v196, v124, v124 wave_shr:1 row_mask:0xf bank_mask:0xf bound_ctrl:1
	v_add_f32_dpp v174, v46, v174 wave_shl:1 row_mask:0xf bank_mask:0xf bound_ctrl:1
	v_add_f32_dpp v175, v47, v175 wave_shl:1 row_mask:0xf bank_mask:0xf bound_ctrl:1
	v_add_f32_dpp v176, v52, v176 wave_shl:1 row_mask:0xf bank_mask:0xf bound_ctrl:1
	v_add_f32_dpp v177, v53, v177 wave_shl:1 row_mask:0xf bank_mask:0xf bound_ctrl:1
	v_add_f32_dpp v178, v54, v178 wave_shl:1 row_mask:0xf bank_mask:0xf bound_ctrl:1
	v_add_f32_dpp v180, v78, v180 wave_shl:1 row_mask:0xf bank_mask:0xf bound_ctrl:1
	v_add_f32_dpp v181, v79, v181 wave_shl:1 row_mask:0xf bank_mask:0xf bound_ctrl:1
	v_add_f32_dpp v182, v88, v182 wave_shl:1 row_mask:0xf bank_mask:0xf bound_ctrl:1
	v_add_f32_dpp v183, v89, v183 wave_shl:1 row_mask:0xf bank_mask:0xf bound_ctrl:1
	v_add_f32_dpp v184, v90, v184 wave_shl:1 row_mask:0xf bank_mask:0xf bound_ctrl:1
	v_add_f32_dpp v186, v114, v186 wave_shl:1 row_mask:0xf bank_mask:0xf bound_ctrl:1
	v_add_f32_dpp v187, v115, v187 wave_shl:1 row_mask:0xf bank_mask:0xf bound_ctrl:1
	v_add_f32_dpp v188, v116, v188 wave_shl:1 row_mask:0xf bank_mask:0xf bound_ctrl:1
	v_add_f32_dpp v189, v117, v189 wave_shl:1 row_mask:0xf bank_mask:0xf bound_ctrl:1
	v_add_f32_dpp v190, v118, v190 wave_shl:1 row_mask:0xf bank_mask:0xf bound_ctrl:1
	v_add_f32_dpp v192, v120, v192 wave_shl:1 row_mask:0xf bank_mask:0xf bound_ctrl:1
	v_add_f32_dpp v193, v121, v193 wave_shl:1 row_mask:0xf bank_mask:0xf bound_ctrl:1
	v_add_f32_dpp v194, v122, v194 wave_shl:1 row_mask:0xf bank_mask:0xf bound_ctrl:1
	v_add_f32_dpp v195, v123, v195 wave_shl:1 row_mask:0xf bank_mask:0xf bound_ctrl:1
	v_add_f32_dpp v196, v124, v196 wave_shl:1 row_mask:0xf bank_mask:0xf bound_ctrl:1
	s_barrier
	ds_read_b128 v[88:91], v23 offset:0
	ds_read_b128 v[116:119], v23 offset:1024
	ds_read_b128 v[120:123], v23 offset:2048
	v_pk_add_f32 v[78:79], v[150:151], v[174:175]
	v_pk_add_f32 v[114:115], v[126:127], v[78:79]
	v_pk_add_f32 v[124:125], v[152:153], v[176:177]
	v_pk_add_f32 v[126:127], v[128:129], v[124:125]
	v_add_f32_e64 v128, v154, v178
	v_add_f32_e64 v150, v130, v128
	v_pk_add_f32 v[130:131], v[156:157], v[180:181]
	v_pk_add_f32 v[152:153], v[132:133], v[130:131]
	v_pk_add_f32 v[132:133], v[158:159], v[182:183]
	v_pk_add_f32 v[154:155], v[134:135], v[132:133]
	v_add_f32_e64 v134, v160, v184
	v_add_f32_e64 v156, v136, v134
	v_pk_add_f32 v[136:137], v[162:163], v[186:187]
	v_pk_add_f32 v[158:159], v[138:139], v[136:137]
	v_pk_add_f32 v[138:139], v[164:165], v[188:189]
	v_pk_add_f32 v[160:161], v[140:141], v[138:139]
	v_add_f32_e64 v140, v166, v190
	v_add_f32_e64 v162, v142, v140
	v_pk_add_f32 v[142:143], v[168:169], v[192:193]
	v_pk_add_f32 v[164:165], v[144:145], v[142:143]
	v_pk_add_f32 v[144:145], v[170:171], v[194:195]
	v_pk_add_f32 v[166:167], v[146:147], v[144:145]
	v_add_f32_e64 v146, v172, v196
	v_add_f32_e64 v168, v148, v146
	s_waitcnt lgkmcnt(2)
	v_pk_fma_f32 v[152:153], v[88:89], v[114:115], v[152:153] op_sel_hi:[0,1,1] neg_lo:[1,0,0] neg_hi:[1,0,0]
	v_pk_fma_f32 v[154:155], v[88:89], v[126:127], v[154:155] op_sel_hi:[0,1,1] neg_lo:[1,0,0] neg_hi:[1,0,0]
	v_fma_f32 v156, -v88, v150, v156
	v_pk_fma_f32 v[158:159], v[88:89], v[114:115], v[158:159] op_sel:[1,0,0] neg_lo:[1,0,0] neg_hi:[1,0,0]
	v_pk_fma_f32 v[160:161], v[88:89], v[126:127], v[160:161] op_sel:[1,0,0] neg_lo:[1,0,0] neg_hi:[1,0,0]
	v_fma_f32 v162, -v89, v150, v162
	v_pk_fma_f32 v[164:165], v[90:91], v[114:115], v[164:165] op_sel_hi:[0,1,1] neg_lo:[1,0,0] neg_hi:[1,0,0]
	v_pk_fma_f32 v[166:167], v[90:91], v[126:127], v[166:167] op_sel_hi:[0,1,1] neg_lo:[1,0,0] neg_hi:[1,0,0]
	v_fma_f32 v168, -v90, v150, v168
	v_pk_mul_f32 v[148:149], v[90:91], v[152:153] op_sel:[1,0]
	v_pk_mul_f32 v[198:199], v[90:91], v[154:155] op_sel:[1,0]
	v_mul_f32_e64 v204, v91, v156
	s_waitcnt lgkmcnt(1)
	v_pk_mul_f32 v[170:171], v[116:117], v[152:153] op_sel_hi:[0,1]
	v_pk_mul_f32 v[200:201], v[116:117], v[154:155] op_sel_hi:[0,1]
	v_mul_f32_e64 v206, v116, v156
	v_pk_mul_f32 v[172:173], v[116:117], v[152:153] op_sel:[1,0]
	v_pk_mul_f32 v[202:203], v[116:117], v[154:155] op_sel:[1,0]
	v_mul_f32_e64 v208, v117, v156
	v_pk_fma_f32 v[148:149], v[116:117], v[158:159], v[148:149] op_sel_hi:[0,1,1]
	v_pk_fma_f32 v[198:199], v[116:117], v[160:161], v[198:199] op_sel_hi:[0,1,1]
	v_fma_f32 v204, v116, v162, v204
	v_pk_fma_f32 v[170:171], v[118:119], v[158:159], v[170:171] op_sel_hi:[0,1,1]
	v_pk_fma_f32 v[200:201], v[118:119], v[160:161], v[200:201] op_sel_hi:[0,1,1]
	v_fma_f32 v206, v118, v162, v206
	v_pk_fma_f32 v[172:173], v[118:119], v[158:159], v[172:173] op_sel:[1,0,0]
	v_pk_fma_f32 v[202:203], v[118:119], v[160:161], v[202:203] op_sel:[1,0,0]
	v_fma_f32 v208, v119, v162, v208
	v_pk_fma_f32 v[148:149], v[116:117], v[164:165], v[148:149] op_sel:[1,0,0]
	v_pk_fma_f32 v[198:199], v[116:117], v[166:167], v[198:199] op_sel:[1,0,0]
	v_fma_f32 v204, v117, v168, v204
	v_pk_fma_f32 v[170:171], v[118:119], v[164:165], v[170:171] op_sel:[1,0,0]
	v_pk_fma_f32 v[200:201], v[118:119], v[166:167], v[200:201] op_sel:[1,0,0]
	v_fma_f32 v206, v119, v168, v206
	s_waitcnt lgkmcnt(0)
	v_pk_fma_f32 v[172:173], v[120:121], v[164:165], v[172:173] op_sel_hi:[0,1,1]
	v_pk_fma_f32 v[202:203], v[120:121], v[166:167], v[202:203] op_sel_hi:[0,1,1]
	v_fma_f32 v208, v120, v168, v208
	v_pk_mul_f32 v[210:211], v[88:89], v[148:149] op_sel_hi:[0,1]
	v_pk_mul_f32 v[212:213], v[88:89], v[198:199] op_sel_hi:[0,1]
	v_mul_f32_e64 v214, v88, v204
	v_pk_fma_f32 v[210:211], v[88:89], v[170:171], v[210:211] op_sel:[1,0,0]
	v_pk_fma_f32 v[212:213], v[88:89], v[200:201], v[212:213] op_sel:[1,0,0]
	v_fma_f32 v214, v89, v206, v214
	v_pk_fma_f32 v[210:211], v[90:91], v[172:173], v[210:211] op_sel_hi:[0,1,1]
	v_pk_fma_f32 v[212:213], v[90:91], v[202:203], v[212:213] op_sel_hi:[0,1,1]
	v_fma_f32 v214, v90, v208, v214
	v_pk_fma_f32 v[210:211], v[120:121], v[114:115], v[210:211] op_sel:[1,0,0] neg_lo:[0,0,1] neg_hi:[0,0,1]
	v_pk_fma_f32 v[212:213], v[120:121], v[126:127], v[212:213] op_sel:[1,0,0] neg_lo:[0,0,1] neg_hi:[0,0,1]
	v_fma_f32 v214, v121, v150, -v214
	v_cmp_eq_u32_e64 s[10:11], 1, v123
	v_cmp_eq_u32_e64 s[14:15], 2, v123
	v_cmp_eq_u32_e64 s[20:21], 3, v123
	v_cmp_eq_u32_e64 s[22:23], 4, v123
	v_cmp_eq_u32_e64 s[30:31], 5, v123
	v_add_f32_dpp v114, v148, v148 wave_shr:1 row_mask:0xf bank_mask:0xf bound_ctrl:1
	v_add_f32_dpp v115, v149, v149 wave_shr:1 row_mask:0xf bank_mask:0xf bound_ctrl:1
	v_add_f32_dpp v126, v198, v198 wave_shr:1 row_mask:0xf bank_mask:0xf bound_ctrl:1
	v_add_f32_dpp v127, v199, v199 wave_shr:1 row_mask:0xf bank_mask:0xf bound_ctrl:1
	v_add_f32_dpp v150, v204, v204 wave_shr:1 row_mask:0xf bank_mask:0xf bound_ctrl:1
	v_add_f32_dpp v152, v170, v170 wave_shr:1 row_mask:0xf bank_mask:0xf bound_ctrl:1
	v_add_f32_dpp v153, v171, v171 wave_shr:1 row_mask:0xf bank_mask:0xf bound_ctrl:1
	v_add_f32_dpp v154, v200, v200 wave_shr:1 row_mask:0xf bank_mask:0xf bound_ctrl:1
	v_add_f32_dpp v155, v201, v201 wave_shr:1 row_mask:0xf bank_mask:0xf bound_ctrl:1
	v_add_f32_dpp v156, v206, v206 wave_shr:1 row_mask:0xf bank_mask:0xf bound_ctrl:1
	v_add_f32_dpp v158, v172, v172 wave_shr:1 row_mask:0xf bank_mask:0xf bound_ctrl:1
	v_add_f32_dpp v159, v173, v173 wave_shr:1 row_mask:0xf bank_mask:0xf bound_ctrl:1
	v_add_f32_dpp v160, v202, v202 wave_shr:1 row_mask:0xf bank_mask:0xf bound_ctrl:1
	v_add_f32_dpp v161, v203, v203 wave_shr:1 row_mask:0xf bank_mask:0xf bound_ctrl:1
	v_add_f32_dpp v162, v208, v208 wave_shr:1 row_mask:0xf bank_mask:0xf bound_ctrl:1
	v_add_f32_dpp v164, v210, v210 wave_shr:1 row_mask:0xf bank_mask:0xf bound_ctrl:1
	v_add_f32_dpp v165, v211, v211 wave_shr:1 row_mask:0xf bank_mask:0xf bound_ctrl:1
	v_add_f32_dpp v166, v212, v212 wave_shr:1 row_mask:0xf bank_mask:0xf bound_ctrl:1
	v_add_f32_dpp v167, v213, v213 wave_shr:1 row_mask:0xf bank_mask:0xf bound_ctrl:1
	v_add_f32_dpp v168, v214, v214 wave_shr:1 row_mask:0xf bank_mask:0xf bound_ctrl:1
	v_add_f32_dpp v114, v148, v114 wave_shl:1 row_mask:0xf bank_mask:0xf bound_ctrl:1
	v_add_f32_dpp v115, v149, v115 wave_shl:1 row_mask:0xf bank_mask:0xf bound_ctrl:1
	v_add_f32_dpp v126, v198, v126 wave_shl:1 row_mask:0xf bank_mask:0xf bound_ctrl:1
	v_add_f32_dpp v127, v199, v127 wave_shl:1 row_mask:0xf bank_mask:0xf bound_ctrl:1
	v_add_f32_dpp v150, v204, v150 wave_shl:1 row_mask:0xf bank_mask:0xf bound_ctrl:1
	v_add_f32_dpp v152, v170, v152 wave_shl:1 row_mask:0xf bank_mask:0xf bound_ctrl:1
	v_add_f32_dpp v153, v171, v153 wave_shl:1 row_mask:0xf bank_mask:0xf bound_ctrl:1
	v_add_f32_dpp v154, v200, v154 wave_shl:1 row_mask:0xf bank_mask:0xf bound_ctrl:1
	v_add_f32_dpp v155, v201, v155 wave_shl:1 row_mask:0xf bank_mask:0xf bound_ctrl:1
	v_add_f32_dpp v156, v206, v156 wave_shl:1 row_mask:0xf bank_mask:0xf bound_ctrl:1
	v_add_f32_dpp v158, v172, v158 wave_shl:1 row_mask:0xf bank_mask:0xf bound_ctrl:1
	v_add_f32_dpp v159, v173, v159 wave_shl:1 row_mask:0xf bank_mask:0xf bound_ctrl:1
	v_add_f32_dpp v160, v202, v160 wave_shl:1 row_mask:0xf bank_mask:0xf bound_ctrl:1
	v_add_f32_dpp v161, v203, v161 wave_shl:1 row_mask:0xf bank_mask:0xf bound_ctrl:1
	v_add_f32_dpp v162, v208, v162 wave_shl:1 row_mask:0xf bank_mask:0xf bound_ctrl:1
	v_add_f32_dpp v164, v210, v164 wave_shl:1 row_mask:0xf bank_mask:0xf bound_ctrl:1
	v_add_f32_dpp v165, v211, v165 wave_shl:1 row_mask:0xf bank_mask:0xf bound_ctrl:1
	v_add_f32_dpp v166, v212, v166 wave_shl:1 row_mask:0xf bank_mask:0xf bound_ctrl:1
	v_add_f32_dpp v167, v213, v167 wave_shl:1 row_mask:0xf bank_mask:0xf bound_ctrl:1
	v_add_f32_dpp v168, v214, v168 wave_shl:1 row_mask:0xf bank_mask:0xf bound_ctrl:1
	v_pk_add_f32 v[148:149], v[56:57], v[114:115]
	v_pk_add_f32 v[170:171], v[82:83], v[148:149]
	v_pk_add_f32 v[56:57], v[58:59], v[126:127]
	v_pk_add_f32 v[82:83], v[92:93], v[56:57]
	v_add_f32_e64 v58, v60, v150
	v_add_f32_e64 v92, v94, v58
	v_pk_add_f32 v[60:61], v[62:63], v[152:153]
	v_pk_add_f32 v[94:95], v[96:97], v[60:61]
	v_pk_add_f32 v[62:63], v[64:65], v[154:155]
	v_pk_add_f32 v[96:97], v[98:99], v[62:63]
	v_add_f32_e64 v64, v66, v156
	v_add_f32_e64 v98, v100, v64
	v_pk_add_f32 v[66:67], v[68:69], v[158:159]
	v_pk_add_f32 v[100:101], v[102:103], v[66:67]
	v_pk_add_f32 v[68:69], v[70:71], v[160:161]
	v_pk_add_f32 v[102:103], v[104:105], v[68:69]
	v_add_f32_e64 v70, v72, v162
	v_add_f32_e64 v104, v106, v70
	v_pk_add_f32 v[72:73], v[74:75], v[164:165]
	v_pk_add_f32 v[106:107], v[108:109], v[72:73]
	v_pk_add_f32 v[74:75], v[76:77], v[166:167]
	v_pk_add_f32 v[108:109], v[110:111], v[74:75]
	v_add_f32_e64 v76, v80, v168
	v_add_f32_e64 v110, v112, v76
	v_pk_fma_f32 v[106:107], v[36:37], v[170:171], v[106:107] op_sel_hi:[0,1,1]
	v_pk_fma_f32 v[108:109], v[36:37], v[82:83], v[108:109] op_sel_hi:[0,1,1]
	v_fma_f32 v110, v36, v92, v110
	v_pk_fma_f32 v[106:107], v[36:37], v[94:95], v[106:107] op_sel:[1,0,0]
	v_pk_fma_f32 v[108:109], v[36:37], v[96:97], v[108:109] op_sel:[1,0,0]
	v_fma_f32 v110, v37, v98, v110
	v_pk_fma_f32 v[106:107], v[38:39], v[100:101], v[106:107] op_sel_hi:[0,1,1]
	v_pk_fma_f32 v[108:109], v[38:39], v[102:103], v[108:109] op_sel_hi:[0,1,1]
	v_fma_f32 v110, v38, v104, v110
	v_cndmask_b32_e64 v80, 0, v1, s[10:11]
	v_cndmask_b32_e64 v81, 0, v1, s[14:15]
	v_cndmask_b32_e64 v112, 0, v1, s[20:21]
	v_cndmask_b32_e64 v113, 0, v1, s[22:23]
	v_cndmask_b32_e64 v172, 0, v1, s[30:31]
	v_pk_fma_f32 v[106:107], v[20:21], v[122:123], v[106:107] op_sel_hi:[1,0,1] neg_lo:[0,0,1] neg_hi:[0,0,1]
	v_pk_fma_f32 v[108:109], v[24:25], v[122:123], v[108:109] op_sel_hi:[1,0,1] neg_lo:[0,0,1] neg_hi:[0,0,1]
	v_fma_f32 v110, v30, v122, -v110
	s_add_i32 s4, s34, 0
	s_cmpk_lt_i32 s4, 0x201
	s_cselect_b64 s[12:13], s[0:1], 0
	v_pk_add_f32 v[106:107], v[106:107], v[80:81] neg_lo:[0,1] neg_hi:[0,1]
	v_pk_add_f32 v[108:109], v[108:109], v[112:113] neg_lo:[0,1] neg_hi:[0,1]
	v_add_f32_e64 v110, v110, -v172
	v_pk_mul_f32 v[198:199], v[106:107], v[106:107]
	v_pk_fma_f32 v[198:199], v[108:109], v[108:109], v[198:199]
	v_add_f32_e32 v198, v198, v199
	v_fma_f32 v198, v110, v110, v198
	v_cndmask_b32_e64 v199, 0, v198, s[12:13]
	v_add_f32_e32 v0, v0, v199
	s_add_i32 s4, s34, 5
	s_min_i32 s4, s4, 0x200
	s_mul_i32 s5, s4, 0x804
	s_add_i32 s5, s5, s35
	s_add_i32 s6, s5, 0x101004
	s_add_i32 s7, s5, 0x202008
	s_add_i32 s8, s5, 0x30300c
	s_add_i32 s11, s5, 0x404010
	s_mul_i32 s9, s4, 0x180c
	s_add_i32 s9, s9, s33
	buffer_load_dword v20, v28, s[16:19], s5 offen nt
	buffer_load_dword v21, v28, s[16:19], s6 offen nt
	buffer_load_dword v24, v28, s[16:19], s7 offen nt
	buffer_load_dword v25, v28, s[16:19], s8 offen nt
	buffer_load_dword v30, v28, s[16:19], s11 offen nt
	buffer_load_dwordx3 v[36:38], v27, s[24:27], s9 offen nt
	s_waitcnt vmcnt(12)
	v_pk_mul_f32 v[80:81], v[2:3], v[8:9] op_sel_hi:[1,0]
	v_pk_mul_f32 v[82:83], v[4:5], v[8:9] op_sel_hi:[1,0]
	v_mul_f32_e64 v88, v6, v8
	v_pk_mul_f32 v[90:91], v[2:3], v[8:9] op_sel:[0,1]
	v_pk_mul_f32 v[92:93], v[4:5], v[8:9] op_sel:[0,1]
	v_mul_f32_e64 v94, v6, v9
	v_pk_mul_f32 v[96:97], v[2:3], v[10:11] op_sel_hi:[1,0]
	v_pk_mul_f32 v[98:99], v[4:5], v[10:11] op_sel_hi:[1,0]
	v_mul_f32_e64 v100, v6, v10
	v_add_f32_dpp v102, v2, v2 wave_shr:1 row_mask:0xf bank_mask:0xf bound_ctrl:1
	v_add_f32_dpp v103, v3, v3 wave_shr:1 row_mask:0xf bank_mask:0xf bound_ctrl:1
	v_add_f32_dpp v104, v4, v4 wave_shr:1 row_mask:0xf bank_mask:0xf bound_ctrl:1
	v_add_f32_dpp v105, v5, v5 wave_shr:1 row_mask:0xf bank_mask:0xf bound_ctrl:1
	v_add_f32_dpp v106, v6, v6 wave_shr:1 row_mask:0xf bank_mask:0xf bound_ctrl:1
	v_add_f32_dpp v108, v80, v80 wave_shr:1 row_mask:0xf bank_mask:0xf bound_ctrl:1
	v_add_f32_dpp v109, v81, v81 wave_shr:1 row_mask:0xf bank_mask:0xf bound_ctrl:1
	v_add_f32_dpp v110, v82, v82 wave_shr:1 row_mask:0xf bank_mask:0xf bound_ctrl:1
	v_add_f32_dpp v111, v83, v83 wave_shr:1 row_mask:0xf bank_mask:0xf bound_ctrl:1
	v_add_f32_dpp v112, v88, v88 wave_shr:1 row_mask:0xf bank_mask:0xf bound_ctrl:1
	v_add_f32_dpp v116, v90, v90 wave_shr:1 row_mask:0xf bank_mask:0xf bound_ctrl:1
	v_add_f32_dpp v117, v91, v91 wave_shr:1 row_mask:0xf bank_mask:0xf bound_ctrl:1
	v_add_f32_dpp v118, v92, v92 wave_shr:1 row_mask:0xf bank_mask:0xf bound_ctrl:1
	v_add_f32_dpp v119, v93, v93 wave_shr:1 row_mask:0xf bank_mask:0xf bound_ctrl:1
	v_add_f32_dpp v120, v94, v94 wave_shr:1 row_mask:0xf bank_mask:0xf bound_ctrl:1
	v_add_f32_dpp v122, v96, v96 wave_shr:1 row_mask:0xf bank_mask:0xf bound_ctrl:1
	v_add_f32_dpp v123, v97, v97 wave_shr:1 row_mask:0xf bank_mask:0xf bound_ctrl:1
	v_add_f32_dpp v170, v98, v98 wave_shr:1 row_mask:0xf bank_mask:0xf bound_ctrl:1
	v_add_f32_dpp v171, v99, v99 wave_shr:1 row_mask:0xf bank_mask:0xf bound_ctrl:1
	v_add_f32_dpp v172, v100, v100 wave_shr:1 row_mask:0xf bank_mask:0xf bound_ctrl:1
	v_add_f32_dpp v102, v2, v102 wave_shl:1 row_mask:0xf bank_mask:0xf bound_ctrl:1
	v_add_f32_dpp v103, v3, v103 wave_shl:1 row_mask:0xf bank_mask:0xf bound_ctrl:1
	v_add_f32_dpp v104, v4, v104 wave_shl:1 row_mask:0xf bank_mask:0xf bound_ctrl:1
	v_add_f32_dpp v105, v5, v105 wave_shl:1 row_mask:0xf bank_mask:0xf bound_ctrl:1
	v_add_f32_dpp v106, v6, v106 wave_shl:1 row_mask:0xf bank_mask:0xf bound_ctrl:1
	v_add_f32_dpp v108, v80, v108 wave_shl:1 row_mask:0xf bank_mask:0xf bound_ctrl:1
	v_add_f32_dpp v109, v81, v109 wave_shl:1 row_mask:0xf bank_mask:0xf bound_ctrl:1
	v_add_f32_dpp v110, v82, v110 wave_shl:1 row_mask:0xf bank_mask:0xf bound_ctrl:1
	v_add_f32_dpp v111, v83, v111 wave_shl:1 row_mask:0xf bank_mask:0xf bound_ctrl:1
	v_add_f32_dpp v112, v88, v112 wave_shl:1 row_mask:0xf bank_mask:0xf bound_ctrl:1
	v_add_f32_dpp v116, v90, v116 wave_shl:1 row_mask:0xf bank_mask:0xf bound_ctrl:1
	v_add_f32_dpp v117, v91, v117 wave_shl:1 row_mask:0xf bank_mask:0xf bound_ctrl:1
	v_add_f32_dpp v118, v92, v118 wave_shl:1 row_mask:0xf bank_mask:0xf bound_ctrl:1
	v_add_f32_dpp v119, v93, v119 wave_shl:1 row_mask:0xf bank_mask:0xf bound_ctrl:1
	v_add_f32_dpp v120, v94, v120 wave_shl:1 row_mask:0xf bank_mask:0xf bound_ctrl:1
	v_add_f32_dpp v122, v96, v122 wave_shl:1 row_mask:0xf bank_mask:0xf bound_ctrl:1
	v_add_f32_dpp v123, v97, v123 wave_shl:1 row_mask:0xf bank_mask:0xf bound_ctrl:1
	v_add_f32_dpp v170, v98, v170 wave_shl:1 row_mask:0xf bank_mask:0xf bound_ctrl:1
	v_add_f32_dpp v171, v99, v171 wave_shl:1 row_mask:0xf bank_mask:0xf bound_ctrl:1
	v_add_f32_dpp v172, v100, v172 wave_shl:1 row_mask:0xf bank_mask:0xf bound_ctrl:1
	s_barrier
	ds_read_b128 v[80:83], v23 offset:3072
	ds_read_b128 v[88:91], v23 offset:4096
	ds_read_b128 v[92:95], v23 offset:5120
	v_pk_add_f32 v[96:97], v[78:79], v[102:103]
	v_pk_add_f32 v[78:79], v[124:125], v[104:105]
	v_add_f32_e64 v98, v128, v106
	v_pk_add_f32 v[100:101], v[130:131], v[108:109]
	v_pk_add_f32 v[124:125], v[132:133], v[110:111]
	v_add_f32_e64 v128, v134, v112
	v_pk_add_f32 v[130:131], v[136:137], v[116:117]
	v_pk_add_f32 v[132:133], v[138:139], v[118:119]
	v_add_f32_e64 v134, v140, v120
	v_pk_add_f32 v[136:137], v[142:143], v[122:123]
	v_pk_add_f32 v[138:139], v[144:145], v[170:171]
	v_add_f32_e64 v140, v146, v172
	s_waitcnt lgkmcnt(2)
	v_pk_fma_f32 v[100:101], v[80:81], v[96:97], v[100:101] op_sel_hi:[0,1,1] neg_lo:[1,0,0] neg_hi:[1,0,0]
	v_pk_fma_f32 v[124:125], v[80:81], v[78:79], v[124:125] op_sel_hi:[0,1,1] neg_lo:[1,0,0] neg_hi:[1,0,0]
	v_fma_f32 v128, -v80, v98, v128
	v_pk_fma_f32 v[130:131], v[80:81], v[96:97], v[130:131] op_sel:[1,0,0] neg_lo:[1,0,0] neg_hi:[1,0,0]
	v_pk_fma_f32 v[132:133], v[80:81], v[78:79], v[132:133] op_sel:[1,0,0] neg_lo:[1,0,0] neg_hi:[1,0,0]
	v_fma_f32 v134, -v81, v98, v134
	v_pk_fma_f32 v[136:137], v[82:83], v[96:97], v[136:137] op_sel_hi:[0,1,1] neg_lo:[1,0,0] neg_hi:[1,0,0]
	v_pk_fma_f32 v[138:139], v[82:83], v[78:79], v[138:139] op_sel_hi:[0,1,1] neg_lo:[1,0,0] neg_hi:[1,0,0]
	v_fma_f32 v140, -v82, v98, v140
	v_pk_mul_f32 v[142:143], v[82:83], v[100:101] op_sel:[1,0]
	v_pk_mul_f32 v[198:199], v[82:83], v[124:125] op_sel:[1,0]
	v_mul_f32_e64 v204, v83, v128
	s_waitcnt lgkmcnt(1)
	v_pk_mul_f32 v[144:145], v[88:89], v[100:101] op_sel_hi:[0,1]
	v_pk_mul_f32 v[200:201], v[88:89], v[124:125] op_sel_hi:[0,1]
	v_mul_f32_e64 v206, v88, v128
	v_pk_mul_f32 v[146:147], v[88:89], v[100:101] op_sel:[1,0]
	v_pk_mul_f32 v[202:203], v[88:89], v[124:125] op_sel:[1,0]
	v_mul_f32_e64 v208, v89, v128
	v_pk_fma_f32 v[142:143], v[88:89], v[130:131], v[142:143] op_sel_hi:[0,1,1]
	v_pk_fma_f32 v[198:199], v[88:89], v[132:133], v[198:199] op_sel_hi:[0,1,1]
	v_fma_f32 v204, v88, v134, v204
	v_pk_fma_f32 v[144:145], v[90:91], v[130:131], v[144:145] op_sel_hi:[0,1,1]
	v_pk_fma_f32 v[200:201], v[90:91], v[132:133], v[200:201] op_sel_hi:[0,1,1]
	v_fma_f32 v206, v90, v134, v206
	v_pk_fma_f32 v[146:147], v[90:91], v[130:131], v[146:147] op_sel:[1,0,0]
	v_pk_fma_f32 v[202:203], v[90:91], v[132:133], v[202:203] op_sel:[1,0,0]
	v_fma_f32 v208, v91, v134, v208
	v_pk_fma_f32 v[142:143], v[88:89], v[136:137], v[142:143] op_sel:[1,0,0]
	v_pk_fma_f32 v[198:199], v[88:89], v[138:139], v[198:199] op_sel:[1,0,0]
	v_fma_f32 v204, v89, v140, v204
	v_pk_fma_f32 v[144:145], v[90:91], v[136:137], v[144:145] op_sel:[1,0,0]
	v_pk_fma_f32 v[200:201], v[90:91], v[138:139], v[200:201] op_sel:[1,0,0]
	v_fma_f32 v206, v91, v140, v206
	s_waitcnt lgkmcnt(0)
	v_pk_fma_f32 v[146:147], v[92:93], v[136:137], v[146:147] op_sel_hi:[0,1,1]
	v_pk_fma_f32 v[202:203], v[92:93], v[138:139], v[202:203] op_sel_hi:[0,1,1]
	v_fma_f32 v208, v92, v140, v208
	v_pk_mul_f32 v[210:211], v[80:81], v[142:143] op_sel_hi:[0,1]
	v_pk_mul_f32 v[212:213], v[80:81], v[198:199] op_sel_hi:[0,1]
	v_mul_f32_e64 v214, v80, v204
	v_pk_fma_f32 v[210:211], v[80:81], v[144:145], v[210:211] op_sel:[1,0,0]
	v_pk_fma_f32 v[212:213], v[80:81], v[200:201], v[212:213] op_sel:[1,0,0]
	v_fma_f32 v214, v81, v206, v214
	v_pk_fma_f32 v[210:211], v[82:83], v[146:147], v[210:211] op_sel_hi:[0,1,1]
	v_pk_fma_f32 v[212:213], v[82:83], v[202:203], v[212:213] op_sel_hi:[0,1,1]
	v_fma_f32 v214, v82, v208, v214
	v_pk_fma_f32 v[210:211], v[92:93], v[96:97], v[210:211] op_sel:[1,0,0] neg_lo:[0,0,1] neg_hi:[0,0,1]
	v_pk_fma_f32 v[212:213], v[92:93], v[78:79], v[212:213] op_sel:[1,0,0] neg_lo:[0,0,1] neg_hi:[0,0,1]
	v_fma_f32 v214, v93, v98, -v214
	v_cmp_eq_u32_e64 s[10:11], 1, v95
	v_cmp_eq_u32_e64 s[14:15], 2, v95
	v_cmp_eq_u32_e64 s[20:21], 3, v95
	v_cmp_eq_u32_e64 s[22:23], 4, v95
	v_cmp_eq_u32_e64 s[30:31], 5, v95
	v_add_f32_dpp v78, v142, v142 wave_shr:1 row_mask:0xf bank_mask:0xf bound_ctrl:1
	v_add_f32_dpp v79, v143, v143 wave_shr:1 row_mask:0xf bank_mask:0xf bound_ctrl:1
	v_add_f32_dpp v96, v198, v198 wave_shr:1 row_mask:0xf bank_mask:0xf bound_ctrl:1
	v_add_f32_dpp v97, v199, v199 wave_shr:1 row_mask:0xf bank_mask:0xf bound_ctrl:1
	v_add_f32_dpp v98, v204, v204 wave_shr:1 row_mask:0xf bank_mask:0xf bound_ctrl:1
	v_add_f32_dpp v100, v144, v144 wave_shr:1 row_mask:0xf bank_mask:0xf bound_ctrl:1
	v_add_f32_dpp v101, v145, v145 wave_shr:1 row_mask:0xf bank_mask:0xf bound_ctrl:1
	v_add_f32_dpp v124, v200, v200 wave_shr:1 row_mask:0xf bank_mask:0xf bound_ctrl:1
	v_add_f32_dpp v125, v201, v201 wave_shr:1 row_mask:0xf bank_mask:0xf bound_ctrl:1
	v_add_f32_dpp v128, v206, v206 wave_shr:1 row_mask:0xf bank_mask:0xf bound_ctrl:1
	v_add_f32_dpp v130, v146, v146 wave_shr:1 row_mask:0xf bank_mask:0xf bound_ctrl:1
	v_add_f32_dpp v131, v147, v147 wave_shr:1 row_mask:0xf bank_mask:0xf bound_ctrl:1
	v_add_f32_dpp v132, v202, v202 wave_shr:1 row_mask:0xf bank_mask:0xf bound_ctrl:1
	v_add_f32_dpp v133, v203, v203 wave_shr:1 row_mask:0xf bank_mask:0xf bound_ctrl:1
	v_add_f32_dpp v134, v208, v208 wave_shr:1 row_mask:0xf bank_mask:0xf bound_ctrl:1
	v_add_f32_dpp v136, v210, v210 wave_shr:1 row_mask:0xf bank_mask:0xf bound_ctrl:1
	v_add_f32_dpp v137, v211, v211 wave_shr:1 row_mask:0xf bank_mask:0xf bound_ctrl:1
	v_add_f32_dpp v138, v212, v212 wave_shr:1 row_mask:0xf bank_mask:0xf bound_ctrl:1
	v_add_f32_dpp v139, v213, v213 wave_shr:1 row_mask:0xf bank_mask:0xf bound_ctrl:1
	v_add_f32_dpp v140, v214, v214 wave_shr:1 row_mask:0xf bank_mask:0xf bound_ctrl:1
	v_add_f32_dpp v78, v142, v78 wave_shl:1 row_mask:0xf bank_mask:0xf bound_ctrl:1
	v_add_f32_dpp v79, v143, v79 wave_shl:1 row_mask:0xf bank_mask:0xf bound_ctrl:1
	v_add_f32_dpp v96, v198, v96 wave_shl:1 row_mask:0xf bank_mask:0xf bound_ctrl:1
	v_add_f32_dpp v97, v199, v97 wave_shl:1 row_mask:0xf bank_mask:0xf bound_ctrl:1
	v_add_f32_dpp v98, v204, v98 wave_shl:1 row_mask:0xf bank_mask:0xf bound_ctrl:1
	v_add_f32_dpp v100, v144, v100 wave_shl:1 row_mask:0xf bank_mask:0xf bound_ctrl:1
	v_add_f32_dpp v101, v145, v101 wave_shl:1 row_mask:0xf bank_mask:0xf bound_ctrl:1
	v_add_f32_dpp v124, v200, v124 wave_shl:1 row_mask:0xf bank_mask:0xf bound_ctrl:1
	v_add_f32_dpp v125, v201, v125 wave_shl:1 row_mask:0xf bank_mask:0xf bound_ctrl:1
	v_add_f32_dpp v128, v206, v128 wave_shl:1 row_mask:0xf bank_mask:0xf bound_ctrl:1
	v_add_f32_dpp v130, v146, v130 wave_shl:1 row_mask:0xf bank_mask:0xf bound_ctrl:1
	v_add_f32_dpp v131, v147, v131 wave_shl:1 row_mask:0xf bank_mask:0xf bound_ctrl:1
	v_add_f32_dpp v132, v202, v132 wave_shl:1 row_mask:0xf bank_mask:0xf bound_ctrl:1
	v_add_f32_dpp v133, v203, v133 wave_shl:1 row_mask:0xf bank_mask:0xf bound_ctrl:1
	v_add_f32_dpp v134, v208, v134 wave_shl:1 row_mask:0xf bank_mask:0xf bound_ctrl:1
	v_add_f32_dpp v136, v210, v136 wave_shl:1 row_mask:0xf bank_mask:0xf bound_ctrl:1
	v_add_f32_dpp v137, v211, v137 wave_shl:1 row_mask:0xf bank_mask:0xf bound_ctrl:1
	v_add_f32_dpp v138, v212, v138 wave_shl:1 row_mask:0xf bank_mask:0xf bound_ctrl:1
	v_add_f32_dpp v139, v213, v139 wave_shl:1 row_mask:0xf bank_mask:0xf bound_ctrl:1
	v_add_f32_dpp v140, v214, v140 wave_shl:1 row_mask:0xf bank_mask:0xf bound_ctrl:1
	v_pk_add_f32 v[142:143], v[148:149], v[78:79]
	v_pk_add_f32 v[144:145], v[56:57], v[96:97]
	v_add_f32_e64 v56, v58, v98
	v_pk_add_f32 v[58:59], v[60:61], v[100:101]
	v_pk_add_f32 v[60:61], v[62:63], v[124:125]
	v_add_f32_e64 v62, v64, v128
	v_pk_add_f32 v[64:65], v[66:67], v[130:131]
	v_pk_add_f32 v[66:67], v[68:69], v[132:133]
	v_add_f32_e64 v68, v70, v134
	v_pk_add_f32 v[70:71], v[72:73], v[136:137]
	v_pk_add_f32 v[72:73], v[74:75], v[138:139]
	v_add_f32_e64 v74, v76, v140
	v_pk_fma_f32 v[70:71], v[48:49], v[142:143], v[70:71] op_sel_hi:[0,1,1]
	v_pk_fma_f32 v[72:73], v[48:49], v[144:145], v[72:73] op_sel_hi:[0,1,1]
	v_fma_f32 v74, v48, v56, v74
	v_pk_fma_f32 v[70:71], v[48:49], v[58:59], v[70:71] op_sel:[1,0,0]
	v_pk_fma_f32 v[72:73], v[48:49], v[60:61], v[72:73] op_sel:[1,0,0]
	v_fma_f32 v74, v49, v62, v74
	v_pk_fma_f32 v[70:71], v[50:51], v[64:65], v[70:71] op_sel_hi:[0,1,1]
	v_pk_fma_f32 v[72:73], v[50:51], v[66:67], v[72:73] op_sel_hi:[0,1,1]
	v_fma_f32 v74, v50, v68, v74
	v_cndmask_b32_e64 v76, 0, v1, s[10:11]
	v_cndmask_b32_e64 v77, 0, v1, s[14:15]
	v_cndmask_b32_e64 v146, 0, v1, s[20:21]
	v_cndmask_b32_e64 v147, 0, v1, s[22:23]
	v_cndmask_b32_e64 v148, 0, v1, s[30:31]
	v_pk_fma_f32 v[70:71], v[40:41], v[94:95], v[70:71] op_sel_hi:[1,0,1] neg_lo:[0,0,1] neg_hi:[0,0,1]
	v_pk_fma_f32 v[72:73], v[42:43], v[94:95], v[72:73] op_sel_hi:[1,0,1] neg_lo:[0,0,1] neg_hi:[0,0,1]
	v_fma_f32 v74, v44, v94, -v74
	s_add_i32 s4, s34, 1
	s_cmpk_lt_i32 s4, 0x201
	s_cselect_b64 s[12:13], s[0:1], 0
	v_pk_add_f32 v[70:71], v[70:71], v[76:77] neg_lo:[0,1] neg_hi:[0,1]
	v_pk_add_f32 v[72:73], v[72:73], v[146:147] neg_lo:[0,1] neg_hi:[0,1]
	v_add_f32_e64 v74, v74, -v148
	v_pk_mul_f32 v[198:199], v[70:71], v[70:71]
	v_pk_fma_f32 v[198:199], v[72:73], v[72:73], v[198:199]
	v_add_f32_e32 v198, v198, v199
	v_fma_f32 v198, v74, v74, v198
	v_cndmask_b32_e64 v199, 0, v198, s[12:13]
	v_add_f32_e32 v0, v0, v199
	s_add_i32 s4, s34, 6
	s_min_i32 s4, s4, 0x200
	s_mul_i32 s5, s4, 0x804
	s_add_i32 s5, s5, s35
	s_add_i32 s6, s5, 0x101004
	s_add_i32 s7, s5, 0x202008
	s_add_i32 s8, s5, 0x30300c
	s_add_i32 s11, s5, 0x404010
	s_mul_i32 s9, s4, 0x180c
	s_add_i32 s9, s9, s33
	buffer_load_dword v40, v28, s[16:19], s5 offen nt
	buffer_load_dword v41, v28, s[16:19], s6 offen nt
	buffer_load_dword v42, v28, s[16:19], s7 offen nt
	buffer_load_dword v43, v28, s[16:19], s8 offen nt
	buffer_load_dword v44, v28, s[16:19], s11 offen nt
	buffer_load_dwordx3 v[48:50], v27, s[24:27], s9 offen nt
	s_waitcnt vmcnt(12)
	v_pk_mul_f32 v[56:57], v[12:13], v[32:33] op_sel_hi:[1,0]
	v_pk_mul_f32 v[58:59], v[14:15], v[32:33] op_sel_hi:[1,0]
	v_mul_f32_e64 v60, v16, v32
	v_pk_mul_f32 v[62:63], v[12:13], v[32:33] op_sel:[0,1]
	v_pk_mul_f32 v[64:65], v[14:15], v[32:33] op_sel:[0,1]
	v_mul_f32_e64 v66, v16, v33
	v_pk_mul_f32 v[68:69], v[12:13], v[34:35] op_sel_hi:[1,0]
	v_pk_mul_f32 v[70:71], v[14:15], v[34:35] op_sel_hi:[1,0]
	v_mul_f32_e64 v72, v16, v34
	v_add_f32_dpp v74, v12, v12 wave_shr:1 row_mask:0xf bank_mask:0xf bound_ctrl:1
	v_add_f32_dpp v75, v13, v13 wave_shr:1 row_mask:0xf bank_mask:0xf bound_ctrl:1
	v_add_f32_dpp v76, v14, v14 wave_shr:1 row_mask:0xf bank_mask:0xf bound_ctrl:1
	v_add_f32_dpp v77, v15, v15 wave_shr:1 row_mask:0xf bank_mask:0xf bound_ctrl:1
	v_add_f32_dpp v80, v16, v16 wave_shr:1 row_mask:0xf bank_mask:0xf bound_ctrl:1
	v_add_f32_dpp v82, v56, v56 wave_shr:1 row_mask:0xf bank_mask:0xf bound_ctrl:1
	v_add_f32_dpp v83, v57, v57 wave_shr:1 row_mask:0xf bank_mask:0xf bound_ctrl:1
	v_add_f32_dpp v88, v58, v58 wave_shr:1 row_mask:0xf bank_mask:0xf bound_ctrl:1
	v_add_f32_dpp v89, v59, v59 wave_shr:1 row_mask:0xf bank_mask:0xf bound_ctrl:1
	v_add_f32_dpp v90, v60, v60 wave_shr:1 row_mask:0xf bank_mask:0xf bound_ctrl:1
	v_add_f32_dpp v92, v62, v62 wave_shr:1 row_mask:0xf bank_mask:0xf bound_ctrl:1
	v_add_f32_dpp v93, v63, v63 wave_shr:1 row_mask:0xf bank_mask:0xf bound_ctrl:1
	v_add_f32_dpp v94, v64, v64 wave_shr:1 row_mask:0xf bank_mask:0xf bound_ctrl:1
	v_add_f32_dpp v95, v65, v65 wave_shr:1 row_mask:0xf bank_mask:0xf bound_ctrl:1
	v_add_f32_dpp v142, v66, v66 wave_shr:1 row_mask:0xf bank_mask:0xf bound_ctrl:1
	v_add_f32_dpp v144, v68, v68 wave_shr:1 row_mask:0xf bank_mask:0xf bound_ctrl:1
	v_add_f32_dpp v145, v69, v69 wave_shr:1 row_mask:0xf bank_mask:0xf bound_ctrl:1
	v_add_f32_dpp v146, v70, v70 wave_shr:1 row_mask:0xf bank_mask:0xf bound_ctrl:1
	v_add_f32_dpp v147, v71, v71 wave_shr:1 row_mask:0xf bank_mask:0xf bound_ctrl:1
	v_add_f32_dpp v148, v72, v72 wave_shr:1 row_mask:0xf bank_mask:0xf bound_ctrl:1
	v_add_f32_dpp v74, v12, v74 wave_shl:1 row_mask:0xf bank_mask:0xf bound_ctrl:1
	v_add_f32_dpp v75, v13, v75 wave_shl:1 row_mask:0xf bank_mask:0xf bound_ctrl:1
	v_add_f32_dpp v76, v14, v76 wave_shl:1 row_mask:0xf bank_mask:0xf bound_ctrl:1
	v_add_f32_dpp v77, v15, v77 wave_shl:1 row_mask:0xf bank_mask:0xf bound_ctrl:1
	v_add_f32_dpp v80, v16, v80 wave_shl:1 row_mask:0xf bank_mask:0xf bound_ctrl:1
	v_add_f32_dpp v82, v56, v82 wave_shl:1 row_mask:0xf bank_mask:0xf bound_ctrl:1
	v_add_f32_dpp v83, v57, v83 wave_shl:1 row_mask:0xf bank_mask:0xf bound_ctrl:1
	v_add_f32_dpp v88, v58, v88 wave_shl:1 row_mask:0xf bank_mask:0xf bound_ctrl:1
	v_add_f32_dpp v89, v59, v89 wave_shl:1 row_mask:0xf bank_mask:0xf bound_ctrl:1
	v_add_f32_dpp v90, v60, v90 wave_shl:1 row_mask:0xf bank_mask:0xf bound_ctrl:1
	v_add_f32_dpp v92, v62, v92 wave_shl:1 row_mask:0xf bank_mask:0xf bound_ctrl:1
	v_add_f32_dpp v93, v63, v93 wave_shl:1 row_mask:0xf bank_mask:0xf bound_ctrl:1
	v_add_f32_dpp v94, v64, v94 wave_shl:1 row_mask:0xf bank_mask:0xf bound_ctrl:1
	v_add_f32_dpp v95, v65, v95 wave_shl:1 row_mask:0xf bank_mask:0xf bound_ctrl:1
	v_add_f32_dpp v142, v66, v142 wave_shl:1 row_mask:0xf bank_mask:0xf bound_ctrl:1
	v_add_f32_dpp v144, v68, v144 wave_shl:1 row_mask:0xf bank_mask:0xf bound_ctrl:1
	v_add_f32_dpp v145, v69, v145 wave_shl:1 row_mask:0xf bank_mask:0xf bound_ctrl:1
	v_add_f32_dpp v146, v70, v146 wave_shl:1 row_mask:0xf bank_mask:0xf bound_ctrl:1
	v_add_f32_dpp v147, v71, v147 wave_shl:1 row_mask:0xf bank_mask:0xf bound_ctrl:1
	v_add_f32_dpp v148, v72, v148 wave_shl:1 row_mask:0xf bank_mask:0xf bound_ctrl:1
	s_barrier
	ds_read_b128 v[56:59], v23 offset:0
	ds_read_b128 v[60:63], v23 offset:1024
	ds_read_b128 v[64:67], v23 offset:2048
	v_pk_add_f32 v[68:69], v[102:103], v[74:75]
	v_pk_add_f32 v[70:71], v[174:175], v[68:69]
	v_pk_add_f32 v[72:73], v[104:105], v[76:77]
	v_pk_add_f32 v[102:103], v[176:177], v[72:73]
	v_add_f32_e64 v104, v106, v80
	v_add_f32_e64 v174, v178, v104
	v_pk_add_f32 v[106:107], v[108:109], v[82:83]
	v_pk_add_f32 v[176:177], v[180:181], v[106:107]
	v_pk_add_f32 v[108:109], v[110:111], v[88:89]
	v_pk_add_f32 v[178:179], v[182:183], v[108:109]
	v_add_f32_e64 v110, v112, v90
	v_add_f32_e64 v180, v184, v110
	v_pk_add_f32 v[112:113], v[116:117], v[92:93]
	v_pk_add_f32 v[182:183], v[186:187], v[112:113]
	v_pk_add_f32 v[116:117], v[118:119], v[94:95]
	v_pk_add_f32 v[184:185], v[188:189], v[116:117]
	v_add_f32_e64 v118, v120, v142
	v_add_f32_e64 v186, v190, v118
	v_pk_add_f32 v[120:121], v[122:123], v[144:145]
	v_pk_add_f32 v[188:189], v[192:193], v[120:121]
	v_pk_add_f32 v[122:123], v[170:171], v[146:147]
	v_pk_add_f32 v[190:191], v[194:195], v[122:123]
	v_add_f32_e64 v170, v172, v148
	v_add_f32_e64 v192, v196, v170
	s_waitcnt lgkmcnt(2)
	v_pk_fma_f32 v[176:177], v[56:57], v[70:71], v[176:177] op_sel_hi:[0,1,1] neg_lo:[1,0,0] neg_hi:[1,0,0]
	v_pk_fma_f32 v[178:179], v[56:57], v[102:103], v[178:179] op_sel_hi:[0,1,1] neg_lo:[1,0,0] neg_hi:[1,0,0]
	v_fma_f32 v180, -v56, v174, v180
	v_pk_fma_f32 v[182:183], v[56:57], v[70:71], v[182:183] op_sel:[1,0,0] neg_lo:[1,0,0] neg_hi:[1,0,0]
	v_pk_fma_f32 v[184:185], v[56:57], v[102:103], v[184:185] op_sel:[1,0,0] neg_lo:[1,0,0] neg_hi:[1,0,0]
	v_fma_f32 v186, -v57, v174, v186
	v_pk_fma_f32 v[188:189], v[58:59], v[70:71], v[188:189] op_sel_hi:[0,1,1] neg_lo:[1,0,0] neg_hi:[1,0,0]
	v_pk_fma_f32 v[190:191], v[58:59], v[102:103], v[190:191] op_sel_hi:[0,1,1] neg_lo:[1,0,0] neg_hi:[1,0,0]
	v_fma_f32 v192, -v58, v174, v192
	v_pk_mul_f32 v[172:173], v[58:59], v[176:177] op_sel:[1,0]
	v_pk_mul_f32 v[198:199], v[58:59], v[178:179] op_sel:[1,0]
	v_mul_f32_e64 v204, v59, v180
	s_waitcnt lgkmcnt(1)
	v_pk_mul_f32 v[194:195], v[60:61], v[176:177] op_sel_hi:[0,1]
	v_pk_mul_f32 v[200:201], v[60:61], v[178:179] op_sel_hi:[0,1]
	v_mul_f32_e64 v206, v60, v180
	v_pk_mul_f32 v[196:197], v[60:61], v[176:177] op_sel:[1,0]
	v_pk_mul_f32 v[202:203], v[60:61], v[178:179] op_sel:[1,0]
	v_mul_f32_e64 v208, v61, v180
	v_pk_fma_f32 v[172:173], v[60:61], v[182:183], v[172:173] op_sel_hi:[0,1,1]
	v_pk_fma_f32 v[198:199], v[60:61], v[184:185], v[198:199] op_sel_hi:[0,1,1]
	v_fma_f32 v204, v60, v186, v204
	v_pk_fma_f32 v[194:195], v[62:63], v[182:183], v[194:195] op_sel_hi:[0,1,1]
	v_pk_fma_f32 v[200:201], v[62:63], v[184:185], v[200:201] op_sel_hi:[0,1,1]
	v_fma_f32 v206, v62, v186, v206
	v_pk_fma_f32 v[196:197], v[62:63], v[182:183], v[196:197] op_sel:[1,0,0]
	v_pk_fma_f32 v[202:203], v[62:63], v[184:185], v[202:203] op_sel:[1,0,0]
	v_fma_f32 v208, v63, v186, v208
	v_pk_fma_f32 v[172:173], v[60:61], v[188:189], v[172:173] op_sel:[1,0,0]
	v_pk_fma_f32 v[198:199], v[60:61], v[190:191], v[198:199] op_sel:[1,0,0]
	v_fma_f32 v204, v61, v192, v204
	v_pk_fma_f32 v[194:195], v[62:63], v[188:189], v[194:195] op_sel:[1,0,0]
	v_pk_fma_f32 v[200:201], v[62:63], v[190:191], v[200:201] op_sel:[1,0,0]
	v_fma_f32 v206, v63, v192, v206
	s_waitcnt lgkmcnt(0)
	v_pk_fma_f32 v[196:197], v[64:65], v[188:189], v[196:197] op_sel_hi:[0,1,1]
	v_pk_fma_f32 v[202:203], v[64:65], v[190:191], v[202:203] op_sel_hi:[0,1,1]
	v_fma_f32 v208, v64, v192, v208
	v_pk_mul_f32 v[210:211], v[56:57], v[172:173] op_sel_hi:[0,1]
	v_pk_mul_f32 v[212:213], v[56:57], v[198:199] op_sel_hi:[0,1]
	v_mul_f32_e64 v214, v56, v204
	v_pk_fma_f32 v[210:211], v[56:57], v[194:195], v[210:211] op_sel:[1,0,0]
	v_pk_fma_f32 v[212:213], v[56:57], v[200:201], v[212:213] op_sel:[1,0,0]
	v_fma_f32 v214, v57, v206, v214
	v_pk_fma_f32 v[210:211], v[58:59], v[196:197], v[210:211] op_sel_hi:[0,1,1]
	v_pk_fma_f32 v[212:213], v[58:59], v[202:203], v[212:213] op_sel_hi:[0,1,1]
	v_fma_f32 v214, v58, v208, v214
	v_pk_fma_f32 v[210:211], v[64:65], v[70:71], v[210:211] op_sel:[1,0,0] neg_lo:[0,0,1] neg_hi:[0,0,1]
	v_pk_fma_f32 v[212:213], v[64:65], v[102:103], v[212:213] op_sel:[1,0,0] neg_lo:[0,0,1] neg_hi:[0,0,1]
	v_fma_f32 v214, v65, v174, -v214
	v_cmp_eq_u32_e64 s[10:11], 1, v67
	v_cmp_eq_u32_e64 s[14:15], 2, v67
	v_cmp_eq_u32_e64 s[20:21], 3, v67
	v_cmp_eq_u32_e64 s[22:23], 4, v67
	v_cmp_eq_u32_e64 s[30:31], 5, v67
	v_add_f32_dpp v70, v172, v172 wave_shr:1 row_mask:0xf bank_mask:0xf bound_ctrl:1
	v_add_f32_dpp v71, v173, v173 wave_shr:1 row_mask:0xf bank_mask:0xf bound_ctrl:1
	v_add_f32_dpp v102, v198, v198 wave_shr:1 row_mask:0xf bank_mask:0xf bound_ctrl:1
	v_add_f32_dpp v103, v199, v199 wave_shr:1 row_mask:0xf bank_mask:0xf bound_ctrl:1
	v_add_f32_dpp v174, v204, v204 wave_shr:1 row_mask:0xf bank_mask:0xf bound_ctrl:1
	v_add_f32_dpp v176, v194, v194 wave_shr:1 row_mask:0xf bank_mask:0xf bound_ctrl:1
	v_add_f32_dpp v177, v195, v195 wave_shr:1 row_mask:0xf bank_mask:0xf bound_ctrl:1
	v_add_f32_dpp v178, v200, v200 wave_shr:1 row_mask:0xf bank_mask:0xf bound_ctrl:1
	v_add_f32_dpp v179, v201, v201 wave_shr:1 row_mask:0xf bank_mask:0xf bound_ctrl:1
	v_add_f32_dpp v180, v206, v206 wave_shr:1 row_mask:0xf bank_mask:0xf bound_ctrl:1
	v_add_f32_dpp v182, v196, v196 wave_shr:1 row_mask:0xf bank_mask:0xf bound_ctrl:1
	v_add_f32_dpp v183, v197, v197 wave_shr:1 row_mask:0xf bank_mask:0xf bound_ctrl:1
	v_add_f32_dpp v184, v202, v202 wave_shr:1 row_mask:0xf bank_mask:0xf bound_ctrl:1
	v_add_f32_dpp v185, v203, v203 wave_shr:1 row_mask:0xf bank_mask:0xf bound_ctrl:1
	v_add_f32_dpp v186, v208, v208 wave_shr:1 row_mask:0xf bank_mask:0xf bound_ctrl:1
	v_add_f32_dpp v188, v210, v210 wave_shr:1 row_mask:0xf bank_mask:0xf bound_ctrl:1
	v_add_f32_dpp v189, v211, v211 wave_shr:1 row_mask:0xf bank_mask:0xf bound_ctrl:1
	v_add_f32_dpp v190, v212, v212 wave_shr:1 row_mask:0xf bank_mask:0xf bound_ctrl:1
	v_add_f32_dpp v191, v213, v213 wave_shr:1 row_mask:0xf bank_mask:0xf bound_ctrl:1
	v_add_f32_dpp v192, v214, v214 wave_shr:1 row_mask:0xf bank_mask:0xf bound_ctrl:1
	v_add_f32_dpp v70, v172, v70 wave_shl:1 row_mask:0xf bank_mask:0xf bound_ctrl:1
	v_add_f32_dpp v71, v173, v71 wave_shl:1 row_mask:0xf bank_mask:0xf bound_ctrl:1
	v_add_f32_dpp v102, v198, v102 wave_shl:1 row_mask:0xf bank_mask:0xf bound_ctrl:1
	v_add_f32_dpp v103, v199, v103 wave_shl:1 row_mask:0xf bank_mask:0xf bound_ctrl:1
	v_add_f32_dpp v174, v204, v174 wave_shl:1 row_mask:0xf bank_mask:0xf bound_ctrl:1
	v_add_f32_dpp v176, v194, v176 wave_shl:1 row_mask:0xf bank_mask:0xf bound_ctrl:1
	v_add_f32_dpp v177, v195, v177 wave_shl:1 row_mask:0xf bank_mask:0xf bound_ctrl:1
	v_add_f32_dpp v178, v200, v178 wave_shl:1 row_mask:0xf bank_mask:0xf bound_ctrl:1
	v_add_f32_dpp v179, v201, v179 wave_shl:1 row_mask:0xf bank_mask:0xf bound_ctrl:1
	v_add_f32_dpp v180, v206, v180 wave_shl:1 row_mask:0xf bank_mask:0xf bound_ctrl:1
	v_add_f32_dpp v182, v196, v182 wave_shl:1 row_mask:0xf bank_mask:0xf bound_ctrl:1
	v_add_f32_dpp v183, v197, v183 wave_shl:1 row_mask:0xf bank_mask:0xf bound_ctrl:1
	v_add_f32_dpp v184, v202, v184 wave_shl:1 row_mask:0xf bank_mask:0xf bound_ctrl:1
	v_add_f32_dpp v185, v203, v185 wave_shl:1 row_mask:0xf bank_mask:0xf bound_ctrl:1
	v_add_f32_dpp v186, v208, v186 wave_shl:1 row_mask:0xf bank_mask:0xf bound_ctrl:1
	v_add_f32_dpp v188, v210, v188 wave_shl:1 row_mask:0xf bank_mask:0xf bound_ctrl:1
	v_add_f32_dpp v189, v211, v189 wave_shl:1 row_mask:0xf bank_mask:0xf bound_ctrl:1
	v_add_f32_dpp v190, v212, v190 wave_shl:1 row_mask:0xf bank_mask:0xf bound_ctrl:1
	v_add_f32_dpp v191, v213, v191 wave_shl:1 row_mask:0xf bank_mask:0xf bound_ctrl:1
	v_add_f32_dpp v192, v214, v192 wave_shl:1 row_mask:0xf bank_mask:0xf bound_ctrl:1
	v_pk_add_f32 v[172:173], v[78:79], v[70:71]
	v_pk_add_f32 v[194:195], v[114:115], v[172:173]
	v_pk_add_f32 v[78:79], v[96:97], v[102:103]
	v_pk_add_f32 v[114:115], v[126:127], v[78:79]
	v_add_f32_e64 v96, v98, v174
	v_add_f32_e64 v126, v150, v96
	v_pk_add_f32 v[98:99], v[100:101], v[176:177]
	v_pk_add_f32 v[150:151], v[152:153], v[98:99]
	v_pk_add_f32 v[100:101], v[124:125], v[178:179]
	v_pk_add_f32 v[152:153], v[154:155], v[100:101]
	v_add_f32_e64 v124, v128, v180
	v_add_f32_e64 v154, v156, v124
	v_pk_add_f32 v[128:129], v[130:131], v[182:183]
	v_pk_add_f32 v[156:157], v[158:159], v[128:129]
	v_pk_add_f32 v[130:131], v[132:133], v[184:185]
	v_pk_add_f32 v[158:159], v[160:161], v[130:131]
	v_add_f32_e64 v132, v134, v186
	v_add_f32_e64 v160, v162, v132
	v_pk_add_f32 v[134:135], v[136:137], v[188:189]
	v_pk_add_f32 v[162:163], v[164:165], v[134:135]
	v_pk_add_f32 v[136:137], v[138:139], v[190:191]
	v_pk_add_f32 v[164:165], v[166:167], v[136:137]
	v_add_f32_e64 v138, v140, v192
	v_add_f32_e64 v166, v168, v138
	v_pk_fma_f32 v[162:163], v[84:85], v[194:195], v[162:163] op_sel_hi:[0,1,1]
	v_pk_fma_f32 v[164:165], v[84:85], v[114:115], v[164:165] op_sel_hi:[0,1,1]
	v_fma_f32 v166, v84, v126, v166
	v_pk_fma_f32 v[162:163], v[84:85], v[150:151], v[162:163] op_sel:[1,0,0]
	v_pk_fma_f32 v[164:165], v[84:85], v[152:153], v[164:165] op_sel:[1,0,0]
	v_fma_f32 v166, v85, v154, v166
	v_pk_fma_f32 v[162:163], v[86:87], v[156:157], v[162:163] op_sel_hi:[0,1,1]
	v_pk_fma_f32 v[164:165], v[86:87], v[158:159], v[164:165] op_sel_hi:[0,1,1]
	v_fma_f32 v166, v86, v160, v166
	v_cndmask_b32_e64 v140, 0, v1, s[10:11]
	v_cndmask_b32_e64 v141, 0, v1, s[14:15]
	v_cndmask_b32_e64 v168, 0, v1, s[20:21]
	v_cndmask_b32_e64 v169, 0, v1, s[22:23]
	v_cndmask_b32_e64 v196, 0, v1, s[30:31]
	v_pk_fma_f32 v[162:163], v[46:47], v[66:67], v[162:163] op_sel_hi:[1,0,1] neg_lo:[0,0,1] neg_hi:[0,0,1]
	v_pk_fma_f32 v[164:165], v[52:53], v[66:67], v[164:165] op_sel_hi:[1,0,1] neg_lo:[0,0,1] neg_hi:[0,0,1]
	v_fma_f32 v166, v54, v66, -v166
	s_add_i32 s4, s34, 2
	s_cmpk_lt_i32 s4, 0x201
	s_cselect_b64 s[12:13], s[0:1], 0
	v_pk_add_f32 v[162:163], v[162:163], v[140:141] neg_lo:[0,1] neg_hi:[0,1]
	v_pk_add_f32 v[164:165], v[164:165], v[168:169] neg_lo:[0,1] neg_hi:[0,1]
	v_add_f32_e64 v166, v166, -v196
	v_pk_mul_f32 v[198:199], v[162:163], v[162:163]
	v_pk_fma_f32 v[198:199], v[164:165], v[164:165], v[198:199]
	v_add_f32_e32 v198, v198, v199
	v_fma_f32 v198, v166, v166, v198
	v_cndmask_b32_e64 v199, 0, v198, s[12:13]
	v_add_f32_e32 v0, v0, v199
	s_add_i32 s4, s34, 7
	s_min_i32 s4, s4, 0x200
	s_mul_i32 s5, s4, 0x804
	s_add_i32 s5, s5, s35
	s_add_i32 s6, s5, 0x101004
	s_add_i32 s7, s5, 0x202008
	s_add_i32 s8, s5, 0x30300c
	s_add_i32 s11, s5, 0x404010
	s_mul_i32 s9, s4, 0x180c
	s_add_i32 s9, s9, s33
	buffer_load_dword v46, v28, s[16:19], s5 offen nt
	buffer_load_dword v47, v28, s[16:19], s6 offen nt
	buffer_load_dword v52, v28, s[16:19], s7 offen nt
	buffer_load_dword v53, v28, s[16:19], s8 offen nt
	buffer_load_dword v54, v28, s[16:19], s11 offen nt
	buffer_load_dwordx3 v[56:58], v27, s[24:27], s9 offen nt
	s_waitcnt vmcnt(12)
	v_pk_mul_f32 v[60:61], v[20:21], v[36:37] op_sel_hi:[1,0]
	v_pk_mul_f32 v[62:63], v[24:25], v[36:37] op_sel_hi:[1,0]
	v_mul_f32_e64 v64, v30, v36
	v_pk_mul_f32 v[66:67], v[20:21], v[36:37] op_sel:[0,1]
	v_pk_mul_f32 v[84:85], v[24:25], v[36:37] op_sel:[0,1]
	v_mul_f32_e64 v86, v30, v37
	v_pk_mul_f32 v[114:115], v[20:21], v[38:39] op_sel_hi:[1,0]
	v_pk_mul_f32 v[126:127], v[24:25], v[38:39] op_sel_hi:[1,0]
	v_mul_f32_e64 v140, v30, v38
	v_add_f32_dpp v150, v20, v20 wave_shr:1 row_mask:0xf bank_mask:0xf bound_ctrl:1
	v_add_f32_dpp v151, v21, v21 wave_shr:1 row_mask:0xf bank_mask:0xf bound_ctrl:1
	v_add_f32_dpp v152, v24, v24 wave_shr:1 row_mask:0xf bank_mask:0xf bound_ctrl:1
	v_add_f32_dpp v153, v25, v25 wave_shr:1 row_mask:0xf bank_mask:0xf bound_ctrl:1
	v_add_f32_dpp v154, v30, v30 wave_shr:1 row_mask:0xf bank_mask:0xf bound_ctrl:1
	v_add_f32_dpp v156, v60, v60 wave_shr:1 row_mask:0xf bank_mask:0xf bound_ctrl:1
	v_add_f32_dpp v157, v61, v61 wave_shr:1 row_mask:0xf bank_mask:0xf bound_ctrl:1
	v_add_f32_dpp v158, v62, v62 wave_shr:1 row_mask:0xf bank_mask:0xf bound_ctrl:1
	v_add_f32_dpp v159, v63, v63 wave_shr:1 row_mask:0xf bank_mask:0xf bound_ctrl:1
	v_add_f32_dpp v160, v64, v64 wave_shr:1 row_mask:0xf bank_mask:0xf bound_ctrl:1
	v_add_f32_dpp v162, v66, v66 wave_shr:1 row_mask:0xf bank_mask:0xf bound_ctrl:1
	v_add_f32_dpp v163, v67, v67 wave_shr:1 row_mask:0xf bank_mask:0xf bound_ctrl:1
	v_add_f32_dpp v164, v84, v84 wave_shr:1 row_mask:0xf bank_mask:0xf bound_ctrl:1
	v_add_f32_dpp v165, v85, v85 wave_shr:1 row_mask:0xf bank_mask:0xf bound_ctrl:1
	v_add_f32_dpp v166, v86, v86 wave_shr:1 row_mask:0xf bank_mask:0xf bound_ctrl:1
	v_add_f32_dpp v168, v114, v114 wave_shr:1 row_mask:0xf bank_mask:0xf bound_ctrl:1
	v_add_f32_dpp v169, v115, v115 wave_shr:1 row_mask:0xf bank_mask:0xf bound_ctrl:1
	v_add_f32_dpp v194, v126, v126 wave_shr:1 row_mask:0xf bank_mask:0xf bound_ctrl:1
	v_add_f32_dpp v195, v127, v127 wave_shr:1 row_mask:0xf bank_mask:0xf bound_ctrl:1
	v_add_f32_dpp v196, v140, v140 wave_shr:1 row_mask:0xf bank_mask:0xf bound_ctrl:1
	v_add_f32_dpp v150, v20, v150 wave_shl:1 row_mask:0xf bank_mask:0xf bound_ctrl:1
	v_add_f32_dpp v151, v21, v151 wave_shl:1 row_mask:0xf bank_mask:0xf bound_ctrl:1
	v_add_f32_dpp v152, v24, v152 wave_shl:1 row_mask:0xf bank_mask:0xf bound_ctrl:1
	v_add_f32_dpp v153, v25, v153 wave_shl:1 row_mask:0xf bank_mask:0xf bound_ctrl:1
	v_add_f32_dpp v154, v30, v154 wave_shl:1 row_mask:0xf bank_mask:0xf bound_ctrl:1
	v_add_f32_dpp v156, v60, v156 wave_shl:1 row_mask:0xf bank_mask:0xf bound_ctrl:1
	v_add_f32_dpp v157, v61, v157 wave_shl:1 row_mask:0xf bank_mask:0xf bound_ctrl:1
	v_add_f32_dpp v158, v62, v158 wave_shl:1 row_mask:0xf bank_mask:0xf bound_ctrl:1
	v_add_f32_dpp v159, v63, v159 wave_shl:1 row_mask:0xf bank_mask:0xf bound_ctrl:1
	v_add_f32_dpp v160, v64, v160 wave_shl:1 row_mask:0xf bank_mask:0xf bound_ctrl:1
	v_add_f32_dpp v162, v66, v162 wave_shl:1 row_mask:0xf bank_mask:0xf bound_ctrl:1
	v_add_f32_dpp v163, v67, v163 wave_shl:1 row_mask:0xf bank_mask:0xf bound_ctrl:1
	v_add_f32_dpp v164, v84, v164 wave_shl:1 row_mask:0xf bank_mask:0xf bound_ctrl:1
	v_add_f32_dpp v165, v85, v165 wave_shl:1 row_mask:0xf bank_mask:0xf bound_ctrl:1
	v_add_f32_dpp v166, v86, v166 wave_shl:1 row_mask:0xf bank_mask:0xf bound_ctrl:1
	v_add_f32_dpp v168, v114, v168 wave_shl:1 row_mask:0xf bank_mask:0xf bound_ctrl:1
	v_add_f32_dpp v169, v115, v169 wave_shl:1 row_mask:0xf bank_mask:0xf bound_ctrl:1
	v_add_f32_dpp v194, v126, v194 wave_shl:1 row_mask:0xf bank_mask:0xf bound_ctrl:1
	v_add_f32_dpp v195, v127, v195 wave_shl:1 row_mask:0xf bank_mask:0xf bound_ctrl:1
	v_add_f32_dpp v196, v140, v196 wave_shl:1 row_mask:0xf bank_mask:0xf bound_ctrl:1
	s_barrier
	ds_read_b128 v[60:63], v23 offset:3072
	ds_read_b128 v[64:67], v23 offset:4096
	ds_read_b128 v[84:87], v23 offset:5120
	v_pk_add_f32 v[114:115], v[68:69], v[150:151]
	v_pk_add_f32 v[68:69], v[72:73], v[152:153]
	v_add_f32_e64 v72, v104, v154
	v_pk_add_f32 v[104:105], v[106:107], v[156:157]
	v_pk_add_f32 v[106:107], v[108:109], v[158:159]
	v_add_f32_e64 v108, v110, v160
	v_pk_add_f32 v[110:111], v[112:113], v[162:163]
	v_pk_add_f32 v[112:113], v[116:117], v[164:165]
	v_add_f32_e64 v116, v118, v166
	v_pk_add_f32 v[118:119], v[120:121], v[168:169]
	v_pk_add_f32 v[120:121], v[122:123], v[194:195]
	v_add_f32_e64 v122, v170, v196
	s_waitcnt lgkmcnt(2)
	v_pk_fma_f32 v[104:105], v[60:61], v[114:115], v[104:105] op_sel_hi:[0,1,1] neg_lo:[1,0,0] neg_hi:[1,0,0]
	v_pk_fma_f32 v[106:107], v[60:61], v[68:69], v[106:107] op_sel_hi:[0,1,1] neg_lo:[1,0,0] neg_hi:[1,0,0]
	v_fma_f32 v108, -v60, v72, v108
	v_pk_fma_f32 v[110:111], v[60:61], v[114:115], v[110:111] op_sel:[1,0,0] neg_lo:[1,0,0] neg_hi:[1,0,0]
	v_pk_fma_f32 v[112:113], v[60:61], v[68:69], v[112:113] op_sel:[1,0,0] neg_lo:[1,0,0] neg_hi:[1,0,0]
	v_fma_f32 v116, -v61, v72, v116
	v_pk_fma_f32 v[118:119], v[62:63], v[114:115], v[118:119] op_sel_hi:[0,1,1] neg_lo:[1,0,0] neg_hi:[1,0,0]
	v_pk_fma_f32 v[120:121], v[62:63], v[68:69], v[120:121] op_sel_hi:[0,1,1] neg_lo:[1,0,0] neg_hi:[1,0,0]
	v_fma_f32 v122, -v62, v72, v122
	v_pk_mul_f32 v[126:127], v[62:63], v[104:105] op_sel:[1,0]
	v_pk_mul_f32 v[198:199], v[62:63], v[106:107] op_sel:[1,0]
	v_mul_f32_e64 v204, v63, v108
	s_waitcnt lgkmcnt(1)
	v_pk_mul_f32 v[140:141], v[64:65], v[104:105] op_sel_hi:[0,1]
	v_pk_mul_f32 v[200:201], v[64:65], v[106:107] op_sel_hi:[0,1]
	v_mul_f32_e64 v206, v64, v108
	v_pk_mul_f32 v[170:171], v[64:65], v[104:105] op_sel:[1,0]
	v_pk_mul_f32 v[202:203], v[64:65], v[106:107] op_sel:[1,0]
	v_mul_f32_e64 v208, v65, v108
	v_pk_fma_f32 v[126:127], v[64:65], v[110:111], v[126:127] op_sel_hi:[0,1,1]
	v_pk_fma_f32 v[198:199], v[64:65], v[112:113], v[198:199] op_sel_hi:[0,1,1]
	v_fma_f32 v204, v64, v116, v204
	v_pk_fma_f32 v[140:141], v[66:67], v[110:111], v[140:141] op_sel_hi:[0,1,1]
	v_pk_fma_f32 v[200:201], v[66:67], v[112:113], v[200:201] op_sel_hi:[0,1,1]
	v_fma_f32 v206, v66, v116, v206
	v_pk_fma_f32 v[170:171], v[66:67], v[110:111], v[170:171] op_sel:[1,0,0]
	v_pk_fma_f32 v[202:203], v[66:67], v[112:113], v[202:203] op_sel:[1,0,0]
	v_fma_f32 v208, v67, v116, v208
	v_pk_fma_f32 v[126:127], v[64:65], v[118:119], v[126:127] op_sel:[1,0,0]
	v_pk_fma_f32 v[198:199], v[64:65], v[120:121], v[198:199] op_sel:[1,0,0]
	v_fma_f32 v204, v65, v122, v204
	v_pk_fma_f32 v[140:141], v[66:67], v[118:119], v[140:141] op_sel:[1,0,0]
	v_pk_fma_f32 v[200:201], v[66:67], v[120:121], v[200:201] op_sel:[1,0,0]
	v_fma_f32 v206, v67, v122, v206
	s_waitcnt lgkmcnt(0)
	v_pk_fma_f32 v[170:171], v[84:85], v[118:119], v[170:171] op_sel_hi:[0,1,1]
	v_pk_fma_f32 v[202:203], v[84:85], v[120:121], v[202:203] op_sel_hi:[0,1,1]
	v_fma_f32 v208, v84, v122, v208
	v_pk_mul_f32 v[210:211], v[60:61], v[126:127] op_sel_hi:[0,1]
	v_pk_mul_f32 v[212:213], v[60:61], v[198:199] op_sel_hi:[0,1]
	v_mul_f32_e64 v214, v60, v204
	v_pk_fma_f32 v[210:211], v[60:61], v[140:141], v[210:211] op_sel:[1,0,0]
	v_pk_fma_f32 v[212:213], v[60:61], v[200:201], v[212:213] op_sel:[1,0,0]
	v_fma_f32 v214, v61, v206, v214
	v_pk_fma_f32 v[210:211], v[62:63], v[170:171], v[210:211] op_sel_hi:[0,1,1]
	v_pk_fma_f32 v[212:213], v[62:63], v[202:203], v[212:213] op_sel_hi:[0,1,1]
	v_fma_f32 v214, v62, v208, v214
	v_pk_fma_f32 v[210:211], v[84:85], v[114:115], v[210:211] op_sel:[1,0,0] neg_lo:[0,0,1] neg_hi:[0,0,1]
	v_pk_fma_f32 v[212:213], v[84:85], v[68:69], v[212:213] op_sel:[1,0,0] neg_lo:[0,0,1] neg_hi:[0,0,1]
	v_fma_f32 v214, v85, v72, -v214
	v_cmp_eq_u32_e64 s[10:11], 1, v87
	v_cmp_eq_u32_e64 s[14:15], 2, v87
	v_cmp_eq_u32_e64 s[20:21], 3, v87
	v_cmp_eq_u32_e64 s[22:23], 4, v87
	v_cmp_eq_u32_e64 s[30:31], 5, v87
	v_add_f32_dpp v68, v126, v126 wave_shr:1 row_mask:0xf bank_mask:0xf bound_ctrl:1
	v_add_f32_dpp v69, v127, v127 wave_shr:1 row_mask:0xf bank_mask:0xf bound_ctrl:1
	v_add_f32_dpp v72, v198, v198 wave_shr:1 row_mask:0xf bank_mask:0xf bound_ctrl:1
	v_add_f32_dpp v73, v199, v199 wave_shr:1 row_mask:0xf bank_mask:0xf bound_ctrl:1
	v_add_f32_dpp v104, v204, v204 wave_shr:1 row_mask:0xf bank_mask:0xf bound_ctrl:1
	v_add_f32_dpp v106, v140, v140 wave_shr:1 row_mask:0xf bank_mask:0xf bound_ctrl:1
	v_add_f32_dpp v107, v141, v141 wave_shr:1 row_mask:0xf bank_mask:0xf bound_ctrl:1
	v_add_f32_dpp v108, v200, v200 wave_shr:1 row_mask:0xf bank_mask:0xf bound_ctrl:1
	v_add_f32_dpp v109, v201, v201 wave_shr:1 row_mask:0xf bank_mask:0xf bound_ctrl:1
	v_add_f32_dpp v110, v206, v206 wave_shr:1 row_mask:0xf bank_mask:0xf bound_ctrl:1
	v_add_f32_dpp v112, v170, v170 wave_shr:1 row_mask:0xf bank_mask:0xf bound_ctrl:1
	v_add_f32_dpp v113, v171, v171 wave_shr:1 row_mask:0xf bank_mask:0xf bound_ctrl:1
	v_add_f32_dpp v114, v202, v202 wave_shr:1 row_mask:0xf bank_mask:0xf bound_ctrl:1
	v_add_f32_dpp v115, v203, v203 wave_shr:1 row_mask:0xf bank_mask:0xf bound_ctrl:1
	v_add_f32_dpp v116, v208, v208 wave_shr:1 row_mask:0xf bank_mask:0xf bound_ctrl:1
	v_add_f32_dpp v118, v210, v210 wave_shr:1 row_mask:0xf bank_mask:0xf bound_ctrl:1
	v_add_f32_dpp v119, v211, v211 wave_shr:1 row_mask:0xf bank_mask:0xf bound_ctrl:1
	v_add_f32_dpp v120, v212, v212 wave_shr:1 row_mask:0xf bank_mask:0xf bound_ctrl:1
	v_add_f32_dpp v121, v213, v213 wave_shr:1 row_mask:0xf bank_mask:0xf bound_ctrl:1
	v_add_f32_dpp v122, v214, v214 wave_shr:1 row_mask:0xf bank_mask:0xf bound_ctrl:1
	v_add_f32_dpp v68, v126, v68 wave_shl:1 row_mask:0xf bank_mask:0xf bound_ctrl:1
	v_add_f32_dpp v69, v127, v69 wave_shl:1 row_mask:0xf bank_mask:0xf bound_ctrl:1
	v_add_f32_dpp v72, v198, v72 wave_shl:1 row_mask:0xf bank_mask:0xf bound_ctrl:1
	v_add_f32_dpp v73, v199, v73 wave_shl:1 row_mask:0xf bank_mask:0xf bound_ctrl:1
	v_add_f32_dpp v104, v204, v104 wave_shl:1 row_mask:0xf bank_mask:0xf bound_ctrl:1
	v_add_f32_dpp v106, v140, v106 wave_shl:1 row_mask:0xf bank_mask:0xf bound_ctrl:1
	v_add_f32_dpp v107, v141, v107 wave_shl:1 row_mask:0xf bank_mask:0xf bound_ctrl:1
	v_add_f32_dpp v108, v200, v108 wave_shl:1 row_mask:0xf bank_mask:0xf bound_ctrl:1
	v_add_f32_dpp v109, v201, v109 wave_shl:1 row_mask:0xf bank_mask:0xf bound_ctrl:1
	v_add_f32_dpp v110, v206, v110 wave_shl:1 row_mask:0xf bank_mask:0xf bound_ctrl:1
	v_add_f32_dpp v112, v170, v112 wave_shl:1 row_mask:0xf bank_mask:0xf bound_ctrl:1
	v_add_f32_dpp v113, v171, v113 wave_shl:1 row_mask:0xf bank_mask:0xf bound_ctrl:1
	v_add_f32_dpp v114, v202, v114 wave_shl:1 row_mask:0xf bank_mask:0xf bound_ctrl:1
	v_add_f32_dpp v115, v203, v115 wave_shl:1 row_mask:0xf bank_mask:0xf bound_ctrl:1
	v_add_f32_dpp v116, v208, v116 wave_shl:1 row_mask:0xf bank_mask:0xf bound_ctrl:1
	v_add_f32_dpp v118, v210, v118 wave_shl:1 row_mask:0xf bank_mask:0xf bound_ctrl:1
	v_add_f32_dpp v119, v211, v119 wave_shl:1 row_mask:0xf bank_mask:0xf bound_ctrl:1
	v_add_f32_dpp v120, v212, v120 wave_shl:1 row_mask:0xf bank_mask:0xf bound_ctrl:1
	v_add_f32_dpp v121, v213, v121 wave_shl:1 row_mask:0xf bank_mask:0xf bound_ctrl:1
	v_add_f32_dpp v122, v214, v122 wave_shl:1 row_mask:0xf bank_mask:0xf bound_ctrl:1
	v_pk_add_f32 v[126:127], v[172:173], v[68:69]
	v_pk_add_f32 v[140:141], v[78:79], v[72:73]
	v_add_f32_e64 v78, v96, v104
	v_pk_add_f32 v[96:97], v[98:99], v[106:107]
	v_pk_add_f32 v[98:99], v[100:101], v[108:109]
	v_add_f32_e64 v100, v124, v110
	v_pk_add_f32 v[124:125], v[128:129], v[112:113]
	v_pk_add_f32 v[128:129], v[130:131], v[114:115]
	v_add_f32_e64 v130, v132, v116
	v_pk_add_f32 v[132:133], v[134:135], v[118:119]
	v_pk_add_f32 v[134:135], v[136:137], v[120:121]
	v_add_f32_e64 v136, v138, v122
	v_pk_fma_f32 v[132:133], v[8:9], v[126:127], v[132:133] op_sel_hi:[0,1,1]
	v_pk_fma_f32 v[134:135], v[8:9], v[140:141], v[134:135] op_sel_hi:[0,1,1]
	v_fma_f32 v136, v8, v78, v136
	v_pk_fma_f32 v[132:133], v[8:9], v[96:97], v[132:133] op_sel:[1,0,0]
	v_pk_fma_f32 v[134:135], v[8:9], v[98:99], v[134:135] op_sel:[1,0,0]
	v_fma_f32 v136, v9, v100, v136
	v_pk_fma_f32 v[132:133], v[10:11], v[124:125], v[132:133] op_sel_hi:[0,1,1]
	v_pk_fma_f32 v[134:135], v[10:11], v[128:129], v[134:135] op_sel_hi:[0,1,1]
	v_fma_f32 v136, v10, v130, v136
	v_cndmask_b32_e64 v138, 0, v1, s[10:11]
	v_cndmask_b32_e64 v139, 0, v1, s[14:15]
	v_cndmask_b32_e64 v170, 0, v1, s[20:21]
	v_cndmask_b32_e64 v171, 0, v1, s[22:23]
	v_cndmask_b32_e64 v172, 0, v1, s[30:31]
	v_pk_fma_f32 v[132:133], v[2:3], v[86:87], v[132:133] op_sel_hi:[1,0,1] neg_lo:[0,0,1] neg_hi:[0,0,1]
	v_pk_fma_f32 v[134:135], v[4:5], v[86:87], v[134:135] op_sel_hi:[1,0,1] neg_lo:[0,0,1] neg_hi:[0,0,1]
	v_fma_f32 v136, v6, v86, -v136
	s_add_i32 s4, s34, 3
	s_cmpk_lt_i32 s4, 0x201
	s_cselect_b64 s[12:13], s[0:1], 0
	v_pk_add_f32 v[132:133], v[132:133], v[138:139] neg_lo:[0,1] neg_hi:[0,1]
	v_pk_add_f32 v[134:135], v[134:135], v[170:171] neg_lo:[0,1] neg_hi:[0,1]
	v_add_f32_e64 v136, v136, -v172
	v_pk_mul_f32 v[198:199], v[132:133], v[132:133]
	v_pk_fma_f32 v[198:199], v[134:135], v[134:135], v[198:199]
	v_add_f32_e32 v198, v198, v199
	v_fma_f32 v198, v136, v136, v198
	v_cndmask_b32_e64 v199, 0, v198, s[12:13]
	v_add_f32_e32 v0, v0, v199
	s_add_i32 s4, s34, 8
	s_min_i32 s4, s4, 0x200
	s_mul_i32 s5, s4, 0x804
	s_add_i32 s5, s5, s35
	s_add_i32 s6, s5, 0x101004
	s_add_i32 s7, s5, 0x202008
	s_add_i32 s8, s5, 0x30300c
	s_add_i32 s11, s5, 0x404010
	s_mul_i32 s9, s4, 0x180c
	s_add_i32 s9, s9, s33
	buffer_load_dword v2, v28, s[16:19], s5 offen nt
	buffer_load_dword v3, v28, s[16:19], s6 offen nt
	buffer_load_dword v4, v28, s[16:19], s7 offen nt
	buffer_load_dword v5, v28, s[16:19], s8 offen nt
	buffer_load_dword v6, v28, s[16:19], s11 offen nt
	buffer_load_dwordx3 v[8:10], v27, s[24:27], s9 offen nt
	s_waitcnt vmcnt(12)
	v_pk_mul_f32 v[60:61], v[40:41], v[48:49] op_sel_hi:[1,0]
	v_pk_mul_f32 v[62:63], v[42:43], v[48:49] op_sel_hi:[1,0]
	v_mul_f32_e64 v64, v44, v48
	v_pk_mul_f32 v[66:67], v[40:41], v[48:49] op_sel:[0,1]
	v_pk_mul_f32 v[78:79], v[42:43], v[48:49] op_sel:[0,1]
	v_mul_f32_e64 v84, v44, v49
	v_pk_mul_f32 v[86:87], v[40:41], v[50:51] op_sel_hi:[1,0]
	v_pk_mul_f32 v[96:97], v[42:43], v[50:51] op_sel_hi:[1,0]
	v_mul_f32_e64 v98, v44, v50
	v_add_f32_dpp v100, v40, v40 wave_shr:1 row_mask:0xf bank_mask:0xf bound_ctrl:1
	v_add_f32_dpp v101, v41, v41 wave_shr:1 row_mask:0xf bank_mask:0xf bound_ctrl:1
	v_add_f32_dpp v124, v42, v42 wave_shr:1 row_mask:0xf bank_mask:0xf bound_ctrl:1
	v_add_f32_dpp v125, v43, v43 wave_shr:1 row_mask:0xf bank_mask:0xf bound_ctrl:1
	v_add_f32_dpp v126, v44, v44 wave_shr:1 row_mask:0xf bank_mask:0xf bound_ctrl:1
	v_add_f32_dpp v128, v60, v60 wave_shr:1 row_mask:0xf bank_mask:0xf bound_ctrl:1
	v_add_f32_dpp v129, v61, v61 wave_shr:1 row_mask:0xf bank_mask:0xf bound_ctrl:1
	v_add_f32_dpp v130, v62, v62 wave_shr:1 row_mask:0xf bank_mask:0xf bound_ctrl:1
	v_add_f32_dpp v131, v63, v63 wave_shr:1 row_mask:0xf bank_mask:0xf bound_ctrl:1
	v_add_f32_dpp v132, v64, v64 wave_shr:1 row_mask:0xf bank_mask:0xf bound_ctrl:1
	v_add_f32_dpp v134, v66, v66 wave_shr:1 row_mask:0xf bank_mask:0xf bound_ctrl:1
	v_add_f32_dpp v135, v67, v67 wave_shr:1 row_mask:0xf bank_mask:0xf bound_ctrl:1
	v_add_f32_dpp v136, v78, v78 wave_shr:1 row_mask:0xf bank_mask:0xf bound_ctrl:1
	v_add_f32_dpp v137, v79, v79 wave_shr:1 row_mask:0xf bank_mask:0xf bound_ctrl:1
	v_add_f32_dpp v138, v84, v84 wave_shr:1 row_mask:0xf bank_mask:0xf bound_ctrl:1
	v_add_f32_dpp v140, v86, v86 wave_shr:1 row_mask:0xf bank_mask:0xf bound_ctrl:1
	v_add_f32_dpp v141, v87, v87 wave_shr:1 row_mask:0xf bank_mask:0xf bound_ctrl:1
	v_add_f32_dpp v170, v96, v96 wave_shr:1 row_mask:0xf bank_mask:0xf bound_ctrl:1
	v_add_f32_dpp v171, v97, v97 wave_shr:1 row_mask:0xf bank_mask:0xf bound_ctrl:1
	v_add_f32_dpp v172, v98, v98 wave_shr:1 row_mask:0xf bank_mask:0xf bound_ctrl:1
	v_add_f32_dpp v100, v40, v100 wave_shl:1 row_mask:0xf bank_mask:0xf bound_ctrl:1
	v_add_f32_dpp v101, v41, v101 wave_shl:1 row_mask:0xf bank_mask:0xf bound_ctrl:1
	v_add_f32_dpp v124, v42, v124 wave_shl:1 row_mask:0xf bank_mask:0xf bound_ctrl:1
	v_add_f32_dpp v125, v43, v125 wave_shl:1 row_mask:0xf bank_mask:0xf bound_ctrl:1
	v_add_f32_dpp v126, v44, v126 wave_shl:1 row_mask:0xf bank_mask:0xf bound_ctrl:1
	v_add_f32_dpp v128, v60, v128 wave_shl:1 row_mask:0xf bank_mask:0xf bound_ctrl:1
	v_add_f32_dpp v129, v61, v129 wave_shl:1 row_mask:0xf bank_mask:0xf bound_ctrl:1
	v_add_f32_dpp v130, v62, v130 wave_shl:1 row_mask:0xf bank_mask:0xf bound_ctrl:1
	v_add_f32_dpp v131, v63, v131 wave_shl:1 row_mask:0xf bank_mask:0xf bound_ctrl:1
	v_add_f32_dpp v132, v64, v132 wave_shl:1 row_mask:0xf bank_mask:0xf bound_ctrl:1
	v_add_f32_dpp v134, v66, v134 wave_shl:1 row_mask:0xf bank_mask:0xf bound_ctrl:1
	v_add_f32_dpp v135, v67, v135 wave_shl:1 row_mask:0xf bank_mask:0xf bound_ctrl:1
	v_add_f32_dpp v136, v78, v136 wave_shl:1 row_mask:0xf bank_mask:0xf bound_ctrl:1
	v_add_f32_dpp v137, v79, v137 wave_shl:1 row_mask:0xf bank_mask:0xf bound_ctrl:1
	v_add_f32_dpp v138, v84, v138 wave_shl:1 row_mask:0xf bank_mask:0xf bound_ctrl:1
	v_add_f32_dpp v140, v86, v140 wave_shl:1 row_mask:0xf bank_mask:0xf bound_ctrl:1
	v_add_f32_dpp v141, v87, v141 wave_shl:1 row_mask:0xf bank_mask:0xf bound_ctrl:1
	v_add_f32_dpp v170, v96, v170 wave_shl:1 row_mask:0xf bank_mask:0xf bound_ctrl:1
	v_add_f32_dpp v171, v97, v171 wave_shl:1 row_mask:0xf bank_mask:0xf bound_ctrl:1
	v_add_f32_dpp v172, v98, v172 wave_shl:1 row_mask:0xf bank_mask:0xf bound_ctrl:1
	s_barrier
	ds_read_b128 v[60:63], v23 offset:0
	ds_read_b128 v[64:67], v23 offset:1024
	ds_read_b128 v[84:87], v23 offset:2048
	v_pk_add_f32 v[78:79], v[150:151], v[100:101]
	v_pk_add_f32 v[96:97], v[74:75], v[78:79]
	v_pk_add_f32 v[74:75], v[152:153], v[124:125]
	v_pk_add_f32 v[98:99], v[76:77], v[74:75]
	v_add_f32_e64 v76, v154, v126
	v_add_f32_e64 v150, v80, v76
	v_pk_add_f32 v[80:81], v[156:157], v[128:129]
	v_pk_add_f32 v[152:153], v[82:83], v[80:81]
	v_pk_add_f32 v[82:83], v[158:159], v[130:131]
	v_pk_add_f32 v[154:155], v[88:89], v[82:83]
	v_add_f32_e64 v88, v160, v132
	v_add_f32_e64 v156, v90, v88
	v_pk_add_f32 v[90:91], v[162:163], v[134:135]
	v_pk_add_f32 v[158:159], v[92:93], v[90:91]
	v_pk_add_f32 v[92:93], v[164:165], v[136:137]
	v_pk_add_f32 v[160:161], v[94:95], v[92:93]
	v_add_f32_e64 v94, v166, v138
	v_add_f32_e64 v162, v142, v94
	v_pk_add_f32 v[142:143], v[168:169], v[140:141]
	v_pk_add_f32 v[164:165], v[144:145], v[142:143]
	v_pk_add_f32 v[144:145], v[194:195], v[170:171]
	v_pk_add_f32 v[166:167], v[146:147], v[144:145]
	v_add_f32_e64 v146, v196, v172
	v_add_f32_e64 v168, v148, v146
	s_waitcnt lgkmcnt(2)
	v_pk_fma_f32 v[152:153], v[60:61], v[96:97], v[152:153] op_sel_hi:[0,1,1] neg_lo:[1,0,0] neg_hi:[1,0,0]
	v_pk_fma_f32 v[154:155], v[60:61], v[98:99], v[154:155] op_sel_hi:[0,1,1] neg_lo:[1,0,0] neg_hi:[1,0,0]
	v_fma_f32 v156, -v60, v150, v156
	v_pk_fma_f32 v[158:159], v[60:61], v[96:97], v[158:159] op_sel:[1,0,0] neg_lo:[1,0,0] neg_hi:[1,0,0]
	v_pk_fma_f32 v[160:161], v[60:61], v[98:99], v[160:161] op_sel:[1,0,0] neg_lo:[1,0,0] neg_hi:[1,0,0]
	v_fma_f32 v162, -v61, v150, v162
	v_pk_fma_f32 v[164:165], v[62:63], v[96:97], v[164:165] op_sel_hi:[0,1,1] neg_lo:[1,0,0] neg_hi:[1,0,0]
	v_pk_fma_f32 v[166:167], v[62:63], v[98:99], v[166:167] op_sel_hi:[0,1,1] neg_lo:[1,0,0] neg_hi:[1,0,0]
	v_fma_f32 v168, -v62, v150, v168
	v_pk_mul_f32 v[148:149], v[62:63], v[152:153] op_sel:[1,0]
	v_pk_mul_f32 v[198:199], v[62:63], v[154:155] op_sel:[1,0]
	v_mul_f32_e64 v204, v63, v156
	s_waitcnt lgkmcnt(1)
	v_pk_mul_f32 v[194:195], v[64:65], v[152:153] op_sel_hi:[0,1]
	v_pk_mul_f32 v[200:201], v[64:65], v[154:155] op_sel_hi:[0,1]
	v_mul_f32_e64 v206, v64, v156
	v_pk_mul_f32 v[196:197], v[64:65], v[152:153] op_sel:[1,0]
	v_pk_mul_f32 v[202:203], v[64:65], v[154:155] op_sel:[1,0]
	v_mul_f32_e64 v208, v65, v156
	v_pk_fma_f32 v[148:149], v[64:65], v[158:159], v[148:149] op_sel_hi:[0,1,1]
	v_pk_fma_f32 v[198:199], v[64:65], v[160:161], v[198:199] op_sel_hi:[0,1,1]
	v_fma_f32 v204, v64, v162, v204
	v_pk_fma_f32 v[194:195], v[66:67], v[158:159], v[194:195] op_sel_hi:[0,1,1]
	v_pk_fma_f32 v[200:201], v[66:67], v[160:161], v[200:201] op_sel_hi:[0,1,1]
	v_fma_f32 v206, v66, v162, v206
	v_pk_fma_f32 v[196:197], v[66:67], v[158:159], v[196:197] op_sel:[1,0,0]
	v_pk_fma_f32 v[202:203], v[66:67], v[160:161], v[202:203] op_sel:[1,0,0]
	v_fma_f32 v208, v67, v162, v208
	v_pk_fma_f32 v[148:149], v[64:65], v[164:165], v[148:149] op_sel:[1,0,0]
	v_pk_fma_f32 v[198:199], v[64:65], v[166:167], v[198:199] op_sel:[1,0,0]
	v_fma_f32 v204, v65, v168, v204
	v_pk_fma_f32 v[194:195], v[66:67], v[164:165], v[194:195] op_sel:[1,0,0]
	v_pk_fma_f32 v[200:201], v[66:67], v[166:167], v[200:201] op_sel:[1,0,0]
	v_fma_f32 v206, v67, v168, v206
	s_waitcnt lgkmcnt(0)
	v_pk_fma_f32 v[196:197], v[84:85], v[164:165], v[196:197] op_sel_hi:[0,1,1]
	v_pk_fma_f32 v[202:203], v[84:85], v[166:167], v[202:203] op_sel_hi:[0,1,1]
	v_fma_f32 v208, v84, v168, v208
	v_pk_mul_f32 v[210:211], v[60:61], v[148:149] op_sel_hi:[0,1]
	v_pk_mul_f32 v[212:213], v[60:61], v[198:199] op_sel_hi:[0,1]
	v_mul_f32_e64 v214, v60, v204
	v_pk_fma_f32 v[210:211], v[60:61], v[194:195], v[210:211] op_sel:[1,0,0]
	v_pk_fma_f32 v[212:213], v[60:61], v[200:201], v[212:213] op_sel:[1,0,0]
	v_fma_f32 v214, v61, v206, v214
	v_pk_fma_f32 v[210:211], v[62:63], v[196:197], v[210:211] op_sel_hi:[0,1,1]
	v_pk_fma_f32 v[212:213], v[62:63], v[202:203], v[212:213] op_sel_hi:[0,1,1]
	v_fma_f32 v214, v62, v208, v214
	v_pk_fma_f32 v[210:211], v[84:85], v[96:97], v[210:211] op_sel:[1,0,0] neg_lo:[0,0,1] neg_hi:[0,0,1]
	v_pk_fma_f32 v[212:213], v[84:85], v[98:99], v[212:213] op_sel:[1,0,0] neg_lo:[0,0,1] neg_hi:[0,0,1]
	v_fma_f32 v214, v85, v150, -v214
	v_cmp_eq_u32_e64 s[10:11], 1, v87
	v_cmp_eq_u32_e64 s[14:15], 2, v87
	v_cmp_eq_u32_e64 s[20:21], 3, v87
	v_cmp_eq_u32_e64 s[22:23], 4, v87
	v_cmp_eq_u32_e64 s[30:31], 5, v87
	v_add_f32_dpp v96, v148, v148 wave_shr:1 row_mask:0xf bank_mask:0xf bound_ctrl:1
	v_add_f32_dpp v97, v149, v149 wave_shr:1 row_mask:0xf bank_mask:0xf bound_ctrl:1
	v_add_f32_dpp v98, v198, v198 wave_shr:1 row_mask:0xf bank_mask:0xf bound_ctrl:1
	v_add_f32_dpp v99, v199, v199 wave_shr:1 row_mask:0xf bank_mask:0xf bound_ctrl:1
	v_add_f32_dpp v150, v204, v204 wave_shr:1 row_mask:0xf bank_mask:0xf bound_ctrl:1
	v_add_f32_dpp v152, v194, v194 wave_shr:1 row_mask:0xf bank_mask:0xf bound_ctrl:1
	v_add_f32_dpp v153, v195, v195 wave_shr:1 row_mask:0xf bank_mask:0xf bound_ctrl:1
	v_add_f32_dpp v154, v200, v200 wave_shr:1 row_mask:0xf bank_mask:0xf bound_ctrl:1
	v_add_f32_dpp v155, v201, v201 wave_shr:1 row_mask:0xf bank_mask:0xf bound_ctrl:1
	v_add_f32_dpp v156, v206, v206 wave_shr:1 row_mask:0xf bank_mask:0xf bound_ctrl:1
	v_add_f32_dpp v158, v196, v196 wave_shr:1 row_mask:0xf bank_mask:0xf bound_ctrl:1
	v_add_f32_dpp v159, v197, v197 wave_shr:1 row_mask:0xf bank_mask:0xf bound_ctrl:1
	v_add_f32_dpp v160, v202, v202 wave_shr:1 row_mask:0xf bank_mask:0xf bound_ctrl:1
	v_add_f32_dpp v161, v203, v203 wave_shr:1 row_mask:0xf bank_mask:0xf bound_ctrl:1
	v_add_f32_dpp v162, v208, v208 wave_shr:1 row_mask:0xf bank_mask:0xf bound_ctrl:1
	v_add_f32_dpp v164, v210, v210 wave_shr:1 row_mask:0xf bank_mask:0xf bound_ctrl:1
	v_add_f32_dpp v165, v211, v211 wave_shr:1 row_mask:0xf bank_mask:0xf bound_ctrl:1
	v_add_f32_dpp v166, v212, v212 wave_shr:1 row_mask:0xf bank_mask:0xf bound_ctrl:1
	v_add_f32_dpp v167, v213, v213 wave_shr:1 row_mask:0xf bank_mask:0xf bound_ctrl:1
	v_add_f32_dpp v168, v214, v214 wave_shr:1 row_mask:0xf bank_mask:0xf bound_ctrl:1
	v_add_f32_dpp v96, v148, v96 wave_shl:1 row_mask:0xf bank_mask:0xf bound_ctrl:1
	v_add_f32_dpp v97, v149, v97 wave_shl:1 row_mask:0xf bank_mask:0xf bound_ctrl:1
	v_add_f32_dpp v98, v198, v98 wave_shl:1 row_mask:0xf bank_mask:0xf bound_ctrl:1
	v_add_f32_dpp v99, v199, v99 wave_shl:1 row_mask:0xf bank_mask:0xf bound_ctrl:1
	v_add_f32_dpp v150, v204, v150 wave_shl:1 row_mask:0xf bank_mask:0xf bound_ctrl:1
	v_add_f32_dpp v152, v194, v152 wave_shl:1 row_mask:0xf bank_mask:0xf bound_ctrl:1
	v_add_f32_dpp v153, v195, v153 wave_shl:1 row_mask:0xf bank_mask:0xf bound_ctrl:1
	v_add_f32_dpp v154, v200, v154 wave_shl:1 row_mask:0xf bank_mask:0xf bound_ctrl:1
	v_add_f32_dpp v155, v201, v155 wave_shl:1 row_mask:0xf bank_mask:0xf bound_ctrl:1
	v_add_f32_dpp v156, v206, v156 wave_shl:1 row_mask:0xf bank_mask:0xf bound_ctrl:1
	v_add_f32_dpp v158, v196, v158 wave_shl:1 row_mask:0xf bank_mask:0xf bound_ctrl:1
	v_add_f32_dpp v159, v197, v159 wave_shl:1 row_mask:0xf bank_mask:0xf bound_ctrl:1
	v_add_f32_dpp v160, v202, v160 wave_shl:1 row_mask:0xf bank_mask:0xf bound_ctrl:1
	v_add_f32_dpp v161, v203, v161 wave_shl:1 row_mask:0xf bank_mask:0xf bound_ctrl:1
	v_add_f32_dpp v162, v208, v162 wave_shl:1 row_mask:0xf bank_mask:0xf bound_ctrl:1
	v_add_f32_dpp v164, v210, v164 wave_shl:1 row_mask:0xf bank_mask:0xf bound_ctrl:1
	v_add_f32_dpp v165, v211, v165 wave_shl:1 row_mask:0xf bank_mask:0xf bound_ctrl:1
	v_add_f32_dpp v166, v212, v166 wave_shl:1 row_mask:0xf bank_mask:0xf bound_ctrl:1
	v_add_f32_dpp v167, v213, v167 wave_shl:1 row_mask:0xf bank_mask:0xf bound_ctrl:1
	v_add_f32_dpp v168, v214, v168 wave_shl:1 row_mask:0xf bank_mask:0xf bound_ctrl:1
	v_pk_add_f32 v[148:149], v[68:69], v[96:97]
	v_pk_add_f32 v[194:195], v[70:71], v[148:149]
	v_pk_add_f32 v[68:69], v[72:73], v[98:99]
	v_pk_add_f32 v[70:71], v[102:103], v[68:69]
	v_add_f32_e64 v72, v104, v150
	v_add_f32_e64 v102, v174, v72
	v_pk_add_f32 v[104:105], v[106:107], v[152:153]
	v_pk_add_f32 v[174:175], v[176:177], v[104:105]
	v_pk_add_f32 v[106:107], v[108:109], v[154:155]
	v_pk_add_f32 v[176:177], v[178:179], v[106:107]
	v_add_f32_e64 v108, v110, v156
	v_add_f32_e64 v178, v180, v108
	v_pk_add_f32 v[110:111], v[112:113], v[158:159]
	v_pk_add_f32 v[180:181], v[182:183], v[110:111]
	v_pk_add_f32 v[112:113], v[114:115], v[160:161]
	v_pk_add_f32 v[182:183], v[184:185], v[112:113]
	v_add_f32_e64 v114, v116, v162
	v_add_f32_e64 v184, v186, v114
	v_pk_add_f32 v[116:117], v[118:119], v[164:165]
	v_pk_add_f32 v[186:187], v[188:189], v[116:117]
	v_pk_add_f32 v[118:119], v[120:121], v[166:167]
	v_pk_add_f32 v[188:189], v[190:191], v[118:119]
	v_add_f32_e64 v120, v122, v168
	v_add_f32_e64 v190, v192, v120
	v_pk_fma_f32 v[186:187], v[32:33], v[194:195], v[186:187] op_sel_hi:[0,1,1]
	v_pk_fma_f32 v[188:189], v[32:33], v[70:71], v[188:189] op_sel_hi:[0,1,1]
	v_fma_f32 v190, v32, v102, v190
	v_pk_fma_f32 v[186:187], v[32:33], v[174:175], v[186:187] op_sel:[1,0,0]
	v_pk_fma_f32 v[188:189], v[32:33], v[176:177], v[188:189] op_sel:[1,0,0]
	v_fma_f32 v190, v33, v178, v190
	v_pk_fma_f32 v[186:187], v[34:35], v[180:181], v[186:187] op_sel_hi:[0,1,1]
	v_pk_fma_f32 v[188:189], v[34:35], v[182:183], v[188:189] op_sel_hi:[0,1,1]
	v_fma_f32 v190, v34, v184, v190
	v_cndmask_b32_e64 v122, 0, v1, s[10:11]
	v_cndmask_b32_e64 v123, 0, v1, s[14:15]
	v_cndmask_b32_e64 v192, 0, v1, s[20:21]
	v_cndmask_b32_e64 v193, 0, v1, s[22:23]
	v_cndmask_b32_e64 v196, 0, v1, s[30:31]
	v_pk_fma_f32 v[186:187], v[12:13], v[86:87], v[186:187] op_sel_hi:[1,0,1] neg_lo:[0,0,1] neg_hi:[0,0,1]
	v_pk_fma_f32 v[188:189], v[14:15], v[86:87], v[188:189] op_sel_hi:[1,0,1] neg_lo:[0,0,1] neg_hi:[0,0,1]
	v_fma_f32 v190, v16, v86, -v190
	s_add_i32 s4, s34, 4
	s_cmpk_lt_i32 s4, 0x201
	s_cselect_b64 s[12:13], s[0:1], 0
	v_pk_add_f32 v[186:187], v[186:187], v[122:123] neg_lo:[0,1] neg_hi:[0,1]
	v_pk_add_f32 v[188:189], v[188:189], v[192:193] neg_lo:[0,1] neg_hi:[0,1]
	v_add_f32_e64 v190, v190, -v196
	v_pk_mul_f32 v[198:199], v[186:187], v[186:187]
	v_pk_fma_f32 v[198:199], v[188:189], v[188:189], v[198:199]
	v_add_f32_e32 v198, v198, v199
	v_fma_f32 v198, v190, v190, v198
	v_cndmask_b32_e64 v199, 0, v198, s[12:13]
	v_add_f32_e32 v0, v0, v199
	s_add_i32 s4, s34, 9
	s_min_i32 s4, s4, 0x200
	s_mul_i32 s5, s4, 0x804
	s_add_i32 s5, s5, s35
	s_add_i32 s6, s5, 0x101004
	s_add_i32 s7, s5, 0x202008
	s_add_i32 s8, s5, 0x30300c
	s_add_i32 s11, s5, 0x404010
	s_mul_i32 s9, s4, 0x180c
	s_add_i32 s9, s9, s33
	buffer_load_dword v12, v28, s[16:19], s5 offen nt
	buffer_load_dword v13, v28, s[16:19], s6 offen nt
	buffer_load_dword v14, v28, s[16:19], s7 offen nt
	buffer_load_dword v15, v28, s[16:19], s8 offen nt
	buffer_load_dword v16, v28, s[16:19], s11 offen nt
	buffer_load_dwordx3 v[32:34], v27, s[24:27], s9 offen nt
	s_waitcnt vmcnt(12)
	v_pk_mul_f32 v[60:61], v[46:47], v[56:57] op_sel_hi:[1,0]
	v_pk_mul_f32 v[62:63], v[52:53], v[56:57] op_sel_hi:[1,0]
	v_mul_f32_e64 v64, v54, v56
	v_pk_mul_f32 v[66:67], v[46:47], v[56:57] op_sel:[0,1]
	v_pk_mul_f32 v[70:71], v[52:53], v[56:57] op_sel:[0,1]
	v_mul_f32_e64 v84, v54, v57
	v_pk_mul_f32 v[86:87], v[46:47], v[58:59] op_sel_hi:[1,0]
	v_pk_mul_f32 v[102:103], v[52:53], v[58:59] op_sel_hi:[1,0]
	v_mul_f32_e64 v122, v54, v58
	v_add_f32_dpp v174, v46, v46 wave_shr:1 row_mask:0xf bank_mask:0xf bound_ctrl:1
	v_add_f32_dpp v175, v47, v47 wave_shr:1 row_mask:0xf bank_mask:0xf bound_ctrl:1
	v_add_f32_dpp v176, v52, v52 wave_shr:1 row_mask:0xf bank_mask:0xf bound_ctrl:1
	v_add_f32_dpp v177, v53, v53 wave_shr:1 row_mask:0xf bank_mask:0xf bound_ctrl:1
	v_add_f32_dpp v178, v54, v54 wave_shr:1 row_mask:0xf bank_mask:0xf bound_ctrl:1
	v_add_f32_dpp v180, v60, v60 wave_shr:1 row_mask:0xf bank_mask:0xf bound_ctrl:1
	v_add_f32_dpp v181, v61, v61 wave_shr:1 row_mask:0xf bank_mask:0xf bound_ctrl:1
	v_add_f32_dpp v182, v62, v62 wave_shr:1 row_mask:0xf bank_mask:0xf bound_ctrl:1
	v_add_f32_dpp v183, v63, v63 wave_shr:1 row_mask:0xf bank_mask:0xf bound_ctrl:1
	v_add_f32_dpp v184, v64, v64 wave_shr:1 row_mask:0xf bank_mask:0xf bound_ctrl:1
	v_add_f32_dpp v186, v66, v66 wave_shr:1 row_mask:0xf bank_mask:0xf bound_ctrl:1
	v_add_f32_dpp v187, v67, v67 wave_shr:1 row_mask:0xf bank_mask:0xf bound_ctrl:1
	v_add_f32_dpp v188, v70, v70 wave_shr:1 row_mask:0xf bank_mask:0xf bound_ctrl:1
	v_add_f32_dpp v189, v71, v71 wave_shr:1 row_mask:0xf bank_mask:0xf bound_ctrl:1
	v_add_f32_dpp v190, v84, v84 wave_shr:1 row_mask:0xf bank_mask:0xf bound_ctrl:1
	v_add_f32_dpp v192, v86, v86 wave_shr:1 row_mask:0xf bank_mask:0xf bound_ctrl:1
	v_add_f32_dpp v193, v87, v87 wave_shr:1 row_mask:0xf bank_mask:0xf bound_ctrl:1
	v_add_f32_dpp v194, v102, v102 wave_shr:1 row_mask:0xf bank_mask:0xf bound_ctrl:1
	v_add_f32_dpp v195, v103, v103 wave_shr:1 row_mask:0xf bank_mask:0xf bound_ctrl:1
	v_add_f32_dpp v196, v122, v122 wave_shr:1 row_mask:0xf bank_mask:0xf bound_ctrl:1
	v_add_f32_dpp v174, v46, v174 wave_shl:1 row_mask:0xf bank_mask:0xf bound_ctrl:1
	v_add_f32_dpp v175, v47, v175 wave_shl:1 row_mask:0xf bank_mask:0xf bound_ctrl:1
	v_add_f32_dpp v176, v52, v176 wave_shl:1 row_mask:0xf bank_mask:0xf bound_ctrl:1
	v_add_f32_dpp v177, v53, v177 wave_shl:1 row_mask:0xf bank_mask:0xf bound_ctrl:1
	v_add_f32_dpp v178, v54, v178 wave_shl:1 row_mask:0xf bank_mask:0xf bound_ctrl:1
	v_add_f32_dpp v180, v60, v180 wave_shl:1 row_mask:0xf bank_mask:0xf bound_ctrl:1
	v_add_f32_dpp v181, v61, v181 wave_shl:1 row_mask:0xf bank_mask:0xf bound_ctrl:1
	v_add_f32_dpp v182, v62, v182 wave_shl:1 row_mask:0xf bank_mask:0xf bound_ctrl:1
	v_add_f32_dpp v183, v63, v183 wave_shl:1 row_mask:0xf bank_mask:0xf bound_ctrl:1
	v_add_f32_dpp v184, v64, v184 wave_shl:1 row_mask:0xf bank_mask:0xf bound_ctrl:1
	v_add_f32_dpp v186, v66, v186 wave_shl:1 row_mask:0xf bank_mask:0xf bound_ctrl:1
	v_add_f32_dpp v187, v67, v187 wave_shl:1 row_mask:0xf bank_mask:0xf bound_ctrl:1
	v_add_f32_dpp v188, v70, v188 wave_shl:1 row_mask:0xf bank_mask:0xf bound_ctrl:1
	v_add_f32_dpp v189, v71, v189 wave_shl:1 row_mask:0xf bank_mask:0xf bound_ctrl:1
	v_add_f32_dpp v190, v84, v190 wave_shl:1 row_mask:0xf bank_mask:0xf bound_ctrl:1
	v_add_f32_dpp v192, v86, v192 wave_shl:1 row_mask:0xf bank_mask:0xf bound_ctrl:1
	v_add_f32_dpp v193, v87, v193 wave_shl:1 row_mask:0xf bank_mask:0xf bound_ctrl:1
	v_add_f32_dpp v194, v102, v194 wave_shl:1 row_mask:0xf bank_mask:0xf bound_ctrl:1
	v_add_f32_dpp v195, v103, v195 wave_shl:1 row_mask:0xf bank_mask:0xf bound_ctrl:1
	v_add_f32_dpp v196, v122, v196 wave_shl:1 row_mask:0xf bank_mask:0xf bound_ctrl:1
	s_barrier
	ds_read_b128 v[60:63], v23 offset:3072
	ds_read_b128 v[64:67], v23 offset:4096
	ds_read_b128 v[84:87], v23 offset:5120
	v_pk_add_f32 v[70:71], v[78:79], v[174:175]
	v_pk_add_f32 v[78:79], v[74:75], v[176:177]
	v_add_f32_e64 v74, v76, v178
	v_pk_add_f32 v[76:77], v[80:81], v[180:181]
	v_pk_add_f32 v[80:81], v[82:83], v[182:183]
	v_add_f32_e64 v82, v88, v184
	v_pk_add_f32 v[88:89], v[90:91], v[186:187]
	v_pk_add_f32 v[90:91], v[92:93], v[188:189]
	v_add_f32_e64 v92, v94, v190
	v_pk_add_f32 v[94:95], v[142:143], v[192:193]
	v_pk_add_f32 v[102:103], v[144:145], v[194:195]
	v_add_f32_e64 v122, v146, v196
	s_waitcnt lgkmcnt(2)
	v_pk_fma_f32 v[76:77], v[60:61], v[70:71], v[76:77] op_sel_hi:[0,1,1] neg_lo:[1,0,0] neg_hi:[1,0,0]
	v_pk_fma_f32 v[80:81], v[60:61], v[78:79], v[80:81] op_sel_hi:[0,1,1] neg_lo:[1,0,0] neg_hi:[1,0,0]
	v_fma_f32 v82, -v60, v74, v82
	v_pk_fma_f32 v[88:89], v[60:61], v[70:71], v[88:89] op_sel:[1,0,0] neg_lo:[1,0,0] neg_hi:[1,0,0]
	v_pk_fma_f32 v[90:91], v[60:61], v[78:79], v[90:91] op_sel:[1,0,0] neg_lo:[1,0,0] neg_hi:[1,0,0]
	v_fma_f32 v92, -v61, v74, v92
	v_pk_fma_f32 v[94:95], v[62:63], v[70:71], v[94:95] op_sel_hi:[0,1,1] neg_lo:[1,0,0] neg_hi:[1,0,0]
	v_pk_fma_f32 v[102:103], v[62:63], v[78:79], v[102:103] op_sel_hi:[0,1,1] neg_lo:[1,0,0] neg_hi:[1,0,0]
	v_fma_f32 v122, -v62, v74, v122
	v_pk_mul_f32 v[142:143], v[62:63], v[76:77] op_sel:[1,0]
	v_pk_mul_f32 v[198:199], v[62:63], v[80:81] op_sel:[1,0]
	v_mul_f32_e64 v204, v63, v82
	s_waitcnt lgkmcnt(1)
	v_pk_mul_f32 v[144:145], v[64:65], v[76:77] op_sel_hi:[0,1]
	v_pk_mul_f32 v[200:201], v[64:65], v[80:81] op_sel_hi:[0,1]
	v_mul_f32_e64 v206, v64, v82
	v_pk_mul_f32 v[146:147], v[64:65], v[76:77] op_sel:[1,0]
	v_pk_mul_f32 v[202:203], v[64:65], v[80:81] op_sel:[1,0]
	v_mul_f32_e64 v208, v65, v82
	v_pk_fma_f32 v[142:143], v[64:65], v[88:89], v[142:143] op_sel_hi:[0,1,1]
	v_pk_fma_f32 v[198:199], v[64:65], v[90:91], v[198:199] op_sel_hi:[0,1,1]
	v_fma_f32 v204, v64, v92, v204
	v_pk_fma_f32 v[144:145], v[66:67], v[88:89], v[144:145] op_sel_hi:[0,1,1]
	v_pk_fma_f32 v[200:201], v[66:67], v[90:91], v[200:201] op_sel_hi:[0,1,1]
	v_fma_f32 v206, v66, v92, v206
	v_pk_fma_f32 v[146:147], v[66:67], v[88:89], v[146:147] op_sel:[1,0,0]
	v_pk_fma_f32 v[202:203], v[66:67], v[90:91], v[202:203] op_sel:[1,0,0]
	v_fma_f32 v208, v67, v92, v208
	v_pk_fma_f32 v[142:143], v[64:65], v[94:95], v[142:143] op_sel:[1,0,0]
	v_pk_fma_f32 v[198:199], v[64:65], v[102:103], v[198:199] op_sel:[1,0,0]
	v_fma_f32 v204, v65, v122, v204
	v_pk_fma_f32 v[144:145], v[66:67], v[94:95], v[144:145] op_sel:[1,0,0]
	v_pk_fma_f32 v[200:201], v[66:67], v[102:103], v[200:201] op_sel:[1,0,0]
	v_fma_f32 v206, v67, v122, v206
	s_waitcnt lgkmcnt(0)
	v_pk_fma_f32 v[146:147], v[84:85], v[94:95], v[146:147] op_sel_hi:[0,1,1]
	v_pk_fma_f32 v[202:203], v[84:85], v[102:103], v[202:203] op_sel_hi:[0,1,1]
	v_fma_f32 v208, v84, v122, v208
	v_pk_mul_f32 v[210:211], v[60:61], v[142:143] op_sel_hi:[0,1]
	v_pk_mul_f32 v[212:213], v[60:61], v[198:199] op_sel_hi:[0,1]
	v_mul_f32_e64 v214, v60, v204
	v_pk_fma_f32 v[210:211], v[60:61], v[144:145], v[210:211] op_sel:[1,0,0]
	v_pk_fma_f32 v[212:213], v[60:61], v[200:201], v[212:213] op_sel:[1,0,0]
	v_fma_f32 v214, v61, v206, v214
	v_pk_fma_f32 v[210:211], v[62:63], v[146:147], v[210:211] op_sel_hi:[0,1,1]
	v_pk_fma_f32 v[212:213], v[62:63], v[202:203], v[212:213] op_sel_hi:[0,1,1]
	v_fma_f32 v214, v62, v208, v214
	v_pk_fma_f32 v[210:211], v[84:85], v[70:71], v[210:211] op_sel:[1,0,0] neg_lo:[0,0,1] neg_hi:[0,0,1]
	v_pk_fma_f32 v[212:213], v[84:85], v[78:79], v[212:213] op_sel:[1,0,0] neg_lo:[0,0,1] neg_hi:[0,0,1]
	v_fma_f32 v214, v85, v74, -v214
	v_cmp_eq_u32_e64 s[10:11], 1, v87
	v_cmp_eq_u32_e64 s[14:15], 2, v87
	v_cmp_eq_u32_e64 s[20:21], 3, v87
	v_cmp_eq_u32_e64 s[22:23], 4, v87
	v_cmp_eq_u32_e64 s[30:31], 5, v87
	v_add_f32_dpp v70, v142, v142 wave_shr:1 row_mask:0xf bank_mask:0xf bound_ctrl:1
	v_add_f32_dpp v71, v143, v143 wave_shr:1 row_mask:0xf bank_mask:0xf bound_ctrl:1
	v_add_f32_dpp v74, v198, v198 wave_shr:1 row_mask:0xf bank_mask:0xf bound_ctrl:1
	v_add_f32_dpp v75, v199, v199 wave_shr:1 row_mask:0xf bank_mask:0xf bound_ctrl:1
	v_add_f32_dpp v76, v204, v204 wave_shr:1 row_mask:0xf bank_mask:0xf bound_ctrl:1
	v_add_f32_dpp v78, v144, v144 wave_shr:1 row_mask:0xf bank_mask:0xf bound_ctrl:1
	v_add_f32_dpp v79, v145, v145 wave_shr:1 row_mask:0xf bank_mask:0xf bound_ctrl:1
	v_add_f32_dpp v80, v200, v200 wave_shr:1 row_mask:0xf bank_mask:0xf bound_ctrl:1
	v_add_f32_dpp v81, v201, v201 wave_shr:1 row_mask:0xf bank_mask:0xf bound_ctrl:1
	v_add_f32_dpp v82, v206, v206 wave_shr:1 row_mask:0xf bank_mask:0xf bound_ctrl:1
	v_add_f32_dpp v88, v146, v146 wave_shr:1 row_mask:0xf bank_mask:0xf bound_ctrl:1
	v_add_f32_dpp v89, v147, v147 wave_shr:1 row_mask:0xf bank_mask:0xf bound_ctrl:1
	v_add_f32_dpp v90, v202, v202 wave_shr:1 row_mask:0xf bank_mask:0xf bound_ctrl:1
	v_add_f32_dpp v91, v203, v203 wave_shr:1 row_mask:0xf bank_mask:0xf bound_ctrl:1
	v_add_f32_dpp v92, v208, v208 wave_shr:1 row_mask:0xf bank_mask:0xf bound_ctrl:1
	v_add_f32_dpp v94, v210, v210 wave_shr:1 row_mask:0xf bank_mask:0xf bound_ctrl:1
	v_add_f32_dpp v95, v211, v211 wave_shr:1 row_mask:0xf bank_mask:0xf bound_ctrl:1
	v_add_f32_dpp v102, v212, v212 wave_shr:1 row_mask:0xf bank_mask:0xf bound_ctrl:1
	v_add_f32_dpp v103, v213, v213 wave_shr:1 row_mask:0xf bank_mask:0xf bound_ctrl:1
	v_add_f32_dpp v122, v214, v214 wave_shr:1 row_mask:0xf bank_mask:0xf bound_ctrl:1
	v_add_f32_dpp v70, v142, v70 wave_shl:1 row_mask:0xf bank_mask:0xf bound_ctrl:1
	v_add_f32_dpp v71, v143, v71 wave_shl:1 row_mask:0xf bank_mask:0xf bound_ctrl:1
	v_add_f32_dpp v74, v198, v74 wave_shl:1 row_mask:0xf bank_mask:0xf bound_ctrl:1
	v_add_f32_dpp v75, v199, v75 wave_shl:1 row_mask:0xf bank_mask:0xf bound_ctrl:1
	v_add_f32_dpp v76, v204, v76 wave_shl:1 row_mask:0xf bank_mask:0xf bound_ctrl:1
	v_add_f32_dpp v78, v144, v78 wave_shl:1 row_mask:0xf bank_mask:0xf bound_ctrl:1
	v_add_f32_dpp v79, v145, v79 wave_shl:1 row_mask:0xf bank_mask:0xf bound_ctrl:1
	v_add_f32_dpp v80, v200, v80 wave_shl:1 row_mask:0xf bank_mask:0xf bound_ctrl:1
	v_add_f32_dpp v81, v201, v81 wave_shl:1 row_mask:0xf bank_mask:0xf bound_ctrl:1
	v_add_f32_dpp v82, v206, v82 wave_shl:1 row_mask:0xf bank_mask:0xf bound_ctrl:1
	v_add_f32_dpp v88, v146, v88 wave_shl:1 row_mask:0xf bank_mask:0xf bound_ctrl:1
	v_add_f32_dpp v89, v147, v89 wave_shl:1 row_mask:0xf bank_mask:0xf bound_ctrl:1
	v_add_f32_dpp v90, v202, v90 wave_shl:1 row_mask:0xf bank_mask:0xf bound_ctrl:1
	v_add_f32_dpp v91, v203, v91 wave_shl:1 row_mask:0xf bank_mask:0xf bound_ctrl:1
	v_add_f32_dpp v92, v208, v92 wave_shl:1 row_mask:0xf bank_mask:0xf bound_ctrl:1
	v_add_f32_dpp v94, v210, v94 wave_shl:1 row_mask:0xf bank_mask:0xf bound_ctrl:1
	v_add_f32_dpp v95, v211, v95 wave_shl:1 row_mask:0xf bank_mask:0xf bound_ctrl:1
	v_add_f32_dpp v102, v212, v102 wave_shl:1 row_mask:0xf bank_mask:0xf bound_ctrl:1
	v_add_f32_dpp v103, v213, v103 wave_shl:1 row_mask:0xf bank_mask:0xf bound_ctrl:1
	v_add_f32_dpp v122, v214, v122 wave_shl:1 row_mask:0xf bank_mask:0xf bound_ctrl:1
	v_pk_add_f32 v[142:143], v[148:149], v[70:71]
	v_pk_add_f32 v[144:145], v[68:69], v[74:75]
	v_add_f32_e64 v68, v72, v76
	v_pk_add_f32 v[72:73], v[104:105], v[78:79]
	v_pk_add_f32 v[104:105], v[106:107], v[80:81]
	v_add_f32_e64 v106, v108, v82
	v_pk_add_f32 v[108:109], v[110:111], v[88:89]
	v_pk_add_f32 v[110:111], v[112:113], v[90:91]
	v_add_f32_e64 v112, v114, v92
	v_pk_add_f32 v[114:115], v[116:117], v[94:95]
	v_pk_add_f32 v[116:117], v[118:119], v[102:103]
	v_add_f32_e64 v118, v120, v122
	v_pk_fma_f32 v[114:115], v[36:37], v[142:143], v[114:115] op_sel_hi:[0,1,1]
	v_pk_fma_f32 v[116:117], v[36:37], v[144:145], v[116:117] op_sel_hi:[0,1,1]
	v_fma_f32 v118, v36, v68, v118
	v_pk_fma_f32 v[114:115], v[36:37], v[72:73], v[114:115] op_sel:[1,0,0]
	v_pk_fma_f32 v[116:117], v[36:37], v[104:105], v[116:117] op_sel:[1,0,0]
	v_fma_f32 v118, v37, v106, v118
	v_pk_fma_f32 v[114:115], v[38:39], v[108:109], v[114:115] op_sel_hi:[0,1,1]
	v_pk_fma_f32 v[116:117], v[38:39], v[110:111], v[116:117] op_sel_hi:[0,1,1]
	v_fma_f32 v118, v38, v112, v118
	v_cndmask_b32_e64 v120, 0, v1, s[10:11]
	v_cndmask_b32_e64 v121, 0, v1, s[14:15]
	v_cndmask_b32_e64 v146, 0, v1, s[20:21]
	v_cndmask_b32_e64 v147, 0, v1, s[22:23]
	v_cndmask_b32_e64 v148, 0, v1, s[30:31]
	v_pk_fma_f32 v[114:115], v[20:21], v[86:87], v[114:115] op_sel_hi:[1,0,1] neg_lo:[0,0,1] neg_hi:[0,0,1]
	v_pk_fma_f32 v[116:117], v[24:25], v[86:87], v[116:117] op_sel_hi:[1,0,1] neg_lo:[0,0,1] neg_hi:[0,0,1]
	v_fma_f32 v118, v30, v86, -v118
	s_add_i32 s4, s34, 5
	s_cmpk_lt_i32 s4, 0x201
	s_cselect_b64 s[12:13], s[0:1], 0
	v_pk_add_f32 v[114:115], v[114:115], v[120:121] neg_lo:[0,1] neg_hi:[0,1]
	v_pk_add_f32 v[116:117], v[116:117], v[146:147] neg_lo:[0,1] neg_hi:[0,1]
	v_add_f32_e64 v118, v118, -v148
	v_pk_mul_f32 v[198:199], v[114:115], v[114:115]
	v_pk_fma_f32 v[198:199], v[116:117], v[116:117], v[198:199]
	v_add_f32_e32 v198, v198, v199
	v_fma_f32 v198, v118, v118, v198
	v_cndmask_b32_e64 v199, 0, v198, s[12:13]
	v_add_f32_e32 v0, v0, v199
	s_add_i32 s4, s34, 10
	s_min_i32 s4, s4, 0x200
	s_mul_i32 s5, s4, 0x804
	s_add_i32 s5, s5, s35
	s_add_i32 s6, s5, 0x101004
	s_add_i32 s7, s5, 0x202008
	s_add_i32 s8, s5, 0x30300c
	s_add_i32 s11, s5, 0x404010
	s_mul_i32 s9, s4, 0x180c
	s_add_i32 s9, s9, s33
	buffer_load_dword v20, v28, s[16:19], s5 offen nt
	buffer_load_dword v21, v28, s[16:19], s6 offen nt
	buffer_load_dword v24, v28, s[16:19], s7 offen nt
	buffer_load_dword v25, v28, s[16:19], s8 offen nt
	buffer_load_dword v30, v28, s[16:19], s11 offen nt
	buffer_load_dwordx3 v[36:38], v27, s[24:27], s9 offen nt
	s_waitcnt vmcnt(12)
	v_pk_mul_f32 v[60:61], v[2:3], v[8:9] op_sel_hi:[1,0]
	v_pk_mul_f32 v[62:63], v[4:5], v[8:9] op_sel_hi:[1,0]
	v_mul_f32_e64 v64, v6, v8
	v_pk_mul_f32 v[66:67], v[2:3], v[8:9] op_sel:[0,1]
	v_pk_mul_f32 v[68:69], v[4:5], v[8:9] op_sel:[0,1]
	v_mul_f32_e64 v72, v6, v9
	v_pk_mul_f32 v[84:85], v[2:3], v[10:11] op_sel_hi:[1,0]
	v_pk_mul_f32 v[86:87], v[4:5], v[10:11] op_sel_hi:[1,0]
	v_mul_f32_e64 v104, v6, v10
	v_add_f32_dpp v106, v2, v2 wave_shr:1 row_mask:0xf bank_mask:0xf bound_ctrl:1
	v_add_f32_dpp v107, v3, v3 wave_shr:1 row_mask:0xf bank_mask:0xf bound_ctrl:1
	v_add_f32_dpp v108, v4, v4 wave_shr:1 row_mask:0xf bank_mask:0xf bound_ctrl:1
	v_add_f32_dpp v109, v5, v5 wave_shr:1 row_mask:0xf bank_mask:0xf bound_ctrl:1
	v_add_f32_dpp v110, v6, v6 wave_shr:1 row_mask:0xf bank_mask:0xf bound_ctrl:1
	v_add_f32_dpp v112, v60, v60 wave_shr:1 row_mask:0xf bank_mask:0xf bound_ctrl:1
	v_add_f32_dpp v113, v61, v61 wave_shr:1 row_mask:0xf bank_mask:0xf bound_ctrl:1
	v_add_f32_dpp v114, v62, v62 wave_shr:1 row_mask:0xf bank_mask:0xf bound_ctrl:1
	v_add_f32_dpp v115, v63, v63 wave_shr:1 row_mask:0xf bank_mask:0xf bound_ctrl:1
	v_add_f32_dpp v116, v64, v64 wave_shr:1 row_mask:0xf bank_mask:0xf bound_ctrl:1
	v_add_f32_dpp v118, v66, v66 wave_shr:1 row_mask:0xf bank_mask:0xf bound_ctrl:1
	v_add_f32_dpp v119, v67, v67 wave_shr:1 row_mask:0xf bank_mask:0xf bound_ctrl:1
	v_add_f32_dpp v120, v68, v68 wave_shr:1 row_mask:0xf bank_mask:0xf bound_ctrl:1
	v_add_f32_dpp v121, v69, v69 wave_shr:1 row_mask:0xf bank_mask:0xf bound_ctrl:1
	v_add_f32_dpp v142, v72, v72 wave_shr:1 row_mask:0xf bank_mask:0xf bound_ctrl:1
	v_add_f32_dpp v144, v84, v84 wave_shr:1 row_mask:0xf bank_mask:0xf bound_ctrl:1
	v_add_f32_dpp v145, v85, v85 wave_shr:1 row_mask:0xf bank_mask:0xf bound_ctrl:1
	v_add_f32_dpp v146, v86, v86 wave_shr:1 row_mask:0xf bank_mask:0xf bound_ctrl:1
	v_add_f32_dpp v147, v87, v87 wave_shr:1 row_mask:0xf bank_mask:0xf bound_ctrl:1
	v_add_f32_dpp v148, v104, v104 wave_shr:1 row_mask:0xf bank_mask:0xf bound_ctrl:1
	v_add_f32_dpp v106, v2, v106 wave_shl:1 row_mask:0xf bank_mask:0xf bound_ctrl:1
	v_add_f32_dpp v107, v3, v107 wave_shl:1 row_mask:0xf bank_mask:0xf bound_ctrl:1
	v_add_f32_dpp v108, v4, v108 wave_shl:1 row_mask:0xf bank_mask:0xf bound_ctrl:1
	v_add_f32_dpp v109, v5, v109 wave_shl:1 row_mask:0xf bank_mask:0xf bound_ctrl:1
	v_add_f32_dpp v110, v6, v110 wave_shl:1 row_mask:0xf bank_mask:0xf bound_ctrl:1
	v_add_f32_dpp v112, v60, v112 wave_shl:1 row_mask:0xf bank_mask:0xf bound_ctrl:1
	v_add_f32_dpp v113, v61, v113 wave_shl:1 row_mask:0xf bank_mask:0xf bound_ctrl:1
	v_add_f32_dpp v114, v62, v114 wave_shl:1 row_mask:0xf bank_mask:0xf bound_ctrl:1
	v_add_f32_dpp v115, v63, v115 wave_shl:1 row_mask:0xf bank_mask:0xf bound_ctrl:1
	v_add_f32_dpp v116, v64, v116 wave_shl:1 row_mask:0xf bank_mask:0xf bound_ctrl:1
	v_add_f32_dpp v118, v66, v118 wave_shl:1 row_mask:0xf bank_mask:0xf bound_ctrl:1
	v_add_f32_dpp v119, v67, v119 wave_shl:1 row_mask:0xf bank_mask:0xf bound_ctrl:1
	v_add_f32_dpp v120, v68, v120 wave_shl:1 row_mask:0xf bank_mask:0xf bound_ctrl:1
	v_add_f32_dpp v121, v69, v121 wave_shl:1 row_mask:0xf bank_mask:0xf bound_ctrl:1
	v_add_f32_dpp v142, v72, v142 wave_shl:1 row_mask:0xf bank_mask:0xf bound_ctrl:1
	v_add_f32_dpp v144, v84, v144 wave_shl:1 row_mask:0xf bank_mask:0xf bound_ctrl:1
	v_add_f32_dpp v145, v85, v145 wave_shl:1 row_mask:0xf bank_mask:0xf bound_ctrl:1
	v_add_f32_dpp v146, v86, v146 wave_shl:1 row_mask:0xf bank_mask:0xf bound_ctrl:1
	v_add_f32_dpp v147, v87, v147 wave_shl:1 row_mask:0xf bank_mask:0xf bound_ctrl:1
	v_add_f32_dpp v148, v104, v148 wave_shl:1 row_mask:0xf bank_mask:0xf bound_ctrl:1
	s_barrier
	ds_read_b128 v[60:63], v23 offset:0
	ds_read_b128 v[64:67], v23 offset:1024
	ds_read_b128 v[84:87], v23 offset:2048
	v_pk_add_f32 v[68:69], v[174:175], v[106:107]
	v_pk_add_f32 v[72:73], v[100:101], v[68:69]
	v_pk_add_f32 v[100:101], v[176:177], v[108:109]
	v_pk_add_f32 v[104:105], v[124:125], v[100:101]
	v_add_f32_e64 v124, v178, v110
	v_add_f32_e64 v174, v126, v124
	v_pk_add_f32 v[126:127], v[180:181], v[112:113]
	v_pk_add_f32 v[176:177], v[128:129], v[126:127]
	v_pk_add_f32 v[128:129], v[182:183], v[114:115]
	v_pk_add_f32 v[178:179], v[130:131], v[128:129]
	v_add_f32_e64 v130, v184, v116
	v_add_f32_e64 v180, v132, v130
	v_pk_add_f32 v[132:133], v[186:187], v[118:119]
	v_pk_add_f32 v[182:183], v[134:135], v[132:133]
	v_pk_add_f32 v[134:135], v[188:189], v[120:121]
	v_pk_add_f32 v[184:185], v[136:137], v[134:135]
	v_add_f32_e64 v136, v190, v142
	v_add_f32_e64 v186, v138, v136
	v_pk_add_f32 v[138:139], v[192:193], v[144:145]
	v_pk_add_f32 v[188:189], v[140:141], v[138:139]
	v_pk_add_f32 v[140:141], v[194:195], v[146:147]
	v_pk_add_f32 v[190:191], v[170:171], v[140:141]
	v_add_f32_e64 v170, v196, v148
	v_add_f32_e64 v192, v172, v170
	s_waitcnt lgkmcnt(2)
	v_pk_fma_f32 v[176:177], v[60:61], v[72:73], v[176:177] op_sel_hi:[0,1,1] neg_lo:[1,0,0] neg_hi:[1,0,0]
	v_pk_fma_f32 v[178:179], v[60:61], v[104:105], v[178:179] op_sel_hi:[0,1,1] neg_lo:[1,0,0] neg_hi:[1,0,0]
	v_fma_f32 v180, -v60, v174, v180
	v_pk_fma_f32 v[182:183], v[60:61], v[72:73], v[182:183] op_sel:[1,0,0] neg_lo:[1,0,0] neg_hi:[1,0,0]
	v_pk_fma_f32 v[184:185], v[60:61], v[104:105], v[184:185] op_sel:[1,0,0] neg_lo:[1,0,0] neg_hi:[1,0,0]
	v_fma_f32 v186, -v61, v174, v186
	v_pk_fma_f32 v[188:189], v[62:63], v[72:73], v[188:189] op_sel_hi:[0,1,1] neg_lo:[1,0,0] neg_hi:[1,0,0]
	v_pk_fma_f32 v[190:191], v[62:63], v[104:105], v[190:191] op_sel_hi:[0,1,1] neg_lo:[1,0,0] neg_hi:[1,0,0]
	v_fma_f32 v192, -v62, v174, v192
	v_pk_mul_f32 v[172:173], v[62:63], v[176:177] op_sel:[1,0]
	v_pk_mul_f32 v[198:199], v[62:63], v[178:179] op_sel:[1,0]
	v_mul_f32_e64 v204, v63, v180
	s_waitcnt lgkmcnt(1)
	v_pk_mul_f32 v[194:195], v[64:65], v[176:177] op_sel_hi:[0,1]
	v_pk_mul_f32 v[200:201], v[64:65], v[178:179] op_sel_hi:[0,1]
	v_mul_f32_e64 v206, v64, v180
	v_pk_mul_f32 v[196:197], v[64:65], v[176:177] op_sel:[1,0]
	v_pk_mul_f32 v[202:203], v[64:65], v[178:179] op_sel:[1,0]
	v_mul_f32_e64 v208, v65, v180
	v_pk_fma_f32 v[172:173], v[64:65], v[182:183], v[172:173] op_sel_hi:[0,1,1]
	v_pk_fma_f32 v[198:199], v[64:65], v[184:185], v[198:199] op_sel_hi:[0,1,1]
	v_fma_f32 v204, v64, v186, v204
	v_pk_fma_f32 v[194:195], v[66:67], v[182:183], v[194:195] op_sel_hi:[0,1,1]
	v_pk_fma_f32 v[200:201], v[66:67], v[184:185], v[200:201] op_sel_hi:[0,1,1]
	v_fma_f32 v206, v66, v186, v206
	v_pk_fma_f32 v[196:197], v[66:67], v[182:183], v[196:197] op_sel:[1,0,0]
	v_pk_fma_f32 v[202:203], v[66:67], v[184:185], v[202:203] op_sel:[1,0,0]
	v_fma_f32 v208, v67, v186, v208
	v_pk_fma_f32 v[172:173], v[64:65], v[188:189], v[172:173] op_sel:[1,0,0]
	v_pk_fma_f32 v[198:199], v[64:65], v[190:191], v[198:199] op_sel:[1,0,0]
	v_fma_f32 v204, v65, v192, v204
	v_pk_fma_f32 v[194:195], v[66:67], v[188:189], v[194:195] op_sel:[1,0,0]
	v_pk_fma_f32 v[200:201], v[66:67], v[190:191], v[200:201] op_sel:[1,0,0]
	v_fma_f32 v206, v67, v192, v206
	s_waitcnt lgkmcnt(0)
	v_pk_fma_f32 v[196:197], v[84:85], v[188:189], v[196:197] op_sel_hi:[0,1,1]
	v_pk_fma_f32 v[202:203], v[84:85], v[190:191], v[202:203] op_sel_hi:[0,1,1]
	v_fma_f32 v208, v84, v192, v208
	v_pk_mul_f32 v[210:211], v[60:61], v[172:173] op_sel_hi:[0,1]
	v_pk_mul_f32 v[212:213], v[60:61], v[198:199] op_sel_hi:[0,1]
	v_mul_f32_e64 v214, v60, v204
	v_pk_fma_f32 v[210:211], v[60:61], v[194:195], v[210:211] op_sel:[1,0,0]
	v_pk_fma_f32 v[212:213], v[60:61], v[200:201], v[212:213] op_sel:[1,0,0]
	v_fma_f32 v214, v61, v206, v214
	v_pk_fma_f32 v[210:211], v[62:63], v[196:197], v[210:211] op_sel_hi:[0,1,1]
	v_pk_fma_f32 v[212:213], v[62:63], v[202:203], v[212:213] op_sel_hi:[0,1,1]
	v_fma_f32 v214, v62, v208, v214
	v_pk_fma_f32 v[210:211], v[84:85], v[72:73], v[210:211] op_sel:[1,0,0] neg_lo:[0,0,1] neg_hi:[0,0,1]
	v_pk_fma_f32 v[212:213], v[84:85], v[104:105], v[212:213] op_sel:[1,0,0] neg_lo:[0,0,1] neg_hi:[0,0,1]
	v_fma_f32 v214, v85, v174, -v214
	v_cmp_eq_u32_e64 s[10:11], 1, v87
	v_cmp_eq_u32_e64 s[14:15], 2, v87
	v_cmp_eq_u32_e64 s[20:21], 3, v87
	v_cmp_eq_u32_e64 s[22:23], 4, v87
	v_cmp_eq_u32_e64 s[30:31], 5, v87
	v_add_f32_dpp v72, v172, v172 wave_shr:1 row_mask:0xf bank_mask:0xf bound_ctrl:1
	v_add_f32_dpp v73, v173, v173 wave_shr:1 row_mask:0xf bank_mask:0xf bound_ctrl:1
	v_add_f32_dpp v104, v198, v198 wave_shr:1 row_mask:0xf bank_mask:0xf bound_ctrl:1
	v_add_f32_dpp v105, v199, v199 wave_shr:1 row_mask:0xf bank_mask:0xf bound_ctrl:1
	v_add_f32_dpp v174, v204, v204 wave_shr:1 row_mask:0xf bank_mask:0xf bound_ctrl:1
	v_add_f32_dpp v176, v194, v194 wave_shr:1 row_mask:0xf bank_mask:0xf bound_ctrl:1
	v_add_f32_dpp v177, v195, v195 wave_shr:1 row_mask:0xf bank_mask:0xf bound_ctrl:1
	v_add_f32_dpp v178, v200, v200 wave_shr:1 row_mask:0xf bank_mask:0xf bound_ctrl:1
	v_add_f32_dpp v179, v201, v201 wave_shr:1 row_mask:0xf bank_mask:0xf bound_ctrl:1
	v_add_f32_dpp v180, v206, v206 wave_shr:1 row_mask:0xf bank_mask:0xf bound_ctrl:1
	v_add_f32_dpp v182, v196, v196 wave_shr:1 row_mask:0xf bank_mask:0xf bound_ctrl:1
	v_add_f32_dpp v183, v197, v197 wave_shr:1 row_mask:0xf bank_mask:0xf bound_ctrl:1
	v_add_f32_dpp v184, v202, v202 wave_shr:1 row_mask:0xf bank_mask:0xf bound_ctrl:1
	v_add_f32_dpp v185, v203, v203 wave_shr:1 row_mask:0xf bank_mask:0xf bound_ctrl:1
	v_add_f32_dpp v186, v208, v208 wave_shr:1 row_mask:0xf bank_mask:0xf bound_ctrl:1
	v_add_f32_dpp v188, v210, v210 wave_shr:1 row_mask:0xf bank_mask:0xf bound_ctrl:1
	v_add_f32_dpp v189, v211, v211 wave_shr:1 row_mask:0xf bank_mask:0xf bound_ctrl:1
	v_add_f32_dpp v190, v212, v212 wave_shr:1 row_mask:0xf bank_mask:0xf bound_ctrl:1
	v_add_f32_dpp v191, v213, v213 wave_shr:1 row_mask:0xf bank_mask:0xf bound_ctrl:1
	v_add_f32_dpp v192, v214, v214 wave_shr:1 row_mask:0xf bank_mask:0xf bound_ctrl:1
	v_add_f32_dpp v72, v172, v72 wave_shl:1 row_mask:0xf bank_mask:0xf bound_ctrl:1
	v_add_f32_dpp v73, v173, v73 wave_shl:1 row_mask:0xf bank_mask:0xf bound_ctrl:1
	v_add_f32_dpp v104, v198, v104 wave_shl:1 row_mask:0xf bank_mask:0xf bound_ctrl:1
	v_add_f32_dpp v105, v199, v105 wave_shl:1 row_mask:0xf bank_mask:0xf bound_ctrl:1
	v_add_f32_dpp v174, v204, v174 wave_shl:1 row_mask:0xf bank_mask:0xf bound_ctrl:1
	v_add_f32_dpp v176, v194, v176 wave_shl:1 row_mask:0xf bank_mask:0xf bound_ctrl:1
	v_add_f32_dpp v177, v195, v177 wave_shl:1 row_mask:0xf bank_mask:0xf bound_ctrl:1
	v_add_f32_dpp v178, v200, v178 wave_shl:1 row_mask:0xf bank_mask:0xf bound_ctrl:1
	v_add_f32_dpp v179, v201, v179 wave_shl:1 row_mask:0xf bank_mask:0xf bound_ctrl:1
	v_add_f32_dpp v180, v206, v180 wave_shl:1 row_mask:0xf bank_mask:0xf bound_ctrl:1
	v_add_f32_dpp v182, v196, v182 wave_shl:1 row_mask:0xf bank_mask:0xf bound_ctrl:1
	v_add_f32_dpp v183, v197, v183 wave_shl:1 row_mask:0xf bank_mask:0xf bound_ctrl:1
	v_add_f32_dpp v184, v202, v184 wave_shl:1 row_mask:0xf bank_mask:0xf bound_ctrl:1
	v_add_f32_dpp v185, v203, v185 wave_shl:1 row_mask:0xf bank_mask:0xf bound_ctrl:1
	v_add_f32_dpp v186, v208, v186 wave_shl:1 row_mask:0xf bank_mask:0xf bound_ctrl:1
	v_add_f32_dpp v188, v210, v188 wave_shl:1 row_mask:0xf bank_mask:0xf bound_ctrl:1
	v_add_f32_dpp v189, v211, v189 wave_shl:1 row_mask:0xf bank_mask:0xf bound_ctrl:1
	v_add_f32_dpp v190, v212, v190 wave_shl:1 row_mask:0xf bank_mask:0xf bound_ctrl:1
	v_add_f32_dpp v191, v213, v191 wave_shl:1 row_mask:0xf bank_mask:0xf bound_ctrl:1
	v_add_f32_dpp v192, v214, v192 wave_shl:1 row_mask:0xf bank_mask:0xf bound_ctrl:1
	v_pk_add_f32 v[172:173], v[70:71], v[72:73]
	v_pk_add_f32 v[194:195], v[96:97], v[172:173]
	v_pk_add_f32 v[70:71], v[74:75], v[104:105]
	v_pk_add_f32 v[96:97], v[98:99], v[70:71]
	v_add_f32_e64 v74, v76, v174
	v_add_f32_e64 v98, v150, v74
	v_pk_add_f32 v[76:77], v[78:79], v[176:177]
	v_pk_add_f32 v[150:151], v[152:153], v[76:77]
	v_pk_add_f32 v[78:79], v[80:81], v[178:179]
	v_pk_add_f32 v[152:153], v[154:155], v[78:79]
	v_add_f32_e64 v80, v82, v180
	v_add_f32_e64 v154, v156, v80
	v_pk_add_f32 v[82:83], v[88:89], v[182:183]
	v_pk_add_f32 v[156:157], v[158:159], v[82:83]
	v_pk_add_f32 v[88:89], v[90:91], v[184:185]
	v_pk_add_f32 v[158:159], v[160:161], v[88:89]
	v_add_f32_e64 v90, v92, v186
	v_add_f32_e64 v160, v162, v90
	v_pk_add_f32 v[92:93], v[94:95], v[188:189]
	v_pk_add_f32 v[162:163], v[164:165], v[92:93]
	v_pk_add_f32 v[94:95], v[102:103], v[190:191]
	v_pk_add_f32 v[164:165], v[166:167], v[94:95]
	v_add_f32_e64 v102, v122, v192
	v_add_f32_e64 v166, v168, v102
	v_pk_fma_f32 v[162:163], v[48:49], v[194:195], v[162:163] op_sel_hi:[0,1,1]
	v_pk_fma_f32 v[164:165], v[48:49], v[96:97], v[164:165] op_sel_hi:[0,1,1]
	v_fma_f32 v166, v48, v98, v166
	v_pk_fma_f32 v[162:163], v[48:49], v[150:151], v[162:163] op_sel:[1,0,0]
	v_pk_fma_f32 v[164:165], v[48:49], v[152:153], v[164:165] op_sel:[1,0,0]
	v_fma_f32 v166, v49, v154, v166
	v_pk_fma_f32 v[162:163], v[50:51], v[156:157], v[162:163] op_sel_hi:[0,1,1]
	v_pk_fma_f32 v[164:165], v[50:51], v[158:159], v[164:165] op_sel_hi:[0,1,1]
	v_fma_f32 v166, v50, v160, v166
	v_cndmask_b32_e64 v122, 0, v1, s[10:11]
	v_cndmask_b32_e64 v123, 0, v1, s[14:15]
	v_cndmask_b32_e64 v168, 0, v1, s[20:21]
	v_cndmask_b32_e64 v169, 0, v1, s[22:23]
	v_cndmask_b32_e64 v196, 0, v1, s[30:31]
	v_pk_fma_f32 v[162:163], v[40:41], v[86:87], v[162:163] op_sel_hi:[1,0,1] neg_lo:[0,0,1] neg_hi:[0,0,1]
	v_pk_fma_f32 v[164:165], v[42:43], v[86:87], v[164:165] op_sel_hi:[1,0,1] neg_lo:[0,0,1] neg_hi:[0,0,1]
	v_fma_f32 v166, v44, v86, -v166
	s_add_i32 s4, s34, 6
	s_cmpk_lt_i32 s4, 0x201
	s_cselect_b64 s[12:13], s[0:1], 0
	v_pk_add_f32 v[162:163], v[162:163], v[122:123] neg_lo:[0,1] neg_hi:[0,1]
	v_pk_add_f32 v[164:165], v[164:165], v[168:169] neg_lo:[0,1] neg_hi:[0,1]
	v_add_f32_e64 v166, v166, -v196
	v_pk_mul_f32 v[198:199], v[162:163], v[162:163]
	v_pk_fma_f32 v[198:199], v[164:165], v[164:165], v[198:199]
	v_add_f32_e32 v198, v198, v199
	v_fma_f32 v198, v166, v166, v198
	v_cndmask_b32_e64 v199, 0, v198, s[12:13]
	v_add_f32_e32 v0, v0, v199
	s_add_i32 s4, s34, 11
	s_min_i32 s4, s4, 0x200
	s_mul_i32 s5, s4, 0x804
	s_add_i32 s5, s5, s35
	s_add_i32 s6, s5, 0x101004
	s_add_i32 s7, s5, 0x202008
	s_add_i32 s8, s5, 0x30300c
	s_add_i32 s11, s5, 0x404010
	s_mul_i32 s9, s4, 0x180c
	s_add_i32 s9, s9, s33
	buffer_load_dword v40, v28, s[16:19], s5 offen nt
	buffer_load_dword v41, v28, s[16:19], s6 offen nt
	buffer_load_dword v42, v28, s[16:19], s7 offen nt
	buffer_load_dword v43, v28, s[16:19], s8 offen nt
	buffer_load_dword v44, v28, s[16:19], s11 offen nt
	buffer_load_dwordx3 v[48:50], v27, s[24:27], s9 offen nt
	s_waitcnt vmcnt(12)
	v_pk_mul_f32 v[60:61], v[12:13], v[32:33] op_sel_hi:[1,0]
	v_pk_mul_f32 v[62:63], v[14:15], v[32:33] op_sel_hi:[1,0]
	v_mul_f32_e64 v64, v16, v32
	v_pk_mul_f32 v[66:67], v[12:13], v[32:33] op_sel:[0,1]
	v_pk_mul_f32 v[84:85], v[14:15], v[32:33] op_sel:[0,1]
	v_mul_f32_e64 v86, v16, v33
	v_pk_mul_f32 v[96:97], v[12:13], v[34:35] op_sel_hi:[1,0]
	v_pk_mul_f32 v[98:99], v[14:15], v[34:35] op_sel_hi:[1,0]
	v_mul_f32_e64 v122, v16, v34
	v_add_f32_dpp v150, v12, v12 wave_shr:1 row_mask:0xf bank_mask:0xf bound_ctrl:1
	v_add_f32_dpp v151, v13, v13 wave_shr:1 row_mask:0xf bank_mask:0xf bound_ctrl:1
	v_add_f32_dpp v152, v14, v14 wave_shr:1 row_mask:0xf bank_mask:0xf bound_ctrl:1
	v_add_f32_dpp v153, v15, v15 wave_shr:1 row_mask:0xf bank_mask:0xf bound_ctrl:1
	v_add_f32_dpp v154, v16, v16 wave_shr:1 row_mask:0xf bank_mask:0xf bound_ctrl:1
	v_add_f32_dpp v156, v60, v60 wave_shr:1 row_mask:0xf bank_mask:0xf bound_ctrl:1
	v_add_f32_dpp v157, v61, v61 wave_shr:1 row_mask:0xf bank_mask:0xf bound_ctrl:1
	v_add_f32_dpp v158, v62, v62 wave_shr:1 row_mask:0xf bank_mask:0xf bound_ctrl:1
	v_add_f32_dpp v159, v63, v63 wave_shr:1 row_mask:0xf bank_mask:0xf bound_ctrl:1
	v_add_f32_dpp v160, v64, v64 wave_shr:1 row_mask:0xf bank_mask:0xf bound_ctrl:1
	v_add_f32_dpp v162, v66, v66 wave_shr:1 row_mask:0xf bank_mask:0xf bound_ctrl:1
	v_add_f32_dpp v163, v67, v67 wave_shr:1 row_mask:0xf bank_mask:0xf bound_ctrl:1
	v_add_f32_dpp v164, v84, v84 wave_shr:1 row_mask:0xf bank_mask:0xf bound_ctrl:1
	v_add_f32_dpp v165, v85, v85 wave_shr:1 row_mask:0xf bank_mask:0xf bound_ctrl:1
	v_add_f32_dpp v166, v86, v86 wave_shr:1 row_mask:0xf bank_mask:0xf bound_ctrl:1
	v_add_f32_dpp v168, v96, v96 wave_shr:1 row_mask:0xf bank_mask:0xf bound_ctrl:1
	v_add_f32_dpp v169, v97, v97 wave_shr:1 row_mask:0xf bank_mask:0xf bound_ctrl:1
	v_add_f32_dpp v194, v98, v98 wave_shr:1 row_mask:0xf bank_mask:0xf bound_ctrl:1
	v_add_f32_dpp v195, v99, v99 wave_shr:1 row_mask:0xf bank_mask:0xf bound_ctrl:1
	v_add_f32_dpp v196, v122, v122 wave_shr:1 row_mask:0xf bank_mask:0xf bound_ctrl:1
	v_add_f32_dpp v150, v12, v150 wave_shl:1 row_mask:0xf bank_mask:0xf bound_ctrl:1
	v_add_f32_dpp v151, v13, v151 wave_shl:1 row_mask:0xf bank_mask:0xf bound_ctrl:1
	v_add_f32_dpp v152, v14, v152 wave_shl:1 row_mask:0xf bank_mask:0xf bound_ctrl:1
	v_add_f32_dpp v153, v15, v153 wave_shl:1 row_mask:0xf bank_mask:0xf bound_ctrl:1
	v_add_f32_dpp v154, v16, v154 wave_shl:1 row_mask:0xf bank_mask:0xf bound_ctrl:1
	v_add_f32_dpp v156, v60, v156 wave_shl:1 row_mask:0xf bank_mask:0xf bound_ctrl:1
	v_add_f32_dpp v157, v61, v157 wave_shl:1 row_mask:0xf bank_mask:0xf bound_ctrl:1
	v_add_f32_dpp v158, v62, v158 wave_shl:1 row_mask:0xf bank_mask:0xf bound_ctrl:1
	v_add_f32_dpp v159, v63, v159 wave_shl:1 row_mask:0xf bank_mask:0xf bound_ctrl:1
	v_add_f32_dpp v160, v64, v160 wave_shl:1 row_mask:0xf bank_mask:0xf bound_ctrl:1
	v_add_f32_dpp v162, v66, v162 wave_shl:1 row_mask:0xf bank_mask:0xf bound_ctrl:1
	v_add_f32_dpp v163, v67, v163 wave_shl:1 row_mask:0xf bank_mask:0xf bound_ctrl:1
	v_add_f32_dpp v164, v84, v164 wave_shl:1 row_mask:0xf bank_mask:0xf bound_ctrl:1
	v_add_f32_dpp v165, v85, v165 wave_shl:1 row_mask:0xf bank_mask:0xf bound_ctrl:1
	v_add_f32_dpp v166, v86, v166 wave_shl:1 row_mask:0xf bank_mask:0xf bound_ctrl:1
	v_add_f32_dpp v168, v96, v168 wave_shl:1 row_mask:0xf bank_mask:0xf bound_ctrl:1
	v_add_f32_dpp v169, v97, v169 wave_shl:1 row_mask:0xf bank_mask:0xf bound_ctrl:1
	v_add_f32_dpp v194, v98, v194 wave_shl:1 row_mask:0xf bank_mask:0xf bound_ctrl:1
	v_add_f32_dpp v195, v99, v195 wave_shl:1 row_mask:0xf bank_mask:0xf bound_ctrl:1
	v_add_f32_dpp v196, v122, v196 wave_shl:1 row_mask:0xf bank_mask:0xf bound_ctrl:1
	s_barrier
	ds_read_b128 v[60:63], v23 offset:3072
	ds_read_b128 v[64:67], v23 offset:4096
	ds_read_b128 v[84:87], v23 offset:5120
	v_pk_add_f32 v[96:97], v[68:69], v[150:151]
	v_pk_add_f32 v[68:69], v[100:101], v[152:153]
	v_add_f32_e64 v98, v124, v154
	v_pk_add_f32 v[100:101], v[126:127], v[156:157]
	v_pk_add_f32 v[122:123], v[128:129], v[158:159]
	v_add_f32_e64 v124, v130, v160
	v_pk_add_f32 v[126:127], v[132:133], v[162:163]
	v_pk_add_f32 v[128:129], v[134:135], v[164:165]
	v_add_f32_e64 v130, v136, v166
	v_pk_add_f32 v[132:133], v[138:139], v[168:169]
	v_pk_add_f32 v[134:135], v[140:141], v[194:195]
	v_add_f32_e64 v136, v170, v196
	s_waitcnt lgkmcnt(2)
	v_pk_fma_f32 v[100:101], v[60:61], v[96:97], v[100:101] op_sel_hi:[0,1,1] neg_lo:[1,0,0] neg_hi:[1,0,0]
	v_pk_fma_f32 v[122:123], v[60:61], v[68:69], v[122:123] op_sel_hi:[0,1,1] neg_lo:[1,0,0] neg_hi:[1,0,0]
	v_fma_f32 v124, -v60, v98, v124
	v_pk_fma_f32 v[126:127], v[60:61], v[96:97], v[126:127] op_sel:[1,0,0] neg_lo:[1,0,0] neg_hi:[1,0,0]
	v_pk_fma_f32 v[128:129], v[60:61], v[68:69], v[128:129] op_sel:[1,0,0] neg_lo:[1,0,0] neg_hi:[1,0,0]
	v_fma_f32 v130, -v61, v98, v130
	v_pk_fma_f32 v[132:133], v[62:63], v[96:97], v[132:133] op_sel_hi:[0,1,1] neg_lo:[1,0,0] neg_hi:[1,0,0]
	v_pk_fma_f32 v[134:135], v[62:63], v[68:69], v[134:135] op_sel_hi:[0,1,1] neg_lo:[1,0,0] neg_hi:[1,0,0]
	v_fma_f32 v136, -v62, v98, v136
	v_pk_mul_f32 v[138:139], v[62:63], v[100:101] op_sel:[1,0]
	v_pk_mul_f32 v[198:199], v[62:63], v[122:123] op_sel:[1,0]
	v_mul_f32_e64 v204, v63, v124
	s_waitcnt lgkmcnt(1)
	v_pk_mul_f32 v[140:141], v[64:65], v[100:101] op_sel_hi:[0,1]
	v_pk_mul_f32 v[200:201], v[64:65], v[122:123] op_sel_hi:[0,1]
	v_mul_f32_e64 v206, v64, v124
	v_pk_mul_f32 v[170:171], v[64:65], v[100:101] op_sel:[1,0]
	v_pk_mul_f32 v[202:203], v[64:65], v[122:123] op_sel:[1,0]
	v_mul_f32_e64 v208, v65, v124
	v_pk_fma_f32 v[138:139], v[64:65], v[126:127], v[138:139] op_sel_hi:[0,1,1]
	v_pk_fma_f32 v[198:199], v[64:65], v[128:129], v[198:199] op_sel_hi:[0,1,1]
	v_fma_f32 v204, v64, v130, v204
	v_pk_fma_f32 v[140:141], v[66:67], v[126:127], v[140:141] op_sel_hi:[0,1,1]
	v_pk_fma_f32 v[200:201], v[66:67], v[128:129], v[200:201] op_sel_hi:[0,1,1]
	v_fma_f32 v206, v66, v130, v206
	v_pk_fma_f32 v[170:171], v[66:67], v[126:127], v[170:171] op_sel:[1,0,0]
	v_pk_fma_f32 v[202:203], v[66:67], v[128:129], v[202:203] op_sel:[1,0,0]
	v_fma_f32 v208, v67, v130, v208
	v_pk_fma_f32 v[138:139], v[64:65], v[132:133], v[138:139] op_sel:[1,0,0]
	v_pk_fma_f32 v[198:199], v[64:65], v[134:135], v[198:199] op_sel:[1,0,0]
	v_fma_f32 v204, v65, v136, v204
	v_pk_fma_f32 v[140:141], v[66:67], v[132:133], v[140:141] op_sel:[1,0,0]
	v_pk_fma_f32 v[200:201], v[66:67], v[134:135], v[200:201] op_sel:[1,0,0]
	v_fma_f32 v206, v67, v136, v206
	s_waitcnt lgkmcnt(0)
	v_pk_fma_f32 v[170:171], v[84:85], v[132:133], v[170:171] op_sel_hi:[0,1,1]
	v_pk_fma_f32 v[202:203], v[84:85], v[134:135], v[202:203] op_sel_hi:[0,1,1]
	v_fma_f32 v208, v84, v136, v208
	v_pk_mul_f32 v[210:211], v[60:61], v[138:139] op_sel_hi:[0,1]
	v_pk_mul_f32 v[212:213], v[60:61], v[198:199] op_sel_hi:[0,1]
	v_mul_f32_e64 v214, v60, v204
	v_pk_fma_f32 v[210:211], v[60:61], v[140:141], v[210:211] op_sel:[1,0,0]
	v_pk_fma_f32 v[212:213], v[60:61], v[200:201], v[212:213] op_sel:[1,0,0]
	v_fma_f32 v214, v61, v206, v214
	v_pk_fma_f32 v[210:211], v[62:63], v[170:171], v[210:211] op_sel_hi:[0,1,1]
	v_pk_fma_f32 v[212:213], v[62:63], v[202:203], v[212:213] op_sel_hi:[0,1,1]
	v_fma_f32 v214, v62, v208, v214
	v_pk_fma_f32 v[210:211], v[84:85], v[96:97], v[210:211] op_sel:[1,0,0] neg_lo:[0,0,1] neg_hi:[0,0,1]
	v_pk_fma_f32 v[212:213], v[84:85], v[68:69], v[212:213] op_sel:[1,0,0] neg_lo:[0,0,1] neg_hi:[0,0,1]
	v_fma_f32 v214, v85, v98, -v214
	v_cmp_eq_u32_e64 s[10:11], 1, v87
	v_cmp_eq_u32_e64 s[14:15], 2, v87
	v_cmp_eq_u32_e64 s[20:21], 3, v87
	v_cmp_eq_u32_e64 s[22:23], 4, v87
	v_cmp_eq_u32_e64 s[30:31], 5, v87
	v_add_f32_dpp v68, v138, v138 wave_shr:1 row_mask:0xf bank_mask:0xf bound_ctrl:1
	v_add_f32_dpp v69, v139, v139 wave_shr:1 row_mask:0xf bank_mask:0xf bound_ctrl:1
	v_add_f32_dpp v96, v198, v198 wave_shr:1 row_mask:0xf bank_mask:0xf bound_ctrl:1
	v_add_f32_dpp v97, v199, v199 wave_shr:1 row_mask:0xf bank_mask:0xf bound_ctrl:1
	v_add_f32_dpp v98, v204, v204 wave_shr:1 row_mask:0xf bank_mask:0xf bound_ctrl:1
	v_add_f32_dpp v100, v140, v140 wave_shr:1 row_mask:0xf bank_mask:0xf bound_ctrl:1
	v_add_f32_dpp v101, v141, v141 wave_shr:1 row_mask:0xf bank_mask:0xf bound_ctrl:1
	v_add_f32_dpp v122, v200, v200 wave_shr:1 row_mask:0xf bank_mask:0xf bound_ctrl:1
	v_add_f32_dpp v123, v201, v201 wave_shr:1 row_mask:0xf bank_mask:0xf bound_ctrl:1
	v_add_f32_dpp v124, v206, v206 wave_shr:1 row_mask:0xf bank_mask:0xf bound_ctrl:1
	v_add_f32_dpp v126, v170, v170 wave_shr:1 row_mask:0xf bank_mask:0xf bound_ctrl:1
	v_add_f32_dpp v127, v171, v171 wave_shr:1 row_mask:0xf bank_mask:0xf bound_ctrl:1
	v_add_f32_dpp v128, v202, v202 wave_shr:1 row_mask:0xf bank_mask:0xf bound_ctrl:1
	v_add_f32_dpp v129, v203, v203 wave_shr:1 row_mask:0xf bank_mask:0xf bound_ctrl:1
	v_add_f32_dpp v130, v208, v208 wave_shr:1 row_mask:0xf bank_mask:0xf bound_ctrl:1
	v_add_f32_dpp v132, v210, v210 wave_shr:1 row_mask:0xf bank_mask:0xf bound_ctrl:1
	v_add_f32_dpp v133, v211, v211 wave_shr:1 row_mask:0xf bank_mask:0xf bound_ctrl:1
	v_add_f32_dpp v134, v212, v212 wave_shr:1 row_mask:0xf bank_mask:0xf bound_ctrl:1
	v_add_f32_dpp v135, v213, v213 wave_shr:1 row_mask:0xf bank_mask:0xf bound_ctrl:1
	v_add_f32_dpp v136, v214, v214 wave_shr:1 row_mask:0xf bank_mask:0xf bound_ctrl:1
	v_add_f32_dpp v68, v138, v68 wave_shl:1 row_mask:0xf bank_mask:0xf bound_ctrl:1
	v_add_f32_dpp v69, v139, v69 wave_shl:1 row_mask:0xf bank_mask:0xf bound_ctrl:1
	v_add_f32_dpp v96, v198, v96 wave_shl:1 row_mask:0xf bank_mask:0xf bound_ctrl:1
	v_add_f32_dpp v97, v199, v97 wave_shl:1 row_mask:0xf bank_mask:0xf bound_ctrl:1
	v_add_f32_dpp v98, v204, v98 wave_shl:1 row_mask:0xf bank_mask:0xf bound_ctrl:1
	v_add_f32_dpp v100, v140, v100 wave_shl:1 row_mask:0xf bank_mask:0xf bound_ctrl:1
	v_add_f32_dpp v101, v141, v101 wave_shl:1 row_mask:0xf bank_mask:0xf bound_ctrl:1
	v_add_f32_dpp v122, v200, v122 wave_shl:1 row_mask:0xf bank_mask:0xf bound_ctrl:1
	v_add_f32_dpp v123, v201, v123 wave_shl:1 row_mask:0xf bank_mask:0xf bound_ctrl:1
	v_add_f32_dpp v124, v206, v124 wave_shl:1 row_mask:0xf bank_mask:0xf bound_ctrl:1
	v_add_f32_dpp v126, v170, v126 wave_shl:1 row_mask:0xf bank_mask:0xf bound_ctrl:1
	v_add_f32_dpp v127, v171, v127 wave_shl:1 row_mask:0xf bank_mask:0xf bound_ctrl:1
	v_add_f32_dpp v128, v202, v128 wave_shl:1 row_mask:0xf bank_mask:0xf bound_ctrl:1
	v_add_f32_dpp v129, v203, v129 wave_shl:1 row_mask:0xf bank_mask:0xf bound_ctrl:1
	v_add_f32_dpp v130, v208, v130 wave_shl:1 row_mask:0xf bank_mask:0xf bound_ctrl:1
	v_add_f32_dpp v132, v210, v132 wave_shl:1 row_mask:0xf bank_mask:0xf bound_ctrl:1
	v_add_f32_dpp v133, v211, v133 wave_shl:1 row_mask:0xf bank_mask:0xf bound_ctrl:1
	v_add_f32_dpp v134, v212, v134 wave_shl:1 row_mask:0xf bank_mask:0xf bound_ctrl:1
	v_add_f32_dpp v135, v213, v135 wave_shl:1 row_mask:0xf bank_mask:0xf bound_ctrl:1
	v_add_f32_dpp v136, v214, v136 wave_shl:1 row_mask:0xf bank_mask:0xf bound_ctrl:1
	v_pk_add_f32 v[138:139], v[172:173], v[68:69]
	v_pk_add_f32 v[140:141], v[70:71], v[96:97]
	v_add_f32_e64 v70, v74, v98
	v_pk_add_f32 v[74:75], v[76:77], v[100:101]
	v_pk_add_f32 v[76:77], v[78:79], v[122:123]
	v_add_f32_e64 v78, v80, v124
	v_pk_add_f32 v[80:81], v[82:83], v[126:127]
	v_pk_add_f32 v[82:83], v[88:89], v[128:129]
	v_add_f32_e64 v88, v90, v130
	v_pk_add_f32 v[90:91], v[92:93], v[132:133]
	v_pk_add_f32 v[92:93], v[94:95], v[134:135]
	v_add_f32_e64 v94, v102, v136
	v_pk_fma_f32 v[90:91], v[56:57], v[138:139], v[90:91] op_sel_hi:[0,1,1]
	v_pk_fma_f32 v[92:93], v[56:57], v[140:141], v[92:93] op_sel_hi:[0,1,1]
	v_fma_f32 v94, v56, v70, v94
	v_pk_fma_f32 v[90:91], v[56:57], v[74:75], v[90:91] op_sel:[1,0,0]
	v_pk_fma_f32 v[92:93], v[56:57], v[76:77], v[92:93] op_sel:[1,0,0]
	v_fma_f32 v94, v57, v78, v94
	v_pk_fma_f32 v[90:91], v[58:59], v[80:81], v[90:91] op_sel_hi:[0,1,1]
	v_pk_fma_f32 v[92:93], v[58:59], v[82:83], v[92:93] op_sel_hi:[0,1,1]
	v_fma_f32 v94, v58, v88, v94
	v_cndmask_b32_e64 v102, 0, v1, s[10:11]
	v_cndmask_b32_e64 v103, 0, v1, s[14:15]
	v_cndmask_b32_e64 v170, 0, v1, s[20:21]
	v_cndmask_b32_e64 v171, 0, v1, s[22:23]
	v_cndmask_b32_e64 v172, 0, v1, s[30:31]
	v_pk_fma_f32 v[90:91], v[46:47], v[86:87], v[90:91] op_sel_hi:[1,0,1] neg_lo:[0,0,1] neg_hi:[0,0,1]
	v_pk_fma_f32 v[92:93], v[52:53], v[86:87], v[92:93] op_sel_hi:[1,0,1] neg_lo:[0,0,1] neg_hi:[0,0,1]
	v_fma_f32 v94, v54, v86, -v94
	s_add_i32 s4, s34, 7
	s_cmpk_lt_i32 s4, 0x201
	s_cselect_b64 s[12:13], s[0:1], 0
	v_pk_add_f32 v[90:91], v[90:91], v[102:103] neg_lo:[0,1] neg_hi:[0,1]
	v_pk_add_f32 v[92:93], v[92:93], v[170:171] neg_lo:[0,1] neg_hi:[0,1]
	v_add_f32_e64 v94, v94, -v172
	v_pk_mul_f32 v[198:199], v[90:91], v[90:91]
	v_pk_fma_f32 v[198:199], v[92:93], v[92:93], v[198:199]
	v_add_f32_e32 v198, v198, v199
	v_fma_f32 v198, v94, v94, v198
	v_cndmask_b32_e64 v199, 0, v198, s[12:13]
	v_add_f32_e32 v0, v0, v199
	s_waitcnt vmcnt(6)
	v_pk_mul_f32 v[46:47], v[20:21], v[36:37] op_sel_hi:[1,0]
	v_pk_mul_f32 v[52:53], v[24:25], v[36:37] op_sel_hi:[1,0]
	v_mul_f32_e64 v54, v30, v36
	v_pk_mul_f32 v[56:57], v[20:21], v[36:37] op_sel:[0,1]
	v_pk_mul_f32 v[58:59], v[24:25], v[36:37] op_sel:[0,1]
	v_mul_f32_e64 v60, v30, v37
	v_pk_mul_f32 v[62:63], v[20:21], v[38:39] op_sel_hi:[1,0]
	v_pk_mul_f32 v[64:65], v[24:25], v[38:39] op_sel_hi:[1,0]
	v_mul_f32_e64 v66, v30, v38
	v_add_f32_dpp v70, v20, v20 wave_shr:1 row_mask:0xf bank_mask:0xf bound_ctrl:1
	v_add_f32_dpp v71, v21, v21 wave_shr:1 row_mask:0xf bank_mask:0xf bound_ctrl:1
	v_add_f32_dpp v74, v24, v24 wave_shr:1 row_mask:0xf bank_mask:0xf bound_ctrl:1
	v_add_f32_dpp v75, v25, v25 wave_shr:1 row_mask:0xf bank_mask:0xf bound_ctrl:1
	v_add_f32_dpp v76, v30, v30 wave_shr:1 row_mask:0xf bank_mask:0xf bound_ctrl:1
	v_add_f32_dpp v78, v46, v46 wave_shr:1 row_mask:0xf bank_mask:0xf bound_ctrl:1
	v_add_f32_dpp v79, v47, v47 wave_shr:1 row_mask:0xf bank_mask:0xf bound_ctrl:1
	v_add_f32_dpp v80, v52, v52 wave_shr:1 row_mask:0xf bank_mask:0xf bound_ctrl:1
	v_add_f32_dpp v81, v53, v53 wave_shr:1 row_mask:0xf bank_mask:0xf bound_ctrl:1
	v_add_f32_dpp v82, v54, v54 wave_shr:1 row_mask:0xf bank_mask:0xf bound_ctrl:1
	v_add_f32_dpp v84, v56, v56 wave_shr:1 row_mask:0xf bank_mask:0xf bound_ctrl:1
	v_add_f32_dpp v85, v57, v57 wave_shr:1 row_mask:0xf bank_mask:0xf bound_ctrl:1
	v_add_f32_dpp v86, v58, v58 wave_shr:1 row_mask:0xf bank_mask:0xf bound_ctrl:1
	v_add_f32_dpp v87, v59, v59 wave_shr:1 row_mask:0xf bank_mask:0xf bound_ctrl:1
	v_add_f32_dpp v88, v60, v60 wave_shr:1 row_mask:0xf bank_mask:0xf bound_ctrl:1
	v_add_f32_dpp v90, v62, v62 wave_shr:1 row_mask:0xf bank_mask:0xf bound_ctrl:1
	v_add_f32_dpp v91, v63, v63 wave_shr:1 row_mask:0xf bank_mask:0xf bound_ctrl:1
	v_add_f32_dpp v92, v64, v64 wave_shr:1 row_mask:0xf bank_mask:0xf bound_ctrl:1
	v_add_f32_dpp v93, v65, v65 wave_shr:1 row_mask:0xf bank_mask:0xf bound_ctrl:1
	v_add_f32_dpp v94, v66, v66 wave_shr:1 row_mask:0xf bank_mask:0xf bound_ctrl:1
	v_add_f32_dpp v70, v20, v70 wave_shl:1 row_mask:0xf bank_mask:0xf bound_ctrl:1
	v_add_f32_dpp v71, v21, v71 wave_shl:1 row_mask:0xf bank_mask:0xf bound_ctrl:1
	v_add_f32_dpp v74, v24, v74 wave_shl:1 row_mask:0xf bank_mask:0xf bound_ctrl:1
	v_add_f32_dpp v75, v25, v75 wave_shl:1 row_mask:0xf bank_mask:0xf bound_ctrl:1
	v_add_f32_dpp v76, v30, v76 wave_shl:1 row_mask:0xf bank_mask:0xf bound_ctrl:1
	v_add_f32_dpp v78, v46, v78 wave_shl:1 row_mask:0xf bank_mask:0xf bound_ctrl:1
	v_add_f32_dpp v79, v47, v79 wave_shl:1 row_mask:0xf bank_mask:0xf bound_ctrl:1
	v_add_f32_dpp v80, v52, v80 wave_shl:1 row_mask:0xf bank_mask:0xf bound_ctrl:1
	v_add_f32_dpp v81, v53, v81 wave_shl:1 row_mask:0xf bank_mask:0xf bound_ctrl:1
	v_add_f32_dpp v82, v54, v82 wave_shl:1 row_mask:0xf bank_mask:0xf bound_ctrl:1
	v_add_f32_dpp v84, v56, v84 wave_shl:1 row_mask:0xf bank_mask:0xf bound_ctrl:1
	v_add_f32_dpp v85, v57, v85 wave_shl:1 row_mask:0xf bank_mask:0xf bound_ctrl:1
	v_add_f32_dpp v86, v58, v86 wave_shl:1 row_mask:0xf bank_mask:0xf bound_ctrl:1
	v_add_f32_dpp v87, v59, v87 wave_shl:1 row_mask:0xf bank_mask:0xf bound_ctrl:1
	v_add_f32_dpp v88, v60, v88 wave_shl:1 row_mask:0xf bank_mask:0xf bound_ctrl:1
	v_add_f32_dpp v90, v62, v90 wave_shl:1 row_mask:0xf bank_mask:0xf bound_ctrl:1
	v_add_f32_dpp v91, v63, v91 wave_shl:1 row_mask:0xf bank_mask:0xf bound_ctrl:1
	v_add_f32_dpp v92, v64, v92 wave_shl:1 row_mask:0xf bank_mask:0xf bound_ctrl:1
	v_add_f32_dpp v93, v65, v93 wave_shl:1 row_mask:0xf bank_mask:0xf bound_ctrl:1
	v_add_f32_dpp v94, v66, v94 wave_shl:1 row_mask:0xf bank_mask:0xf bound_ctrl:1
	s_barrier
	ds_read_b128 v[52:55], v23 offset:0
	ds_read_b128 v[56:59], v23 offset:1024
	ds_read_b128 v[60:63], v23 offset:2048
	v_pk_add_f32 v[46:47], v[150:151], v[70:71]
	v_pk_add_f32 v[64:65], v[106:107], v[46:47]
	v_pk_add_f32 v[66:67], v[152:153], v[74:75]
	v_pk_add_f32 v[102:103], v[108:109], v[66:67]
	v_add_f32_e64 v106, v154, v76
	v_add_f32_e64 v108, v110, v106
	v_pk_add_f32 v[110:111], v[156:157], v[78:79]
	v_pk_add_f32 v[138:139], v[112:113], v[110:111]
	v_pk_add_f32 v[112:113], v[158:159], v[80:81]
	v_pk_add_f32 v[140:141], v[114:115], v[112:113]
	v_add_f32_e64 v114, v160, v82
	v_add_f32_e64 v150, v116, v114
	v_pk_add_f32 v[116:117], v[162:163], v[84:85]
	v_pk_add_f32 v[152:153], v[118:119], v[116:117]
	v_pk_add_f32 v[118:119], v[164:165], v[86:87]
	v_pk_add_f32 v[154:155], v[120:121], v[118:119]
	v_add_f32_e64 v120, v166, v88
	v_add_f32_e64 v156, v142, v120
	v_pk_add_f32 v[142:143], v[168:169], v[90:91]
	v_pk_add_f32 v[158:159], v[144:145], v[142:143]
	v_pk_add_f32 v[144:145], v[194:195], v[92:93]
	v_pk_add_f32 v[160:161], v[146:147], v[144:145]
	v_add_f32_e64 v146, v196, v94
	v_add_f32_e64 v162, v148, v146
	s_waitcnt lgkmcnt(2)
	v_pk_fma_f32 v[138:139], v[52:53], v[64:65], v[138:139] op_sel_hi:[0,1,1] neg_lo:[1,0,0] neg_hi:[1,0,0]
	v_pk_fma_f32 v[140:141], v[52:53], v[102:103], v[140:141] op_sel_hi:[0,1,1] neg_lo:[1,0,0] neg_hi:[1,0,0]
	v_fma_f32 v150, -v52, v108, v150
	v_pk_fma_f32 v[152:153], v[52:53], v[64:65], v[152:153] op_sel:[1,0,0] neg_lo:[1,0,0] neg_hi:[1,0,0]
	v_pk_fma_f32 v[154:155], v[52:53], v[102:103], v[154:155] op_sel:[1,0,0] neg_lo:[1,0,0] neg_hi:[1,0,0]
	v_fma_f32 v156, -v53, v108, v156
	v_pk_fma_f32 v[158:159], v[54:55], v[64:65], v[158:159] op_sel_hi:[0,1,1] neg_lo:[1,0,0] neg_hi:[1,0,0]
	v_pk_fma_f32 v[160:161], v[54:55], v[102:103], v[160:161] op_sel_hi:[0,1,1] neg_lo:[1,0,0] neg_hi:[1,0,0]
	v_fma_f32 v162, -v54, v108, v162
	v_pk_mul_f32 v[148:149], v[54:55], v[138:139] op_sel:[1,0]
	v_pk_mul_f32 v[168:169], v[54:55], v[140:141] op_sel:[1,0]
	v_mul_f32_e64 v194, v55, v150
	s_waitcnt lgkmcnt(1)
	v_pk_mul_f32 v[164:165], v[56:57], v[138:139] op_sel_hi:[0,1]
	v_pk_mul_f32 v[170:171], v[56:57], v[140:141] op_sel_hi:[0,1]
	v_mul_f32_e64 v196, v56, v150
	v_pk_mul_f32 v[166:167], v[56:57], v[138:139] op_sel:[1,0]
	v_pk_mul_f32 v[172:173], v[56:57], v[140:141] op_sel:[1,0]
	v_mul_f32_e64 v198, v57, v150
	v_pk_fma_f32 v[148:149], v[56:57], v[152:153], v[148:149] op_sel_hi:[0,1,1]
	v_pk_fma_f32 v[168:169], v[56:57], v[154:155], v[168:169] op_sel_hi:[0,1,1]
	v_fma_f32 v194, v56, v156, v194
	v_pk_fma_f32 v[164:165], v[58:59], v[152:153], v[164:165] op_sel_hi:[0,1,1]
	v_pk_fma_f32 v[170:171], v[58:59], v[154:155], v[170:171] op_sel_hi:[0,1,1]
	v_fma_f32 v196, v58, v156, v196
	v_pk_fma_f32 v[166:167], v[58:59], v[152:153], v[166:167] op_sel:[1,0,0]
	v_pk_fma_f32 v[172:173], v[58:59], v[154:155], v[172:173] op_sel:[1,0,0]
	v_fma_f32 v198, v59, v156, v198
	v_pk_fma_f32 v[148:149], v[56:57], v[158:159], v[148:149] op_sel:[1,0,0]
	v_pk_fma_f32 v[168:169], v[56:57], v[160:161], v[168:169] op_sel:[1,0,0]
	v_fma_f32 v194, v57, v162, v194
	v_pk_fma_f32 v[164:165], v[58:59], v[158:159], v[164:165] op_sel:[1,0,0]
	v_pk_fma_f32 v[170:171], v[58:59], v[160:161], v[170:171] op_sel:[1,0,0]
	v_fma_f32 v196, v59, v162, v196
	s_waitcnt lgkmcnt(0)
	v_pk_fma_f32 v[166:167], v[60:61], v[158:159], v[166:167] op_sel_hi:[0,1,1]
	v_pk_fma_f32 v[172:173], v[60:61], v[160:161], v[172:173] op_sel_hi:[0,1,1]
	v_fma_f32 v198, v60, v162, v198
	v_pk_mul_f32 v[200:201], v[52:53], v[148:149] op_sel_hi:[0,1]
	v_pk_mul_f32 v[202:203], v[52:53], v[168:169] op_sel_hi:[0,1]
	v_mul_f32_e64 v204, v52, v194
	v_pk_fma_f32 v[200:201], v[52:53], v[164:165], v[200:201] op_sel:[1,0,0]
	v_pk_fma_f32 v[202:203], v[52:53], v[170:171], v[202:203] op_sel:[1,0,0]
	v_fma_f32 v204, v53, v196, v204
	v_pk_fma_f32 v[200:201], v[54:55], v[166:167], v[200:201] op_sel_hi:[0,1,1]
	v_pk_fma_f32 v[202:203], v[54:55], v[172:173], v[202:203] op_sel_hi:[0,1,1]
	v_fma_f32 v204, v54, v198, v204
	v_pk_fma_f32 v[200:201], v[60:61], v[64:65], v[200:201] op_sel:[1,0,0] neg_lo:[0,0,1] neg_hi:[0,0,1]
	v_pk_fma_f32 v[202:203], v[60:61], v[102:103], v[202:203] op_sel:[1,0,0] neg_lo:[0,0,1] neg_hi:[0,0,1]
	v_fma_f32 v204, v61, v108, -v204
	v_cmp_eq_u32_e64 s[10:11], 1, v63
	v_cmp_eq_u32_e64 s[14:15], 2, v63
	v_cmp_eq_u32_e64 s[20:21], 3, v63
	v_cmp_eq_u32_e64 s[22:23], 4, v63
	v_cmp_eq_u32_e64 s[30:31], 5, v63
	v_add_f32_dpp v64, v148, v148 wave_shr:1 row_mask:0xf bank_mask:0xf bound_ctrl:1
	v_add_f32_dpp v65, v149, v149 wave_shr:1 row_mask:0xf bank_mask:0xf bound_ctrl:1
	v_add_f32_dpp v102, v168, v168 wave_shr:1 row_mask:0xf bank_mask:0xf bound_ctrl:1
	v_add_f32_dpp v103, v169, v169 wave_shr:1 row_mask:0xf bank_mask:0xf bound_ctrl:1
	v_add_f32_dpp v108, v194, v194 wave_shr:1 row_mask:0xf bank_mask:0xf bound_ctrl:1
	v_add_f32_dpp v138, v164, v164 wave_shr:1 row_mask:0xf bank_mask:0xf bound_ctrl:1
	v_add_f32_dpp v139, v165, v165 wave_shr:1 row_mask:0xf bank_mask:0xf bound_ctrl:1
	v_add_f32_dpp v140, v170, v170 wave_shr:1 row_mask:0xf bank_mask:0xf bound_ctrl:1
	v_add_f32_dpp v141, v171, v171 wave_shr:1 row_mask:0xf bank_mask:0xf bound_ctrl:1
	v_add_f32_dpp v150, v196, v196 wave_shr:1 row_mask:0xf bank_mask:0xf bound_ctrl:1
	v_add_f32_dpp v152, v166, v166 wave_shr:1 row_mask:0xf bank_mask:0xf bound_ctrl:1
	v_add_f32_dpp v153, v167, v167 wave_shr:1 row_mask:0xf bank_mask:0xf bound_ctrl:1
	v_add_f32_dpp v154, v172, v172 wave_shr:1 row_mask:0xf bank_mask:0xf bound_ctrl:1
	v_add_f32_dpp v155, v173, v173 wave_shr:1 row_mask:0xf bank_mask:0xf bound_ctrl:1
	v_add_f32_dpp v156, v198, v198 wave_shr:1 row_mask:0xf bank_mask:0xf bound_ctrl:1
	v_add_f32_dpp v158, v200, v200 wave_shr:1 row_mask:0xf bank_mask:0xf bound_ctrl:1
	v_add_f32_dpp v159, v201, v201 wave_shr:1 row_mask:0xf bank_mask:0xf bound_ctrl:1
	v_add_f32_dpp v160, v202, v202 wave_shr:1 row_mask:0xf bank_mask:0xf bound_ctrl:1
	v_add_f32_dpp v161, v203, v203 wave_shr:1 row_mask:0xf bank_mask:0xf bound_ctrl:1
	v_add_f32_dpp v162, v204, v204 wave_shr:1 row_mask:0xf bank_mask:0xf bound_ctrl:1
	v_add_f32_dpp v64, v148, v64 wave_shl:1 row_mask:0xf bank_mask:0xf bound_ctrl:1
	v_add_f32_dpp v65, v149, v65 wave_shl:1 row_mask:0xf bank_mask:0xf bound_ctrl:1
	v_add_f32_dpp v102, v168, v102 wave_shl:1 row_mask:0xf bank_mask:0xf bound_ctrl:1
	v_add_f32_dpp v103, v169, v103 wave_shl:1 row_mask:0xf bank_mask:0xf bound_ctrl:1
	v_add_f32_dpp v108, v194, v108 wave_shl:1 row_mask:0xf bank_mask:0xf bound_ctrl:1
	v_add_f32_dpp v138, v164, v138 wave_shl:1 row_mask:0xf bank_mask:0xf bound_ctrl:1
	v_add_f32_dpp v139, v165, v139 wave_shl:1 row_mask:0xf bank_mask:0xf bound_ctrl:1
	v_add_f32_dpp v140, v170, v140 wave_shl:1 row_mask:0xf bank_mask:0xf bound_ctrl:1
	v_add_f32_dpp v141, v171, v141 wave_shl:1 row_mask:0xf bank_mask:0xf bound_ctrl:1
	v_add_f32_dpp v150, v196, v150 wave_shl:1 row_mask:0xf bank_mask:0xf bound_ctrl:1
	v_add_f32_dpp v152, v166, v152 wave_shl:1 row_mask:0xf bank_mask:0xf bound_ctrl:1
	v_add_f32_dpp v153, v167, v153 wave_shl:1 row_mask:0xf bank_mask:0xf bound_ctrl:1
	v_add_f32_dpp v154, v172, v154 wave_shl:1 row_mask:0xf bank_mask:0xf bound_ctrl:1
	v_add_f32_dpp v155, v173, v155 wave_shl:1 row_mask:0xf bank_mask:0xf bound_ctrl:1
	v_add_f32_dpp v156, v198, v156 wave_shl:1 row_mask:0xf bank_mask:0xf bound_ctrl:1
	v_add_f32_dpp v158, v200, v158 wave_shl:1 row_mask:0xf bank_mask:0xf bound_ctrl:1
	v_add_f32_dpp v159, v201, v159 wave_shl:1 row_mask:0xf bank_mask:0xf bound_ctrl:1
	v_add_f32_dpp v160, v202, v160 wave_shl:1 row_mask:0xf bank_mask:0xf bound_ctrl:1
	v_add_f32_dpp v161, v203, v161 wave_shl:1 row_mask:0xf bank_mask:0xf bound_ctrl:1
	v_add_f32_dpp v162, v204, v162 wave_shl:1 row_mask:0xf bank_mask:0xf bound_ctrl:1
	v_pk_add_f32 v[148:149], v[68:69], v[64:65]
	v_pk_add_f32 v[164:165], v[72:73], v[148:149]
	v_pk_add_f32 v[68:69], v[96:97], v[102:103]
	v_pk_add_f32 v[72:73], v[104:105], v[68:69]
	v_add_f32_e64 v96, v98, v108
	v_add_f32_e64 v104, v174, v96
	v_pk_add_f32 v[98:99], v[100:101], v[138:139]
	v_pk_add_f32 v[166:167], v[176:177], v[98:99]
	v_pk_add_f32 v[100:101], v[122:123], v[140:141]
	v_pk_add_f32 v[168:169], v[178:179], v[100:101]
	v_add_f32_e64 v122, v124, v150
	v_add_f32_e64 v170, v180, v122
	v_pk_add_f32 v[124:125], v[126:127], v[152:153]
	v_pk_add_f32 v[172:173], v[182:183], v[124:125]
	v_pk_add_f32 v[126:127], v[128:129], v[154:155]
	v_pk_add_f32 v[174:175], v[184:185], v[126:127]
	v_add_f32_e64 v128, v130, v156
	v_add_f32_e64 v176, v186, v128
	v_pk_add_f32 v[130:131], v[132:133], v[158:159]
	v_pk_add_f32 v[178:179], v[188:189], v[130:131]
	v_pk_add_f32 v[132:133], v[134:135], v[160:161]
	v_pk_add_f32 v[180:181], v[190:191], v[132:133]
	v_add_f32_e64 v134, v136, v162
	v_add_f32_e64 v182, v192, v134
	v_pk_fma_f32 v[178:179], v[8:9], v[164:165], v[178:179] op_sel_hi:[0,1,1]
	v_pk_fma_f32 v[180:181], v[8:9], v[72:73], v[180:181] op_sel_hi:[0,1,1]
	v_fma_f32 v182, v8, v104, v182
	v_pk_fma_f32 v[178:179], v[8:9], v[166:167], v[178:179] op_sel:[1,0,0]
	v_pk_fma_f32 v[180:181], v[8:9], v[168:169], v[180:181] op_sel:[1,0,0]
	v_fma_f32 v182, v9, v170, v182
	v_pk_fma_f32 v[178:179], v[10:11], v[172:173], v[178:179] op_sel_hi:[0,1,1]
	v_pk_fma_f32 v[180:181], v[10:11], v[174:175], v[180:181] op_sel_hi:[0,1,1]
	v_fma_f32 v182, v10, v176, v182
	v_cndmask_b32_e64 v136, 0, v1, s[10:11]
	v_cndmask_b32_e64 v137, 0, v1, s[14:15]
	v_cndmask_b32_e64 v184, 0, v1, s[20:21]
	v_cndmask_b32_e64 v185, 0, v1, s[22:23]
	v_cndmask_b32_e64 v186, 0, v1, s[30:31]
	v_pk_fma_f32 v[178:179], v[2:3], v[62:63], v[178:179] op_sel_hi:[1,0,1] neg_lo:[0,0,1] neg_hi:[0,0,1]
	v_pk_fma_f32 v[180:181], v[4:5], v[62:63], v[180:181] op_sel_hi:[1,0,1] neg_lo:[0,0,1] neg_hi:[0,0,1]
	v_fma_f32 v182, v6, v62, -v182
	s_add_i32 s4, s34, 8
	s_cmpk_lt_i32 s4, 0x201
	s_cselect_b64 s[12:13], s[0:1], 0
	v_pk_add_f32 v[178:179], v[178:179], v[136:137] neg_lo:[0,1] neg_hi:[0,1]
	v_pk_add_f32 v[180:181], v[180:181], v[184:185] neg_lo:[0,1] neg_hi:[0,1]
	v_add_f32_e64 v182, v182, -v186
	v_pk_mul_f32 v[188:189], v[178:179], v[178:179]
	v_pk_fma_f32 v[188:189], v[180:181], v[180:181], v[188:189]
	v_add_f32_e32 v188, v188, v189
	v_fma_f32 v188, v182, v182, v188
	v_cndmask_b32_e64 v189, 0, v188, s[12:13]
	v_add_f32_e32 v0, v0, v189
	s_waitcnt vmcnt(0)
	v_pk_mul_f32 v[2:3], v[40:41], v[48:49] op_sel_hi:[1,0]
	v_pk_mul_f32 v[4:5], v[42:43], v[48:49] op_sel_hi:[1,0]
	v_mul_f32_e64 v6, v44, v48
	v_pk_mul_f32 v[8:9], v[40:41], v[48:49] op_sel:[0,1]
	v_pk_mul_f32 v[10:11], v[42:43], v[48:49] op_sel:[0,1]
	v_mul_f32_e64 v52, v44, v49
	v_pk_mul_f32 v[54:55], v[40:41], v[50:51] op_sel_hi:[1,0]
	v_pk_mul_f32 v[56:57], v[42:43], v[50:51] op_sel_hi:[1,0]
	v_mul_f32_e64 v58, v44, v50
	v_add_f32_dpp v60, v40, v40 wave_shr:1 row_mask:0xf bank_mask:0xf bound_ctrl:1
	v_add_f32_dpp v61, v41, v41 wave_shr:1 row_mask:0xf bank_mask:0xf bound_ctrl:1
	v_add_f32_dpp v62, v42, v42 wave_shr:1 row_mask:0xf bank_mask:0xf bound_ctrl:1
	v_add_f32_dpp v63, v43, v43 wave_shr:1 row_mask:0xf bank_mask:0xf bound_ctrl:1
	v_add_f32_dpp v72, v44, v44 wave_shr:1 row_mask:0xf bank_mask:0xf bound_ctrl:1
	v_add_f32_dpp v104, v2, v2 wave_shr:1 row_mask:0xf bank_mask:0xf bound_ctrl:1
	v_add_f32_dpp v105, v3, v3 wave_shr:1 row_mask:0xf bank_mask:0xf bound_ctrl:1
	v_add_f32_dpp v136, v4, v4 wave_shr:1 row_mask:0xf bank_mask:0xf bound_ctrl:1
	v_add_f32_dpp v137, v5, v5 wave_shr:1 row_mask:0xf bank_mask:0xf bound_ctrl:1
	v_add_f32_dpp v164, v6, v6 wave_shr:1 row_mask:0xf bank_mask:0xf bound_ctrl:1
	v_add_f32_dpp v166, v8, v8 wave_shr:1 row_mask:0xf bank_mask:0xf bound_ctrl:1
	v_add_f32_dpp v167, v9, v9 wave_shr:1 row_mask:0xf bank_mask:0xf bound_ctrl:1
	v_add_f32_dpp v168, v10, v10 wave_shr:1 row_mask:0xf bank_mask:0xf bound_ctrl:1
	v_add_f32_dpp v169, v11, v11 wave_shr:1 row_mask:0xf bank_mask:0xf bound_ctrl:1
	v_add_f32_dpp v170, v52, v52 wave_shr:1 row_mask:0xf bank_mask:0xf bound_ctrl:1
	v_add_f32_dpp v172, v54, v54 wave_shr:1 row_mask:0xf bank_mask:0xf bound_ctrl:1
	v_add_f32_dpp v173, v55, v55 wave_shr:1 row_mask:0xf bank_mask:0xf bound_ctrl:1
	v_add_f32_dpp v174, v56, v56 wave_shr:1 row_mask:0xf bank_mask:0xf bound_ctrl:1
	v_add_f32_dpp v175, v57, v57 wave_shr:1 row_mask:0xf bank_mask:0xf bound_ctrl:1
	v_add_f32_dpp v176, v58, v58 wave_shr:1 row_mask:0xf bank_mask:0xf bound_ctrl:1
	v_add_f32_dpp v60, v40, v60 wave_shl:1 row_mask:0xf bank_mask:0xf bound_ctrl:1
	v_add_f32_dpp v61, v41, v61 wave_shl:1 row_mask:0xf bank_mask:0xf bound_ctrl:1
	v_add_f32_dpp v62, v42, v62 wave_shl:1 row_mask:0xf bank_mask:0xf bound_ctrl:1
	v_add_f32_dpp v63, v43, v63 wave_shl:1 row_mask:0xf bank_mask:0xf bound_ctrl:1
	v_add_f32_dpp v72, v44, v72 wave_shl:1 row_mask:0xf bank_mask:0xf bound_ctrl:1
	v_add_f32_dpp v104, v2, v104 wave_shl:1 row_mask:0xf bank_mask:0xf bound_ctrl:1
	v_add_f32_dpp v105, v3, v105 wave_shl:1 row_mask:0xf bank_mask:0xf bound_ctrl:1
	v_add_f32_dpp v136, v4, v136 wave_shl:1 row_mask:0xf bank_mask:0xf bound_ctrl:1
	v_add_f32_dpp v137, v5, v137 wave_shl:1 row_mask:0xf bank_mask:0xf bound_ctrl:1
	v_add_f32_dpp v164, v6, v164 wave_shl:1 row_mask:0xf bank_mask:0xf bound_ctrl:1
	v_add_f32_dpp v166, v8, v166 wave_shl:1 row_mask:0xf bank_mask:0xf bound_ctrl:1
	v_add_f32_dpp v167, v9, v167 wave_shl:1 row_mask:0xf bank_mask:0xf bound_ctrl:1
	v_add_f32_dpp v168, v10, v168 wave_shl:1 row_mask:0xf bank_mask:0xf bound_ctrl:1
	v_add_f32_dpp v169, v11, v169 wave_shl:1 row_mask:0xf bank_mask:0xf bound_ctrl:1
	v_add_f32_dpp v170, v52, v170 wave_shl:1 row_mask:0xf bank_mask:0xf bound_ctrl:1
	v_add_f32_dpp v172, v54, v172 wave_shl:1 row_mask:0xf bank_mask:0xf bound_ctrl:1
	v_add_f32_dpp v173, v55, v173 wave_shl:1 row_mask:0xf bank_mask:0xf bound_ctrl:1
	v_add_f32_dpp v174, v56, v174 wave_shl:1 row_mask:0xf bank_mask:0xf bound_ctrl:1
	v_add_f32_dpp v175, v57, v175 wave_shl:1 row_mask:0xf bank_mask:0xf bound_ctrl:1
	v_add_f32_dpp v176, v58, v176 wave_shl:1 row_mask:0xf bank_mask:0xf bound_ctrl:1
	s_barrier
	ds_read_b128 v[4:7], v23 offset:3072
	ds_read_b128 v[8:11], v23 offset:4096
	ds_read_b128 v[52:55], v23 offset:5120
	v_pk_add_f32 v[2:3], v[46:47], v[60:61]
	v_pk_add_f32 v[46:47], v[66:67], v[62:63]
	v_add_f32_e64 v56, v106, v72
	v_pk_add_f32 v[58:59], v[110:111], v[104:105]
	v_pk_add_f32 v[66:67], v[112:113], v[136:137]
	v_add_f32_e64 v106, v114, v164
	v_pk_add_f32 v[110:111], v[116:117], v[166:167]
	v_pk_add_f32 v[112:113], v[118:119], v[168:169]
	v_add_f32_e64 v114, v120, v170
	v_pk_add_f32 v[116:117], v[142:143], v[172:173]
	v_pk_add_f32 v[118:119], v[144:145], v[174:175]
	v_add_f32_e64 v120, v146, v176
	s_waitcnt lgkmcnt(2)
	v_pk_fma_f32 v[58:59], v[4:5], v[2:3], v[58:59] op_sel_hi:[0,1,1] neg_lo:[1,0,0] neg_hi:[1,0,0]
	v_pk_fma_f32 v[66:67], v[4:5], v[46:47], v[66:67] op_sel_hi:[0,1,1] neg_lo:[1,0,0] neg_hi:[1,0,0]
	v_fma_f32 v106, -v4, v56, v106
	v_pk_fma_f32 v[110:111], v[4:5], v[2:3], v[110:111] op_sel:[1,0,0] neg_lo:[1,0,0] neg_hi:[1,0,0]
	v_pk_fma_f32 v[112:113], v[4:5], v[46:47], v[112:113] op_sel:[1,0,0] neg_lo:[1,0,0] neg_hi:[1,0,0]
	v_fma_f32 v114, -v5, v56, v114
	v_pk_fma_f32 v[116:117], v[6:7], v[2:3], v[116:117] op_sel_hi:[0,1,1] neg_lo:[1,0,0] neg_hi:[1,0,0]
	v_pk_fma_f32 v[118:119], v[6:7], v[46:47], v[118:119] op_sel_hi:[0,1,1] neg_lo:[1,0,0] neg_hi:[1,0,0]
	v_fma_f32 v120, -v6, v56, v120
	v_pk_mul_f32 v[142:143], v[6:7], v[58:59] op_sel:[1,0]
	v_pk_mul_f32 v[178:179], v[6:7], v[66:67] op_sel:[1,0]
	v_mul_f32_e64 v184, v7, v106
	s_waitcnt lgkmcnt(1)
	v_pk_mul_f32 v[144:145], v[8:9], v[58:59] op_sel_hi:[0,1]
	v_pk_mul_f32 v[180:181], v[8:9], v[66:67] op_sel_hi:[0,1]
	v_mul_f32_e64 v186, v8, v106
	v_pk_mul_f32 v[146:147], v[8:9], v[58:59] op_sel:[1,0]
	v_pk_mul_f32 v[182:183], v[8:9], v[66:67] op_sel:[1,0]
	v_mul_f32_e64 v188, v9, v106
	v_pk_fma_f32 v[142:143], v[8:9], v[110:111], v[142:143] op_sel_hi:[0,1,1]
	v_pk_fma_f32 v[178:179], v[8:9], v[112:113], v[178:179] op_sel_hi:[0,1,1]
	v_fma_f32 v184, v8, v114, v184
	v_pk_fma_f32 v[144:145], v[10:11], v[110:111], v[144:145] op_sel_hi:[0,1,1]
	v_pk_fma_f32 v[180:181], v[10:11], v[112:113], v[180:181] op_sel_hi:[0,1,1]
	v_fma_f32 v186, v10, v114, v186
	v_pk_fma_f32 v[146:147], v[10:11], v[110:111], v[146:147] op_sel:[1,0,0]
	v_pk_fma_f32 v[182:183], v[10:11], v[112:113], v[182:183] op_sel:[1,0,0]
	v_fma_f32 v188, v11, v114, v188
	v_pk_fma_f32 v[142:143], v[8:9], v[116:117], v[142:143] op_sel:[1,0,0]
	v_pk_fma_f32 v[178:179], v[8:9], v[118:119], v[178:179] op_sel:[1,0,0]
	v_fma_f32 v184, v9, v120, v184
	v_pk_fma_f32 v[144:145], v[10:11], v[116:117], v[144:145] op_sel:[1,0,0]
	v_pk_fma_f32 v[180:181], v[10:11], v[118:119], v[180:181] op_sel:[1,0,0]
	v_fma_f32 v186, v11, v120, v186
	s_waitcnt lgkmcnt(0)
	v_pk_fma_f32 v[146:147], v[52:53], v[116:117], v[146:147] op_sel_hi:[0,1,1]
	v_pk_fma_f32 v[182:183], v[52:53], v[118:119], v[182:183] op_sel_hi:[0,1,1]
	v_fma_f32 v188, v52, v120, v188
	v_pk_mul_f32 v[190:191], v[4:5], v[142:143] op_sel_hi:[0,1]
	v_pk_mul_f32 v[192:193], v[4:5], v[178:179] op_sel_hi:[0,1]
	v_mul_f32_e64 v194, v4, v184
	v_pk_fma_f32 v[190:191], v[4:5], v[144:145], v[190:191] op_sel:[1,0,0]
	v_pk_fma_f32 v[192:193], v[4:5], v[180:181], v[192:193] op_sel:[1,0,0]
	v_fma_f32 v194, v5, v186, v194
	v_pk_fma_f32 v[190:191], v[6:7], v[146:147], v[190:191] op_sel_hi:[0,1,1]
	v_pk_fma_f32 v[192:193], v[6:7], v[182:183], v[192:193] op_sel_hi:[0,1,1]
	v_fma_f32 v194, v6, v188, v194
	v_pk_fma_f32 v[190:191], v[52:53], v[2:3], v[190:191] op_sel:[1,0,0] neg_lo:[0,0,1] neg_hi:[0,0,1]
	v_pk_fma_f32 v[192:193], v[52:53], v[46:47], v[192:193] op_sel:[1,0,0] neg_lo:[0,0,1] neg_hi:[0,0,1]
	v_fma_f32 v194, v53, v56, -v194
	v_cmp_eq_u32_e64 s[10:11], 1, v55
	v_cmp_eq_u32_e64 s[14:15], 2, v55
	v_cmp_eq_u32_e64 s[20:21], 3, v55
	v_cmp_eq_u32_e64 s[22:23], 4, v55
	v_cmp_eq_u32_e64 s[30:31], 5, v55
	v_add_f32_dpp v2, v142, v142 wave_shr:1 row_mask:0xf bank_mask:0xf bound_ctrl:1
	v_add_f32_dpp v3, v143, v143 wave_shr:1 row_mask:0xf bank_mask:0xf bound_ctrl:1
	v_add_f32_dpp v46, v178, v178 wave_shr:1 row_mask:0xf bank_mask:0xf bound_ctrl:1
	v_add_f32_dpp v47, v179, v179 wave_shr:1 row_mask:0xf bank_mask:0xf bound_ctrl:1
	v_add_f32_dpp v56, v184, v184 wave_shr:1 row_mask:0xf bank_mask:0xf bound_ctrl:1
	v_add_f32_dpp v58, v144, v144 wave_shr:1 row_mask:0xf bank_mask:0xf bound_ctrl:1
	v_add_f32_dpp v59, v145, v145 wave_shr:1 row_mask:0xf bank_mask:0xf bound_ctrl:1
	v_add_f32_dpp v66, v180, v180 wave_shr:1 row_mask:0xf bank_mask:0xf bound_ctrl:1
	v_add_f32_dpp v67, v181, v181 wave_shr:1 row_mask:0xf bank_mask:0xf bound_ctrl:1
	v_add_f32_dpp v106, v186, v186 wave_shr:1 row_mask:0xf bank_mask:0xf bound_ctrl:1
	v_add_f32_dpp v110, v146, v146 wave_shr:1 row_mask:0xf bank_mask:0xf bound_ctrl:1
	v_add_f32_dpp v111, v147, v147 wave_shr:1 row_mask:0xf bank_mask:0xf bound_ctrl:1
	v_add_f32_dpp v112, v182, v182 wave_shr:1 row_mask:0xf bank_mask:0xf bound_ctrl:1
	v_add_f32_dpp v113, v183, v183 wave_shr:1 row_mask:0xf bank_mask:0xf bound_ctrl:1
	v_add_f32_dpp v114, v188, v188 wave_shr:1 row_mask:0xf bank_mask:0xf bound_ctrl:1
	v_add_f32_dpp v116, v190, v190 wave_shr:1 row_mask:0xf bank_mask:0xf bound_ctrl:1
	v_add_f32_dpp v117, v191, v191 wave_shr:1 row_mask:0xf bank_mask:0xf bound_ctrl:1
	v_add_f32_dpp v118, v192, v192 wave_shr:1 row_mask:0xf bank_mask:0xf bound_ctrl:1
	v_add_f32_dpp v119, v193, v193 wave_shr:1 row_mask:0xf bank_mask:0xf bound_ctrl:1
	v_add_f32_dpp v120, v194, v194 wave_shr:1 row_mask:0xf bank_mask:0xf bound_ctrl:1
	v_add_f32_dpp v2, v142, v2 wave_shl:1 row_mask:0xf bank_mask:0xf bound_ctrl:1
	v_add_f32_dpp v3, v143, v3 wave_shl:1 row_mask:0xf bank_mask:0xf bound_ctrl:1
	v_add_f32_dpp v46, v178, v46 wave_shl:1 row_mask:0xf bank_mask:0xf bound_ctrl:1
	v_add_f32_dpp v47, v179, v47 wave_shl:1 row_mask:0xf bank_mask:0xf bound_ctrl:1
	v_add_f32_dpp v56, v184, v56 wave_shl:1 row_mask:0xf bank_mask:0xf bound_ctrl:1
	v_add_f32_dpp v58, v144, v58 wave_shl:1 row_mask:0xf bank_mask:0xf bound_ctrl:1
	v_add_f32_dpp v59, v145, v59 wave_shl:1 row_mask:0xf bank_mask:0xf bound_ctrl:1
	v_add_f32_dpp v66, v180, v66 wave_shl:1 row_mask:0xf bank_mask:0xf bound_ctrl:1
	v_add_f32_dpp v67, v181, v67 wave_shl:1 row_mask:0xf bank_mask:0xf bound_ctrl:1
	v_add_f32_dpp v106, v186, v106 wave_shl:1 row_mask:0xf bank_mask:0xf bound_ctrl:1
	v_add_f32_dpp v110, v146, v110 wave_shl:1 row_mask:0xf bank_mask:0xf bound_ctrl:1
	v_add_f32_dpp v111, v147, v111 wave_shl:1 row_mask:0xf bank_mask:0xf bound_ctrl:1
	v_add_f32_dpp v112, v182, v112 wave_shl:1 row_mask:0xf bank_mask:0xf bound_ctrl:1
	v_add_f32_dpp v113, v183, v113 wave_shl:1 row_mask:0xf bank_mask:0xf bound_ctrl:1
	v_add_f32_dpp v114, v188, v114 wave_shl:1 row_mask:0xf bank_mask:0xf bound_ctrl:1
	v_add_f32_dpp v116, v190, v116 wave_shl:1 row_mask:0xf bank_mask:0xf bound_ctrl:1
	v_add_f32_dpp v117, v191, v117 wave_shl:1 row_mask:0xf bank_mask:0xf bound_ctrl:1
	v_add_f32_dpp v118, v192, v118 wave_shl:1 row_mask:0xf bank_mask:0xf bound_ctrl:1
	v_add_f32_dpp v119, v193, v119 wave_shl:1 row_mask:0xf bank_mask:0xf bound_ctrl:1
	v_add_f32_dpp v120, v194, v120 wave_shl:1 row_mask:0xf bank_mask:0xf bound_ctrl:1
	v_pk_add_f32 v[142:143], v[148:149], v[2:3]
	v_pk_add_f32 v[144:145], v[68:69], v[46:47]
	v_add_f32_e64 v68, v96, v56
	v_pk_add_f32 v[96:97], v[98:99], v[58:59]
	v_pk_add_f32 v[98:99], v[100:101], v[66:67]
	v_add_f32_e64 v100, v122, v106
	v_pk_add_f32 v[122:123], v[124:125], v[110:111]
	v_pk_add_f32 v[124:125], v[126:127], v[112:113]
	v_add_f32_e64 v126, v128, v114
	v_pk_add_f32 v[128:129], v[130:131], v[116:117]
	v_pk_add_f32 v[130:131], v[132:133], v[118:119]
	v_add_f32_e64 v132, v134, v120
	v_pk_fma_f32 v[128:129], v[32:33], v[142:143], v[128:129] op_sel_hi:[0,1,1]
	v_pk_fma_f32 v[130:131], v[32:33], v[144:145], v[130:131] op_sel_hi:[0,1,1]
	v_fma_f32 v132, v32, v68, v132
	v_pk_fma_f32 v[128:129], v[32:33], v[96:97], v[128:129] op_sel:[1,0,0]
	v_pk_fma_f32 v[130:131], v[32:33], v[98:99], v[130:131] op_sel:[1,0,0]
	v_fma_f32 v132, v33, v100, v132
	v_pk_fma_f32 v[128:129], v[34:35], v[122:123], v[128:129] op_sel_hi:[0,1,1]
	v_pk_fma_f32 v[130:131], v[34:35], v[124:125], v[130:131] op_sel_hi:[0,1,1]
	v_fma_f32 v132, v34, v126, v132
	v_cndmask_b32_e64 v134, 0, v1, s[10:11]
	v_cndmask_b32_e64 v135, 0, v1, s[14:15]
	v_cndmask_b32_e64 v146, 0, v1, s[20:21]
	v_cndmask_b32_e64 v147, 0, v1, s[22:23]
	v_cndmask_b32_e64 v148, 0, v1, s[30:31]
	v_pk_fma_f32 v[128:129], v[12:13], v[54:55], v[128:129] op_sel_hi:[1,0,1] neg_lo:[0,0,1] neg_hi:[0,0,1]
	v_pk_fma_f32 v[130:131], v[14:15], v[54:55], v[130:131] op_sel_hi:[1,0,1] neg_lo:[0,0,1] neg_hi:[0,0,1]
	v_fma_f32 v132, v16, v54, -v132
	s_add_i32 s4, s34, 9
	s_cmpk_lt_i32 s4, 0x201
	s_cselect_b64 s[12:13], s[0:1], 0
	v_pk_add_f32 v[128:129], v[128:129], v[134:135] neg_lo:[0,1] neg_hi:[0,1]
	v_pk_add_f32 v[130:131], v[130:131], v[146:147] neg_lo:[0,1] neg_hi:[0,1]
	v_add_f32_e64 v132, v132, -v148
	v_pk_mul_f32 v[178:179], v[128:129], v[128:129]
	v_pk_fma_f32 v[178:179], v[130:131], v[130:131], v[178:179]
	v_add_f32_e32 v178, v178, v179
	v_fma_f32 v178, v132, v132, v178
	v_cndmask_b32_e64 v179, 0, v178, s[12:13]
	v_add_f32_e32 v0, v0, v179

	.amdhsa_kernel _Z16closed_form_mainPKfS0_PKiPf
		.amdhsa_group_segment_fixed_size 6144
		.amdhsa_private_segment_fixed_size 0
		.amdhsa_kernarg_size 32
		.amdhsa_user_sgpr_count 2
		.amdhsa_user_sgpr_dispatch_ptr 0
		.amdhsa_user_sgpr_queue_ptr 0
		.amdhsa_user_sgpr_kernarg_segment_ptr 1
		.amdhsa_user_sgpr_dispatch_id 0
		.amdhsa_user_sgpr_kernarg_preload_length 0
		.amdhsa_user_sgpr_kernarg_preload_offset 0
		.amdhsa_user_sgpr_private_segment_size 0
		.amdhsa_uses_dynamic_stack 0
		.amdhsa_enable_private_segment 0
		.amdhsa_system_sgpr_workgroup_id_x 1
		.amdhsa_system_sgpr_workgroup_id_y 0
		.amdhsa_system_sgpr_workgroup_id_z 0
		.amdhsa_system_sgpr_workgroup_info 0
		.amdhsa_system_vgpr_workitem_id 0
		.amdhsa_next_free_vgpr 216
		.amdhsa_next_free_sgpr 44
		.amdhsa_accum_offset 216
		.amdhsa_reserve_vcc 1
		.amdhsa_float_round_mode_32 0
		.amdhsa_float_round_mode_16_64 0
		.amdhsa_float_denorm_mode_32 3
		.amdhsa_float_denorm_mode_16_64 3
		.amdhsa_dx10_clamp 1
		.amdhsa_ieee_mode 1
		.amdhsa_fp16_overflow 0
		.amdhsa_tg_split 0
		.amdhsa_exception_fp_ieee_invalid_op 0
		.amdhsa_exception_fp_denorm_src 0
		.amdhsa_exception_fp_ieee_div_zero 0
		.amdhsa_exception_fp_ieee_overflow 0
		.amdhsa_exception_fp_ieee_underflow 0
		.amdhsa_exception_fp_ieee_inexact 0
		.amdhsa_exception_int_div_zero 0
	.end_amdhsa_kernel

amdhsa.kernels:
  - .agpr_count:     0
    .args:
      - .address_space:  global
        .offset:         0
        .size:           8
        .value_kind:     global_buffer
      - .address_space:  global
        .offset:         8
        .size:           8
        .value_kind:     global_buffer
      - .address_space:  global
        .offset:         16
        .size:           8
        .value_kind:     global_buffer
      - .address_space:  global
        .offset:         24
        .size:           8
        .value_kind:     global_buffer
    .group_segment_fixed_size: 6144
    .kernarg_segment_align: 8
    .kernarg_segment_size: 32
    .language:       OpenCL C
    .language_version:
      - 2
      - 0
    .max_flat_workgroup_size: 128
    .name:           _Z16closed_form_mainPKfS0_PKiPf
    .private_segment_fixed_size: 0
    .sgpr_count:     50
    .sgpr_spill_count: 0
    .symbol:         _Z16closed_form_mainPKfS0_PKiPf.kd
    .uniform_work_group_size: 1
    .uses_dynamic_stack: false
    .vgpr_count:     216
    .vgpr_spill_count: 0
    .wavefront_size: 64
  - .agpr_count:     0
    .args:
      - .actual_access:  read_only
        .address_space:  global
        .offset:         0
        .size:           8
        .value_kind:     global_buffer
      - .actual_access:  write_only
        .address_space:  global
        .offset:         8
        .size:           8
        .value_kind:     global_buffer
    .group_segment_fixed_size: 0
    .kernarg_segment_align: 8
    .kernarg_segment_size: 16
    .language:       OpenCL C
    .language_version:
      - 2
      - 0
    .max_flat_workgroup_size: 64
    .name:           _Z17closed_form_finalPK15HIP_vector_typeIfLj4EEPf
    .private_segment_fixed_size: 0
    .sgpr_count:     10
    .sgpr_spill_count: 0
    .symbol:         _Z17closed_form_finalPK15HIP_vector_typeIfLj4EEPf.kd
    .uniform_work_group_size: 1
    .uses_dynamic_stack: false
    .vgpr_count:     36
    .vgpr_spill_count: 0
    .wavefront_size: 64
